# PEER gather u pass: row offsets premultiplied, bpermutes in two bursts, one wait per group of four MFMAs (on top of v47)
# baseline (speedup 1.0000x reference)
.LBB0_1138:
	v_and_b32_e32 v4, 15, v148
	v_cmp_eq_u32_e32 vcc, 0, v4
	v_lshlrev_b32_e32 v5, 5, v40
	v_add_u32_e32 v10, 0x80, v148
	v_cndmask_b32_e32 v10, v10, v5, vcc
	v_cmp_gt_u32_e64 s[6:7], 8, v4
	v_lshl_add_u32 v32, v10, 2, v111
	v_and_b32_e32 v36, 12, v148
	v_cndmask_b32_e64 v10, 0, v252, s[6:7]
	v_cmp_lt_u32_e64 s[6:7], 3, v4
	v_lshl_or_b32 v4, v41, 3, v5
	v_add_u32_e32 v34, 0x400, v4
	v_lshlrev_b32_e32 v4, 4, v41
	v_lshl_or_b32 v35, v40, 6, v4
	v_mul_u32_u24_e32 v250, 0x600, v130
	ds_bpermute_b32 v4, v36, v250
	v_cmp_eq_u32_e32 vcc, 3, v41
	v_cmp_eq_u32_e64 s[2:3], 2, v41
	v_cmp_eq_u32_e64 s[4:5], 1, v41
	v_lshlrev_b32_e32 v129, 4, v148
	s_waitcnt lgkmcnt(0)
	v_add_u32_e32 v5, v4, v35
	v_add_u32_e32 v4, v4, v34
	buffer_load_dwordx4 v[38:41], v5, s[44:47], 0 offen
	buffer_load_dwordx2 v[42:43], v4, s[44:47], 0 offen
	buffer_load_dwordx4 v[44:47], v5, s[44:47], s21 offen
	buffer_load_dwordx2 v[48:49], v4, s[44:47], s33 offen
	buffer_load_dwordx4 v[50:53], v5, s[44:47], s20 offen
	buffer_load_dwordx2 v[54:55], v4, s[44:47], s21 offen
	buffer_load_dwordx4 v[56:59], v5, s[44:47], s23 offen
	buffer_load_dwordx2 v[60:61], v4, s[44:47], s94 offen
	s_mov_b32 s0, 0
	v_cndmask_b32_e64 v33, 1.0, v10, s[6:7]
	ds_bpermute_b32 v222, v36, v250 offset:32
	ds_bpermute_b32 v223, v36, v250 offset:48
	ds_bpermute_b32 v224, v36, v250 offset:64
	ds_bpermute_b32 v225, v36, v250 offset:80
	ds_bpermute_b32 v226, v36, v250 offset:96
	ds_bpermute_b32 v227, v36, v250 offset:112
	ds_bpermute_b32 v228, v36, v250 offset:128
	ds_bpermute_b32 v229, v36, v250 offset:144
	ds_bpermute_b32 v230, v36, v250 offset:160
	ds_bpermute_b32 v231, v36, v250 offset:176
	ds_bpermute_b32 v232, v36, v250 offset:192
	ds_bpermute_b32 v233, v36, v250 offset:208
	ds_bpermute_b32 v234, v36, v250 offset:224
	ds_bpermute_b32 v235, v36, v250 offset:240
	ds_bpermute_b32 v4, v36, v250 offset:16
	s_waitcnt lgkmcnt(0)
	v_add_u32_e32 v5, v4, v35
	v_add_u32_e32 v4, v4, v34
	buffer_load_dwordx4 v[62:65], v5, s[44:47], 0 offen
	buffer_load_dwordx4 v[68:71], v5, s[44:47], s20 offen
	buffer_load_dwordx4 v[74:77], v5, s[44:47], s21 offen
	buffer_load_dwordx4 v[86:89], v5, s[44:47], s23 offen
	buffer_load_dwordx2 v[66:67], v4, s[44:47], 0 offen
	buffer_load_dwordx2 v[78:79], v4, s[44:47], s33 offen
	buffer_load_dwordx2 v[72:73], v4, s[44:47], s21 offen
	buffer_load_dwordx2 v[90:91], v4, s[44:47], s94 offen
	v_add_u32_e32 v5, v222, v35
	v_add_u32_e32 v4, v222, v34
	buffer_load_dwordx4 v[92:95], v5, s[44:47], 0 offen
	buffer_load_dwordx4 v[98:101], v5, s[44:47], s20 offen
	buffer_load_dwordx4 v[150:153], v5, s[44:47], s21 offen
	buffer_load_dwordx4 v[156:159], v5, s[44:47], s23 offen
	buffer_load_dwordx2 v[96:97], v4, s[44:47], 0 offen
	buffer_load_dwordx2 v[154:155], v4, s[44:47], s33 offen
	buffer_load_dwordx2 v[102:103], v4, s[44:47], s21 offen
	buffer_load_dwordx2 v[160:161], v4, s[44:47], s94 offen
	v_add_u32_e32 v5, v223, v35
	v_add_u32_e32 v4, v223, v34
	buffer_load_dwordx4 v[162:165], v5, s[44:47], 0 offen
	buffer_load_dwordx4 v[168:171], v5, s[44:47], s20 offen
	buffer_load_dwordx4 v[174:177], v5, s[44:47], s21 offen
	buffer_load_dwordx4 v[216:219], v5, s[44:47], s23 offen
	buffer_load_dwordx2 v[166:167], v4, s[44:47], 0 offen
	buffer_load_dwordx2 v[178:179], v4, s[44:47], s33 offen
	buffer_load_dwordx2 v[172:173], v4, s[44:47], s21 offen
	buffer_load_dwordx2 v[220:221], v4, s[44:47], s94 offen
	v_mov_b32_e32 v22, v28
	v_mov_b32_e32 v23, v29
	v_mov_b32_e32 v16, v30
	v_mov_b32_e32 v17, v31
	s_waitcnt vmcnt(24)
	v_mfma_f32_16x16x128_f8f6f4 v[38:41], v[38:43], v[18:23], 0 cbsz:2 blgp:2
	v_mov_b32_e32 v10, v24
	v_mov_b32_e32 v11, v25
	v_mov_b32_e32 v4, v26
	v_mfma_f32_16x16x128_f8f6f4 v[28:31], v[44:49], v[12:17], v[38:41] cbsz:2 blgp:2
	v_mov_b32_e32 v5, v27
	v_mfma_f32_16x16x128_f8f6f4 v[28:31], v[50:55], v[6:11], v[28:31] cbsz:2 blgp:2
	v_mfma_f32_16x16x128_f8f6f4 v[24:27], v[56:61], v[0:5], v[28:31] cbsz:2 blgp:2
	s_nop 7
	v_cndmask_b32_e64 v24, v24, v25, s[4:5]
	v_cndmask_b32_e64 v24, v24, v26, s[2:3]
	v_cndmask_b32_e32 v24, v24, v27, vcc
	v_mul_f32_e32 v25, v33, v24
	s_nop 1
	v_mov_b32_dpp v25, v25 quad_perm:[1,0,3,2] row_mask:0xf bank_mask:0xf bound_ctrl:1
	v_fmac_f32_e32 v25, v33, v24
	s_nop 1
	v_add_f32_dpp v24, v25, v25 quad_perm:[2,3,0,1] row_mask:0xf bank_mask:0xf bound_ctrl:1
	s_nop 1
	v_add_f32_dpp v24, v24, v24 row_half_mirror row_mask:0xf bank_mask:0xf bound_ctrl:1
	ds_write_b32 v32, v24 offset:49152
	v_add_u32_e32 v28, v224, v35
	v_add_u32_e32 v30, v224, v34
	buffer_load_dwordx4 v[24:27], v28, s[44:47], 0 offen
	buffer_load_dwordx4 v[38:41], v28, s[44:47], s20 offen
	buffer_load_dwordx4 v[44:47], v28, s[44:47], s21 offen
	buffer_load_dwordx4 v[50:53], v28, s[44:47], s23 offen
	s_nop 0
	buffer_load_dwordx2 v[28:29], v30, s[44:47], 0 offen
	buffer_load_dwordx2 v[48:49], v30, s[44:47], s33 offen
	buffer_load_dwordx2 v[42:43], v30, s[44:47], s21 offen
	buffer_load_dwordx2 v[54:55], v30, s[44:47], s94 offen
	s_waitcnt vmcnt(24)
	v_mfma_f32_16x16x128_f8f6f4 v[56:59], v[62:67], v[18:23], 0 cbsz:2 blgp:2
	v_mfma_f32_16x16x128_f8f6f4 v[56:59], v[74:79], v[12:17], v[56:59] cbsz:2 blgp:2
	v_mfma_f32_16x16x128_f8f6f4 v[56:59], v[68:73], v[6:11], v[56:59] cbsz:2 blgp:2
	v_mfma_f32_16x16x128_f8f6f4 v[56:59], v[86:91], v[0:5], v[56:59] cbsz:2 blgp:2
	s_nop 7
	v_cndmask_b32_e64 v30, v56, v57, s[4:5]
	v_cndmask_b32_e64 v30, v30, v58, s[2:3]
	v_cndmask_b32_e32 v30, v30, v59, vcc
	v_mul_f32_e32 v31, v33, v30
	s_nop 1
	v_mov_b32_dpp v31, v31 quad_perm:[1,0,3,2] row_mask:0xf bank_mask:0xf bound_ctrl:1
	v_fmac_f32_e32 v31, v33, v30
	s_nop 1
	v_add_f32_dpp v30, v31, v31 quad_perm:[2,3,0,1] row_mask:0xf bank_mask:0xf bound_ctrl:1
	s_nop 1
	v_add_f32_dpp v30, v30, v30 row_half_mirror row_mask:0xf bank_mask:0xf bound_ctrl:1
	ds_write_b32 v32, v30 offset:49156
	v_add_u32_e32 v31, v225, v35
	v_add_u32_e32 v30, v225, v34
	buffer_load_dwordx4 v[56:59], v31, s[44:47], 0 offen
	buffer_load_dwordx4 v[62:65], v31, s[44:47], s20 offen
	buffer_load_dwordx4 v[68:71], v31, s[44:47], s21 offen
	buffer_load_dwordx4 v[74:77], v31, s[44:47], s23 offen
	buffer_load_dwordx2 v[60:61], v30, s[44:47], 0 offen
	buffer_load_dwordx2 v[72:73], v30, s[44:47], s33 offen
	buffer_load_dwordx2 v[66:67], v30, s[44:47], s21 offen
	buffer_load_dwordx2 v[78:79], v30, s[44:47], s94 offen
	s_waitcnt vmcnt(24)
	v_mfma_f32_16x16x128_f8f6f4 v[86:89], v[92:97], v[18:23], 0 cbsz:2 blgp:2
	v_mfma_f32_16x16x128_f8f6f4 v[86:89], v[150:155], v[12:17], v[86:89] cbsz:2 blgp:2
	v_mfma_f32_16x16x128_f8f6f4 v[86:89], v[98:103], v[6:11], v[86:89] cbsz:2 blgp:2
	v_mfma_f32_16x16x128_f8f6f4 v[86:89], v[156:161], v[0:5], v[86:89] cbsz:2 blgp:2
	s_nop 7
	v_cndmask_b32_e64 v30, v86, v87, s[4:5]
	v_cndmask_b32_e64 v30, v30, v88, s[2:3]
	v_cndmask_b32_e32 v30, v30, v89, vcc
	v_mul_f32_e32 v31, v33, v30
	s_nop 1
	v_mov_b32_dpp v31, v31 quad_perm:[1,0,3,2] row_mask:0xf bank_mask:0xf bound_ctrl:1
	v_fmac_f32_e32 v31, v33, v30
	s_nop 1
	v_add_f32_dpp v30, v31, v31 quad_perm:[2,3,0,1] row_mask:0xf bank_mask:0xf bound_ctrl:1
	s_nop 1
	v_add_f32_dpp v30, v30, v30 row_half_mirror row_mask:0xf bank_mask:0xf bound_ctrl:1
	ds_write_b32 v32, v30 offset:49160
	v_add_u32_e32 v31, v226, v35
	v_add_u32_e32 v30, v226, v34
	buffer_load_dwordx4 v[86:89], v31, s[44:47], 0 offen
	buffer_load_dwordx4 v[92:95], v31, s[44:47], s20 offen
	buffer_load_dwordx4 v[98:101], v31, s[44:47], s21 offen
	buffer_load_dwordx4 v[150:153], v31, s[44:47], s23 offen
	buffer_load_dwordx2 v[90:91], v30, s[44:47], 0 offen
	buffer_load_dwordx2 v[102:103], v30, s[44:47], s33 offen
	buffer_load_dwordx2 v[96:97], v30, s[44:47], s21 offen
	buffer_load_dwordx2 v[154:155], v30, s[44:47], s94 offen
	s_waitcnt vmcnt(24)
	v_mfma_f32_16x16x128_f8f6f4 v[156:159], v[162:167], v[18:23], 0 cbsz:2 blgp:2
	v_mfma_f32_16x16x128_f8f6f4 v[156:159], v[174:179], v[12:17], v[156:159] cbsz:2 blgp:2
	v_mfma_f32_16x16x128_f8f6f4 v[156:159], v[168:173], v[6:11], v[156:159] cbsz:2 blgp:2
	v_mfma_f32_16x16x128_f8f6f4 v[156:159], v[216:221], v[0:5], v[156:159] cbsz:2 blgp:2
	s_nop 7
	v_cndmask_b32_e64 v30, v156, v157, s[4:5]
	v_cndmask_b32_e64 v30, v30, v158, s[2:3]
	v_cndmask_b32_e32 v30, v30, v159, vcc
	v_mul_f32_e32 v31, v33, v30
	s_nop 1
	v_mov_b32_dpp v31, v31 quad_perm:[1,0,3,2] row_mask:0xf bank_mask:0xf bound_ctrl:1
	v_fmac_f32_e32 v31, v33, v30
	s_nop 1
	v_add_f32_dpp v30, v31, v31 quad_perm:[2,3,0,1] row_mask:0xf bank_mask:0xf bound_ctrl:1
	s_nop 1
	v_add_f32_dpp v30, v30, v30 row_half_mirror row_mask:0xf bank_mask:0xf bound_ctrl:1
	ds_write_b32 v32, v30 offset:49164
	v_add_u32_e32 v31, v227, v35
	v_add_u32_e32 v30, v227, v34
	buffer_load_dwordx4 v[156:159], v31, s[44:47], 0 offen
	buffer_load_dwordx4 v[162:165], v31, s[44:47], s20 offen
	buffer_load_dwordx4 v[168:171], v31, s[44:47], s21 offen
	buffer_load_dwordx4 v[174:177], v31, s[44:47], s23 offen
	buffer_load_dwordx2 v[160:161], v30, s[44:47], 0 offen
	buffer_load_dwordx2 v[172:173], v30, s[44:47], s33 offen
	buffer_load_dwordx2 v[166:167], v30, s[44:47], s21 offen
	buffer_load_dwordx2 v[178:179], v30, s[44:47], s94 offen
	s_waitcnt vmcnt(24)
	v_mfma_f32_16x16x128_f8f6f4 v[24:27], v[24:29], v[18:23], 0 cbsz:2 blgp:2
	v_mfma_f32_16x16x128_f8f6f4 v[24:27], v[44:49], v[12:17], v[24:27] cbsz:2 blgp:2
	v_mfma_f32_16x16x128_f8f6f4 v[24:27], v[38:43], v[6:11], v[24:27] cbsz:2 blgp:2
	v_mfma_f32_16x16x128_f8f6f4 v[24:27], v[50:55], v[0:5], v[24:27] cbsz:2 blgp:2
	s_nop 7
	v_cndmask_b32_e64 v24, v24, v25, s[4:5]
	v_cndmask_b32_e64 v24, v24, v26, s[2:3]
	v_cndmask_b32_e32 v24, v24, v27, vcc
	v_mul_f32_e32 v25, v33, v24
	s_nop 1
	v_mov_b32_dpp v25, v25 quad_perm:[1,0,3,2] row_mask:0xf bank_mask:0xf bound_ctrl:1
	v_fmac_f32_e32 v25, v33, v24
	s_nop 1
	v_add_f32_dpp v24, v25, v25 quad_perm:[2,3,0,1] row_mask:0xf bank_mask:0xf bound_ctrl:1
	s_nop 1
	v_add_f32_dpp v24, v24, v24 row_half_mirror row_mask:0xf bank_mask:0xf bound_ctrl:1
	ds_write_b32 v32, v24 offset:49168
	v_add_u32_e32 v28, v228, v35
	v_add_u32_e32 v30, v228, v34
	buffer_load_dwordx4 v[24:27], v28, s[44:47], 0 offen
	buffer_load_dwordx4 v[38:41], v28, s[44:47], s20 offen
	buffer_load_dwordx4 v[44:47], v28, s[44:47], s21 offen
	buffer_load_dwordx4 v[50:53], v28, s[44:47], s23 offen
	s_nop 0
	buffer_load_dwordx2 v[28:29], v30, s[44:47], 0 offen
	buffer_load_dwordx2 v[48:49], v30, s[44:47], s33 offen
	buffer_load_dwordx2 v[42:43], v30, s[44:47], s21 offen
	buffer_load_dwordx2 v[54:55], v30, s[44:47], s94 offen
	s_waitcnt vmcnt(24)
	v_mfma_f32_16x16x128_f8f6f4 v[56:59], v[56:61], v[18:23], 0 cbsz:2 blgp:2
	v_mfma_f32_16x16x128_f8f6f4 v[56:59], v[68:73], v[12:17], v[56:59] cbsz:2 blgp:2
	v_mfma_f32_16x16x128_f8f6f4 v[56:59], v[62:67], v[6:11], v[56:59] cbsz:2 blgp:2
	v_mfma_f32_16x16x128_f8f6f4 v[56:59], v[74:79], v[0:5], v[56:59] cbsz:2 blgp:2
	s_nop 7
	v_cndmask_b32_e64 v30, v56, v57, s[4:5]
	v_cndmask_b32_e64 v30, v30, v58, s[2:3]
	v_cndmask_b32_e32 v30, v30, v59, vcc
	v_mul_f32_e32 v31, v33, v30
	s_nop 1
	v_mov_b32_dpp v31, v31 quad_perm:[1,0,3,2] row_mask:0xf bank_mask:0xf bound_ctrl:1
	v_fmac_f32_e32 v31, v33, v30
	s_nop 1
	v_add_f32_dpp v30, v31, v31 quad_perm:[2,3,0,1] row_mask:0xf bank_mask:0xf bound_ctrl:1
	s_nop 1
	v_add_f32_dpp v30, v30, v30 row_half_mirror row_mask:0xf bank_mask:0xf bound_ctrl:1
	ds_write_b32 v32, v30 offset:49172
	v_add_u32_e32 v31, v229, v35
	v_add_u32_e32 v30, v229, v34
	buffer_load_dwordx4 v[56:59], v31, s[44:47], 0 offen
	buffer_load_dwordx4 v[62:65], v31, s[44:47], s20 offen
	buffer_load_dwordx4 v[68:71], v31, s[44:47], s21 offen
	buffer_load_dwordx4 v[74:77], v31, s[44:47], s23 offen
	buffer_load_dwordx2 v[60:61], v30, s[44:47], 0 offen
	buffer_load_dwordx2 v[72:73], v30, s[44:47], s33 offen
	buffer_load_dwordx2 v[66:67], v30, s[44:47], s21 offen
	buffer_load_dwordx2 v[78:79], v30, s[44:47], s94 offen
	s_waitcnt vmcnt(24)
	v_mfma_f32_16x16x128_f8f6f4 v[86:89], v[86:91], v[18:23], 0 cbsz:2 blgp:2
	v_mfma_f32_16x16x128_f8f6f4 v[86:89], v[98:103], v[12:17], v[86:89] cbsz:2 blgp:2
	v_mfma_f32_16x16x128_f8f6f4 v[86:89], v[92:97], v[6:11], v[86:89] cbsz:2 blgp:2
	v_mfma_f32_16x16x128_f8f6f4 v[86:89], v[150:155], v[0:5], v[86:89] cbsz:2 blgp:2
	s_nop 7
	v_cndmask_b32_e64 v30, v86, v87, s[4:5]
	v_cndmask_b32_e64 v30, v30, v88, s[2:3]
	v_cndmask_b32_e32 v30, v30, v89, vcc
	v_mul_f32_e32 v31, v33, v30
	s_nop 1
	v_mov_b32_dpp v31, v31 quad_perm:[1,0,3,2] row_mask:0xf bank_mask:0xf bound_ctrl:1
	v_fmac_f32_e32 v31, v33, v30
	s_nop 1
	v_add_f32_dpp v30, v31, v31 quad_perm:[2,3,0,1] row_mask:0xf bank_mask:0xf bound_ctrl:1
	s_nop 1
	v_add_f32_dpp v30, v30, v30 row_half_mirror row_mask:0xf bank_mask:0xf bound_ctrl:1
	ds_write_b32 v32, v30 offset:49176
	v_add_u32_e32 v31, v230, v35
	v_add_u32_e32 v30, v230, v34
	buffer_load_dwordx4 v[86:89], v31, s[44:47], 0 offen
	buffer_load_dwordx4 v[92:95], v31, s[44:47], s20 offen
	buffer_load_dwordx4 v[98:101], v31, s[44:47], s21 offen
	buffer_load_dwordx4 v[150:153], v31, s[44:47], s23 offen
	buffer_load_dwordx2 v[90:91], v30, s[44:47], 0 offen
	buffer_load_dwordx2 v[102:103], v30, s[44:47], s33 offen
	buffer_load_dwordx2 v[96:97], v30, s[44:47], s21 offen
	buffer_load_dwordx2 v[154:155], v30, s[44:47], s94 offen
	s_waitcnt vmcnt(24)
	v_mfma_f32_16x16x128_f8f6f4 v[156:159], v[156:161], v[18:23], 0 cbsz:2 blgp:2
	v_mfma_f32_16x16x128_f8f6f4 v[156:159], v[168:173], v[12:17], v[156:159] cbsz:2 blgp:2
	v_mfma_f32_16x16x128_f8f6f4 v[156:159], v[162:167], v[6:11], v[156:159] cbsz:2 blgp:2
	v_mfma_f32_16x16x128_f8f6f4 v[156:159], v[174:179], v[0:5], v[156:159] cbsz:2 blgp:2
	s_nop 7
	v_cndmask_b32_e64 v30, v156, v157, s[4:5]
	v_cndmask_b32_e64 v30, v30, v158, s[2:3]
	v_cndmask_b32_e32 v30, v30, v159, vcc
	v_mul_f32_e32 v31, v33, v30
	s_nop 1
	v_mov_b32_dpp v31, v31 quad_perm:[1,0,3,2] row_mask:0xf bank_mask:0xf bound_ctrl:1
	v_fmac_f32_e32 v31, v33, v30
	s_nop 1
	v_add_f32_dpp v30, v31, v31 quad_perm:[2,3,0,1] row_mask:0xf bank_mask:0xf bound_ctrl:1
	s_nop 1
	v_add_f32_dpp v30, v30, v30 row_half_mirror row_mask:0xf bank_mask:0xf bound_ctrl:1
	ds_write_b32 v32, v30 offset:49180
	v_add_u32_e32 v31, v231, v35
	v_add_u32_e32 v30, v231, v34
	buffer_load_dwordx4 v[156:159], v31, s[44:47], 0 offen
	buffer_load_dwordx4 v[162:165], v31, s[44:47], s20 offen
	buffer_load_dwordx4 v[168:171], v31, s[44:47], s21 offen
	buffer_load_dwordx4 v[174:177], v31, s[44:47], s23 offen
	buffer_load_dwordx2 v[160:161], v30, s[44:47], 0 offen
	buffer_load_dwordx2 v[172:173], v30, s[44:47], s33 offen
	buffer_load_dwordx2 v[166:167], v30, s[44:47], s21 offen
	buffer_load_dwordx2 v[178:179], v30, s[44:47], s94 offen
	s_waitcnt vmcnt(24)
	v_mfma_f32_16x16x128_f8f6f4 v[24:27], v[24:29], v[18:23], 0 cbsz:2 blgp:2
	v_mfma_f32_16x16x128_f8f6f4 v[24:27], v[44:49], v[12:17], v[24:27] cbsz:2 blgp:2
	v_mfma_f32_16x16x128_f8f6f4 v[24:27], v[38:43], v[6:11], v[24:27] cbsz:2 blgp:2
	v_mfma_f32_16x16x128_f8f6f4 v[24:27], v[50:55], v[0:5], v[24:27] cbsz:2 blgp:2
	s_nop 7
	v_cndmask_b32_e64 v24, v24, v25, s[4:5]
	v_cndmask_b32_e64 v24, v24, v26, s[2:3]
	v_cndmask_b32_e32 v24, v24, v27, vcc
	v_mul_f32_e32 v25, v33, v24
	s_nop 1
	v_mov_b32_dpp v25, v25 quad_perm:[1,0,3,2] row_mask:0xf bank_mask:0xf bound_ctrl:1
	v_fmac_f32_e32 v25, v33, v24
	s_nop 1
	v_add_f32_dpp v24, v25, v25 quad_perm:[2,3,0,1] row_mask:0xf bank_mask:0xf bound_ctrl:1
	s_nop 1
	v_add_f32_dpp v24, v24, v24 row_half_mirror row_mask:0xf bank_mask:0xf bound_ctrl:1
	ds_write_b32 v32, v24 offset:49184
	v_add_u32_e32 v28, v232, v35
	v_add_u32_e32 v30, v232, v34
	buffer_load_dwordx4 v[24:27], v28, s[44:47], 0 offen
	buffer_load_dwordx4 v[38:41], v28, s[44:47], s20 offen
	buffer_load_dwordx4 v[44:47], v28, s[44:47], s21 offen
	buffer_load_dwordx4 v[50:53], v28, s[44:47], s23 offen
	s_nop 0
	buffer_load_dwordx2 v[28:29], v30, s[44:47], 0 offen
	buffer_load_dwordx2 v[48:49], v30, s[44:47], s33 offen
	buffer_load_dwordx2 v[42:43], v30, s[44:47], s21 offen
	buffer_load_dwordx2 v[54:55], v30, s[44:47], s94 offen
	s_waitcnt vmcnt(24)
	v_mfma_f32_16x16x128_f8f6f4 v[56:59], v[56:61], v[18:23], 0 cbsz:2 blgp:2
	v_mfma_f32_16x16x128_f8f6f4 v[56:59], v[68:73], v[12:17], v[56:59] cbsz:2 blgp:2
	v_mfma_f32_16x16x128_f8f6f4 v[56:59], v[62:67], v[6:11], v[56:59] cbsz:2 blgp:2
	v_mfma_f32_16x16x128_f8f6f4 v[56:59], v[74:79], v[0:5], v[56:59] cbsz:2 blgp:2
	s_nop 7
	v_cndmask_b32_e64 v30, v56, v57, s[4:5]
	v_cndmask_b32_e64 v30, v30, v58, s[2:3]
	v_cndmask_b32_e32 v30, v30, v59, vcc
	v_mul_f32_e32 v31, v33, v30
	s_nop 1
	v_mov_b32_dpp v31, v31 quad_perm:[1,0,3,2] row_mask:0xf bank_mask:0xf bound_ctrl:1
	v_fmac_f32_e32 v31, v33, v30
	s_nop 1
	v_add_f32_dpp v30, v31, v31 quad_perm:[2,3,0,1] row_mask:0xf bank_mask:0xf bound_ctrl:1
	s_nop 1
	v_add_f32_dpp v30, v30, v30 row_half_mirror row_mask:0xf bank_mask:0xf bound_ctrl:1
	ds_write_b32 v32, v30 offset:49188
	v_add_u32_e32 v31, v233, v35
	v_add_u32_e32 v30, v233, v34
	buffer_load_dwordx4 v[56:59], v31, s[44:47], 0 offen
	buffer_load_dwordx4 v[62:65], v31, s[44:47], s20 offen
	buffer_load_dwordx4 v[68:71], v31, s[44:47], s21 offen
	buffer_load_dwordx4 v[74:77], v31, s[44:47], s23 offen
	buffer_load_dwordx2 v[60:61], v30, s[44:47], 0 offen
	buffer_load_dwordx2 v[72:73], v30, s[44:47], s33 offen
	buffer_load_dwordx2 v[66:67], v30, s[44:47], s21 offen
	buffer_load_dwordx2 v[78:79], v30, s[44:47], s94 offen
	s_waitcnt vmcnt(24)
	v_mfma_f32_16x16x128_f8f6f4 v[86:89], v[86:91], v[18:23], 0 cbsz:2 blgp:2
	v_mfma_f32_16x16x128_f8f6f4 v[86:89], v[98:103], v[12:17], v[86:89] cbsz:2 blgp:2
	v_mfma_f32_16x16x128_f8f6f4 v[86:89], v[92:97], v[6:11], v[86:89] cbsz:2 blgp:2
	v_mfma_f32_16x16x128_f8f6f4 v[86:89], v[150:155], v[0:5], v[86:89] cbsz:2 blgp:2
	s_nop 7
	v_cndmask_b32_e64 v30, v86, v87, s[4:5]
	v_cndmask_b32_e64 v30, v30, v88, s[2:3]
	v_cndmask_b32_e32 v30, v30, v89, vcc
	v_mul_f32_e32 v31, v33, v30
	s_nop 1
	v_mov_b32_dpp v31, v31 quad_perm:[1,0,3,2] row_mask:0xf bank_mask:0xf bound_ctrl:1
	v_fmac_f32_e32 v31, v33, v30
	s_nop 1
	v_add_f32_dpp v30, v31, v31 quad_perm:[2,3,0,1] row_mask:0xf bank_mask:0xf bound_ctrl:1
	s_nop 1
	v_add_f32_dpp v30, v30, v30 row_half_mirror row_mask:0xf bank_mask:0xf bound_ctrl:1
	ds_write_b32 v32, v30 offset:49192
	v_add_u32_e32 v31, v234, v35
	v_add_u32_e32 v30, v234, v34
	buffer_load_dwordx4 v[86:89], v31, s[44:47], 0 offen
	buffer_load_dwordx4 v[92:95], v31, s[44:47], s20 offen
	buffer_load_dwordx4 v[98:101], v31, s[44:47], s21 offen
	buffer_load_dwordx4 v[150:153], v31, s[44:47], s23 offen
	buffer_load_dwordx2 v[90:91], v30, s[44:47], 0 offen
	buffer_load_dwordx2 v[102:103], v30, s[44:47], s33 offen
	buffer_load_dwordx2 v[96:97], v30, s[44:47], s21 offen
	buffer_load_dwordx2 v[154:155], v30, s[44:47], s94 offen
	s_waitcnt vmcnt(24)
	v_mfma_f32_16x16x128_f8f6f4 v[156:159], v[156:161], v[18:23], 0 cbsz:2 blgp:2
	v_mfma_f32_16x16x128_f8f6f4 v[156:159], v[168:173], v[12:17], v[156:159] cbsz:2 blgp:2
	v_mfma_f32_16x16x128_f8f6f4 v[156:159], v[162:167], v[6:11], v[156:159] cbsz:2 blgp:2
	v_mfma_f32_16x16x128_f8f6f4 v[156:159], v[174:179], v[0:5], v[156:159] cbsz:2 blgp:2
	s_nop 7
	v_cndmask_b32_e64 v30, v156, v157, s[4:5]
	v_cndmask_b32_e64 v30, v30, v158, s[2:3]
	v_cndmask_b32_e32 v30, v30, v159, vcc
	v_mul_f32_e32 v31, v33, v30
	s_nop 1
	v_mov_b32_dpp v31, v31 quad_perm:[1,0,3,2] row_mask:0xf bank_mask:0xf bound_ctrl:1
	v_fmac_f32_e32 v31, v33, v30
	s_nop 1
	v_add_f32_dpp v30, v31, v31 quad_perm:[2,3,0,1] row_mask:0xf bank_mask:0xf bound_ctrl:1
	s_nop 1
	v_add_f32_dpp v30, v30, v30 row_half_mirror row_mask:0xf bank_mask:0xf bound_ctrl:1
	ds_write_b32 v32, v30 offset:49196
	v_add_u32_e32 v31, v235, v35
	v_add_u32_e32 v30, v235, v34
	buffer_load_dwordx4 v[156:159], v31, s[44:47], 0 offen
	buffer_load_dwordx4 v[162:165], v31, s[44:47], s20 offen
	buffer_load_dwordx4 v[168:171], v31, s[44:47], s21 offen
	buffer_load_dwordx4 v[174:177], v31, s[44:47], s23 offen
	buffer_load_dwordx2 v[160:161], v30, s[44:47], 0 offen
	buffer_load_dwordx2 v[172:173], v30, s[44:47], s33 offen
	buffer_load_dwordx2 v[166:167], v30, s[44:47], s21 offen
	buffer_load_dwordx2 v[178:179], v30, s[44:47], s94 offen
	s_waitcnt vmcnt(24)
	v_mfma_f32_16x16x128_f8f6f4 v[24:27], v[24:29], v[18:23], 0 cbsz:2 blgp:2
	v_mfma_f32_16x16x128_f8f6f4 v[24:27], v[44:49], v[12:17], v[24:27] cbsz:2 blgp:2
	v_mfma_f32_16x16x128_f8f6f4 v[24:27], v[38:43], v[6:11], v[24:27] cbsz:2 blgp:2
	v_mfma_f32_16x16x128_f8f6f4 v[24:27], v[50:55], v[0:5], v[24:27] cbsz:2 blgp:2
	s_nop 7
	v_cndmask_b32_e64 v24, v24, v25, s[4:5]
	v_cndmask_b32_e64 v24, v24, v26, s[2:3]
	v_cndmask_b32_e32 v24, v24, v27, vcc
	v_mul_f32_e32 v25, v33, v24
	s_nop 1
	v_mov_b32_dpp v25, v25 quad_perm:[1,0,3,2] row_mask:0xf bank_mask:0xf bound_ctrl:1
	v_fmac_f32_e32 v25, v33, v24
	s_nop 1
	v_add_f32_dpp v24, v25, v25 quad_perm:[2,3,0,1] row_mask:0xf bank_mask:0xf bound_ctrl:1
	s_nop 1
	v_add_f32_dpp v24, v24, v24 row_half_mirror row_mask:0xf bank_mask:0xf bound_ctrl:1
	ds_write_b32 v32, v24 offset:49200
	v_mul_u32_u24_e32 v251, 0x600, v128
	ds_bpermute_b32 v236, v36, v251 offset:16
	ds_bpermute_b32 v237, v36, v251 offset:32
	ds_bpermute_b32 v238, v36, v251 offset:48
	ds_bpermute_b32 v239, v36, v251 offset:64
	ds_bpermute_b32 v240, v36, v251 offset:80
	ds_bpermute_b32 v241, v36, v251 offset:96
	ds_bpermute_b32 v242, v36, v251 offset:112
	ds_bpermute_b32 v243, v36, v251 offset:128
	ds_bpermute_b32 v244, v36, v251 offset:144
	ds_bpermute_b32 v245, v36, v251 offset:160
	ds_bpermute_b32 v246, v36, v251 offset:176
	ds_bpermute_b32 v247, v36, v251 offset:192
	ds_bpermute_b32 v248, v36, v251 offset:208
	ds_bpermute_b32 v249, v36, v251 offset:224
	ds_bpermute_b32 v24, v36, v251
	s_waitcnt lgkmcnt(0)
	v_add_u32_e32 v28, v24, v35
	v_add_u32_e32 v30, v24, v34
	buffer_load_dwordx4 v[24:27], v28, s[44:47], 0 offen
	buffer_load_dwordx4 v[38:41], v28, s[44:47], s20 offen
	buffer_load_dwordx4 v[44:47], v28, s[44:47], s21 offen
	buffer_load_dwordx4 v[50:53], v28, s[44:47], s23 offen
	s_nop 0
	buffer_load_dwordx2 v[28:29], v30, s[44:47], 0 offen
	buffer_load_dwordx2 v[48:49], v30, s[44:47], s33 offen
	buffer_load_dwordx2 v[42:43], v30, s[44:47], s21 offen
	buffer_load_dwordx2 v[54:55], v30, s[44:47], s94 offen
	s_waitcnt vmcnt(24)
	v_mfma_f32_16x16x128_f8f6f4 v[56:59], v[56:61], v[18:23], 0 cbsz:2 blgp:2
	v_mfma_f32_16x16x128_f8f6f4 v[56:59], v[68:73], v[12:17], v[56:59] cbsz:2 blgp:2
	v_mfma_f32_16x16x128_f8f6f4 v[56:59], v[62:67], v[6:11], v[56:59] cbsz:2 blgp:2
	v_mfma_f32_16x16x128_f8f6f4 v[56:59], v[74:79], v[0:5], v[56:59] cbsz:2 blgp:2
	s_nop 7
	v_cndmask_b32_e64 v30, v56, v57, s[4:5]
	v_cndmask_b32_e64 v30, v30, v58, s[2:3]
	v_cndmask_b32_e32 v30, v30, v59, vcc
	v_mul_f32_e32 v31, v33, v30
	s_nop 1
	v_mov_b32_dpp v31, v31 quad_perm:[1,0,3,2] row_mask:0xf bank_mask:0xf bound_ctrl:1
	v_fmac_f32_e32 v31, v33, v30
	s_nop 1
	v_add_f32_dpp v30, v31, v31 quad_perm:[2,3,0,1] row_mask:0xf bank_mask:0xf bound_ctrl:1
	s_nop 1
	v_add_f32_dpp v30, v30, v30 row_half_mirror row_mask:0xf bank_mask:0xf bound_ctrl:1
	ds_write_b32 v32, v30 offset:49204
	v_add_u32_e32 v31, v236, v35
	v_add_u32_e32 v30, v236, v34
	buffer_load_dwordx4 v[56:59], v31, s[44:47], 0 offen
	buffer_load_dwordx4 v[62:65], v31, s[44:47], s20 offen
	buffer_load_dwordx4 v[68:71], v31, s[44:47], s21 offen
	buffer_load_dwordx4 v[74:77], v31, s[44:47], s23 offen
	buffer_load_dwordx2 v[60:61], v30, s[44:47], 0 offen
	buffer_load_dwordx2 v[72:73], v30, s[44:47], s33 offen
	buffer_load_dwordx2 v[66:67], v30, s[44:47], s21 offen
	buffer_load_dwordx2 v[78:79], v30, s[44:47], s94 offen
	s_waitcnt vmcnt(24)
	v_mfma_f32_16x16x128_f8f6f4 v[86:89], v[86:91], v[18:23], 0 cbsz:2 blgp:2
	v_mfma_f32_16x16x128_f8f6f4 v[86:89], v[98:103], v[12:17], v[86:89] cbsz:2 blgp:2
	v_mfma_f32_16x16x128_f8f6f4 v[86:89], v[92:97], v[6:11], v[86:89] cbsz:2 blgp:2
	v_mfma_f32_16x16x128_f8f6f4 v[86:89], v[150:155], v[0:5], v[86:89] cbsz:2 blgp:2
	s_nop 7
	v_cndmask_b32_e64 v30, v86, v87, s[4:5]
	v_cndmask_b32_e64 v30, v30, v88, s[2:3]
	v_cndmask_b32_e32 v30, v30, v89, vcc
	v_mul_f32_e32 v31, v33, v30
	s_nop 1
	v_mov_b32_dpp v31, v31 quad_perm:[1,0,3,2] row_mask:0xf bank_mask:0xf bound_ctrl:1
	v_fmac_f32_e32 v31, v33, v30
	s_nop 1
	v_add_f32_dpp v30, v31, v31 quad_perm:[2,3,0,1] row_mask:0xf bank_mask:0xf bound_ctrl:1
	s_nop 1
	v_add_f32_dpp v30, v30, v30 row_half_mirror row_mask:0xf bank_mask:0xf bound_ctrl:1
	ds_write_b32 v32, v30 offset:49208
	v_add_u32_e32 v31, v237, v35
	v_add_u32_e32 v30, v237, v34
	buffer_load_dwordx4 v[86:89], v31, s[44:47], 0 offen
	buffer_load_dwordx4 v[92:95], v31, s[44:47], s20 offen
	buffer_load_dwordx4 v[98:101], v31, s[44:47], s21 offen
	buffer_load_dwordx4 v[150:153], v31, s[44:47], s23 offen
	buffer_load_dwordx2 v[90:91], v30, s[44:47], 0 offen
	buffer_load_dwordx2 v[102:103], v30, s[44:47], s33 offen
	buffer_load_dwordx2 v[96:97], v30, s[44:47], s21 offen
	buffer_load_dwordx2 v[154:155], v30, s[44:47], s94 offen
	s_waitcnt vmcnt(24)
	v_mfma_f32_16x16x128_f8f6f4 v[156:159], v[156:161], v[18:23], 0 cbsz:2 blgp:2
	v_mfma_f32_16x16x128_f8f6f4 v[156:159], v[168:173], v[12:17], v[156:159] cbsz:2 blgp:2
	v_mfma_f32_16x16x128_f8f6f4 v[156:159], v[162:167], v[6:11], v[156:159] cbsz:2 blgp:2
	v_mfma_f32_16x16x128_f8f6f4 v[156:159], v[174:179], v[0:5], v[156:159] cbsz:2 blgp:2
	s_nop 7
	v_cndmask_b32_e64 v30, v156, v157, s[4:5]
	v_cndmask_b32_e64 v30, v30, v158, s[2:3]
	v_cndmask_b32_e32 v30, v30, v159, vcc
	v_mul_f32_e32 v31, v33, v30
	s_nop 1
	v_mov_b32_dpp v31, v31 quad_perm:[1,0,3,2] row_mask:0xf bank_mask:0xf bound_ctrl:1
	v_fmac_f32_e32 v31, v33, v30
	s_nop 1
	v_add_f32_dpp v30, v31, v31 quad_perm:[2,3,0,1] row_mask:0xf bank_mask:0xf bound_ctrl:1
	s_nop 1
	v_add_f32_dpp v30, v30, v30 row_half_mirror row_mask:0xf bank_mask:0xf bound_ctrl:1
	ds_write_b32 v32, v30 offset:49212
	v_add_u32_e32 v31, v238, v35
	v_add_u32_e32 v30, v238, v34
	buffer_load_dwordx4 v[156:159], v31, s[44:47], 0 offen
	buffer_load_dwordx4 v[162:165], v31, s[44:47], s20 offen
	buffer_load_dwordx4 v[168:171], v31, s[44:47], s21 offen
	buffer_load_dwordx4 v[174:177], v31, s[44:47], s23 offen
	buffer_load_dwordx2 v[160:161], v30, s[44:47], 0 offen
	buffer_load_dwordx2 v[172:173], v30, s[44:47], s33 offen
	buffer_load_dwordx2 v[166:167], v30, s[44:47], s21 offen
	buffer_load_dwordx2 v[178:179], v30, s[44:47], s94 offen
	s_waitcnt vmcnt(24)
	v_mfma_f32_16x16x128_f8f6f4 v[24:27], v[24:29], v[18:23], 0 cbsz:2 blgp:2
	v_mfma_f32_16x16x128_f8f6f4 v[24:27], v[44:49], v[12:17], v[24:27] cbsz:2 blgp:2
	v_mfma_f32_16x16x128_f8f6f4 v[24:27], v[38:43], v[6:11], v[24:27] cbsz:2 blgp:2
	v_mfma_f32_16x16x128_f8f6f4 v[24:27], v[50:55], v[0:5], v[24:27] cbsz:2 blgp:2
	s_nop 7
	v_cndmask_b32_e64 v24, v24, v25, s[4:5]
	v_cndmask_b32_e64 v24, v24, v26, s[2:3]
	v_cndmask_b32_e32 v24, v24, v27, vcc
	v_mul_f32_e32 v25, v33, v24
	s_nop 1
	v_mov_b32_dpp v25, v25 quad_perm:[1,0,3,2] row_mask:0xf bank_mask:0xf bound_ctrl:1
	v_fmac_f32_e32 v25, v33, v24
	s_nop 1
	v_add_f32_dpp v24, v25, v25 quad_perm:[2,3,0,1] row_mask:0xf bank_mask:0xf bound_ctrl:1
	s_nop 1
	v_add_f32_dpp v24, v24, v24 row_half_mirror row_mask:0xf bank_mask:0xf bound_ctrl:1
	ds_write_b32 v32, v24 offset:49216
	v_add_u32_e32 v28, v239, v35
	v_add_u32_e32 v30, v239, v34
	buffer_load_dwordx4 v[24:27], v28, s[44:47], 0 offen
	buffer_load_dwordx4 v[38:41], v28, s[44:47], s20 offen
	buffer_load_dwordx4 v[44:47], v28, s[44:47], s21 offen
	buffer_load_dwordx4 v[50:53], v28, s[44:47], s23 offen
	s_nop 0
	buffer_load_dwordx2 v[28:29], v30, s[44:47], 0 offen
	buffer_load_dwordx2 v[48:49], v30, s[44:47], s33 offen
	buffer_load_dwordx2 v[42:43], v30, s[44:47], s21 offen
	buffer_load_dwordx2 v[54:55], v30, s[44:47], s94 offen
	s_waitcnt vmcnt(24)
	v_mfma_f32_16x16x128_f8f6f4 v[56:59], v[56:61], v[18:23], 0 cbsz:2 blgp:2
	v_mfma_f32_16x16x128_f8f6f4 v[56:59], v[68:73], v[12:17], v[56:59] cbsz:2 blgp:2
	v_mfma_f32_16x16x128_f8f6f4 v[56:59], v[62:67], v[6:11], v[56:59] cbsz:2 blgp:2
	v_mfma_f32_16x16x128_f8f6f4 v[56:59], v[74:79], v[0:5], v[56:59] cbsz:2 blgp:2
	s_nop 7
	v_cndmask_b32_e64 v30, v56, v57, s[4:5]
	v_cndmask_b32_e64 v30, v30, v58, s[2:3]
	v_cndmask_b32_e32 v30, v30, v59, vcc
	v_mul_f32_e32 v31, v33, v30
	s_nop 1
	v_mov_b32_dpp v31, v31 quad_perm:[1,0,3,2] row_mask:0xf bank_mask:0xf bound_ctrl:1
	v_fmac_f32_e32 v31, v33, v30
	s_nop 1
	v_add_f32_dpp v30, v31, v31 quad_perm:[2,3,0,1] row_mask:0xf bank_mask:0xf bound_ctrl:1
	s_nop 1
	v_add_f32_dpp v30, v30, v30 row_half_mirror row_mask:0xf bank_mask:0xf bound_ctrl:1
	ds_write_b32 v32, v30 offset:49220
	v_add_u32_e32 v31, v240, v35
	v_add_u32_e32 v30, v240, v34
	buffer_load_dwordx4 v[56:59], v31, s[44:47], 0 offen
	buffer_load_dwordx4 v[62:65], v31, s[44:47], s20 offen
	buffer_load_dwordx4 v[68:71], v31, s[44:47], s21 offen
	buffer_load_dwordx4 v[74:77], v31, s[44:47], s23 offen
	buffer_load_dwordx2 v[60:61], v30, s[44:47], 0 offen
	buffer_load_dwordx2 v[72:73], v30, s[44:47], s33 offen
	buffer_load_dwordx2 v[66:67], v30, s[44:47], s21 offen
	buffer_load_dwordx2 v[78:79], v30, s[44:47], s94 offen
	s_waitcnt vmcnt(24)
	v_mfma_f32_16x16x128_f8f6f4 v[86:89], v[86:91], v[18:23], 0 cbsz:2 blgp:2
	v_mfma_f32_16x16x128_f8f6f4 v[86:89], v[98:103], v[12:17], v[86:89] cbsz:2 blgp:2
	v_mfma_f32_16x16x128_f8f6f4 v[86:89], v[92:97], v[6:11], v[86:89] cbsz:2 blgp:2
	v_mfma_f32_16x16x128_f8f6f4 v[86:89], v[150:155], v[0:5], v[86:89] cbsz:2 blgp:2
	s_nop 7
	v_cndmask_b32_e64 v30, v86, v87, s[4:5]
	v_cndmask_b32_e64 v30, v30, v88, s[2:3]
	v_cndmask_b32_e32 v30, v30, v89, vcc
	v_mul_f32_e32 v31, v33, v30
	s_nop 1
	v_mov_b32_dpp v31, v31 quad_perm:[1,0,3,2] row_mask:0xf bank_mask:0xf bound_ctrl:1
	v_fmac_f32_e32 v31, v33, v30
	s_nop 1
	v_add_f32_dpp v30, v31, v31 quad_perm:[2,3,0,1] row_mask:0xf bank_mask:0xf bound_ctrl:1
	s_nop 1
	v_add_f32_dpp v30, v30, v30 row_half_mirror row_mask:0xf bank_mask:0xf bound_ctrl:1
	ds_write_b32 v32, v30 offset:49224
	v_add_u32_e32 v31, v241, v35
	v_add_u32_e32 v30, v241, v34
	buffer_load_dwordx4 v[86:89], v31, s[44:47], 0 offen
	buffer_load_dwordx4 v[92:95], v31, s[44:47], s20 offen
	buffer_load_dwordx4 v[98:101], v31, s[44:47], s21 offen
	buffer_load_dwordx4 v[150:153], v31, s[44:47], s23 offen
	buffer_load_dwordx2 v[90:91], v30, s[44:47], 0 offen
	buffer_load_dwordx2 v[102:103], v30, s[44:47], s33 offen
	buffer_load_dwordx2 v[96:97], v30, s[44:47], s21 offen
	buffer_load_dwordx2 v[154:155], v30, s[44:47], s94 offen
	s_waitcnt vmcnt(24)
	v_mfma_f32_16x16x128_f8f6f4 v[156:159], v[156:161], v[18:23], 0 cbsz:2 blgp:2
	v_mfma_f32_16x16x128_f8f6f4 v[156:159], v[168:173], v[12:17], v[156:159] cbsz:2 blgp:2
	v_mfma_f32_16x16x128_f8f6f4 v[156:159], v[162:167], v[6:11], v[156:159] cbsz:2 blgp:2
	v_mfma_f32_16x16x128_f8f6f4 v[156:159], v[174:179], v[0:5], v[156:159] cbsz:2 blgp:2
	s_nop 7
	v_cndmask_b32_e64 v30, v156, v157, s[4:5]
	v_cndmask_b32_e64 v30, v30, v158, s[2:3]
	v_cndmask_b32_e32 v30, v30, v159, vcc
	v_mul_f32_e32 v31, v33, v30
	s_nop 1
	v_mov_b32_dpp v31, v31 quad_perm:[1,0,3,2] row_mask:0xf bank_mask:0xf bound_ctrl:1
	v_fmac_f32_e32 v31, v33, v30
	s_nop 1
	v_add_f32_dpp v30, v31, v31 quad_perm:[2,3,0,1] row_mask:0xf bank_mask:0xf bound_ctrl:1
	s_nop 1
	v_add_f32_dpp v30, v30, v30 row_half_mirror row_mask:0xf bank_mask:0xf bound_ctrl:1
	ds_write_b32 v32, v30 offset:49228
	v_add_u32_e32 v31, v242, v35
	v_add_u32_e32 v30, v242, v34
	buffer_load_dwordx4 v[156:159], v31, s[44:47], 0 offen
	buffer_load_dwordx4 v[162:165], v31, s[44:47], s20 offen
	buffer_load_dwordx4 v[168:171], v31, s[44:47], s21 offen
	buffer_load_dwordx4 v[174:177], v31, s[44:47], s23 offen
	buffer_load_dwordx2 v[160:161], v30, s[44:47], 0 offen
	buffer_load_dwordx2 v[172:173], v30, s[44:47], s33 offen
	buffer_load_dwordx2 v[166:167], v30, s[44:47], s21 offen
	buffer_load_dwordx2 v[178:179], v30, s[44:47], s94 offen
	s_waitcnt vmcnt(24)
	v_mfma_f32_16x16x128_f8f6f4 v[24:27], v[24:29], v[18:23], 0 cbsz:2 blgp:2
	v_mfma_f32_16x16x128_f8f6f4 v[24:27], v[44:49], v[12:17], v[24:27] cbsz:2 blgp:2
	v_mfma_f32_16x16x128_f8f6f4 v[24:27], v[38:43], v[6:11], v[24:27] cbsz:2 blgp:2
	v_mfma_f32_16x16x128_f8f6f4 v[24:27], v[50:55], v[0:5], v[24:27] cbsz:2 blgp:2
	s_nop 7
	v_cndmask_b32_e64 v24, v24, v25, s[4:5]
	v_cndmask_b32_e64 v24, v24, v26, s[2:3]
	v_cndmask_b32_e32 v24, v24, v27, vcc
	v_mul_f32_e32 v25, v33, v24
	s_nop 1
	v_mov_b32_dpp v25, v25 quad_perm:[1,0,3,2] row_mask:0xf bank_mask:0xf bound_ctrl:1
	v_fmac_f32_e32 v25, v33, v24
	s_nop 1
	v_add_f32_dpp v24, v25, v25 quad_perm:[2,3,0,1] row_mask:0xf bank_mask:0xf bound_ctrl:1
	s_nop 1
	v_add_f32_dpp v24, v24, v24 row_half_mirror row_mask:0xf bank_mask:0xf bound_ctrl:1
	ds_write_b32 v32, v24 offset:49232
	v_add_u32_e32 v28, v243, v35
	v_add_u32_e32 v30, v243, v34
	buffer_load_dwordx4 v[24:27], v28, s[44:47], 0 offen
	buffer_load_dwordx4 v[38:41], v28, s[44:47], s20 offen
	buffer_load_dwordx4 v[44:47], v28, s[44:47], s21 offen
	buffer_load_dwordx4 v[50:53], v28, s[44:47], s23 offen
	s_nop 0
	buffer_load_dwordx2 v[28:29], v30, s[44:47], 0 offen
	buffer_load_dwordx2 v[48:49], v30, s[44:47], s33 offen
	buffer_load_dwordx2 v[42:43], v30, s[44:47], s21 offen
	buffer_load_dwordx2 v[54:55], v30, s[44:47], s94 offen
	s_waitcnt vmcnt(24)
	v_mfma_f32_16x16x128_f8f6f4 v[56:59], v[56:61], v[18:23], 0 cbsz:2 blgp:2
	v_mfma_f32_16x16x128_f8f6f4 v[56:59], v[68:73], v[12:17], v[56:59] cbsz:2 blgp:2
	v_mfma_f32_16x16x128_f8f6f4 v[56:59], v[62:67], v[6:11], v[56:59] cbsz:2 blgp:2
	v_mfma_f32_16x16x128_f8f6f4 v[56:59], v[74:79], v[0:5], v[56:59] cbsz:2 blgp:2
	s_nop 7
	v_cndmask_b32_e64 v30, v56, v57, s[4:5]
	v_cndmask_b32_e64 v30, v30, v58, s[2:3]
	v_cndmask_b32_e32 v30, v30, v59, vcc
	v_mul_f32_e32 v31, v33, v30
	s_nop 1
	v_mov_b32_dpp v31, v31 quad_perm:[1,0,3,2] row_mask:0xf bank_mask:0xf bound_ctrl:1
	v_fmac_f32_e32 v31, v33, v30
	s_nop 1
	v_add_f32_dpp v30, v31, v31 quad_perm:[2,3,0,1] row_mask:0xf bank_mask:0xf bound_ctrl:1
	s_nop 1
	v_add_f32_dpp v30, v30, v30 row_half_mirror row_mask:0xf bank_mask:0xf bound_ctrl:1
	ds_write_b32 v32, v30 offset:49236
	v_add_u32_e32 v31, v244, v35
	v_add_u32_e32 v30, v244, v34
	buffer_load_dwordx4 v[56:59], v31, s[44:47], 0 offen
	buffer_load_dwordx4 v[62:65], v31, s[44:47], s20 offen
	buffer_load_dwordx4 v[68:71], v31, s[44:47], s21 offen
	buffer_load_dwordx4 v[74:77], v31, s[44:47], s23 offen
	buffer_load_dwordx2 v[60:61], v30, s[44:47], 0 offen
	buffer_load_dwordx2 v[72:73], v30, s[44:47], s33 offen
	buffer_load_dwordx2 v[66:67], v30, s[44:47], s21 offen
	buffer_load_dwordx2 v[78:79], v30, s[44:47], s94 offen
	s_waitcnt vmcnt(24)
	v_mfma_f32_16x16x128_f8f6f4 v[86:89], v[86:91], v[18:23], 0 cbsz:2 blgp:2
	v_mfma_f32_16x16x128_f8f6f4 v[86:89], v[98:103], v[12:17], v[86:89] cbsz:2 blgp:2
	v_mfma_f32_16x16x128_f8f6f4 v[86:89], v[92:97], v[6:11], v[86:89] cbsz:2 blgp:2
	v_mfma_f32_16x16x128_f8f6f4 v[86:89], v[150:155], v[0:5], v[86:89] cbsz:2 blgp:2
	s_nop 7
	v_cndmask_b32_e64 v30, v86, v87, s[4:5]
	v_cndmask_b32_e64 v30, v30, v88, s[2:3]
	v_cndmask_b32_e32 v30, v30, v89, vcc
	v_mul_f32_e32 v31, v33, v30
	s_nop 1
	v_mov_b32_dpp v31, v31 quad_perm:[1,0,3,2] row_mask:0xf bank_mask:0xf bound_ctrl:1
	v_fmac_f32_e32 v31, v33, v30
	s_nop 1
	v_add_f32_dpp v30, v31, v31 quad_perm:[2,3,0,1] row_mask:0xf bank_mask:0xf bound_ctrl:1
	s_nop 1
	v_add_f32_dpp v30, v30, v30 row_half_mirror row_mask:0xf bank_mask:0xf bound_ctrl:1
	ds_write_b32 v32, v30 offset:49240
	v_add_u32_e32 v31, v245, v35
	v_add_u32_e32 v30, v245, v34
	buffer_load_dwordx4 v[86:89], v31, s[44:47], 0 offen
	buffer_load_dwordx4 v[92:95], v31, s[44:47], s20 offen
	buffer_load_dwordx4 v[98:101], v31, s[44:47], s21 offen
	buffer_load_dwordx4 v[150:153], v31, s[44:47], s23 offen
	buffer_load_dwordx2 v[90:91], v30, s[44:47], 0 offen
	buffer_load_dwordx2 v[102:103], v30, s[44:47], s33 offen
	buffer_load_dwordx2 v[96:97], v30, s[44:47], s21 offen
	buffer_load_dwordx2 v[154:155], v30, s[44:47], s94 offen
	s_waitcnt vmcnt(24)
	v_mfma_f32_16x16x128_f8f6f4 v[156:159], v[156:161], v[18:23], 0 cbsz:2 blgp:2
	v_mfma_f32_16x16x128_f8f6f4 v[156:159], v[168:173], v[12:17], v[156:159] cbsz:2 blgp:2
	v_mfma_f32_16x16x128_f8f6f4 v[156:159], v[162:167], v[6:11], v[156:159] cbsz:2 blgp:2
	v_mfma_f32_16x16x128_f8f6f4 v[156:159], v[174:179], v[0:5], v[156:159] cbsz:2 blgp:2
	s_nop 7
	v_cndmask_b32_e64 v30, v156, v157, s[4:5]
	v_cndmask_b32_e64 v30, v30, v158, s[2:3]
	v_cndmask_b32_e32 v30, v30, v159, vcc
	v_mul_f32_e32 v31, v33, v30
	s_nop 1
	v_mov_b32_dpp v31, v31 quad_perm:[1,0,3,2] row_mask:0xf bank_mask:0xf bound_ctrl:1
	v_fmac_f32_e32 v31, v33, v30
	s_nop 1
	v_add_f32_dpp v30, v31, v31 quad_perm:[2,3,0,1] row_mask:0xf bank_mask:0xf bound_ctrl:1
	s_nop 1
	v_add_f32_dpp v30, v30, v30 row_half_mirror row_mask:0xf bank_mask:0xf bound_ctrl:1
	ds_write_b32 v32, v30 offset:49244
	v_add_u32_e32 v31, v246, v35
	v_add_u32_e32 v30, v246, v34
	buffer_load_dwordx4 v[156:159], v31, s[44:47], 0 offen
	buffer_load_dwordx4 v[162:165], v31, s[44:47], s20 offen
	buffer_load_dwordx4 v[168:171], v31, s[44:47], s21 offen
	buffer_load_dwordx4 v[174:177], v31, s[44:47], s23 offen
	buffer_load_dwordx2 v[160:161], v30, s[44:47], 0 offen
	buffer_load_dwordx2 v[172:173], v30, s[44:47], s33 offen
	buffer_load_dwordx2 v[166:167], v30, s[44:47], s21 offen
	buffer_load_dwordx2 v[178:179], v30, s[44:47], s94 offen
	s_waitcnt vmcnt(24)
	v_mfma_f32_16x16x128_f8f6f4 v[24:27], v[24:29], v[18:23], 0 cbsz:2 blgp:2
	v_mfma_f32_16x16x128_f8f6f4 v[24:27], v[44:49], v[12:17], v[24:27] cbsz:2 blgp:2
	v_mfma_f32_16x16x128_f8f6f4 v[24:27], v[38:43], v[6:11], v[24:27] cbsz:2 blgp:2
	v_mfma_f32_16x16x128_f8f6f4 v[24:27], v[50:55], v[0:5], v[24:27] cbsz:2 blgp:2
	s_nop 7
	v_cndmask_b32_e64 v24, v24, v25, s[4:5]
	v_cndmask_b32_e64 v24, v24, v26, s[2:3]
	v_cndmask_b32_e32 v24, v24, v27, vcc
	v_mul_f32_e32 v25, v33, v24
	s_nop 1
	v_mov_b32_dpp v25, v25 quad_perm:[1,0,3,2] row_mask:0xf bank_mask:0xf bound_ctrl:1
	v_fmac_f32_e32 v25, v33, v24
	s_nop 1
	v_add_f32_dpp v24, v25, v25 quad_perm:[2,3,0,1] row_mask:0xf bank_mask:0xf bound_ctrl:1
	s_nop 1
	v_add_f32_dpp v24, v24, v24 row_half_mirror row_mask:0xf bank_mask:0xf bound_ctrl:1
	ds_write_b32 v32, v24 offset:49248
	v_add_u32_e32 v28, v247, v35
	v_add_u32_e32 v30, v247, v34
	buffer_load_dwordx4 v[24:27], v28, s[44:47], 0 offen
	buffer_load_dwordx4 v[38:41], v28, s[44:47], s20 offen
	buffer_load_dwordx4 v[44:47], v28, s[44:47], s21 offen
	buffer_load_dwordx4 v[50:53], v28, s[44:47], s23 offen
	s_nop 0
	buffer_load_dwordx2 v[28:29], v30, s[44:47], 0 offen
	buffer_load_dwordx2 v[48:49], v30, s[44:47], s33 offen
	buffer_load_dwordx2 v[42:43], v30, s[44:47], s21 offen
	buffer_load_dwordx2 v[54:55], v30, s[44:47], s94 offen
	s_waitcnt vmcnt(24)
	v_mfma_f32_16x16x128_f8f6f4 v[56:59], v[56:61], v[18:23], 0 cbsz:2 blgp:2
	v_mfma_f32_16x16x128_f8f6f4 v[56:59], v[68:73], v[12:17], v[56:59] cbsz:2 blgp:2
	v_mfma_f32_16x16x128_f8f6f4 v[56:59], v[62:67], v[6:11], v[56:59] cbsz:2 blgp:2
	v_mfma_f32_16x16x128_f8f6f4 v[56:59], v[74:79], v[0:5], v[56:59] cbsz:2 blgp:2
	s_nop 7
	v_cndmask_b32_e64 v30, v56, v57, s[4:5]
	v_cndmask_b32_e64 v30, v30, v58, s[2:3]
	v_cndmask_b32_e32 v30, v30, v59, vcc
	v_mul_f32_e32 v31, v33, v30
	s_nop 1
	v_mov_b32_dpp v31, v31 quad_perm:[1,0,3,2] row_mask:0xf bank_mask:0xf bound_ctrl:1
	v_fmac_f32_e32 v31, v33, v30
	s_nop 1
	v_add_f32_dpp v30, v31, v31 quad_perm:[2,3,0,1] row_mask:0xf bank_mask:0xf bound_ctrl:1
	s_nop 1
	v_add_f32_dpp v30, v30, v30 row_half_mirror row_mask:0xf bank_mask:0xf bound_ctrl:1
	ds_write_b32 v32, v30 offset:49252
	v_add_u32_e32 v31, v248, v35
	v_add_u32_e32 v30, v248, v34
	buffer_load_dwordx4 v[56:59], v31, s[44:47], 0 offen
	buffer_load_dwordx4 v[62:65], v31, s[44:47], s20 offen
	buffer_load_dwordx4 v[68:71], v31, s[44:47], s21 offen
	buffer_load_dwordx4 v[74:77], v31, s[44:47], s23 offen
	buffer_load_dwordx2 v[60:61], v30, s[44:47], 0 offen
	buffer_load_dwordx2 v[72:73], v30, s[44:47], s33 offen
	buffer_load_dwordx2 v[66:67], v30, s[44:47], s21 offen
	buffer_load_dwordx2 v[78:79], v30, s[44:47], s94 offen
	s_waitcnt vmcnt(24)
	v_mfma_f32_16x16x128_f8f6f4 v[86:89], v[86:91], v[18:23], 0 cbsz:2 blgp:2
	v_mfma_f32_16x16x128_f8f6f4 v[86:89], v[98:103], v[12:17], v[86:89] cbsz:2 blgp:2
	v_mfma_f32_16x16x128_f8f6f4 v[86:89], v[92:97], v[6:11], v[86:89] cbsz:2 blgp:2
	v_mfma_f32_16x16x128_f8f6f4 v[86:89], v[150:155], v[0:5], v[86:89] cbsz:2 blgp:2
	s_nop 7
	v_cndmask_b32_e64 v30, v86, v87, s[4:5]
	v_cndmask_b32_e64 v30, v30, v88, s[2:3]
	v_cndmask_b32_e32 v30, v30, v89, vcc
	v_mul_f32_e32 v31, v33, v30
	s_nop 1
	v_mov_b32_dpp v31, v31 quad_perm:[1,0,3,2] row_mask:0xf bank_mask:0xf bound_ctrl:1
	v_fmac_f32_e32 v31, v33, v30
	s_nop 1
	v_add_f32_dpp v30, v31, v31 quad_perm:[2,3,0,1] row_mask:0xf bank_mask:0xf bound_ctrl:1
	s_nop 1
	v_add_f32_dpp v30, v30, v30 row_half_mirror row_mask:0xf bank_mask:0xf bound_ctrl:1
	ds_write_b32 v32, v30 offset:49256
	v_add_u32_e32 v31, v249, v35
	v_add_u32_e32 v30, v249, v34
	buffer_load_dwordx4 v[86:89], v31, s[44:47], 0 offen
	buffer_load_dwordx4 v[92:95], v31, s[44:47], s20 offen
	buffer_load_dwordx4 v[98:101], v31, s[44:47], s21 offen
	buffer_load_dwordx4 v[150:153], v31, s[44:47], s23 offen
	buffer_load_dwordx2 v[90:91], v30, s[44:47], 0 offen
	buffer_load_dwordx2 v[102:103], v30, s[44:47], s33 offen
	buffer_load_dwordx2 v[96:97], v30, s[44:47], s21 offen
	buffer_load_dwordx2 v[154:155], v30, s[44:47], s94 offen
	s_waitcnt vmcnt(24)
	v_mfma_f32_16x16x128_f8f6f4 v[156:159], v[156:161], v[18:23], 0 cbsz:2 blgp:2
	v_mfma_f32_16x16x128_f8f6f4 v[156:159], v[168:173], v[12:17], v[156:159] cbsz:2 blgp:2
	v_mfma_f32_16x16x128_f8f6f4 v[156:159], v[162:167], v[6:11], v[156:159] cbsz:2 blgp:2
	v_mfma_f32_16x16x128_f8f6f4 v[156:159], v[174:179], v[0:5], v[156:159] cbsz:2 blgp:2
	s_nop 7
	v_cndmask_b32_e64 v30, v156, v157, s[4:5]
	v_cndmask_b32_e64 v30, v30, v158, s[2:3]
	v_cndmask_b32_e32 v30, v30, v159, vcc
	v_mul_f32_e32 v31, v33, v30
	s_nop 1
	v_mov_b32_dpp v31, v31 quad_perm:[1,0,3,2] row_mask:0xf bank_mask:0xf bound_ctrl:1
	v_fmac_f32_e32 v31, v33, v30
	s_nop 1
	v_add_f32_dpp v30, v31, v31 quad_perm:[2,3,0,1] row_mask:0xf bank_mask:0xf bound_ctrl:1
	s_nop 1
	v_add_f32_dpp v30, v30, v30 row_half_mirror row_mask:0xf bank_mask:0xf bound_ctrl:1
	ds_write_b32 v32, v30 offset:49260
	ds_bpermute_b32 v30, v36, v251 offset:240
	s_waitcnt lgkmcnt(0)
	v_add_u32_e32 v31, v30, v35
	v_add_u32_e32 v30, v30, v34
	buffer_load_dwordx4 v[156:159], v31, s[44:47], 0 offen
	buffer_load_dwordx4 v[162:165], v31, s[44:47], s20 offen
	buffer_load_dwordx4 v[168:171], v31, s[44:47], s21 offen
	buffer_load_dwordx4 v[174:177], v31, s[44:47], s23 offen
	buffer_load_dwordx2 v[160:161], v30, s[44:47], 0 offen
	buffer_load_dwordx2 v[172:173], v30, s[44:47], s33 offen
	buffer_load_dwordx2 v[166:167], v30, s[44:47], s21 offen
	buffer_load_dwordx2 v[178:179], v30, s[44:47], s94 offen
	s_waitcnt vmcnt(24)
	v_mfma_f32_16x16x128_f8f6f4 v[24:27], v[24:29], v[18:23], 0 cbsz:2 blgp:2
	v_mfma_f32_16x16x128_f8f6f4 v[24:27], v[44:49], v[12:17], v[24:27] cbsz:2 blgp:2
	v_mfma_f32_16x16x128_f8f6f4 v[24:27], v[38:43], v[6:11], v[24:27] cbsz:2 blgp:2
	v_mfma_f32_16x16x128_f8f6f4 v[24:27], v[50:55], v[0:5], v[24:27] cbsz:2 blgp:2
	s_nop 7
	v_cndmask_b32_e64 v24, v24, v25, s[4:5]
	v_cndmask_b32_e64 v24, v24, v26, s[2:3]
	v_cndmask_b32_e32 v24, v24, v27, vcc
	v_mul_f32_e32 v25, v33, v24
	s_nop 1
	v_mov_b32_dpp v25, v25 quad_perm:[1,0,3,2] row_mask:0xf bank_mask:0xf bound_ctrl:1
	v_fmac_f32_e32 v25, v33, v24
	s_nop 1
	v_add_f32_dpp v24, v25, v25 quad_perm:[2,3,0,1] row_mask:0xf bank_mask:0xf bound_ctrl:1
	s_nop 1
	v_add_f32_dpp v24, v24, v24 row_half_mirror row_mask:0xf bank_mask:0xf bound_ctrl:1
	ds_write_b32 v32, v24 offset:49264
	s_waitcnt vmcnt(16)
	v_mfma_f32_16x16x128_f8f6f4 v[24:27], v[56:61], v[18:23], 0 cbsz:2 blgp:2
	v_mfma_f32_16x16x128_f8f6f4 v[24:27], v[68:73], v[12:17], v[24:27] cbsz:2 blgp:2
	v_mfma_f32_16x16x128_f8f6f4 v[24:27], v[62:67], v[6:11], v[24:27] cbsz:2 blgp:2
	v_mfma_f32_16x16x128_f8f6f4 v[24:27], v[74:79], v[0:5], v[24:27] cbsz:2 blgp:2
	s_nop 7
	v_cndmask_b32_e64 v24, v24, v25, s[4:5]
	v_cndmask_b32_e64 v24, v24, v26, s[2:3]
	v_cndmask_b32_e32 v24, v24, v27, vcc
	v_mul_f32_e32 v25, v33, v24
	s_nop 1
	v_mov_b32_dpp v25, v25 quad_perm:[1,0,3,2] row_mask:0xf bank_mask:0xf bound_ctrl:1
	v_fmac_f32_e32 v25, v33, v24
	s_nop 1
	v_add_f32_dpp v24, v25, v25 quad_perm:[2,3,0,1] row_mask:0xf bank_mask:0xf bound_ctrl:1
	s_nop 1
	v_add_f32_dpp v24, v24, v24 row_half_mirror row_mask:0xf bank_mask:0xf bound_ctrl:1
	ds_write_b32 v32, v24 offset:49268
	s_waitcnt vmcnt(8)
	v_mfma_f32_16x16x128_f8f6f4 v[24:27], v[86:91], v[18:23], 0 cbsz:2 blgp:2
	v_mfma_f32_16x16x128_f8f6f4 v[24:27], v[98:103], v[12:17], v[24:27] cbsz:2 blgp:2
	v_mfma_f32_16x16x128_f8f6f4 v[24:27], v[92:97], v[6:11], v[24:27] cbsz:2 blgp:2
	v_mfma_f32_16x16x128_f8f6f4 v[24:27], v[150:155], v[0:5], v[24:27] cbsz:2 blgp:2
	s_nop 7
	v_cndmask_b32_e64 v24, v24, v25, s[4:5]
	v_cndmask_b32_e64 v24, v24, v26, s[2:3]
	v_cndmask_b32_e32 v24, v24, v27, vcc
	v_mul_f32_e32 v25, v33, v24
	s_nop 1
	v_mov_b32_dpp v25, v25 quad_perm:[1,0,3,2] row_mask:0xf bank_mask:0xf bound_ctrl:1
	v_fmac_f32_e32 v25, v33, v24
	s_nop 1
	v_add_f32_dpp v24, v25, v25 quad_perm:[2,3,0,1] row_mask:0xf bank_mask:0xf bound_ctrl:1
	s_nop 1
	v_add_f32_dpp v24, v24, v24 row_half_mirror row_mask:0xf bank_mask:0xf bound_ctrl:1
	ds_write_b32 v32, v24 offset:49272
	s_waitcnt vmcnt(0)
	v_mfma_f32_16x16x128_f8f6f4 v[18:21], v[156:161], v[18:23], 0 cbsz:2 blgp:2
	v_mfma_f32_16x16x128_f8f6f4 v[12:15], v[168:173], v[12:17], v[18:21] cbsz:2 blgp:2
	v_mfma_f32_16x16x128_f8f6f4 v[6:9], v[162:167], v[6:11], v[12:15] cbsz:2 blgp:2
	v_mfma_f32_16x16x128_f8f6f4 v[0:3], v[174:179], v[0:5], v[6:9] cbsz:2 blgp:2
	s_nop 7
	v_cndmask_b32_e64 v0, v0, v1, s[4:5]
	v_cndmask_b32_e64 v0, v0, v2, s[2:3]
	v_cndmask_b32_e32 v0, v0, v3, vcc
	v_mul_f32_e32 v1, v33, v0
	s_nop 1
	v_mov_b32_dpp v1, v1 quad_perm:[1,0,3,2] row_mask:0xf bank_mask:0xf bound_ctrl:1
	v_fmac_f32_e32 v1, v33, v0
	s_nop 1
	v_add_f32_dpp v0, v1, v1 quad_perm:[2,3,0,1] row_mask:0xf bank_mask:0xf bound_ctrl:1
	s_nop 1
	v_add_f32_dpp v0, v0, v0 row_half_mirror row_mask:0xf bank_mask:0xf bound_ctrl:1
	ds_write_b32 v32, v0 offset:49276
	v_mul_u32_u24_e32 v240, 0x600, v130
	v_mul_u32_u24_e32 v241, 0x600, v128
	v_add_u32_e32 v240, 0x8000000, v240
	v_add_u32_e32 v241, 0x8000000, v241
	v_lshrrev_b32_e32 v0, 1, v129
	v_readlane_b32 s100, v240, 0
	v_readlane_b32 s101, v240, 1
	v_readlane_b32 s2, v240, 2
	v_readlane_b32 s3, v240, 3
	s_nop 1
	buffer_load_dwordx4 v[74:77], v129, s[44:47], s100 offen
	buffer_load_dwordx2 v[78:79], v0, s[44:47], s100 offen offset:1024
	buffer_load_dwordx4 v[68:71], v129, s[44:47], s101 offen
	buffer_load_dwordx2 v[72:73], v0, s[44:47], s101 offen offset:1024
	buffer_load_dwordx4 v[56:59], v129, s[44:47], s2 offen
	buffer_load_dwordx2 v[60:61], v0, s[44:47], s2 offen offset:1024
	buffer_load_dwordx4 v[44:47], v129, s[44:47], s3 offen
	buffer_load_dwordx2 v[48:49], v0, s[44:47], s3 offen offset:1024
	v_add_u32_e32 v210, 0x400, v0
	v_readlane_b32 s100, v240, 4
	v_readlane_b32 s101, v240, 5
	v_readlane_b32 s2, v240, 6
	v_readlane_b32 s3, v240, 7
	s_nop 1
	buffer_load_dwordx4 v[62:65], v129, s[44:47], s100 offen
	buffer_load_dwordx2 v[66:67], v0, s[44:47], s100 offen offset:1024
	buffer_load_dwordx4 v[50:53], v129, s[44:47], s101 offen
	buffer_load_dwordx2 v[54:55], v0, s[44:47], s101 offen offset:1024
	buffer_load_dwordx4 v[38:41], v129, s[44:47], s2 offen
	buffer_load_dwordx2 v[42:43], v0, s[44:47], s2 offen offset:1024
	buffer_load_dwordx4 v[32:35], v129, s[44:47], s3 offen
	buffer_load_dwordx2 v[36:37], v0, s[44:47], s3 offen offset:1024
	v_div_scale_f32 v2, s[2:3], v80, v80, 1.0
	v_rcp_f32_e32 v3, v2
	v_div_scale_f32 v4, vcc, 1.0, v80, 1.0
	v_and_b32_e32 v1, -4, v148
	v_fma_f32 v0, -v2, v3, 1.0
	v_fmac_f32_e32 v3, v0, v3
	v_mul_f32_e32 v5, v4, v3
	v_fma_f32 v0, -v2, v5, v4
	v_fmac_f32_e32 v5, v0, v3
	v_lshlrev_b32_e32 v0, 7, v148
	v_and_b32_e32 v0, 0x180, v0
	v_add3_u32 v0, v111, v0, v1
	v_add_u32_e32 v0, 0xc000, v0
	ds_read2_b32 v[0:1], v0 offset1:16
	v_fma_f32 v2, -v2, v5, v4
	v_div_fmas_f32 v2, v2, v3, v5
	v_div_fixup_f32 v2, v2, v80, 1.0
	s_mov_b32 s1, 0x3e6d3388
	s_waitcnt lgkmcnt(0)
	v_mul_f32_e32 v0, v2, v0
	v_mul_f32_e32 v0, v83, v0
	v_fma_f32 v3, |v0|, s1, 1.0
	v_rcp_f32_e32 v3, v3
	v_mul_f32_e32 v5, v0, v0
	v_mul_f32_e32 v5, 0xbf38aa3b, v5
	v_exp_f32_e32 v5, v5
	v_fmamk_f32 v4, v3, 0x3f07dc22, v184
	v_fmaak_f32 v4, v3, v4, 0x3f35f0e3
	v_fmaak_f32 v4, v3, v4, 0xbe11a98e
	v_mul_f32_e32 v1, v2, v1
	v_fmaak_f32 v4, v3, v4, 0x3e027906
	v_mul_f32_e32 v3, v3, v4
	v_mul_f32_e32 v1, v82, v1
	v_mul_f32_e32 v3, v5, v3
	v_fma_f32 v5, |v1|, s1, 1.0
	v_rcp_f32_e32 v5, v5
	v_mul_f32_e32 v4, v0, v3
	v_fma_f32 v3, -v0, v3, v0
	v_cmp_gt_f32_e32 vcc, 0, v0
	v_mul_f32_e32 v2, v206, v84
	v_mov_b32_e32 v180, 0
	v_cndmask_b32_e32 v0, v3, v4, vcc
	v_mul_f32_e32 v211, v2, v0
	v_mul_f32_e32 v2, v1, v1
	v_fmamk_f32 v0, v5, 0x3f07dc22, v184
	v_mul_f32_e32 v2, 0xbf38aa3b, v2
	v_fmaak_f32 v0, v5, v0, 0x3f35f0e3
	v_exp_f32_e32 v2, v2
	v_fmaak_f32 v0, v5, v0, 0xbe11a98e
	v_fmaak_f32 v0, v5, v0, 0x3e027906
	v_mul_f32_e32 v0, v5, v0
	v_mul_f32_e32 v0, v2, v0
	v_mul_f32_e32 v2, v1, v0
	v_fma_f32 v0, -v1, v0, v1
	v_cmp_gt_f32_e32 vcc, 0, v1
	v_mul_f32_e32 v1, v205, v81
	v_mov_b32_e32 v181, v180
	v_cndmask_b32_e32 v0, v0, v2, vcc
	v_mul_f32_e32 v131, v1, v0
	v_mov_b32_e32 v178, v180
	v_mov_b32_e32 v179, v180
	v_mov_b32_e32 v176, v180
	v_mov_b32_e32 v177, v180
	v_mov_b32_e32 v174, v180
	v_mov_b32_e32 v175, v180
	v_mov_b32_e32 v172, v180
	v_mov_b32_e32 v173, v180
	v_mov_b32_e32 v170, v180
	v_mov_b32_e32 v171, v180
	v_mov_b32_e32 v168, v180
	v_mov_b32_e32 v169, v180
	v_mov_b32_e32 v166, v180
	v_mov_b32_e32 v167, v180
	v_mov_b32_e32 v164, v180
	v_mov_b32_e32 v165, v180
	v_mov_b32_e32 v162, v180
	v_mov_b32_e32 v163, v180
	v_mov_b32_e32 v160, v180
	v_mov_b32_e32 v161, v180
	v_mov_b32_e32 v158, v180
	v_mov_b32_e32 v159, v180
	v_mov_b32_e32 v156, v180
	v_mov_b32_e32 v157, v180
	v_mov_b32_e32 v154, v180
	v_mov_b32_e32 v155, v180
	v_mov_b32_e32 v152, v180
	v_mov_b32_e32 v153, v180
	v_mov_b32_e32 v150, v180
	v_mov_b32_e32 v151, v180
	v_readlane_b32 s2, v240, 8
	v_readlane_b32 s3, v240, 9
	v_readlane_b32 s100, v240, 10
	v_readlane_b32 s101, v240, 11
	s_nop 1
	buffer_load_dwordx4 v[98:101], v129, s[44:47], s2 offen
	buffer_load_dwordx2 v[102:103], v210, s[44:47], s2 offen
	buffer_load_dwordx4 v[92:95], v129, s[44:47], s3 offen
	buffer_load_dwordx2 v[96:97], v210, s[44:47], s3 offen
	buffer_load_dwordx4 v[86:89], v129, s[44:47], s100 offen
	buffer_load_dwordx2 v[90:91], v210, s[44:47], s100 offen
	buffer_load_dwordx4 v[80:83], v129, s[44:47], s101 offen
	buffer_load_dwordx2 v[84:85], v210, s[44:47], s101 offen
	v_readlane_b32 s2, v211, 0
	s_waitcnt vmcnt(22)
	v_cvt_scalef32_pk32_f32_fp6 v[0:31], v[74:79], 1.0
	v_pk_fma_f32 v[74:75], v[0:1], s[2:3], v[180:181] op_sel_hi:[1,0,1]
	v_pk_fma_f32 v[76:77], v[2:3], s[2:3], v[178:179] op_sel_hi:[1,0,1]
	v_pk_fma_f32 v[78:79], v[4:5], s[2:3], v[176:177] op_sel_hi:[1,0,1]
	v_pk_fma_f32 v[174:175], v[6:7], s[2:3], v[174:175] op_sel_hi:[1,0,1]
	v_pk_fma_f32 v[172:173], v[8:9], s[2:3], v[172:173] op_sel_hi:[1,0,1]
	v_pk_fma_f32 v[170:171], v[10:11], s[2:3], v[170:171] op_sel_hi:[1,0,1]
	v_pk_fma_f32 v[168:169], v[12:13], s[2:3], v[168:169] op_sel_hi:[1,0,1]
	v_pk_fma_f32 v[166:167], v[14:15], s[2:3], v[166:167] op_sel_hi:[1,0,1]
	v_pk_fma_f32 v[164:165], v[16:17], s[2:3], v[164:165] op_sel_hi:[1,0,1]
	v_pk_fma_f32 v[162:163], v[18:19], s[2:3], v[162:163] op_sel_hi:[1,0,1]
	v_pk_fma_f32 v[160:161], v[20:21], s[2:3], v[160:161] op_sel_hi:[1,0,1]
	v_pk_fma_f32 v[158:159], v[22:23], s[2:3], v[158:159] op_sel_hi:[1,0,1]
	v_pk_fma_f32 v[156:157], v[24:25], s[2:3], v[156:157] op_sel_hi:[1,0,1]
	v_pk_fma_f32 v[154:155], v[26:27], s[2:3], v[154:155] op_sel_hi:[1,0,1]
	v_pk_fma_f32 v[152:153], v[28:29], s[2:3], v[152:153] op_sel_hi:[1,0,1]
	v_pk_fma_f32 v[150:151], v[30:31], s[2:3], v[150:151] op_sel_hi:[1,0,1]
	v_readlane_b32 s2, v211, 1
	s_waitcnt vmcnt(20)
	v_cvt_scalef32_pk32_f32_fp6 v[0:31], v[68:73], 1.0
	v_pk_fma_f32 v[68:69], v[0:1], s[2:3], v[74:75] op_sel_hi:[1,0,1]
	v_pk_fma_f32 v[70:71], v[2:3], s[2:3], v[76:77] op_sel_hi:[1,0,1]
	v_pk_fma_f32 v[72:73], v[4:5], s[2:3], v[78:79] op_sel_hi:[1,0,1]
	v_pk_fma_f32 v[74:75], v[6:7], s[2:3], v[174:175] op_sel_hi:[1,0,1]
	v_pk_fma_f32 v[76:77], v[8:9], s[2:3], v[172:173] op_sel_hi:[1,0,1]
	v_pk_fma_f32 v[78:79], v[10:11], s[2:3], v[170:171] op_sel_hi:[1,0,1]
	v_pk_fma_f32 v[168:169], v[12:13], s[2:3], v[168:169] op_sel_hi:[1,0,1]
	v_pk_fma_f32 v[166:167], v[14:15], s[2:3], v[166:167] op_sel_hi:[1,0,1]
	v_pk_fma_f32 v[164:165], v[16:17], s[2:3], v[164:165] op_sel_hi:[1,0,1]
	v_pk_fma_f32 v[162:163], v[18:19], s[2:3], v[162:163] op_sel_hi:[1,0,1]
	v_pk_fma_f32 v[160:161], v[20:21], s[2:3], v[160:161] op_sel_hi:[1,0,1]
	v_pk_fma_f32 v[158:159], v[22:23], s[2:3], v[158:159] op_sel_hi:[1,0,1]
	v_pk_fma_f32 v[156:157], v[24:25], s[2:3], v[156:157] op_sel_hi:[1,0,1]
	v_pk_fma_f32 v[154:155], v[26:27], s[2:3], v[154:155] op_sel_hi:[1,0,1]
	v_pk_fma_f32 v[152:153], v[28:29], s[2:3], v[152:153] op_sel_hi:[1,0,1]
	v_pk_fma_f32 v[150:151], v[30:31], s[2:3], v[150:151] op_sel_hi:[1,0,1]
	v_readlane_b32 s2, v211, 2
	s_waitcnt vmcnt(18)
	v_cvt_scalef32_pk32_f32_fp6 v[0:31], v[56:61], 1.0
	v_pk_fma_f32 v[56:57], v[0:1], s[2:3], v[68:69] op_sel_hi:[1,0,1]
	v_pk_fma_f32 v[58:59], v[2:3], s[2:3], v[70:71] op_sel_hi:[1,0,1]
	v_pk_fma_f32 v[60:61], v[4:5], s[2:3], v[72:73] op_sel_hi:[1,0,1]
	v_pk_fma_f32 v[68:69], v[6:7], s[2:3], v[74:75] op_sel_hi:[1,0,1]
	v_pk_fma_f32 v[70:71], v[8:9], s[2:3], v[76:77] op_sel_hi:[1,0,1]
	v_pk_fma_f32 v[72:73], v[10:11], s[2:3], v[78:79] op_sel_hi:[1,0,1]
	v_pk_fma_f32 v[74:75], v[12:13], s[2:3], v[168:169] op_sel_hi:[1,0,1]
	v_pk_fma_f32 v[76:77], v[14:15], s[2:3], v[166:167] op_sel_hi:[1,0,1]
	v_pk_fma_f32 v[78:79], v[16:17], s[2:3], v[164:165] op_sel_hi:[1,0,1]
	v_pk_fma_f32 v[162:163], v[18:19], s[2:3], v[162:163] op_sel_hi:[1,0,1]
	v_pk_fma_f32 v[160:161], v[20:21], s[2:3], v[160:161] op_sel_hi:[1,0,1]
	v_pk_fma_f32 v[158:159], v[22:23], s[2:3], v[158:159] op_sel_hi:[1,0,1]
	v_pk_fma_f32 v[156:157], v[24:25], s[2:3], v[156:157] op_sel_hi:[1,0,1]
	v_pk_fma_f32 v[154:155], v[26:27], s[2:3], v[154:155] op_sel_hi:[1,0,1]
	v_pk_fma_f32 v[152:153], v[28:29], s[2:3], v[152:153] op_sel_hi:[1,0,1]
	v_pk_fma_f32 v[150:151], v[30:31], s[2:3], v[150:151] op_sel_hi:[1,0,1]
	v_readlane_b32 s2, v211, 3
	s_waitcnt vmcnt(16)
	v_cvt_scalef32_pk32_f32_fp6 v[0:31], v[44:49], 1.0
	v_pk_fma_f32 v[164:165], v[0:1], s[2:3], v[56:57] op_sel_hi:[1,0,1]
	v_pk_fma_f32 v[166:167], v[2:3], s[2:3], v[58:59] op_sel_hi:[1,0,1]
	v_pk_fma_f32 v[168:169], v[4:5], s[2:3], v[60:61] op_sel_hi:[1,0,1]
	v_pk_fma_f32 v[170:171], v[6:7], s[2:3], v[68:69] op_sel_hi:[1,0,1]
	v_pk_fma_f32 v[172:173], v[8:9], s[2:3], v[70:71] op_sel_hi:[1,0,1]
	v_pk_fma_f32 v[174:175], v[10:11], s[2:3], v[72:73] op_sel_hi:[1,0,1]
	v_pk_fma_f32 v[176:177], v[12:13], s[2:3], v[74:75] op_sel_hi:[1,0,1]
	v_pk_fma_f32 v[178:179], v[14:15], s[2:3], v[76:77] op_sel_hi:[1,0,1]
	v_pk_fma_f32 v[180:181], v[16:17], s[2:3], v[78:79] op_sel_hi:[1,0,1]
	v_pk_fma_f32 v[162:163], v[18:19], s[2:3], v[162:163] op_sel_hi:[1,0,1]
	v_pk_fma_f32 v[160:161], v[20:21], s[2:3], v[160:161] op_sel_hi:[1,0,1]
	v_pk_fma_f32 v[158:159], v[22:23], s[2:3], v[158:159] op_sel_hi:[1,0,1]
	v_pk_fma_f32 v[156:157], v[24:25], s[2:3], v[156:157] op_sel_hi:[1,0,1]
	v_pk_fma_f32 v[154:155], v[26:27], s[2:3], v[154:155] op_sel_hi:[1,0,1]
	v_pk_fma_f32 v[152:153], v[28:29], s[2:3], v[152:153] op_sel_hi:[1,0,1]
	v_pk_fma_f32 v[150:151], v[30:31], s[2:3], v[150:151] op_sel_hi:[1,0,1]
	v_readlane_b32 s2, v240, 12
	v_readlane_b32 s3, v240, 13
	v_readlane_b32 s100, v240, 14
	v_readlane_b32 s101, v240, 15
	s_nop 1
	buffer_load_dwordx4 v[74:77], v129, s[44:47], s2 offen
	buffer_load_dwordx2 v[78:79], v210, s[44:47], s2 offen
	buffer_load_dwordx4 v[68:71], v129, s[44:47], s3 offen
	buffer_load_dwordx2 v[72:73], v210, s[44:47], s3 offen
	buffer_load_dwordx4 v[56:59], v129, s[44:47], s100 offen
	buffer_load_dwordx2 v[60:61], v210, s[44:47], s100 offen
	buffer_load_dwordx4 v[44:47], v129, s[44:47], s101 offen
	buffer_load_dwordx2 v[48:49], v210, s[44:47], s101 offen
	v_readlane_b32 s2, v211, 4
	s_waitcnt vmcnt(22)
	v_cvt_scalef32_pk32_f32_fp6 v[0:31], v[62:67], 1.0
	v_pk_fma_f32 v[62:63], v[0:1], s[2:3], v[164:165] op_sel_hi:[1,0,1]
	v_pk_fma_f32 v[64:65], v[2:3], s[2:3], v[166:167] op_sel_hi:[1,0,1]
	v_pk_fma_f32 v[66:67], v[4:5], s[2:3], v[168:169] op_sel_hi:[1,0,1]
	v_pk_fma_f32 v[164:165], v[6:7], s[2:3], v[170:171] op_sel_hi:[1,0,1]
	v_pk_fma_f32 v[166:167], v[8:9], s[2:3], v[172:173] op_sel_hi:[1,0,1]
	v_pk_fma_f32 v[168:169], v[10:11], s[2:3], v[174:175] op_sel_hi:[1,0,1]
	v_pk_fma_f32 v[170:171], v[12:13], s[2:3], v[176:177] op_sel_hi:[1,0,1]
	v_pk_fma_f32 v[172:173], v[14:15], s[2:3], v[178:179] op_sel_hi:[1,0,1]
	v_pk_fma_f32 v[174:175], v[16:17], s[2:3], v[180:181] op_sel_hi:[1,0,1]
	v_pk_fma_f32 v[162:163], v[18:19], s[2:3], v[162:163] op_sel_hi:[1,0,1]
	v_pk_fma_f32 v[160:161], v[20:21], s[2:3], v[160:161] op_sel_hi:[1,0,1]
	v_pk_fma_f32 v[158:159], v[22:23], s[2:3], v[158:159] op_sel_hi:[1,0,1]
	v_pk_fma_f32 v[156:157], v[24:25], s[2:3], v[156:157] op_sel_hi:[1,0,1]
	v_pk_fma_f32 v[154:155], v[26:27], s[2:3], v[154:155] op_sel_hi:[1,0,1]
	v_pk_fma_f32 v[152:153], v[28:29], s[2:3], v[152:153] op_sel_hi:[1,0,1]
	v_pk_fma_f32 v[150:151], v[30:31], s[2:3], v[150:151] op_sel_hi:[1,0,1]
	v_readlane_b32 s2, v211, 5
	s_waitcnt vmcnt(20)
	v_cvt_scalef32_pk32_f32_fp6 v[0:31], v[50:55], 1.0
	v_pk_fma_f32 v[50:51], v[0:1], s[2:3], v[62:63] op_sel_hi:[1,0,1]
	v_pk_fma_f32 v[52:53], v[2:3], s[2:3], v[64:65] op_sel_hi:[1,0,1]
	v_pk_fma_f32 v[54:55], v[4:5], s[2:3], v[66:67] op_sel_hi:[1,0,1]
	v_pk_fma_f32 v[62:63], v[6:7], s[2:3], v[164:165] op_sel_hi:[1,0,1]
	v_pk_fma_f32 v[64:65], v[8:9], s[2:3], v[166:167] op_sel_hi:[1,0,1]
	v_pk_fma_f32 v[66:67], v[10:11], s[2:3], v[168:169] op_sel_hi:[1,0,1]
	v_pk_fma_f32 v[164:165], v[12:13], s[2:3], v[170:171] op_sel_hi:[1,0,1]
	v_pk_fma_f32 v[166:167], v[14:15], s[2:3], v[172:173] op_sel_hi:[1,0,1]
	v_pk_fma_f32 v[168:169], v[16:17], s[2:3], v[174:175] op_sel_hi:[1,0,1]
	v_pk_fma_f32 v[162:163], v[18:19], s[2:3], v[162:163] op_sel_hi:[1,0,1]
	v_pk_fma_f32 v[160:161], v[20:21], s[2:3], v[160:161] op_sel_hi:[1,0,1]
	v_pk_fma_f32 v[158:159], v[22:23], s[2:3], v[158:159] op_sel_hi:[1,0,1]
	v_pk_fma_f32 v[156:157], v[24:25], s[2:3], v[156:157] op_sel_hi:[1,0,1]
	v_pk_fma_f32 v[154:155], v[26:27], s[2:3], v[154:155] op_sel_hi:[1,0,1]
	v_pk_fma_f32 v[152:153], v[28:29], s[2:3], v[152:153] op_sel_hi:[1,0,1]
	v_pk_fma_f32 v[150:151], v[30:31], s[2:3], v[150:151] op_sel_hi:[1,0,1]
	v_readlane_b32 s2, v211, 6
	s_waitcnt vmcnt(18)
	v_cvt_scalef32_pk32_f32_fp6 v[0:31], v[38:43], 1.0
	v_pk_fma_f32 v[38:39], v[0:1], s[2:3], v[50:51] op_sel_hi:[1,0,1]
	v_pk_fma_f32 v[40:41], v[2:3], s[2:3], v[52:53] op_sel_hi:[1,0,1]
	v_pk_fma_f32 v[42:43], v[4:5], s[2:3], v[54:55] op_sel_hi:[1,0,1]
	v_pk_fma_f32 v[50:51], v[6:7], s[2:3], v[62:63] op_sel_hi:[1,0,1]
	v_pk_fma_f32 v[52:53], v[8:9], s[2:3], v[64:65] op_sel_hi:[1,0,1]
	v_pk_fma_f32 v[54:55], v[10:11], s[2:3], v[66:67] op_sel_hi:[1,0,1]
	v_pk_fma_f32 v[62:63], v[12:13], s[2:3], v[164:165] op_sel_hi:[1,0,1]
	v_pk_fma_f32 v[64:65], v[14:15], s[2:3], v[166:167] op_sel_hi:[1,0,1]
	v_pk_fma_f32 v[66:67], v[16:17], s[2:3], v[168:169] op_sel_hi:[1,0,1]
	v_pk_fma_f32 v[162:163], v[18:19], s[2:3], v[162:163] op_sel_hi:[1,0,1]
	v_pk_fma_f32 v[160:161], v[20:21], s[2:3], v[160:161] op_sel_hi:[1,0,1]
	v_pk_fma_f32 v[158:159], v[22:23], s[2:3], v[158:159] op_sel_hi:[1,0,1]
	v_pk_fma_f32 v[156:157], v[24:25], s[2:3], v[156:157] op_sel_hi:[1,0,1]
	v_pk_fma_f32 v[154:155], v[26:27], s[2:3], v[154:155] op_sel_hi:[1,0,1]
	v_pk_fma_f32 v[152:153], v[28:29], s[2:3], v[152:153] op_sel_hi:[1,0,1]
	v_pk_fma_f32 v[150:151], v[30:31], s[2:3], v[150:151] op_sel_hi:[1,0,1]
	v_readlane_b32 s2, v211, 7
	s_waitcnt vmcnt(16)
	v_cvt_scalef32_pk32_f32_fp6 v[0:31], v[32:37], 1.0
	v_pk_fma_f32 v[164:165], v[0:1], s[2:3], v[38:39] op_sel_hi:[1,0,1]
	v_pk_fma_f32 v[166:167], v[2:3], s[2:3], v[40:41] op_sel_hi:[1,0,1]
	v_pk_fma_f32 v[168:169], v[4:5], s[2:3], v[42:43] op_sel_hi:[1,0,1]
	v_pk_fma_f32 v[170:171], v[6:7], s[2:3], v[50:51] op_sel_hi:[1,0,1]
	v_pk_fma_f32 v[172:173], v[8:9], s[2:3], v[52:53] op_sel_hi:[1,0,1]
	v_pk_fma_f32 v[174:175], v[10:11], s[2:3], v[54:55] op_sel_hi:[1,0,1]
	v_pk_fma_f32 v[176:177], v[12:13], s[2:3], v[62:63] op_sel_hi:[1,0,1]
	v_pk_fma_f32 v[178:179], v[14:15], s[2:3], v[64:65] op_sel_hi:[1,0,1]
	v_pk_fma_f32 v[180:181], v[16:17], s[2:3], v[66:67] op_sel_hi:[1,0,1]
	v_pk_fma_f32 v[162:163], v[18:19], s[2:3], v[162:163] op_sel_hi:[1,0,1]
	v_pk_fma_f32 v[160:161], v[20:21], s[2:3], v[160:161] op_sel_hi:[1,0,1]
	v_pk_fma_f32 v[158:159], v[22:23], s[2:3], v[158:159] op_sel_hi:[1,0,1]
	v_pk_fma_f32 v[156:157], v[24:25], s[2:3], v[156:157] op_sel_hi:[1,0,1]
	v_pk_fma_f32 v[154:155], v[26:27], s[2:3], v[154:155] op_sel_hi:[1,0,1]
	v_pk_fma_f32 v[152:153], v[28:29], s[2:3], v[152:153] op_sel_hi:[1,0,1]
	v_pk_fma_f32 v[150:151], v[30:31], s[2:3], v[150:151] op_sel_hi:[1,0,1]
	v_readlane_b32 s2, v240, 16
	v_readlane_b32 s3, v240, 17
	v_readlane_b32 s100, v240, 18
	v_readlane_b32 s101, v240, 19
	s_nop 1
	buffer_load_dwordx4 v[62:65], v129, s[44:47], s2 offen
	buffer_load_dwordx2 v[66:67], v210, s[44:47], s2 offen
	buffer_load_dwordx4 v[50:53], v129, s[44:47], s3 offen
	buffer_load_dwordx2 v[54:55], v210, s[44:47], s3 offen
	buffer_load_dwordx4 v[38:41], v129, s[44:47], s100 offen
	buffer_load_dwordx2 v[42:43], v210, s[44:47], s100 offen
	buffer_load_dwordx4 v[32:35], v129, s[44:47], s101 offen
	buffer_load_dwordx2 v[36:37], v210, s[44:47], s101 offen
	v_readlane_b32 s2, v211, 8
	s_waitcnt vmcnt(22)
	v_cvt_scalef32_pk32_f32_fp6 v[0:31], v[98:103], 1.0
	v_pk_fma_f32 v[98:99], v[0:1], s[2:3], v[164:165] op_sel_hi:[1,0,1]
	v_pk_fma_f32 v[100:101], v[2:3], s[2:3], v[166:167] op_sel_hi:[1,0,1]
	v_pk_fma_f32 v[102:103], v[4:5], s[2:3], v[168:169] op_sel_hi:[1,0,1]
	v_pk_fma_f32 v[164:165], v[6:7], s[2:3], v[170:171] op_sel_hi:[1,0,1]
	v_pk_fma_f32 v[166:167], v[8:9], s[2:3], v[172:173] op_sel_hi:[1,0,1]
	v_pk_fma_f32 v[168:169], v[10:11], s[2:3], v[174:175] op_sel_hi:[1,0,1]
	v_pk_fma_f32 v[170:171], v[12:13], s[2:3], v[176:177] op_sel_hi:[1,0,1]
	v_pk_fma_f32 v[172:173], v[14:15], s[2:3], v[178:179] op_sel_hi:[1,0,1]
	v_pk_fma_f32 v[174:175], v[16:17], s[2:3], v[180:181] op_sel_hi:[1,0,1]
	v_pk_fma_f32 v[162:163], v[18:19], s[2:3], v[162:163] op_sel_hi:[1,0,1]
	v_pk_fma_f32 v[160:161], v[20:21], s[2:3], v[160:161] op_sel_hi:[1,0,1]
	v_pk_fma_f32 v[158:159], v[22:23], s[2:3], v[158:159] op_sel_hi:[1,0,1]
	v_pk_fma_f32 v[156:157], v[24:25], s[2:3], v[156:157] op_sel_hi:[1,0,1]
	v_pk_fma_f32 v[154:155], v[26:27], s[2:3], v[154:155] op_sel_hi:[1,0,1]
	v_pk_fma_f32 v[152:153], v[28:29], s[2:3], v[152:153] op_sel_hi:[1,0,1]
	v_pk_fma_f32 v[150:151], v[30:31], s[2:3], v[150:151] op_sel_hi:[1,0,1]
	v_readlane_b32 s2, v211, 9
	s_waitcnt vmcnt(20)
	v_cvt_scalef32_pk32_f32_fp6 v[0:31], v[92:97], 1.0
	v_pk_fma_f32 v[92:93], v[0:1], s[2:3], v[98:99] op_sel_hi:[1,0,1]
	v_pk_fma_f32 v[94:95], v[2:3], s[2:3], v[100:101] op_sel_hi:[1,0,1]
	v_pk_fma_f32 v[96:97], v[4:5], s[2:3], v[102:103] op_sel_hi:[1,0,1]
	v_pk_fma_f32 v[98:99], v[6:7], s[2:3], v[164:165] op_sel_hi:[1,0,1]
	v_pk_fma_f32 v[100:101], v[8:9], s[2:3], v[166:167] op_sel_hi:[1,0,1]
	v_pk_fma_f32 v[102:103], v[10:11], s[2:3], v[168:169] op_sel_hi:[1,0,1]
	v_pk_fma_f32 v[164:165], v[12:13], s[2:3], v[170:171] op_sel_hi:[1,0,1]
	v_pk_fma_f32 v[166:167], v[14:15], s[2:3], v[172:173] op_sel_hi:[1,0,1]
	v_pk_fma_f32 v[168:169], v[16:17], s[2:3], v[174:175] op_sel_hi:[1,0,1]
	v_pk_fma_f32 v[162:163], v[18:19], s[2:3], v[162:163] op_sel_hi:[1,0,1]
	v_pk_fma_f32 v[160:161], v[20:21], s[2:3], v[160:161] op_sel_hi:[1,0,1]
	v_pk_fma_f32 v[158:159], v[22:23], s[2:3], v[158:159] op_sel_hi:[1,0,1]
	v_pk_fma_f32 v[156:157], v[24:25], s[2:3], v[156:157] op_sel_hi:[1,0,1]
	v_pk_fma_f32 v[154:155], v[26:27], s[2:3], v[154:155] op_sel_hi:[1,0,1]
	v_pk_fma_f32 v[152:153], v[28:29], s[2:3], v[152:153] op_sel_hi:[1,0,1]
	v_pk_fma_f32 v[150:151], v[30:31], s[2:3], v[150:151] op_sel_hi:[1,0,1]
	v_readlane_b32 s2, v211, 10
	s_waitcnt vmcnt(18)
	v_cvt_scalef32_pk32_f32_fp6 v[0:31], v[86:91], 1.0
	v_pk_fma_f32 v[86:87], v[0:1], s[2:3], v[92:93] op_sel_hi:[1,0,1]
	v_pk_fma_f32 v[88:89], v[2:3], s[2:3], v[94:95] op_sel_hi:[1,0,1]
	v_pk_fma_f32 v[90:91], v[4:5], s[2:3], v[96:97] op_sel_hi:[1,0,1]
	v_pk_fma_f32 v[92:93], v[6:7], s[2:3], v[98:99] op_sel_hi:[1,0,1]
	v_pk_fma_f32 v[94:95], v[8:9], s[2:3], v[100:101] op_sel_hi:[1,0,1]
	v_pk_fma_f32 v[96:97], v[10:11], s[2:3], v[102:103] op_sel_hi:[1,0,1]
	v_pk_fma_f32 v[98:99], v[12:13], s[2:3], v[164:165] op_sel_hi:[1,0,1]
	v_pk_fma_f32 v[100:101], v[14:15], s[2:3], v[166:167] op_sel_hi:[1,0,1]
	v_pk_fma_f32 v[102:103], v[16:17], s[2:3], v[168:169] op_sel_hi:[1,0,1]
	v_pk_fma_f32 v[162:163], v[18:19], s[2:3], v[162:163] op_sel_hi:[1,0,1]
	v_pk_fma_f32 v[160:161], v[20:21], s[2:3], v[160:161] op_sel_hi:[1,0,1]
	v_pk_fma_f32 v[158:159], v[22:23], s[2:3], v[158:159] op_sel_hi:[1,0,1]
	v_pk_fma_f32 v[156:157], v[24:25], s[2:3], v[156:157] op_sel_hi:[1,0,1]
	v_pk_fma_f32 v[154:155], v[26:27], s[2:3], v[154:155] op_sel_hi:[1,0,1]
	v_pk_fma_f32 v[152:153], v[28:29], s[2:3], v[152:153] op_sel_hi:[1,0,1]
	v_pk_fma_f32 v[150:151], v[30:31], s[2:3], v[150:151] op_sel_hi:[1,0,1]
	v_readlane_b32 s2, v211, 11
	s_waitcnt vmcnt(16)
	v_cvt_scalef32_pk32_f32_fp6 v[0:31], v[80:85], 1.0
	v_pk_fma_f32 v[180:181], v[0:1], s[2:3], v[86:87] op_sel_hi:[1,0,1]
	v_pk_fma_f32 v[178:179], v[2:3], s[2:3], v[88:89] op_sel_hi:[1,0,1]
	v_pk_fma_f32 v[176:177], v[4:5], s[2:3], v[90:91] op_sel_hi:[1,0,1]
	v_pk_fma_f32 v[174:175], v[6:7], s[2:3], v[92:93] op_sel_hi:[1,0,1]
	v_pk_fma_f32 v[172:173], v[8:9], s[2:3], v[94:95] op_sel_hi:[1,0,1]
	v_pk_fma_f32 v[170:171], v[10:11], s[2:3], v[96:97] op_sel_hi:[1,0,1]
	v_pk_fma_f32 v[168:169], v[12:13], s[2:3], v[98:99] op_sel_hi:[1,0,1]
	v_pk_fma_f32 v[166:167], v[14:15], s[2:3], v[100:101] op_sel_hi:[1,0,1]
	v_pk_fma_f32 v[164:165], v[16:17], s[2:3], v[102:103] op_sel_hi:[1,0,1]
	v_pk_fma_f32 v[162:163], v[18:19], s[2:3], v[162:163] op_sel_hi:[1,0,1]
	v_pk_fma_f32 v[160:161], v[20:21], s[2:3], v[160:161] op_sel_hi:[1,0,1]
	v_pk_fma_f32 v[158:159], v[22:23], s[2:3], v[158:159] op_sel_hi:[1,0,1]
	v_pk_fma_f32 v[156:157], v[24:25], s[2:3], v[156:157] op_sel_hi:[1,0,1]
	v_pk_fma_f32 v[154:155], v[26:27], s[2:3], v[154:155] op_sel_hi:[1,0,1]
	v_pk_fma_f32 v[152:153], v[28:29], s[2:3], v[152:153] op_sel_hi:[1,0,1]
	v_pk_fma_f32 v[150:151], v[30:31], s[2:3], v[150:151] op_sel_hi:[1,0,1]
	v_readlane_b32 s2, v240, 20
	v_readlane_b32 s3, v240, 21
	v_readlane_b32 s100, v240, 22
	v_readlane_b32 s101, v240, 23
	s_nop 1
	buffer_load_dwordx4 v[98:101], v129, s[44:47], s2 offen
	buffer_load_dwordx2 v[102:103], v210, s[44:47], s2 offen
	buffer_load_dwordx4 v[92:95], v129, s[44:47], s3 offen
	buffer_load_dwordx2 v[96:97], v210, s[44:47], s3 offen
	buffer_load_dwordx4 v[86:89], v129, s[44:47], s100 offen
	buffer_load_dwordx2 v[90:91], v210, s[44:47], s100 offen
	buffer_load_dwordx4 v[80:83], v129, s[44:47], s101 offen
	buffer_load_dwordx2 v[84:85], v210, s[44:47], s101 offen
	v_readlane_b32 s2, v211, 12
	s_waitcnt vmcnt(22)
	v_cvt_scalef32_pk32_f32_fp6 v[0:31], v[74:79], 1.0
	v_pk_fma_f32 v[74:75], v[0:1], s[2:3], v[180:181] op_sel_hi:[1,0,1]
	v_pk_fma_f32 v[76:77], v[2:3], s[2:3], v[178:179] op_sel_hi:[1,0,1]
	v_pk_fma_f32 v[78:79], v[4:5], s[2:3], v[176:177] op_sel_hi:[1,0,1]
	v_pk_fma_f32 v[174:175], v[6:7], s[2:3], v[174:175] op_sel_hi:[1,0,1]
	v_pk_fma_f32 v[172:173], v[8:9], s[2:3], v[172:173] op_sel_hi:[1,0,1]
	v_pk_fma_f32 v[170:171], v[10:11], s[2:3], v[170:171] op_sel_hi:[1,0,1]
	v_pk_fma_f32 v[168:169], v[12:13], s[2:3], v[168:169] op_sel_hi:[1,0,1]
	v_pk_fma_f32 v[166:167], v[14:15], s[2:3], v[166:167] op_sel_hi:[1,0,1]
	v_pk_fma_f32 v[164:165], v[16:17], s[2:3], v[164:165] op_sel_hi:[1,0,1]
	v_pk_fma_f32 v[162:163], v[18:19], s[2:3], v[162:163] op_sel_hi:[1,0,1]
	v_pk_fma_f32 v[160:161], v[20:21], s[2:3], v[160:161] op_sel_hi:[1,0,1]
	v_pk_fma_f32 v[158:159], v[22:23], s[2:3], v[158:159] op_sel_hi:[1,0,1]
	v_pk_fma_f32 v[156:157], v[24:25], s[2:3], v[156:157] op_sel_hi:[1,0,1]
	v_pk_fma_f32 v[154:155], v[26:27], s[2:3], v[154:155] op_sel_hi:[1,0,1]
	v_pk_fma_f32 v[152:153], v[28:29], s[2:3], v[152:153] op_sel_hi:[1,0,1]
	v_pk_fma_f32 v[150:151], v[30:31], s[2:3], v[150:151] op_sel_hi:[1,0,1]
	v_readlane_b32 s2, v211, 13
	s_waitcnt vmcnt(20)
	v_cvt_scalef32_pk32_f32_fp6 v[0:31], v[68:73], 1.0
	v_pk_fma_f32 v[68:69], v[0:1], s[2:3], v[74:75] op_sel_hi:[1,0,1]
	v_pk_fma_f32 v[70:71], v[2:3], s[2:3], v[76:77] op_sel_hi:[1,0,1]
	v_pk_fma_f32 v[72:73], v[4:5], s[2:3], v[78:79] op_sel_hi:[1,0,1]
	v_pk_fma_f32 v[74:75], v[6:7], s[2:3], v[174:175] op_sel_hi:[1,0,1]
	v_pk_fma_f32 v[76:77], v[8:9], s[2:3], v[172:173] op_sel_hi:[1,0,1]
	v_pk_fma_f32 v[78:79], v[10:11], s[2:3], v[170:171] op_sel_hi:[1,0,1]
	v_pk_fma_f32 v[168:169], v[12:13], s[2:3], v[168:169] op_sel_hi:[1,0,1]
	v_pk_fma_f32 v[166:167], v[14:15], s[2:3], v[166:167] op_sel_hi:[1,0,1]
	v_pk_fma_f32 v[164:165], v[16:17], s[2:3], v[164:165] op_sel_hi:[1,0,1]
	v_pk_fma_f32 v[162:163], v[18:19], s[2:3], v[162:163] op_sel_hi:[1,0,1]
	v_pk_fma_f32 v[160:161], v[20:21], s[2:3], v[160:161] op_sel_hi:[1,0,1]
	v_pk_fma_f32 v[158:159], v[22:23], s[2:3], v[158:159] op_sel_hi:[1,0,1]
	v_pk_fma_f32 v[156:157], v[24:25], s[2:3], v[156:157] op_sel_hi:[1,0,1]
	v_pk_fma_f32 v[154:155], v[26:27], s[2:3], v[154:155] op_sel_hi:[1,0,1]
	v_pk_fma_f32 v[152:153], v[28:29], s[2:3], v[152:153] op_sel_hi:[1,0,1]
	v_pk_fma_f32 v[150:151], v[30:31], s[2:3], v[150:151] op_sel_hi:[1,0,1]
	v_readlane_b32 s2, v211, 14
	s_waitcnt vmcnt(18)
	v_cvt_scalef32_pk32_f32_fp6 v[0:31], v[56:61], 1.0
	v_pk_fma_f32 v[56:57], v[0:1], s[2:3], v[68:69] op_sel_hi:[1,0,1]
	v_pk_fma_f32 v[58:59], v[2:3], s[2:3], v[70:71] op_sel_hi:[1,0,1]
	v_pk_fma_f32 v[60:61], v[4:5], s[2:3], v[72:73] op_sel_hi:[1,0,1]
	v_pk_fma_f32 v[68:69], v[6:7], s[2:3], v[74:75] op_sel_hi:[1,0,1]
	v_pk_fma_f32 v[70:71], v[8:9], s[2:3], v[76:77] op_sel_hi:[1,0,1]
	v_pk_fma_f32 v[72:73], v[10:11], s[2:3], v[78:79] op_sel_hi:[1,0,1]
	v_pk_fma_f32 v[74:75], v[12:13], s[2:3], v[168:169] op_sel_hi:[1,0,1]
	v_pk_fma_f32 v[76:77], v[14:15], s[2:3], v[166:167] op_sel_hi:[1,0,1]
	v_pk_fma_f32 v[78:79], v[16:17], s[2:3], v[164:165] op_sel_hi:[1,0,1]
	v_pk_fma_f32 v[162:163], v[18:19], s[2:3], v[162:163] op_sel_hi:[1,0,1]
	v_pk_fma_f32 v[160:161], v[20:21], s[2:3], v[160:161] op_sel_hi:[1,0,1]
	v_pk_fma_f32 v[158:159], v[22:23], s[2:3], v[158:159] op_sel_hi:[1,0,1]
	v_pk_fma_f32 v[156:157], v[24:25], s[2:3], v[156:157] op_sel_hi:[1,0,1]
	v_pk_fma_f32 v[154:155], v[26:27], s[2:3], v[154:155] op_sel_hi:[1,0,1]
	v_pk_fma_f32 v[152:153], v[28:29], s[2:3], v[152:153] op_sel_hi:[1,0,1]
	v_pk_fma_f32 v[150:151], v[30:31], s[2:3], v[150:151] op_sel_hi:[1,0,1]
	v_readlane_b32 s2, v211, 15
	s_waitcnt vmcnt(16)
	v_cvt_scalef32_pk32_f32_fp6 v[0:31], v[44:49], 1.0
	v_pk_fma_f32 v[164:165], v[0:1], s[2:3], v[56:57] op_sel_hi:[1,0,1]
	v_pk_fma_f32 v[166:167], v[2:3], s[2:3], v[58:59] op_sel_hi:[1,0,1]
	v_pk_fma_f32 v[168:169], v[4:5], s[2:3], v[60:61] op_sel_hi:[1,0,1]
	v_pk_fma_f32 v[170:171], v[6:7], s[2:3], v[68:69] op_sel_hi:[1,0,1]
	v_pk_fma_f32 v[172:173], v[8:9], s[2:3], v[70:71] op_sel_hi:[1,0,1]
	v_pk_fma_f32 v[174:175], v[10:11], s[2:3], v[72:73] op_sel_hi:[1,0,1]
	v_pk_fma_f32 v[176:177], v[12:13], s[2:3], v[74:75] op_sel_hi:[1,0,1]
	v_pk_fma_f32 v[178:179], v[14:15], s[2:3], v[76:77] op_sel_hi:[1,0,1]
	v_pk_fma_f32 v[180:181], v[16:17], s[2:3], v[78:79] op_sel_hi:[1,0,1]
	v_pk_fma_f32 v[162:163], v[18:19], s[2:3], v[162:163] op_sel_hi:[1,0,1]
	v_pk_fma_f32 v[160:161], v[20:21], s[2:3], v[160:161] op_sel_hi:[1,0,1]
	v_pk_fma_f32 v[158:159], v[22:23], s[2:3], v[158:159] op_sel_hi:[1,0,1]
	v_pk_fma_f32 v[156:157], v[24:25], s[2:3], v[156:157] op_sel_hi:[1,0,1]
	v_pk_fma_f32 v[154:155], v[26:27], s[2:3], v[154:155] op_sel_hi:[1,0,1]
	v_pk_fma_f32 v[152:153], v[28:29], s[2:3], v[152:153] op_sel_hi:[1,0,1]
	v_pk_fma_f32 v[150:151], v[30:31], s[2:3], v[150:151] op_sel_hi:[1,0,1]
	v_readlane_b32 s2, v240, 24
	v_readlane_b32 s3, v240, 25
	v_readlane_b32 s100, v240, 26
	v_readlane_b32 s101, v240, 27
	s_nop 1
	buffer_load_dwordx4 v[74:77], v129, s[44:47], s2 offen
	buffer_load_dwordx2 v[78:79], v210, s[44:47], s2 offen
	buffer_load_dwordx4 v[68:71], v129, s[44:47], s3 offen
	buffer_load_dwordx2 v[72:73], v210, s[44:47], s3 offen
	buffer_load_dwordx4 v[56:59], v129, s[44:47], s100 offen
	buffer_load_dwordx2 v[60:61], v210, s[44:47], s100 offen
	buffer_load_dwordx4 v[44:47], v129, s[44:47], s101 offen
	buffer_load_dwordx2 v[48:49], v210, s[44:47], s101 offen
	v_readlane_b32 s2, v211, 16
	s_waitcnt vmcnt(22)
	v_cvt_scalef32_pk32_f32_fp6 v[0:31], v[62:67], 1.0
	v_pk_fma_f32 v[62:63], v[0:1], s[2:3], v[164:165] op_sel_hi:[1,0,1]
	v_pk_fma_f32 v[64:65], v[2:3], s[2:3], v[166:167] op_sel_hi:[1,0,1]
	v_pk_fma_f32 v[66:67], v[4:5], s[2:3], v[168:169] op_sel_hi:[1,0,1]
	v_pk_fma_f32 v[164:165], v[6:7], s[2:3], v[170:171] op_sel_hi:[1,0,1]
	v_pk_fma_f32 v[166:167], v[8:9], s[2:3], v[172:173] op_sel_hi:[1,0,1]
	v_pk_fma_f32 v[168:169], v[10:11], s[2:3], v[174:175] op_sel_hi:[1,0,1]
	v_pk_fma_f32 v[170:171], v[12:13], s[2:3], v[176:177] op_sel_hi:[1,0,1]
	v_pk_fma_f32 v[172:173], v[14:15], s[2:3], v[178:179] op_sel_hi:[1,0,1]
	v_pk_fma_f32 v[174:175], v[16:17], s[2:3], v[180:181] op_sel_hi:[1,0,1]
	v_pk_fma_f32 v[162:163], v[18:19], s[2:3], v[162:163] op_sel_hi:[1,0,1]
	v_pk_fma_f32 v[160:161], v[20:21], s[2:3], v[160:161] op_sel_hi:[1,0,1]
	v_pk_fma_f32 v[158:159], v[22:23], s[2:3], v[158:159] op_sel_hi:[1,0,1]
	v_pk_fma_f32 v[156:157], v[24:25], s[2:3], v[156:157] op_sel_hi:[1,0,1]
	v_pk_fma_f32 v[154:155], v[26:27], s[2:3], v[154:155] op_sel_hi:[1,0,1]
	v_pk_fma_f32 v[152:153], v[28:29], s[2:3], v[152:153] op_sel_hi:[1,0,1]
	v_pk_fma_f32 v[150:151], v[30:31], s[2:3], v[150:151] op_sel_hi:[1,0,1]
	v_readlane_b32 s2, v211, 17
	s_waitcnt vmcnt(20)
	v_cvt_scalef32_pk32_f32_fp6 v[0:31], v[50:55], 1.0
	v_pk_fma_f32 v[50:51], v[0:1], s[2:3], v[62:63] op_sel_hi:[1,0,1]
	v_pk_fma_f32 v[52:53], v[2:3], s[2:3], v[64:65] op_sel_hi:[1,0,1]
	v_pk_fma_f32 v[54:55], v[4:5], s[2:3], v[66:67] op_sel_hi:[1,0,1]
	v_pk_fma_f32 v[62:63], v[6:7], s[2:3], v[164:165] op_sel_hi:[1,0,1]
	v_pk_fma_f32 v[64:65], v[8:9], s[2:3], v[166:167] op_sel_hi:[1,0,1]
	v_pk_fma_f32 v[66:67], v[10:11], s[2:3], v[168:169] op_sel_hi:[1,0,1]
	v_pk_fma_f32 v[164:165], v[12:13], s[2:3], v[170:171] op_sel_hi:[1,0,1]
	v_pk_fma_f32 v[166:167], v[14:15], s[2:3], v[172:173] op_sel_hi:[1,0,1]
	v_pk_fma_f32 v[168:169], v[16:17], s[2:3], v[174:175] op_sel_hi:[1,0,1]
	v_pk_fma_f32 v[162:163], v[18:19], s[2:3], v[162:163] op_sel_hi:[1,0,1]
	v_pk_fma_f32 v[160:161], v[20:21], s[2:3], v[160:161] op_sel_hi:[1,0,1]
	v_pk_fma_f32 v[158:159], v[22:23], s[2:3], v[158:159] op_sel_hi:[1,0,1]
	v_pk_fma_f32 v[156:157], v[24:25], s[2:3], v[156:157] op_sel_hi:[1,0,1]
	v_pk_fma_f32 v[154:155], v[26:27], s[2:3], v[154:155] op_sel_hi:[1,0,1]
	v_pk_fma_f32 v[152:153], v[28:29], s[2:3], v[152:153] op_sel_hi:[1,0,1]
	v_pk_fma_f32 v[150:151], v[30:31], s[2:3], v[150:151] op_sel_hi:[1,0,1]
	v_readlane_b32 s2, v211, 18
	s_waitcnt vmcnt(18)
	v_cvt_scalef32_pk32_f32_fp6 v[0:31], v[38:43], 1.0
	v_pk_fma_f32 v[38:39], v[0:1], s[2:3], v[50:51] op_sel_hi:[1,0,1]
	v_pk_fma_f32 v[40:41], v[2:3], s[2:3], v[52:53] op_sel_hi:[1,0,1]
	v_pk_fma_f32 v[42:43], v[4:5], s[2:3], v[54:55] op_sel_hi:[1,0,1]
	v_pk_fma_f32 v[50:51], v[6:7], s[2:3], v[62:63] op_sel_hi:[1,0,1]
	v_pk_fma_f32 v[52:53], v[8:9], s[2:3], v[64:65] op_sel_hi:[1,0,1]
	v_pk_fma_f32 v[54:55], v[10:11], s[2:3], v[66:67] op_sel_hi:[1,0,1]
	v_pk_fma_f32 v[62:63], v[12:13], s[2:3], v[164:165] op_sel_hi:[1,0,1]
	v_pk_fma_f32 v[64:65], v[14:15], s[2:3], v[166:167] op_sel_hi:[1,0,1]
	v_pk_fma_f32 v[66:67], v[16:17], s[2:3], v[168:169] op_sel_hi:[1,0,1]
	v_pk_fma_f32 v[162:163], v[18:19], s[2:3], v[162:163] op_sel_hi:[1,0,1]
	v_pk_fma_f32 v[160:161], v[20:21], s[2:3], v[160:161] op_sel_hi:[1,0,1]
	v_pk_fma_f32 v[158:159], v[22:23], s[2:3], v[158:159] op_sel_hi:[1,0,1]
	v_pk_fma_f32 v[156:157], v[24:25], s[2:3], v[156:157] op_sel_hi:[1,0,1]
	v_pk_fma_f32 v[154:155], v[26:27], s[2:3], v[154:155] op_sel_hi:[1,0,1]
	v_pk_fma_f32 v[152:153], v[28:29], s[2:3], v[152:153] op_sel_hi:[1,0,1]
	v_pk_fma_f32 v[150:151], v[30:31], s[2:3], v[150:151] op_sel_hi:[1,0,1]
	v_readlane_b32 s2, v211, 19
	s_waitcnt vmcnt(16)
	v_cvt_scalef32_pk32_f32_fp6 v[0:31], v[32:37], 1.0
	v_pk_fma_f32 v[164:165], v[0:1], s[2:3], v[38:39] op_sel_hi:[1,0,1]
	v_pk_fma_f32 v[166:167], v[2:3], s[2:3], v[40:41] op_sel_hi:[1,0,1]
	v_pk_fma_f32 v[168:169], v[4:5], s[2:3], v[42:43] op_sel_hi:[1,0,1]
	v_pk_fma_f32 v[170:171], v[6:7], s[2:3], v[50:51] op_sel_hi:[1,0,1]
	v_pk_fma_f32 v[172:173], v[8:9], s[2:3], v[52:53] op_sel_hi:[1,0,1]
	v_pk_fma_f32 v[174:175], v[10:11], s[2:3], v[54:55] op_sel_hi:[1,0,1]
	v_pk_fma_f32 v[176:177], v[12:13], s[2:3], v[62:63] op_sel_hi:[1,0,1]
	v_pk_fma_f32 v[178:179], v[14:15], s[2:3], v[64:65] op_sel_hi:[1,0,1]
	v_pk_fma_f32 v[180:181], v[16:17], s[2:3], v[66:67] op_sel_hi:[1,0,1]
	v_pk_fma_f32 v[162:163], v[18:19], s[2:3], v[162:163] op_sel_hi:[1,0,1]
	v_pk_fma_f32 v[160:161], v[20:21], s[2:3], v[160:161] op_sel_hi:[1,0,1]
	v_pk_fma_f32 v[158:159], v[22:23], s[2:3], v[158:159] op_sel_hi:[1,0,1]
	v_pk_fma_f32 v[156:157], v[24:25], s[2:3], v[156:157] op_sel_hi:[1,0,1]
	v_pk_fma_f32 v[154:155], v[26:27], s[2:3], v[154:155] op_sel_hi:[1,0,1]
	v_pk_fma_f32 v[152:153], v[28:29], s[2:3], v[152:153] op_sel_hi:[1,0,1]
	v_pk_fma_f32 v[150:151], v[30:31], s[2:3], v[150:151] op_sel_hi:[1,0,1]
	v_readlane_b32 s2, v240, 28
	v_readlane_b32 s3, v240, 29
	v_readlane_b32 s100, v240, 30
	v_readlane_b32 s101, v240, 31
	s_nop 1
	buffer_load_dwordx4 v[62:65], v129, s[44:47], s2 offen
	buffer_load_dwordx2 v[66:67], v210, s[44:47], s2 offen
	buffer_load_dwordx4 v[50:53], v129, s[44:47], s3 offen
	buffer_load_dwordx2 v[54:55], v210, s[44:47], s3 offen
	buffer_load_dwordx4 v[38:41], v129, s[44:47], s100 offen
	buffer_load_dwordx2 v[42:43], v210, s[44:47], s100 offen
	buffer_load_dwordx4 v[32:35], v129, s[44:47], s101 offen
	buffer_load_dwordx2 v[36:37], v210, s[44:47], s101 offen
	v_readlane_b32 s2, v211, 20
	s_waitcnt vmcnt(22)
	v_cvt_scalef32_pk32_f32_fp6 v[0:31], v[98:103], 1.0
	v_pk_fma_f32 v[98:99], v[0:1], s[2:3], v[164:165] op_sel_hi:[1,0,1]
	v_pk_fma_f32 v[100:101], v[2:3], s[2:3], v[166:167] op_sel_hi:[1,0,1]
	v_pk_fma_f32 v[102:103], v[4:5], s[2:3], v[168:169] op_sel_hi:[1,0,1]
	v_pk_fma_f32 v[164:165], v[6:7], s[2:3], v[170:171] op_sel_hi:[1,0,1]
	v_pk_fma_f32 v[166:167], v[8:9], s[2:3], v[172:173] op_sel_hi:[1,0,1]
	v_pk_fma_f32 v[168:169], v[10:11], s[2:3], v[174:175] op_sel_hi:[1,0,1]
	v_pk_fma_f32 v[170:171], v[12:13], s[2:3], v[176:177] op_sel_hi:[1,0,1]
	v_pk_fma_f32 v[172:173], v[14:15], s[2:3], v[178:179] op_sel_hi:[1,0,1]
	v_pk_fma_f32 v[174:175], v[16:17], s[2:3], v[180:181] op_sel_hi:[1,0,1]
	v_pk_fma_f32 v[162:163], v[18:19], s[2:3], v[162:163] op_sel_hi:[1,0,1]
	v_pk_fma_f32 v[160:161], v[20:21], s[2:3], v[160:161] op_sel_hi:[1,0,1]
	v_pk_fma_f32 v[158:159], v[22:23], s[2:3], v[158:159] op_sel_hi:[1,0,1]
	v_pk_fma_f32 v[156:157], v[24:25], s[2:3], v[156:157] op_sel_hi:[1,0,1]
	v_pk_fma_f32 v[154:155], v[26:27], s[2:3], v[154:155] op_sel_hi:[1,0,1]
	v_pk_fma_f32 v[152:153], v[28:29], s[2:3], v[152:153] op_sel_hi:[1,0,1]
	v_pk_fma_f32 v[150:151], v[30:31], s[2:3], v[150:151] op_sel_hi:[1,0,1]
	v_readlane_b32 s2, v211, 21
	s_waitcnt vmcnt(20)
	v_cvt_scalef32_pk32_f32_fp6 v[0:31], v[92:97], 1.0
	v_pk_fma_f32 v[92:93], v[0:1], s[2:3], v[98:99] op_sel_hi:[1,0,1]
	v_pk_fma_f32 v[94:95], v[2:3], s[2:3], v[100:101] op_sel_hi:[1,0,1]
	v_pk_fma_f32 v[96:97], v[4:5], s[2:3], v[102:103] op_sel_hi:[1,0,1]
	v_pk_fma_f32 v[98:99], v[6:7], s[2:3], v[164:165] op_sel_hi:[1,0,1]
	v_pk_fma_f32 v[100:101], v[8:9], s[2:3], v[166:167] op_sel_hi:[1,0,1]
	v_pk_fma_f32 v[102:103], v[10:11], s[2:3], v[168:169] op_sel_hi:[1,0,1]
	v_pk_fma_f32 v[164:165], v[12:13], s[2:3], v[170:171] op_sel_hi:[1,0,1]
	v_pk_fma_f32 v[166:167], v[14:15], s[2:3], v[172:173] op_sel_hi:[1,0,1]
	v_pk_fma_f32 v[168:169], v[16:17], s[2:3], v[174:175] op_sel_hi:[1,0,1]
	v_pk_fma_f32 v[162:163], v[18:19], s[2:3], v[162:163] op_sel_hi:[1,0,1]
	v_pk_fma_f32 v[160:161], v[20:21], s[2:3], v[160:161] op_sel_hi:[1,0,1]
	v_pk_fma_f32 v[158:159], v[22:23], s[2:3], v[158:159] op_sel_hi:[1,0,1]
	v_pk_fma_f32 v[156:157], v[24:25], s[2:3], v[156:157] op_sel_hi:[1,0,1]
	v_pk_fma_f32 v[154:155], v[26:27], s[2:3], v[154:155] op_sel_hi:[1,0,1]
	v_pk_fma_f32 v[152:153], v[28:29], s[2:3], v[152:153] op_sel_hi:[1,0,1]
	v_pk_fma_f32 v[150:151], v[30:31], s[2:3], v[150:151] op_sel_hi:[1,0,1]
	v_readlane_b32 s2, v211, 22
	s_waitcnt vmcnt(18)
	v_cvt_scalef32_pk32_f32_fp6 v[0:31], v[86:91], 1.0
	v_pk_fma_f32 v[86:87], v[0:1], s[2:3], v[92:93] op_sel_hi:[1,0,1]
	v_pk_fma_f32 v[88:89], v[2:3], s[2:3], v[94:95] op_sel_hi:[1,0,1]
	v_pk_fma_f32 v[90:91], v[4:5], s[2:3], v[96:97] op_sel_hi:[1,0,1]
	v_pk_fma_f32 v[92:93], v[6:7], s[2:3], v[98:99] op_sel_hi:[1,0,1]
	v_pk_fma_f32 v[94:95], v[8:9], s[2:3], v[100:101] op_sel_hi:[1,0,1]
	v_pk_fma_f32 v[96:97], v[10:11], s[2:3], v[102:103] op_sel_hi:[1,0,1]
	v_pk_fma_f32 v[98:99], v[12:13], s[2:3], v[164:165] op_sel_hi:[1,0,1]
	v_pk_fma_f32 v[100:101], v[14:15], s[2:3], v[166:167] op_sel_hi:[1,0,1]
	v_pk_fma_f32 v[102:103], v[16:17], s[2:3], v[168:169] op_sel_hi:[1,0,1]
	v_pk_fma_f32 v[162:163], v[18:19], s[2:3], v[162:163] op_sel_hi:[1,0,1]
	v_pk_fma_f32 v[160:161], v[20:21], s[2:3], v[160:161] op_sel_hi:[1,0,1]
	v_pk_fma_f32 v[158:159], v[22:23], s[2:3], v[158:159] op_sel_hi:[1,0,1]
	v_pk_fma_f32 v[156:157], v[24:25], s[2:3], v[156:157] op_sel_hi:[1,0,1]
	v_pk_fma_f32 v[154:155], v[26:27], s[2:3], v[154:155] op_sel_hi:[1,0,1]
	v_pk_fma_f32 v[152:153], v[28:29], s[2:3], v[152:153] op_sel_hi:[1,0,1]
	v_pk_fma_f32 v[150:151], v[30:31], s[2:3], v[150:151] op_sel_hi:[1,0,1]
	v_readlane_b32 s2, v211, 23
	s_waitcnt vmcnt(16)
	v_cvt_scalef32_pk32_f32_fp6 v[0:31], v[80:85], 1.0
	v_pk_fma_f32 v[180:181], v[0:1], s[2:3], v[86:87] op_sel_hi:[1,0,1]
	v_pk_fma_f32 v[178:179], v[2:3], s[2:3], v[88:89] op_sel_hi:[1,0,1]
	v_pk_fma_f32 v[176:177], v[4:5], s[2:3], v[90:91] op_sel_hi:[1,0,1]
	v_pk_fma_f32 v[174:175], v[6:7], s[2:3], v[92:93] op_sel_hi:[1,0,1]
	v_pk_fma_f32 v[172:173], v[8:9], s[2:3], v[94:95] op_sel_hi:[1,0,1]
	v_pk_fma_f32 v[170:171], v[10:11], s[2:3], v[96:97] op_sel_hi:[1,0,1]
	v_pk_fma_f32 v[168:169], v[12:13], s[2:3], v[98:99] op_sel_hi:[1,0,1]
	v_pk_fma_f32 v[166:167], v[14:15], s[2:3], v[100:101] op_sel_hi:[1,0,1]
	v_pk_fma_f32 v[164:165], v[16:17], s[2:3], v[102:103] op_sel_hi:[1,0,1]
	v_pk_fma_f32 v[162:163], v[18:19], s[2:3], v[162:163] op_sel_hi:[1,0,1]
	v_pk_fma_f32 v[160:161], v[20:21], s[2:3], v[160:161] op_sel_hi:[1,0,1]
	v_pk_fma_f32 v[158:159], v[22:23], s[2:3], v[158:159] op_sel_hi:[1,0,1]
	v_pk_fma_f32 v[156:157], v[24:25], s[2:3], v[156:157] op_sel_hi:[1,0,1]
	v_pk_fma_f32 v[154:155], v[26:27], s[2:3], v[154:155] op_sel_hi:[1,0,1]
	v_pk_fma_f32 v[152:153], v[28:29], s[2:3], v[152:153] op_sel_hi:[1,0,1]
	v_pk_fma_f32 v[150:151], v[30:31], s[2:3], v[150:151] op_sel_hi:[1,0,1]
	v_readlane_b32 s2, v240, 32
	v_readlane_b32 s3, v240, 33
	v_readlane_b32 s100, v240, 34
	v_readlane_b32 s101, v240, 35
	s_nop 1
	buffer_load_dwordx4 v[98:101], v129, s[44:47], s2 offen
	buffer_load_dwordx2 v[102:103], v210, s[44:47], s2 offen
	buffer_load_dwordx4 v[92:95], v129, s[44:47], s3 offen
	buffer_load_dwordx2 v[96:97], v210, s[44:47], s3 offen
	buffer_load_dwordx4 v[86:89], v129, s[44:47], s100 offen
	buffer_load_dwordx2 v[90:91], v210, s[44:47], s100 offen
	buffer_load_dwordx4 v[80:83], v129, s[44:47], s101 offen
	buffer_load_dwordx2 v[84:85], v210, s[44:47], s101 offen
	v_readlane_b32 s2, v211, 24
	s_waitcnt vmcnt(22)
	v_cvt_scalef32_pk32_f32_fp6 v[0:31], v[74:79], 1.0
	v_pk_fma_f32 v[74:75], v[0:1], s[2:3], v[180:181] op_sel_hi:[1,0,1]
	v_pk_fma_f32 v[76:77], v[2:3], s[2:3], v[178:179] op_sel_hi:[1,0,1]
	v_pk_fma_f32 v[78:79], v[4:5], s[2:3], v[176:177] op_sel_hi:[1,0,1]
	v_pk_fma_f32 v[174:175], v[6:7], s[2:3], v[174:175] op_sel_hi:[1,0,1]
	v_pk_fma_f32 v[172:173], v[8:9], s[2:3], v[172:173] op_sel_hi:[1,0,1]
	v_pk_fma_f32 v[170:171], v[10:11], s[2:3], v[170:171] op_sel_hi:[1,0,1]
	v_pk_fma_f32 v[168:169], v[12:13], s[2:3], v[168:169] op_sel_hi:[1,0,1]
	v_pk_fma_f32 v[166:167], v[14:15], s[2:3], v[166:167] op_sel_hi:[1,0,1]
	v_pk_fma_f32 v[164:165], v[16:17], s[2:3], v[164:165] op_sel_hi:[1,0,1]
	v_pk_fma_f32 v[162:163], v[18:19], s[2:3], v[162:163] op_sel_hi:[1,0,1]
	v_pk_fma_f32 v[160:161], v[20:21], s[2:3], v[160:161] op_sel_hi:[1,0,1]
	v_pk_fma_f32 v[158:159], v[22:23], s[2:3], v[158:159] op_sel_hi:[1,0,1]
	v_pk_fma_f32 v[156:157], v[24:25], s[2:3], v[156:157] op_sel_hi:[1,0,1]
	v_pk_fma_f32 v[154:155], v[26:27], s[2:3], v[154:155] op_sel_hi:[1,0,1]
	v_pk_fma_f32 v[152:153], v[28:29], s[2:3], v[152:153] op_sel_hi:[1,0,1]
	v_pk_fma_f32 v[150:151], v[30:31], s[2:3], v[150:151] op_sel_hi:[1,0,1]
	v_readlane_b32 s2, v211, 25
	s_waitcnt vmcnt(20)
	v_cvt_scalef32_pk32_f32_fp6 v[0:31], v[68:73], 1.0
	v_pk_fma_f32 v[68:69], v[0:1], s[2:3], v[74:75] op_sel_hi:[1,0,1]
	v_pk_fma_f32 v[70:71], v[2:3], s[2:3], v[76:77] op_sel_hi:[1,0,1]
	v_pk_fma_f32 v[72:73], v[4:5], s[2:3], v[78:79] op_sel_hi:[1,0,1]
	v_pk_fma_f32 v[74:75], v[6:7], s[2:3], v[174:175] op_sel_hi:[1,0,1]
	v_pk_fma_f32 v[76:77], v[8:9], s[2:3], v[172:173] op_sel_hi:[1,0,1]
	v_pk_fma_f32 v[78:79], v[10:11], s[2:3], v[170:171] op_sel_hi:[1,0,1]
	v_pk_fma_f32 v[168:169], v[12:13], s[2:3], v[168:169] op_sel_hi:[1,0,1]
	v_pk_fma_f32 v[166:167], v[14:15], s[2:3], v[166:167] op_sel_hi:[1,0,1]
	v_pk_fma_f32 v[164:165], v[16:17], s[2:3], v[164:165] op_sel_hi:[1,0,1]
	v_pk_fma_f32 v[162:163], v[18:19], s[2:3], v[162:163] op_sel_hi:[1,0,1]
	v_pk_fma_f32 v[160:161], v[20:21], s[2:3], v[160:161] op_sel_hi:[1,0,1]
	v_pk_fma_f32 v[158:159], v[22:23], s[2:3], v[158:159] op_sel_hi:[1,0,1]
	v_pk_fma_f32 v[156:157], v[24:25], s[2:3], v[156:157] op_sel_hi:[1,0,1]
	v_pk_fma_f32 v[154:155], v[26:27], s[2:3], v[154:155] op_sel_hi:[1,0,1]
	v_pk_fma_f32 v[152:153], v[28:29], s[2:3], v[152:153] op_sel_hi:[1,0,1]
	v_pk_fma_f32 v[150:151], v[30:31], s[2:3], v[150:151] op_sel_hi:[1,0,1]
	v_readlane_b32 s2, v211, 26
	s_waitcnt vmcnt(18)
	v_cvt_scalef32_pk32_f32_fp6 v[0:31], v[56:61], 1.0
	v_pk_fma_f32 v[56:57], v[0:1], s[2:3], v[68:69] op_sel_hi:[1,0,1]
	v_pk_fma_f32 v[58:59], v[2:3], s[2:3], v[70:71] op_sel_hi:[1,0,1]
	v_pk_fma_f32 v[60:61], v[4:5], s[2:3], v[72:73] op_sel_hi:[1,0,1]
	v_pk_fma_f32 v[68:69], v[6:7], s[2:3], v[74:75] op_sel_hi:[1,0,1]
	v_pk_fma_f32 v[70:71], v[8:9], s[2:3], v[76:77] op_sel_hi:[1,0,1]
	v_pk_fma_f32 v[72:73], v[10:11], s[2:3], v[78:79] op_sel_hi:[1,0,1]
	v_pk_fma_f32 v[74:75], v[12:13], s[2:3], v[168:169] op_sel_hi:[1,0,1]
	v_pk_fma_f32 v[76:77], v[14:15], s[2:3], v[166:167] op_sel_hi:[1,0,1]
	v_pk_fma_f32 v[78:79], v[16:17], s[2:3], v[164:165] op_sel_hi:[1,0,1]
	v_pk_fma_f32 v[162:163], v[18:19], s[2:3], v[162:163] op_sel_hi:[1,0,1]
	v_pk_fma_f32 v[160:161], v[20:21], s[2:3], v[160:161] op_sel_hi:[1,0,1]
	v_pk_fma_f32 v[158:159], v[22:23], s[2:3], v[158:159] op_sel_hi:[1,0,1]
	v_pk_fma_f32 v[156:157], v[24:25], s[2:3], v[156:157] op_sel_hi:[1,0,1]
	v_pk_fma_f32 v[154:155], v[26:27], s[2:3], v[154:155] op_sel_hi:[1,0,1]
	v_pk_fma_f32 v[152:153], v[28:29], s[2:3], v[152:153] op_sel_hi:[1,0,1]
	v_pk_fma_f32 v[150:151], v[30:31], s[2:3], v[150:151] op_sel_hi:[1,0,1]
	v_readlane_b32 s2, v211, 27
	s_waitcnt vmcnt(16)
	v_cvt_scalef32_pk32_f32_fp6 v[0:31], v[44:49], 1.0
	v_pk_fma_f32 v[164:165], v[0:1], s[2:3], v[56:57] op_sel_hi:[1,0,1]
	v_pk_fma_f32 v[166:167], v[2:3], s[2:3], v[58:59] op_sel_hi:[1,0,1]
	v_pk_fma_f32 v[168:169], v[4:5], s[2:3], v[60:61] op_sel_hi:[1,0,1]
	v_pk_fma_f32 v[170:171], v[6:7], s[2:3], v[68:69] op_sel_hi:[1,0,1]
	v_pk_fma_f32 v[172:173], v[8:9], s[2:3], v[70:71] op_sel_hi:[1,0,1]
	v_pk_fma_f32 v[174:175], v[10:11], s[2:3], v[72:73] op_sel_hi:[1,0,1]
	v_pk_fma_f32 v[176:177], v[12:13], s[2:3], v[74:75] op_sel_hi:[1,0,1]
	v_pk_fma_f32 v[178:179], v[14:15], s[2:3], v[76:77] op_sel_hi:[1,0,1]
	v_pk_fma_f32 v[180:181], v[16:17], s[2:3], v[78:79] op_sel_hi:[1,0,1]
	v_pk_fma_f32 v[162:163], v[18:19], s[2:3], v[162:163] op_sel_hi:[1,0,1]
	v_pk_fma_f32 v[160:161], v[20:21], s[2:3], v[160:161] op_sel_hi:[1,0,1]
	v_pk_fma_f32 v[158:159], v[22:23], s[2:3], v[158:159] op_sel_hi:[1,0,1]
	v_pk_fma_f32 v[156:157], v[24:25], s[2:3], v[156:157] op_sel_hi:[1,0,1]
	v_pk_fma_f32 v[154:155], v[26:27], s[2:3], v[154:155] op_sel_hi:[1,0,1]
	v_pk_fma_f32 v[152:153], v[28:29], s[2:3], v[152:153] op_sel_hi:[1,0,1]
	v_pk_fma_f32 v[150:151], v[30:31], s[2:3], v[150:151] op_sel_hi:[1,0,1]
	v_readlane_b32 s2, v240, 36
	v_readlane_b32 s3, v240, 37
	v_readlane_b32 s100, v240, 38
	v_readlane_b32 s101, v240, 39
	s_nop 1
	buffer_load_dwordx4 v[74:77], v129, s[44:47], s2 offen
	buffer_load_dwordx2 v[78:79], v210, s[44:47], s2 offen
	buffer_load_dwordx4 v[68:71], v129, s[44:47], s3 offen
	buffer_load_dwordx2 v[72:73], v210, s[44:47], s3 offen
	buffer_load_dwordx4 v[56:59], v129, s[44:47], s100 offen
	buffer_load_dwordx2 v[60:61], v210, s[44:47], s100 offen
	buffer_load_dwordx4 v[44:47], v129, s[44:47], s101 offen
	buffer_load_dwordx2 v[48:49], v210, s[44:47], s101 offen
	v_readlane_b32 s2, v211, 28
	s_waitcnt vmcnt(22)
	v_cvt_scalef32_pk32_f32_fp6 v[0:31], v[62:67], 1.0
	v_pk_fma_f32 v[62:63], v[0:1], s[2:3], v[164:165] op_sel_hi:[1,0,1]
	v_pk_fma_f32 v[64:65], v[2:3], s[2:3], v[166:167] op_sel_hi:[1,0,1]
	v_pk_fma_f32 v[66:67], v[4:5], s[2:3], v[168:169] op_sel_hi:[1,0,1]
	v_pk_fma_f32 v[164:165], v[6:7], s[2:3], v[170:171] op_sel_hi:[1,0,1]
	v_pk_fma_f32 v[166:167], v[8:9], s[2:3], v[172:173] op_sel_hi:[1,0,1]
	v_pk_fma_f32 v[168:169], v[10:11], s[2:3], v[174:175] op_sel_hi:[1,0,1]
	v_pk_fma_f32 v[170:171], v[12:13], s[2:3], v[176:177] op_sel_hi:[1,0,1]
	v_pk_fma_f32 v[172:173], v[14:15], s[2:3], v[178:179] op_sel_hi:[1,0,1]
	v_pk_fma_f32 v[174:175], v[16:17], s[2:3], v[180:181] op_sel_hi:[1,0,1]
	v_pk_fma_f32 v[162:163], v[18:19], s[2:3], v[162:163] op_sel_hi:[1,0,1]
	v_pk_fma_f32 v[160:161], v[20:21], s[2:3], v[160:161] op_sel_hi:[1,0,1]
	v_pk_fma_f32 v[158:159], v[22:23], s[2:3], v[158:159] op_sel_hi:[1,0,1]
	v_pk_fma_f32 v[156:157], v[24:25], s[2:3], v[156:157] op_sel_hi:[1,0,1]
	v_pk_fma_f32 v[154:155], v[26:27], s[2:3], v[154:155] op_sel_hi:[1,0,1]
	v_pk_fma_f32 v[152:153], v[28:29], s[2:3], v[152:153] op_sel_hi:[1,0,1]
	v_pk_fma_f32 v[150:151], v[30:31], s[2:3], v[150:151] op_sel_hi:[1,0,1]
	v_readlane_b32 s2, v211, 29
	s_waitcnt vmcnt(20)
	v_cvt_scalef32_pk32_f32_fp6 v[0:31], v[50:55], 1.0
	v_pk_fma_f32 v[50:51], v[0:1], s[2:3], v[62:63] op_sel_hi:[1,0,1]
	v_pk_fma_f32 v[52:53], v[2:3], s[2:3], v[64:65] op_sel_hi:[1,0,1]
	v_pk_fma_f32 v[54:55], v[4:5], s[2:3], v[66:67] op_sel_hi:[1,0,1]
	v_pk_fma_f32 v[62:63], v[6:7], s[2:3], v[164:165] op_sel_hi:[1,0,1]
	v_pk_fma_f32 v[64:65], v[8:9], s[2:3], v[166:167] op_sel_hi:[1,0,1]
	v_pk_fma_f32 v[66:67], v[10:11], s[2:3], v[168:169] op_sel_hi:[1,0,1]
	v_pk_fma_f32 v[164:165], v[12:13], s[2:3], v[170:171] op_sel_hi:[1,0,1]
	v_pk_fma_f32 v[166:167], v[14:15], s[2:3], v[172:173] op_sel_hi:[1,0,1]
	v_pk_fma_f32 v[168:169], v[16:17], s[2:3], v[174:175] op_sel_hi:[1,0,1]
	v_pk_fma_f32 v[162:163], v[18:19], s[2:3], v[162:163] op_sel_hi:[1,0,1]
	v_pk_fma_f32 v[160:161], v[20:21], s[2:3], v[160:161] op_sel_hi:[1,0,1]
	v_pk_fma_f32 v[158:159], v[22:23], s[2:3], v[158:159] op_sel_hi:[1,0,1]
	v_pk_fma_f32 v[156:157], v[24:25], s[2:3], v[156:157] op_sel_hi:[1,0,1]
	v_pk_fma_f32 v[154:155], v[26:27], s[2:3], v[154:155] op_sel_hi:[1,0,1]
	v_pk_fma_f32 v[152:153], v[28:29], s[2:3], v[152:153] op_sel_hi:[1,0,1]
	v_pk_fma_f32 v[150:151], v[30:31], s[2:3], v[150:151] op_sel_hi:[1,0,1]
	v_readlane_b32 s2, v211, 30
	s_waitcnt vmcnt(18)
	v_cvt_scalef32_pk32_f32_fp6 v[0:31], v[38:43], 1.0
	v_pk_fma_f32 v[38:39], v[0:1], s[2:3], v[50:51] op_sel_hi:[1,0,1]
	v_pk_fma_f32 v[40:41], v[2:3], s[2:3], v[52:53] op_sel_hi:[1,0,1]
	v_pk_fma_f32 v[42:43], v[4:5], s[2:3], v[54:55] op_sel_hi:[1,0,1]
	v_pk_fma_f32 v[50:51], v[6:7], s[2:3], v[62:63] op_sel_hi:[1,0,1]
	v_pk_fma_f32 v[52:53], v[8:9], s[2:3], v[64:65] op_sel_hi:[1,0,1]
	v_pk_fma_f32 v[54:55], v[10:11], s[2:3], v[66:67] op_sel_hi:[1,0,1]
	v_pk_fma_f32 v[62:63], v[12:13], s[2:3], v[164:165] op_sel_hi:[1,0,1]
	v_pk_fma_f32 v[64:65], v[14:15], s[2:3], v[166:167] op_sel_hi:[1,0,1]
	v_pk_fma_f32 v[66:67], v[16:17], s[2:3], v[168:169] op_sel_hi:[1,0,1]
	v_pk_fma_f32 v[162:163], v[18:19], s[2:3], v[162:163] op_sel_hi:[1,0,1]
	v_pk_fma_f32 v[160:161], v[20:21], s[2:3], v[160:161] op_sel_hi:[1,0,1]
	v_pk_fma_f32 v[158:159], v[22:23], s[2:3], v[158:159] op_sel_hi:[1,0,1]
	v_pk_fma_f32 v[156:157], v[24:25], s[2:3], v[156:157] op_sel_hi:[1,0,1]
	v_pk_fma_f32 v[154:155], v[26:27], s[2:3], v[154:155] op_sel_hi:[1,0,1]
	v_pk_fma_f32 v[152:153], v[28:29], s[2:3], v[152:153] op_sel_hi:[1,0,1]
	v_pk_fma_f32 v[150:151], v[30:31], s[2:3], v[150:151] op_sel_hi:[1,0,1]
	v_readlane_b32 s2, v211, 31
	s_waitcnt vmcnt(16)
	v_cvt_scalef32_pk32_f32_fp6 v[0:31], v[32:37], 1.0
	v_pk_fma_f32 v[164:165], v[0:1], s[2:3], v[38:39] op_sel_hi:[1,0,1]
	v_pk_fma_f32 v[166:167], v[2:3], s[2:3], v[40:41] op_sel_hi:[1,0,1]
	v_pk_fma_f32 v[168:169], v[4:5], s[2:3], v[42:43] op_sel_hi:[1,0,1]
	v_pk_fma_f32 v[170:171], v[6:7], s[2:3], v[50:51] op_sel_hi:[1,0,1]
	v_pk_fma_f32 v[172:173], v[8:9], s[2:3], v[52:53] op_sel_hi:[1,0,1]
	v_pk_fma_f32 v[174:175], v[10:11], s[2:3], v[54:55] op_sel_hi:[1,0,1]
	v_pk_fma_f32 v[176:177], v[12:13], s[2:3], v[62:63] op_sel_hi:[1,0,1]
	v_pk_fma_f32 v[178:179], v[14:15], s[2:3], v[64:65] op_sel_hi:[1,0,1]
	v_pk_fma_f32 v[180:181], v[16:17], s[2:3], v[66:67] op_sel_hi:[1,0,1]
	v_pk_fma_f32 v[162:163], v[18:19], s[2:3], v[162:163] op_sel_hi:[1,0,1]
	v_pk_fma_f32 v[160:161], v[20:21], s[2:3], v[160:161] op_sel_hi:[1,0,1]
	v_pk_fma_f32 v[158:159], v[22:23], s[2:3], v[158:159] op_sel_hi:[1,0,1]
	v_pk_fma_f32 v[156:157], v[24:25], s[2:3], v[156:157] op_sel_hi:[1,0,1]
	v_pk_fma_f32 v[154:155], v[26:27], s[2:3], v[154:155] op_sel_hi:[1,0,1]
	v_pk_fma_f32 v[152:153], v[28:29], s[2:3], v[152:153] op_sel_hi:[1,0,1]
	v_pk_fma_f32 v[150:151], v[30:31], s[2:3], v[150:151] op_sel_hi:[1,0,1]
	v_readlane_b32 s2, v240, 40
	v_readlane_b32 s3, v240, 41
	v_readlane_b32 s100, v240, 42
	v_readlane_b32 s101, v240, 43
	s_nop 1
	buffer_load_dwordx4 v[62:65], v129, s[44:47], s2 offen
	buffer_load_dwordx2 v[66:67], v210, s[44:47], s2 offen
	buffer_load_dwordx4 v[50:53], v129, s[44:47], s3 offen
	buffer_load_dwordx2 v[54:55], v210, s[44:47], s3 offen
	buffer_load_dwordx4 v[38:41], v129, s[44:47], s100 offen
	buffer_load_dwordx2 v[42:43], v210, s[44:47], s100 offen
	buffer_load_dwordx4 v[32:35], v129, s[44:47], s101 offen
	buffer_load_dwordx2 v[36:37], v210, s[44:47], s101 offen
	v_readlane_b32 s2, v211, 32
	s_waitcnt vmcnt(22)
	v_cvt_scalef32_pk32_f32_fp6 v[0:31], v[98:103], 1.0
	v_pk_fma_f32 v[98:99], v[0:1], s[2:3], v[164:165] op_sel_hi:[1,0,1]
	v_pk_fma_f32 v[100:101], v[2:3], s[2:3], v[166:167] op_sel_hi:[1,0,1]
	v_pk_fma_f32 v[102:103], v[4:5], s[2:3], v[168:169] op_sel_hi:[1,0,1]
	v_pk_fma_f32 v[164:165], v[6:7], s[2:3], v[170:171] op_sel_hi:[1,0,1]
	v_pk_fma_f32 v[166:167], v[8:9], s[2:3], v[172:173] op_sel_hi:[1,0,1]
	v_pk_fma_f32 v[168:169], v[10:11], s[2:3], v[174:175] op_sel_hi:[1,0,1]
	v_pk_fma_f32 v[170:171], v[12:13], s[2:3], v[176:177] op_sel_hi:[1,0,1]
	v_pk_fma_f32 v[172:173], v[14:15], s[2:3], v[178:179] op_sel_hi:[1,0,1]
	v_pk_fma_f32 v[174:175], v[16:17], s[2:3], v[180:181] op_sel_hi:[1,0,1]
	v_pk_fma_f32 v[162:163], v[18:19], s[2:3], v[162:163] op_sel_hi:[1,0,1]
	v_pk_fma_f32 v[160:161], v[20:21], s[2:3], v[160:161] op_sel_hi:[1,0,1]
	v_pk_fma_f32 v[158:159], v[22:23], s[2:3], v[158:159] op_sel_hi:[1,0,1]
	v_pk_fma_f32 v[156:157], v[24:25], s[2:3], v[156:157] op_sel_hi:[1,0,1]
	v_pk_fma_f32 v[154:155], v[26:27], s[2:3], v[154:155] op_sel_hi:[1,0,1]
	v_pk_fma_f32 v[152:153], v[28:29], s[2:3], v[152:153] op_sel_hi:[1,0,1]
	v_pk_fma_f32 v[150:151], v[30:31], s[2:3], v[150:151] op_sel_hi:[1,0,1]
	v_readlane_b32 s2, v211, 33
	s_waitcnt vmcnt(20)
	v_cvt_scalef32_pk32_f32_fp6 v[0:31], v[92:97], 1.0
	v_pk_fma_f32 v[92:93], v[0:1], s[2:3], v[98:99] op_sel_hi:[1,0,1]
	v_pk_fma_f32 v[94:95], v[2:3], s[2:3], v[100:101] op_sel_hi:[1,0,1]
	v_pk_fma_f32 v[96:97], v[4:5], s[2:3], v[102:103] op_sel_hi:[1,0,1]
	v_pk_fma_f32 v[98:99], v[6:7], s[2:3], v[164:165] op_sel_hi:[1,0,1]
	v_pk_fma_f32 v[100:101], v[8:9], s[2:3], v[166:167] op_sel_hi:[1,0,1]
	v_pk_fma_f32 v[102:103], v[10:11], s[2:3], v[168:169] op_sel_hi:[1,0,1]
	v_pk_fma_f32 v[164:165], v[12:13], s[2:3], v[170:171] op_sel_hi:[1,0,1]
	v_pk_fma_f32 v[166:167], v[14:15], s[2:3], v[172:173] op_sel_hi:[1,0,1]
	v_pk_fma_f32 v[168:169], v[16:17], s[2:3], v[174:175] op_sel_hi:[1,0,1]
	v_pk_fma_f32 v[162:163], v[18:19], s[2:3], v[162:163] op_sel_hi:[1,0,1]
	v_pk_fma_f32 v[160:161], v[20:21], s[2:3], v[160:161] op_sel_hi:[1,0,1]
	v_pk_fma_f32 v[158:159], v[22:23], s[2:3], v[158:159] op_sel_hi:[1,0,1]
	v_pk_fma_f32 v[156:157], v[24:25], s[2:3], v[156:157] op_sel_hi:[1,0,1]
	v_pk_fma_f32 v[154:155], v[26:27], s[2:3], v[154:155] op_sel_hi:[1,0,1]
	v_pk_fma_f32 v[152:153], v[28:29], s[2:3], v[152:153] op_sel_hi:[1,0,1]
	v_pk_fma_f32 v[150:151], v[30:31], s[2:3], v[150:151] op_sel_hi:[1,0,1]
	v_readlane_b32 s2, v211, 34
	s_waitcnt vmcnt(18)
	v_cvt_scalef32_pk32_f32_fp6 v[0:31], v[86:91], 1.0
	v_pk_fma_f32 v[86:87], v[0:1], s[2:3], v[92:93] op_sel_hi:[1,0,1]
	v_pk_fma_f32 v[88:89], v[2:3], s[2:3], v[94:95] op_sel_hi:[1,0,1]
	v_pk_fma_f32 v[90:91], v[4:5], s[2:3], v[96:97] op_sel_hi:[1,0,1]
	v_pk_fma_f32 v[92:93], v[6:7], s[2:3], v[98:99] op_sel_hi:[1,0,1]
	v_pk_fma_f32 v[94:95], v[8:9], s[2:3], v[100:101] op_sel_hi:[1,0,1]
	v_pk_fma_f32 v[96:97], v[10:11], s[2:3], v[102:103] op_sel_hi:[1,0,1]
	v_pk_fma_f32 v[98:99], v[12:13], s[2:3], v[164:165] op_sel_hi:[1,0,1]
	v_pk_fma_f32 v[100:101], v[14:15], s[2:3], v[166:167] op_sel_hi:[1,0,1]
	v_pk_fma_f32 v[102:103], v[16:17], s[2:3], v[168:169] op_sel_hi:[1,0,1]
	v_pk_fma_f32 v[162:163], v[18:19], s[2:3], v[162:163] op_sel_hi:[1,0,1]
	v_pk_fma_f32 v[160:161], v[20:21], s[2:3], v[160:161] op_sel_hi:[1,0,1]
	v_pk_fma_f32 v[158:159], v[22:23], s[2:3], v[158:159] op_sel_hi:[1,0,1]
	v_pk_fma_f32 v[156:157], v[24:25], s[2:3], v[156:157] op_sel_hi:[1,0,1]
	v_pk_fma_f32 v[154:155], v[26:27], s[2:3], v[154:155] op_sel_hi:[1,0,1]
	v_pk_fma_f32 v[152:153], v[28:29], s[2:3], v[152:153] op_sel_hi:[1,0,1]
	v_pk_fma_f32 v[150:151], v[30:31], s[2:3], v[150:151] op_sel_hi:[1,0,1]
	v_readlane_b32 s2, v211, 35
	s_waitcnt vmcnt(16)
	v_cvt_scalef32_pk32_f32_fp6 v[0:31], v[80:85], 1.0
	v_pk_fma_f32 v[180:181], v[0:1], s[2:3], v[86:87] op_sel_hi:[1,0,1]
	v_pk_fma_f32 v[178:179], v[2:3], s[2:3], v[88:89] op_sel_hi:[1,0,1]
	v_pk_fma_f32 v[176:177], v[4:5], s[2:3], v[90:91] op_sel_hi:[1,0,1]
	v_pk_fma_f32 v[174:175], v[6:7], s[2:3], v[92:93] op_sel_hi:[1,0,1]
	v_pk_fma_f32 v[172:173], v[8:9], s[2:3], v[94:95] op_sel_hi:[1,0,1]
	v_pk_fma_f32 v[170:171], v[10:11], s[2:3], v[96:97] op_sel_hi:[1,0,1]
	v_pk_fma_f32 v[168:169], v[12:13], s[2:3], v[98:99] op_sel_hi:[1,0,1]
	v_pk_fma_f32 v[166:167], v[14:15], s[2:3], v[100:101] op_sel_hi:[1,0,1]
	v_pk_fma_f32 v[164:165], v[16:17], s[2:3], v[102:103] op_sel_hi:[1,0,1]
	v_pk_fma_f32 v[162:163], v[18:19], s[2:3], v[162:163] op_sel_hi:[1,0,1]
	v_pk_fma_f32 v[160:161], v[20:21], s[2:3], v[160:161] op_sel_hi:[1,0,1]
	v_pk_fma_f32 v[158:159], v[22:23], s[2:3], v[158:159] op_sel_hi:[1,0,1]
	v_pk_fma_f32 v[156:157], v[24:25], s[2:3], v[156:157] op_sel_hi:[1,0,1]
	v_pk_fma_f32 v[154:155], v[26:27], s[2:3], v[154:155] op_sel_hi:[1,0,1]
	v_pk_fma_f32 v[152:153], v[28:29], s[2:3], v[152:153] op_sel_hi:[1,0,1]
	v_pk_fma_f32 v[150:151], v[30:31], s[2:3], v[150:151] op_sel_hi:[1,0,1]
	v_readlane_b32 s2, v240, 44
	v_readlane_b32 s3, v240, 45
	v_readlane_b32 s100, v240, 46
	v_readlane_b32 s101, v240, 47
	s_nop 1
	buffer_load_dwordx4 v[98:101], v129, s[44:47], s2 offen
	buffer_load_dwordx2 v[102:103], v210, s[44:47], s2 offen
	buffer_load_dwordx4 v[92:95], v129, s[44:47], s3 offen
	buffer_load_dwordx2 v[96:97], v210, s[44:47], s3 offen
	buffer_load_dwordx4 v[86:89], v129, s[44:47], s100 offen
	buffer_load_dwordx2 v[90:91], v210, s[44:47], s100 offen
	buffer_load_dwordx4 v[80:83], v129, s[44:47], s101 offen
	buffer_load_dwordx2 v[84:85], v210, s[44:47], s101 offen
	v_readlane_b32 s2, v211, 36
	s_waitcnt vmcnt(22)
	v_cvt_scalef32_pk32_f32_fp6 v[0:31], v[74:79], 1.0
	v_pk_fma_f32 v[74:75], v[0:1], s[2:3], v[180:181] op_sel_hi:[1,0,1]
	v_pk_fma_f32 v[76:77], v[2:3], s[2:3], v[178:179] op_sel_hi:[1,0,1]
	v_pk_fma_f32 v[78:79], v[4:5], s[2:3], v[176:177] op_sel_hi:[1,0,1]
	v_pk_fma_f32 v[174:175], v[6:7], s[2:3], v[174:175] op_sel_hi:[1,0,1]
	v_pk_fma_f32 v[172:173], v[8:9], s[2:3], v[172:173] op_sel_hi:[1,0,1]
	v_pk_fma_f32 v[170:171], v[10:11], s[2:3], v[170:171] op_sel_hi:[1,0,1]
	v_pk_fma_f32 v[168:169], v[12:13], s[2:3], v[168:169] op_sel_hi:[1,0,1]
	v_pk_fma_f32 v[166:167], v[14:15], s[2:3], v[166:167] op_sel_hi:[1,0,1]
	v_pk_fma_f32 v[164:165], v[16:17], s[2:3], v[164:165] op_sel_hi:[1,0,1]
	v_pk_fma_f32 v[162:163], v[18:19], s[2:3], v[162:163] op_sel_hi:[1,0,1]
	v_pk_fma_f32 v[160:161], v[20:21], s[2:3], v[160:161] op_sel_hi:[1,0,1]
	v_pk_fma_f32 v[158:159], v[22:23], s[2:3], v[158:159] op_sel_hi:[1,0,1]
	v_pk_fma_f32 v[156:157], v[24:25], s[2:3], v[156:157] op_sel_hi:[1,0,1]
	v_pk_fma_f32 v[154:155], v[26:27], s[2:3], v[154:155] op_sel_hi:[1,0,1]
	v_pk_fma_f32 v[152:153], v[28:29], s[2:3], v[152:153] op_sel_hi:[1,0,1]
	v_pk_fma_f32 v[150:151], v[30:31], s[2:3], v[150:151] op_sel_hi:[1,0,1]
	v_readlane_b32 s2, v211, 37
	s_waitcnt vmcnt(20)
	v_cvt_scalef32_pk32_f32_fp6 v[0:31], v[68:73], 1.0
	v_pk_fma_f32 v[68:69], v[0:1], s[2:3], v[74:75] op_sel_hi:[1,0,1]
	v_pk_fma_f32 v[70:71], v[2:3], s[2:3], v[76:77] op_sel_hi:[1,0,1]
	v_pk_fma_f32 v[72:73], v[4:5], s[2:3], v[78:79] op_sel_hi:[1,0,1]
	v_pk_fma_f32 v[74:75], v[6:7], s[2:3], v[174:175] op_sel_hi:[1,0,1]
	v_pk_fma_f32 v[76:77], v[8:9], s[2:3], v[172:173] op_sel_hi:[1,0,1]
	v_pk_fma_f32 v[78:79], v[10:11], s[2:3], v[170:171] op_sel_hi:[1,0,1]
	v_pk_fma_f32 v[168:169], v[12:13], s[2:3], v[168:169] op_sel_hi:[1,0,1]
	v_pk_fma_f32 v[166:167], v[14:15], s[2:3], v[166:167] op_sel_hi:[1,0,1]
	v_pk_fma_f32 v[164:165], v[16:17], s[2:3], v[164:165] op_sel_hi:[1,0,1]
	v_pk_fma_f32 v[162:163], v[18:19], s[2:3], v[162:163] op_sel_hi:[1,0,1]
	v_pk_fma_f32 v[160:161], v[20:21], s[2:3], v[160:161] op_sel_hi:[1,0,1]
	v_pk_fma_f32 v[158:159], v[22:23], s[2:3], v[158:159] op_sel_hi:[1,0,1]
	v_pk_fma_f32 v[156:157], v[24:25], s[2:3], v[156:157] op_sel_hi:[1,0,1]
	v_pk_fma_f32 v[154:155], v[26:27], s[2:3], v[154:155] op_sel_hi:[1,0,1]
	v_pk_fma_f32 v[152:153], v[28:29], s[2:3], v[152:153] op_sel_hi:[1,0,1]
	v_pk_fma_f32 v[150:151], v[30:31], s[2:3], v[150:151] op_sel_hi:[1,0,1]
	v_readlane_b32 s2, v211, 38
	s_waitcnt vmcnt(18)
	v_cvt_scalef32_pk32_f32_fp6 v[0:31], v[56:61], 1.0
	v_pk_fma_f32 v[56:57], v[0:1], s[2:3], v[68:69] op_sel_hi:[1,0,1]
	v_pk_fma_f32 v[58:59], v[2:3], s[2:3], v[70:71] op_sel_hi:[1,0,1]
	v_pk_fma_f32 v[60:61], v[4:5], s[2:3], v[72:73] op_sel_hi:[1,0,1]
	v_pk_fma_f32 v[68:69], v[6:7], s[2:3], v[74:75] op_sel_hi:[1,0,1]
	v_pk_fma_f32 v[70:71], v[8:9], s[2:3], v[76:77] op_sel_hi:[1,0,1]
	v_pk_fma_f32 v[72:73], v[10:11], s[2:3], v[78:79] op_sel_hi:[1,0,1]
	v_pk_fma_f32 v[74:75], v[12:13], s[2:3], v[168:169] op_sel_hi:[1,0,1]
	v_pk_fma_f32 v[76:77], v[14:15], s[2:3], v[166:167] op_sel_hi:[1,0,1]
	v_pk_fma_f32 v[78:79], v[16:17], s[2:3], v[164:165] op_sel_hi:[1,0,1]
	v_pk_fma_f32 v[162:163], v[18:19], s[2:3], v[162:163] op_sel_hi:[1,0,1]
	v_pk_fma_f32 v[160:161], v[20:21], s[2:3], v[160:161] op_sel_hi:[1,0,1]
	v_pk_fma_f32 v[158:159], v[22:23], s[2:3], v[158:159] op_sel_hi:[1,0,1]
	v_pk_fma_f32 v[156:157], v[24:25], s[2:3], v[156:157] op_sel_hi:[1,0,1]
	v_pk_fma_f32 v[154:155], v[26:27], s[2:3], v[154:155] op_sel_hi:[1,0,1]
	v_pk_fma_f32 v[152:153], v[28:29], s[2:3], v[152:153] op_sel_hi:[1,0,1]
	v_pk_fma_f32 v[150:151], v[30:31], s[2:3], v[150:151] op_sel_hi:[1,0,1]
	v_readlane_b32 s2, v211, 39
	s_waitcnt vmcnt(16)
	v_cvt_scalef32_pk32_f32_fp6 v[0:31], v[44:49], 1.0
	v_pk_fma_f32 v[164:165], v[0:1], s[2:3], v[56:57] op_sel_hi:[1,0,1]
	v_pk_fma_f32 v[166:167], v[2:3], s[2:3], v[58:59] op_sel_hi:[1,0,1]
	v_pk_fma_f32 v[168:169], v[4:5], s[2:3], v[60:61] op_sel_hi:[1,0,1]
	v_pk_fma_f32 v[170:171], v[6:7], s[2:3], v[68:69] op_sel_hi:[1,0,1]
	v_pk_fma_f32 v[172:173], v[8:9], s[2:3], v[70:71] op_sel_hi:[1,0,1]
	v_pk_fma_f32 v[174:175], v[10:11], s[2:3], v[72:73] op_sel_hi:[1,0,1]
	v_pk_fma_f32 v[176:177], v[12:13], s[2:3], v[74:75] op_sel_hi:[1,0,1]
	v_pk_fma_f32 v[178:179], v[14:15], s[2:3], v[76:77] op_sel_hi:[1,0,1]
	v_pk_fma_f32 v[180:181], v[16:17], s[2:3], v[78:79] op_sel_hi:[1,0,1]
	v_pk_fma_f32 v[162:163], v[18:19], s[2:3], v[162:163] op_sel_hi:[1,0,1]
	v_pk_fma_f32 v[160:161], v[20:21], s[2:3], v[160:161] op_sel_hi:[1,0,1]
	v_pk_fma_f32 v[158:159], v[22:23], s[2:3], v[158:159] op_sel_hi:[1,0,1]
	v_pk_fma_f32 v[156:157], v[24:25], s[2:3], v[156:157] op_sel_hi:[1,0,1]
	v_pk_fma_f32 v[154:155], v[26:27], s[2:3], v[154:155] op_sel_hi:[1,0,1]
	v_pk_fma_f32 v[152:153], v[28:29], s[2:3], v[152:153] op_sel_hi:[1,0,1]
	v_pk_fma_f32 v[150:151], v[30:31], s[2:3], v[150:151] op_sel_hi:[1,0,1]
	v_readlane_b32 s2, v240, 48
	v_readlane_b32 s3, v240, 49
	v_readlane_b32 s100, v240, 50
	v_readlane_b32 s101, v240, 51
	s_nop 1
	buffer_load_dwordx4 v[74:77], v129, s[44:47], s2 offen
	buffer_load_dwordx2 v[78:79], v210, s[44:47], s2 offen
	buffer_load_dwordx4 v[68:71], v129, s[44:47], s3 offen
	buffer_load_dwordx2 v[72:73], v210, s[44:47], s3 offen
	buffer_load_dwordx4 v[56:59], v129, s[44:47], s100 offen
	buffer_load_dwordx2 v[60:61], v210, s[44:47], s100 offen
	buffer_load_dwordx4 v[44:47], v129, s[44:47], s101 offen
	buffer_load_dwordx2 v[48:49], v210, s[44:47], s101 offen
	v_readlane_b32 s2, v211, 40
	s_waitcnt vmcnt(22)
	v_cvt_scalef32_pk32_f32_fp6 v[0:31], v[62:67], 1.0
	v_pk_fma_f32 v[62:63], v[0:1], s[2:3], v[164:165] op_sel_hi:[1,0,1]
	v_pk_fma_f32 v[64:65], v[2:3], s[2:3], v[166:167] op_sel_hi:[1,0,1]
	v_pk_fma_f32 v[66:67], v[4:5], s[2:3], v[168:169] op_sel_hi:[1,0,1]
	v_pk_fma_f32 v[164:165], v[6:7], s[2:3], v[170:171] op_sel_hi:[1,0,1]
	v_pk_fma_f32 v[166:167], v[8:9], s[2:3], v[172:173] op_sel_hi:[1,0,1]
	v_pk_fma_f32 v[168:169], v[10:11], s[2:3], v[174:175] op_sel_hi:[1,0,1]
	v_pk_fma_f32 v[170:171], v[12:13], s[2:3], v[176:177] op_sel_hi:[1,0,1]
	v_pk_fma_f32 v[172:173], v[14:15], s[2:3], v[178:179] op_sel_hi:[1,0,1]
	v_pk_fma_f32 v[174:175], v[16:17], s[2:3], v[180:181] op_sel_hi:[1,0,1]
	v_pk_fma_f32 v[162:163], v[18:19], s[2:3], v[162:163] op_sel_hi:[1,0,1]
	v_pk_fma_f32 v[160:161], v[20:21], s[2:3], v[160:161] op_sel_hi:[1,0,1]
	v_pk_fma_f32 v[158:159], v[22:23], s[2:3], v[158:159] op_sel_hi:[1,0,1]
	v_pk_fma_f32 v[156:157], v[24:25], s[2:3], v[156:157] op_sel_hi:[1,0,1]
	v_pk_fma_f32 v[154:155], v[26:27], s[2:3], v[154:155] op_sel_hi:[1,0,1]
	v_pk_fma_f32 v[152:153], v[28:29], s[2:3], v[152:153] op_sel_hi:[1,0,1]
	v_pk_fma_f32 v[150:151], v[30:31], s[2:3], v[150:151] op_sel_hi:[1,0,1]
	v_readlane_b32 s2, v211, 41
	s_waitcnt vmcnt(20)
	v_cvt_scalef32_pk32_f32_fp6 v[0:31], v[50:55], 1.0
	v_pk_fma_f32 v[50:51], v[0:1], s[2:3], v[62:63] op_sel_hi:[1,0,1]
	v_pk_fma_f32 v[52:53], v[2:3], s[2:3], v[64:65] op_sel_hi:[1,0,1]
	v_pk_fma_f32 v[54:55], v[4:5], s[2:3], v[66:67] op_sel_hi:[1,0,1]
	v_pk_fma_f32 v[62:63], v[6:7], s[2:3], v[164:165] op_sel_hi:[1,0,1]
	v_pk_fma_f32 v[64:65], v[8:9], s[2:3], v[166:167] op_sel_hi:[1,0,1]
	v_pk_fma_f32 v[66:67], v[10:11], s[2:3], v[168:169] op_sel_hi:[1,0,1]
	v_pk_fma_f32 v[164:165], v[12:13], s[2:3], v[170:171] op_sel_hi:[1,0,1]
	v_pk_fma_f32 v[166:167], v[14:15], s[2:3], v[172:173] op_sel_hi:[1,0,1]
	v_pk_fma_f32 v[168:169], v[16:17], s[2:3], v[174:175] op_sel_hi:[1,0,1]
	v_pk_fma_f32 v[162:163], v[18:19], s[2:3], v[162:163] op_sel_hi:[1,0,1]
	v_pk_fma_f32 v[160:161], v[20:21], s[2:3], v[160:161] op_sel_hi:[1,0,1]
	v_pk_fma_f32 v[158:159], v[22:23], s[2:3], v[158:159] op_sel_hi:[1,0,1]
	v_pk_fma_f32 v[156:157], v[24:25], s[2:3], v[156:157] op_sel_hi:[1,0,1]
	v_pk_fma_f32 v[154:155], v[26:27], s[2:3], v[154:155] op_sel_hi:[1,0,1]
	v_pk_fma_f32 v[152:153], v[28:29], s[2:3], v[152:153] op_sel_hi:[1,0,1]
	v_pk_fma_f32 v[150:151], v[30:31], s[2:3], v[150:151] op_sel_hi:[1,0,1]
	v_readlane_b32 s2, v211, 42
	s_waitcnt vmcnt(18)
	v_cvt_scalef32_pk32_f32_fp6 v[0:31], v[38:43], 1.0
	v_pk_fma_f32 v[38:39], v[0:1], s[2:3], v[50:51] op_sel_hi:[1,0,1]
	v_pk_fma_f32 v[40:41], v[2:3], s[2:3], v[52:53] op_sel_hi:[1,0,1]
	v_pk_fma_f32 v[42:43], v[4:5], s[2:3], v[54:55] op_sel_hi:[1,0,1]
	v_pk_fma_f32 v[50:51], v[6:7], s[2:3], v[62:63] op_sel_hi:[1,0,1]
	v_pk_fma_f32 v[52:53], v[8:9], s[2:3], v[64:65] op_sel_hi:[1,0,1]
	v_pk_fma_f32 v[54:55], v[10:11], s[2:3], v[66:67] op_sel_hi:[1,0,1]
	v_pk_fma_f32 v[62:63], v[12:13], s[2:3], v[164:165] op_sel_hi:[1,0,1]
	v_pk_fma_f32 v[64:65], v[14:15], s[2:3], v[166:167] op_sel_hi:[1,0,1]
	v_pk_fma_f32 v[66:67], v[16:17], s[2:3], v[168:169] op_sel_hi:[1,0,1]
	v_pk_fma_f32 v[162:163], v[18:19], s[2:3], v[162:163] op_sel_hi:[1,0,1]
	v_pk_fma_f32 v[160:161], v[20:21], s[2:3], v[160:161] op_sel_hi:[1,0,1]
	v_pk_fma_f32 v[158:159], v[22:23], s[2:3], v[158:159] op_sel_hi:[1,0,1]
	v_pk_fma_f32 v[156:157], v[24:25], s[2:3], v[156:157] op_sel_hi:[1,0,1]
	v_pk_fma_f32 v[154:155], v[26:27], s[2:3], v[154:155] op_sel_hi:[1,0,1]
	v_pk_fma_f32 v[152:153], v[28:29], s[2:3], v[152:153] op_sel_hi:[1,0,1]
	v_pk_fma_f32 v[150:151], v[30:31], s[2:3], v[150:151] op_sel_hi:[1,0,1]
	v_readlane_b32 s2, v211, 43
	s_waitcnt vmcnt(16)
	v_cvt_scalef32_pk32_f32_fp6 v[0:31], v[32:37], 1.0
	v_pk_fma_f32 v[164:165], v[0:1], s[2:3], v[38:39] op_sel_hi:[1,0,1]
	v_pk_fma_f32 v[166:167], v[2:3], s[2:3], v[40:41] op_sel_hi:[1,0,1]
	v_pk_fma_f32 v[168:169], v[4:5], s[2:3], v[42:43] op_sel_hi:[1,0,1]
	v_pk_fma_f32 v[170:171], v[6:7], s[2:3], v[50:51] op_sel_hi:[1,0,1]
	v_pk_fma_f32 v[172:173], v[8:9], s[2:3], v[52:53] op_sel_hi:[1,0,1]
	v_pk_fma_f32 v[174:175], v[10:11], s[2:3], v[54:55] op_sel_hi:[1,0,1]
	v_pk_fma_f32 v[176:177], v[12:13], s[2:3], v[62:63] op_sel_hi:[1,0,1]
	v_pk_fma_f32 v[178:179], v[14:15], s[2:3], v[64:65] op_sel_hi:[1,0,1]
	v_pk_fma_f32 v[180:181], v[16:17], s[2:3], v[66:67] op_sel_hi:[1,0,1]
	v_pk_fma_f32 v[162:163], v[18:19], s[2:3], v[162:163] op_sel_hi:[1,0,1]
	v_pk_fma_f32 v[160:161], v[20:21], s[2:3], v[160:161] op_sel_hi:[1,0,1]
	v_pk_fma_f32 v[158:159], v[22:23], s[2:3], v[158:159] op_sel_hi:[1,0,1]
	v_pk_fma_f32 v[156:157], v[24:25], s[2:3], v[156:157] op_sel_hi:[1,0,1]
	v_pk_fma_f32 v[154:155], v[26:27], s[2:3], v[154:155] op_sel_hi:[1,0,1]
	v_pk_fma_f32 v[152:153], v[28:29], s[2:3], v[152:153] op_sel_hi:[1,0,1]
	v_pk_fma_f32 v[150:151], v[30:31], s[2:3], v[150:151] op_sel_hi:[1,0,1]
	v_readlane_b32 s2, v240, 52
	v_readlane_b32 s3, v240, 53
	v_readlane_b32 s100, v240, 54
	v_readlane_b32 s101, v240, 55
	s_nop 1
	buffer_load_dwordx4 v[62:65], v129, s[44:47], s2 offen
	buffer_load_dwordx2 v[66:67], v210, s[44:47], s2 offen
	buffer_load_dwordx4 v[50:53], v129, s[44:47], s3 offen
	buffer_load_dwordx2 v[54:55], v210, s[44:47], s3 offen
	buffer_load_dwordx4 v[38:41], v129, s[44:47], s100 offen
	buffer_load_dwordx2 v[42:43], v210, s[44:47], s100 offen
	buffer_load_dwordx4 v[32:35], v129, s[44:47], s101 offen
	buffer_load_dwordx2 v[36:37], v210, s[44:47], s101 offen
	v_readlane_b32 s2, v211, 44
	s_waitcnt vmcnt(22)
	v_cvt_scalef32_pk32_f32_fp6 v[0:31], v[98:103], 1.0
	v_pk_fma_f32 v[98:99], v[0:1], s[2:3], v[164:165] op_sel_hi:[1,0,1]
	v_pk_fma_f32 v[100:101], v[2:3], s[2:3], v[166:167] op_sel_hi:[1,0,1]
	v_pk_fma_f32 v[102:103], v[4:5], s[2:3], v[168:169] op_sel_hi:[1,0,1]
	v_pk_fma_f32 v[164:165], v[6:7], s[2:3], v[170:171] op_sel_hi:[1,0,1]
	v_pk_fma_f32 v[166:167], v[8:9], s[2:3], v[172:173] op_sel_hi:[1,0,1]
	v_pk_fma_f32 v[168:169], v[10:11], s[2:3], v[174:175] op_sel_hi:[1,0,1]
	v_pk_fma_f32 v[170:171], v[12:13], s[2:3], v[176:177] op_sel_hi:[1,0,1]
	v_pk_fma_f32 v[172:173], v[14:15], s[2:3], v[178:179] op_sel_hi:[1,0,1]
	v_pk_fma_f32 v[174:175], v[16:17], s[2:3], v[180:181] op_sel_hi:[1,0,1]
	v_pk_fma_f32 v[162:163], v[18:19], s[2:3], v[162:163] op_sel_hi:[1,0,1]
	v_pk_fma_f32 v[160:161], v[20:21], s[2:3], v[160:161] op_sel_hi:[1,0,1]
	v_pk_fma_f32 v[158:159], v[22:23], s[2:3], v[158:159] op_sel_hi:[1,0,1]
	v_pk_fma_f32 v[156:157], v[24:25], s[2:3], v[156:157] op_sel_hi:[1,0,1]
	v_pk_fma_f32 v[154:155], v[26:27], s[2:3], v[154:155] op_sel_hi:[1,0,1]
	v_pk_fma_f32 v[152:153], v[28:29], s[2:3], v[152:153] op_sel_hi:[1,0,1]
	v_pk_fma_f32 v[150:151], v[30:31], s[2:3], v[150:151] op_sel_hi:[1,0,1]
	v_readlane_b32 s2, v211, 45
	s_waitcnt vmcnt(20)
	v_cvt_scalef32_pk32_f32_fp6 v[0:31], v[92:97], 1.0
	v_pk_fma_f32 v[92:93], v[0:1], s[2:3], v[98:99] op_sel_hi:[1,0,1]
	v_pk_fma_f32 v[94:95], v[2:3], s[2:3], v[100:101] op_sel_hi:[1,0,1]
	v_pk_fma_f32 v[96:97], v[4:5], s[2:3], v[102:103] op_sel_hi:[1,0,1]
	v_pk_fma_f32 v[98:99], v[6:7], s[2:3], v[164:165] op_sel_hi:[1,0,1]
	v_pk_fma_f32 v[100:101], v[8:9], s[2:3], v[166:167] op_sel_hi:[1,0,1]
	v_pk_fma_f32 v[102:103], v[10:11], s[2:3], v[168:169] op_sel_hi:[1,0,1]
	v_pk_fma_f32 v[164:165], v[12:13], s[2:3], v[170:171] op_sel_hi:[1,0,1]
	v_pk_fma_f32 v[166:167], v[14:15], s[2:3], v[172:173] op_sel_hi:[1,0,1]
	v_pk_fma_f32 v[168:169], v[16:17], s[2:3], v[174:175] op_sel_hi:[1,0,1]
	v_pk_fma_f32 v[162:163], v[18:19], s[2:3], v[162:163] op_sel_hi:[1,0,1]
	v_pk_fma_f32 v[160:161], v[20:21], s[2:3], v[160:161] op_sel_hi:[1,0,1]
	v_pk_fma_f32 v[158:159], v[22:23], s[2:3], v[158:159] op_sel_hi:[1,0,1]
	v_pk_fma_f32 v[156:157], v[24:25], s[2:3], v[156:157] op_sel_hi:[1,0,1]
	v_pk_fma_f32 v[154:155], v[26:27], s[2:3], v[154:155] op_sel_hi:[1,0,1]
	v_pk_fma_f32 v[152:153], v[28:29], s[2:3], v[152:153] op_sel_hi:[1,0,1]
	v_pk_fma_f32 v[150:151], v[30:31], s[2:3], v[150:151] op_sel_hi:[1,0,1]
	v_readlane_b32 s2, v211, 46
	s_waitcnt vmcnt(18)
	v_cvt_scalef32_pk32_f32_fp6 v[0:31], v[86:91], 1.0
	v_pk_fma_f32 v[86:87], v[0:1], s[2:3], v[92:93] op_sel_hi:[1,0,1]
	v_pk_fma_f32 v[88:89], v[2:3], s[2:3], v[94:95] op_sel_hi:[1,0,1]
	v_pk_fma_f32 v[90:91], v[4:5], s[2:3], v[96:97] op_sel_hi:[1,0,1]
	v_pk_fma_f32 v[92:93], v[6:7], s[2:3], v[98:99] op_sel_hi:[1,0,1]
	v_pk_fma_f32 v[94:95], v[8:9], s[2:3], v[100:101] op_sel_hi:[1,0,1]
	v_pk_fma_f32 v[96:97], v[10:11], s[2:3], v[102:103] op_sel_hi:[1,0,1]
	v_pk_fma_f32 v[98:99], v[12:13], s[2:3], v[164:165] op_sel_hi:[1,0,1]
	v_pk_fma_f32 v[100:101], v[14:15], s[2:3], v[166:167] op_sel_hi:[1,0,1]
	v_pk_fma_f32 v[102:103], v[16:17], s[2:3], v[168:169] op_sel_hi:[1,0,1]
	v_pk_fma_f32 v[162:163], v[18:19], s[2:3], v[162:163] op_sel_hi:[1,0,1]
	v_pk_fma_f32 v[160:161], v[20:21], s[2:3], v[160:161] op_sel_hi:[1,0,1]
	v_pk_fma_f32 v[158:159], v[22:23], s[2:3], v[158:159] op_sel_hi:[1,0,1]
	v_pk_fma_f32 v[156:157], v[24:25], s[2:3], v[156:157] op_sel_hi:[1,0,1]
	v_pk_fma_f32 v[154:155], v[26:27], s[2:3], v[154:155] op_sel_hi:[1,0,1]
	v_pk_fma_f32 v[152:153], v[28:29], s[2:3], v[152:153] op_sel_hi:[1,0,1]
	v_pk_fma_f32 v[150:151], v[30:31], s[2:3], v[150:151] op_sel_hi:[1,0,1]
	v_readlane_b32 s2, v211, 47
	s_waitcnt vmcnt(16)
	v_cvt_scalef32_pk32_f32_fp6 v[0:31], v[80:85], 1.0
	v_pk_fma_f32 v[180:181], v[0:1], s[2:3], v[86:87] op_sel_hi:[1,0,1]
	v_pk_fma_f32 v[178:179], v[2:3], s[2:3], v[88:89] op_sel_hi:[1,0,1]
	v_pk_fma_f32 v[176:177], v[4:5], s[2:3], v[90:91] op_sel_hi:[1,0,1]
	v_pk_fma_f32 v[174:175], v[6:7], s[2:3], v[92:93] op_sel_hi:[1,0,1]
	v_pk_fma_f32 v[172:173], v[8:9], s[2:3], v[94:95] op_sel_hi:[1,0,1]
	v_pk_fma_f32 v[170:171], v[10:11], s[2:3], v[96:97] op_sel_hi:[1,0,1]
	v_pk_fma_f32 v[168:169], v[12:13], s[2:3], v[98:99] op_sel_hi:[1,0,1]
	v_pk_fma_f32 v[166:167], v[14:15], s[2:3], v[100:101] op_sel_hi:[1,0,1]
	v_pk_fma_f32 v[164:165], v[16:17], s[2:3], v[102:103] op_sel_hi:[1,0,1]
	v_pk_fma_f32 v[162:163], v[18:19], s[2:3], v[162:163] op_sel_hi:[1,0,1]
	v_pk_fma_f32 v[160:161], v[20:21], s[2:3], v[160:161] op_sel_hi:[1,0,1]
	v_pk_fma_f32 v[158:159], v[22:23], s[2:3], v[158:159] op_sel_hi:[1,0,1]
	v_pk_fma_f32 v[156:157], v[24:25], s[2:3], v[156:157] op_sel_hi:[1,0,1]
	v_pk_fma_f32 v[154:155], v[26:27], s[2:3], v[154:155] op_sel_hi:[1,0,1]
	v_pk_fma_f32 v[152:153], v[28:29], s[2:3], v[152:153] op_sel_hi:[1,0,1]
	v_pk_fma_f32 v[150:151], v[30:31], s[2:3], v[150:151] op_sel_hi:[1,0,1]
	v_readlane_b32 s2, v240, 56
	v_readlane_b32 s3, v240, 57
	v_readlane_b32 s100, v240, 58
	v_readlane_b32 s101, v240, 59
	s_nop 1
	buffer_load_dwordx4 v[98:101], v129, s[44:47], s2 offen
	buffer_load_dwordx2 v[102:103], v210, s[44:47], s2 offen
	buffer_load_dwordx4 v[92:95], v129, s[44:47], s3 offen
	buffer_load_dwordx2 v[96:97], v210, s[44:47], s3 offen
	buffer_load_dwordx4 v[86:89], v129, s[44:47], s100 offen
	buffer_load_dwordx2 v[90:91], v210, s[44:47], s100 offen
	buffer_load_dwordx4 v[80:83], v129, s[44:47], s101 offen
	buffer_load_dwordx2 v[84:85], v210, s[44:47], s101 offen
	v_readlane_b32 s2, v211, 48
	s_waitcnt vmcnt(22)
	v_cvt_scalef32_pk32_f32_fp6 v[0:31], v[74:79], 1.0
	v_pk_fma_f32 v[74:75], v[0:1], s[2:3], v[180:181] op_sel_hi:[1,0,1]
	v_pk_fma_f32 v[76:77], v[2:3], s[2:3], v[178:179] op_sel_hi:[1,0,1]
	v_pk_fma_f32 v[78:79], v[4:5], s[2:3], v[176:177] op_sel_hi:[1,0,1]
	v_pk_fma_f32 v[174:175], v[6:7], s[2:3], v[174:175] op_sel_hi:[1,0,1]
	v_pk_fma_f32 v[172:173], v[8:9], s[2:3], v[172:173] op_sel_hi:[1,0,1]
	v_pk_fma_f32 v[170:171], v[10:11], s[2:3], v[170:171] op_sel_hi:[1,0,1]
	v_pk_fma_f32 v[168:169], v[12:13], s[2:3], v[168:169] op_sel_hi:[1,0,1]
	v_pk_fma_f32 v[166:167], v[14:15], s[2:3], v[166:167] op_sel_hi:[1,0,1]
	v_pk_fma_f32 v[164:165], v[16:17], s[2:3], v[164:165] op_sel_hi:[1,0,1]
	v_pk_fma_f32 v[162:163], v[18:19], s[2:3], v[162:163] op_sel_hi:[1,0,1]
	v_pk_fma_f32 v[160:161], v[20:21], s[2:3], v[160:161] op_sel_hi:[1,0,1]
	v_pk_fma_f32 v[158:159], v[22:23], s[2:3], v[158:159] op_sel_hi:[1,0,1]
	v_pk_fma_f32 v[156:157], v[24:25], s[2:3], v[156:157] op_sel_hi:[1,0,1]
	v_pk_fma_f32 v[154:155], v[26:27], s[2:3], v[154:155] op_sel_hi:[1,0,1]
	v_pk_fma_f32 v[152:153], v[28:29], s[2:3], v[152:153] op_sel_hi:[1,0,1]
	v_pk_fma_f32 v[150:151], v[30:31], s[2:3], v[150:151] op_sel_hi:[1,0,1]
	v_readlane_b32 s2, v211, 49
	s_waitcnt vmcnt(20)
	v_cvt_scalef32_pk32_f32_fp6 v[0:31], v[68:73], 1.0
	v_pk_fma_f32 v[68:69], v[0:1], s[2:3], v[74:75] op_sel_hi:[1,0,1]
	v_pk_fma_f32 v[70:71], v[2:3], s[2:3], v[76:77] op_sel_hi:[1,0,1]
	v_pk_fma_f32 v[72:73], v[4:5], s[2:3], v[78:79] op_sel_hi:[1,0,1]
	v_pk_fma_f32 v[74:75], v[6:7], s[2:3], v[174:175] op_sel_hi:[1,0,1]
	v_pk_fma_f32 v[76:77], v[8:9], s[2:3], v[172:173] op_sel_hi:[1,0,1]
	v_pk_fma_f32 v[78:79], v[10:11], s[2:3], v[170:171] op_sel_hi:[1,0,1]
	v_pk_fma_f32 v[168:169], v[12:13], s[2:3], v[168:169] op_sel_hi:[1,0,1]
	v_pk_fma_f32 v[166:167], v[14:15], s[2:3], v[166:167] op_sel_hi:[1,0,1]
	v_pk_fma_f32 v[164:165], v[16:17], s[2:3], v[164:165] op_sel_hi:[1,0,1]
	v_pk_fma_f32 v[162:163], v[18:19], s[2:3], v[162:163] op_sel_hi:[1,0,1]
	v_pk_fma_f32 v[160:161], v[20:21], s[2:3], v[160:161] op_sel_hi:[1,0,1]
	v_pk_fma_f32 v[158:159], v[22:23], s[2:3], v[158:159] op_sel_hi:[1,0,1]
	v_pk_fma_f32 v[156:157], v[24:25], s[2:3], v[156:157] op_sel_hi:[1,0,1]
	v_pk_fma_f32 v[154:155], v[26:27], s[2:3], v[154:155] op_sel_hi:[1,0,1]
	v_pk_fma_f32 v[152:153], v[28:29], s[2:3], v[152:153] op_sel_hi:[1,0,1]
	v_pk_fma_f32 v[150:151], v[30:31], s[2:3], v[150:151] op_sel_hi:[1,0,1]
	v_readlane_b32 s2, v211, 50
	s_waitcnt vmcnt(18)
	v_cvt_scalef32_pk32_f32_fp6 v[0:31], v[56:61], 1.0
	v_pk_fma_f32 v[56:57], v[0:1], s[2:3], v[68:69] op_sel_hi:[1,0,1]
	v_pk_fma_f32 v[58:59], v[2:3], s[2:3], v[70:71] op_sel_hi:[1,0,1]
	v_pk_fma_f32 v[60:61], v[4:5], s[2:3], v[72:73] op_sel_hi:[1,0,1]
	v_pk_fma_f32 v[68:69], v[6:7], s[2:3], v[74:75] op_sel_hi:[1,0,1]
	v_pk_fma_f32 v[70:71], v[8:9], s[2:3], v[76:77] op_sel_hi:[1,0,1]
	v_pk_fma_f32 v[72:73], v[10:11], s[2:3], v[78:79] op_sel_hi:[1,0,1]
	v_pk_fma_f32 v[74:75], v[12:13], s[2:3], v[168:169] op_sel_hi:[1,0,1]
	v_pk_fma_f32 v[76:77], v[14:15], s[2:3], v[166:167] op_sel_hi:[1,0,1]
	v_pk_fma_f32 v[78:79], v[16:17], s[2:3], v[164:165] op_sel_hi:[1,0,1]
	v_pk_fma_f32 v[162:163], v[18:19], s[2:3], v[162:163] op_sel_hi:[1,0,1]
	v_pk_fma_f32 v[160:161], v[20:21], s[2:3], v[160:161] op_sel_hi:[1,0,1]
	v_pk_fma_f32 v[158:159], v[22:23], s[2:3], v[158:159] op_sel_hi:[1,0,1]
	v_pk_fma_f32 v[156:157], v[24:25], s[2:3], v[156:157] op_sel_hi:[1,0,1]
	v_pk_fma_f32 v[154:155], v[26:27], s[2:3], v[154:155] op_sel_hi:[1,0,1]
	v_pk_fma_f32 v[152:153], v[28:29], s[2:3], v[152:153] op_sel_hi:[1,0,1]
	v_pk_fma_f32 v[150:151], v[30:31], s[2:3], v[150:151] op_sel_hi:[1,0,1]
	v_readlane_b32 s2, v211, 51
	s_waitcnt vmcnt(16)
	v_cvt_scalef32_pk32_f32_fp6 v[0:31], v[44:49], 1.0
	v_pk_fma_f32 v[164:165], v[0:1], s[2:3], v[56:57] op_sel_hi:[1,0,1]
	v_pk_fma_f32 v[166:167], v[2:3], s[2:3], v[58:59] op_sel_hi:[1,0,1]
	v_pk_fma_f32 v[168:169], v[4:5], s[2:3], v[60:61] op_sel_hi:[1,0,1]
	v_pk_fma_f32 v[170:171], v[6:7], s[2:3], v[68:69] op_sel_hi:[1,0,1]
	v_pk_fma_f32 v[172:173], v[8:9], s[2:3], v[70:71] op_sel_hi:[1,0,1]
	v_pk_fma_f32 v[174:175], v[10:11], s[2:3], v[72:73] op_sel_hi:[1,0,1]
	v_pk_fma_f32 v[176:177], v[12:13], s[2:3], v[74:75] op_sel_hi:[1,0,1]
	v_pk_fma_f32 v[178:179], v[14:15], s[2:3], v[76:77] op_sel_hi:[1,0,1]
	v_pk_fma_f32 v[180:181], v[16:17], s[2:3], v[78:79] op_sel_hi:[1,0,1]
	v_pk_fma_f32 v[162:163], v[18:19], s[2:3], v[162:163] op_sel_hi:[1,0,1]
	v_pk_fma_f32 v[160:161], v[20:21], s[2:3], v[160:161] op_sel_hi:[1,0,1]
	v_pk_fma_f32 v[158:159], v[22:23], s[2:3], v[158:159] op_sel_hi:[1,0,1]
	v_pk_fma_f32 v[156:157], v[24:25], s[2:3], v[156:157] op_sel_hi:[1,0,1]
	v_pk_fma_f32 v[154:155], v[26:27], s[2:3], v[154:155] op_sel_hi:[1,0,1]
	v_pk_fma_f32 v[152:153], v[28:29], s[2:3], v[152:153] op_sel_hi:[1,0,1]
	v_pk_fma_f32 v[150:151], v[30:31], s[2:3], v[150:151] op_sel_hi:[1,0,1]
	v_readlane_b32 s2, v240, 60
	v_readlane_b32 s3, v240, 61
	v_readlane_b32 s100, v240, 62
	v_readlane_b32 s101, v240, 63
	s_nop 1
	buffer_load_dwordx4 v[74:77], v129, s[44:47], s2 offen
	buffer_load_dwordx2 v[78:79], v210, s[44:47], s2 offen
	buffer_load_dwordx4 v[68:71], v129, s[44:47], s3 offen
	buffer_load_dwordx2 v[72:73], v210, s[44:47], s3 offen
	buffer_load_dwordx4 v[56:59], v129, s[44:47], s100 offen
	buffer_load_dwordx2 v[60:61], v210, s[44:47], s100 offen
	buffer_load_dwordx4 v[44:47], v129, s[44:47], s101 offen
	buffer_load_dwordx2 v[48:49], v210, s[44:47], s101 offen
	v_readlane_b32 s2, v211, 52
	s_waitcnt vmcnt(22)
	v_cvt_scalef32_pk32_f32_fp6 v[0:31], v[62:67], 1.0
	v_pk_fma_f32 v[62:63], v[0:1], s[2:3], v[164:165] op_sel_hi:[1,0,1]
	v_pk_fma_f32 v[64:65], v[2:3], s[2:3], v[166:167] op_sel_hi:[1,0,1]
	v_pk_fma_f32 v[66:67], v[4:5], s[2:3], v[168:169] op_sel_hi:[1,0,1]
	v_pk_fma_f32 v[164:165], v[6:7], s[2:3], v[170:171] op_sel_hi:[1,0,1]
	v_pk_fma_f32 v[166:167], v[8:9], s[2:3], v[172:173] op_sel_hi:[1,0,1]
	v_pk_fma_f32 v[168:169], v[10:11], s[2:3], v[174:175] op_sel_hi:[1,0,1]
	v_pk_fma_f32 v[170:171], v[12:13], s[2:3], v[176:177] op_sel_hi:[1,0,1]
	v_pk_fma_f32 v[172:173], v[14:15], s[2:3], v[178:179] op_sel_hi:[1,0,1]
	v_pk_fma_f32 v[174:175], v[16:17], s[2:3], v[180:181] op_sel_hi:[1,0,1]
	v_pk_fma_f32 v[162:163], v[18:19], s[2:3], v[162:163] op_sel_hi:[1,0,1]
	v_pk_fma_f32 v[160:161], v[20:21], s[2:3], v[160:161] op_sel_hi:[1,0,1]
	v_pk_fma_f32 v[158:159], v[22:23], s[2:3], v[158:159] op_sel_hi:[1,0,1]
	v_pk_fma_f32 v[156:157], v[24:25], s[2:3], v[156:157] op_sel_hi:[1,0,1]
	v_pk_fma_f32 v[154:155], v[26:27], s[2:3], v[154:155] op_sel_hi:[1,0,1]
	v_pk_fma_f32 v[152:153], v[28:29], s[2:3], v[152:153] op_sel_hi:[1,0,1]
	v_pk_fma_f32 v[150:151], v[30:31], s[2:3], v[150:151] op_sel_hi:[1,0,1]
	v_readlane_b32 s2, v211, 53
	s_waitcnt vmcnt(20)
	v_cvt_scalef32_pk32_f32_fp6 v[0:31], v[50:55], 1.0
	v_pk_fma_f32 v[50:51], v[0:1], s[2:3], v[62:63] op_sel_hi:[1,0,1]
	v_pk_fma_f32 v[52:53], v[2:3], s[2:3], v[64:65] op_sel_hi:[1,0,1]
	v_pk_fma_f32 v[54:55], v[4:5], s[2:3], v[66:67] op_sel_hi:[1,0,1]
	v_pk_fma_f32 v[62:63], v[6:7], s[2:3], v[164:165] op_sel_hi:[1,0,1]
	v_pk_fma_f32 v[64:65], v[8:9], s[2:3], v[166:167] op_sel_hi:[1,0,1]
	v_pk_fma_f32 v[66:67], v[10:11], s[2:3], v[168:169] op_sel_hi:[1,0,1]
	v_pk_fma_f32 v[164:165], v[12:13], s[2:3], v[170:171] op_sel_hi:[1,0,1]
	v_pk_fma_f32 v[166:167], v[14:15], s[2:3], v[172:173] op_sel_hi:[1,0,1]
	v_pk_fma_f32 v[168:169], v[16:17], s[2:3], v[174:175] op_sel_hi:[1,0,1]
	v_pk_fma_f32 v[162:163], v[18:19], s[2:3], v[162:163] op_sel_hi:[1,0,1]
	v_pk_fma_f32 v[160:161], v[20:21], s[2:3], v[160:161] op_sel_hi:[1,0,1]
	v_pk_fma_f32 v[158:159], v[22:23], s[2:3], v[158:159] op_sel_hi:[1,0,1]
	v_pk_fma_f32 v[156:157], v[24:25], s[2:3], v[156:157] op_sel_hi:[1,0,1]
	v_pk_fma_f32 v[154:155], v[26:27], s[2:3], v[154:155] op_sel_hi:[1,0,1]
	v_pk_fma_f32 v[152:153], v[28:29], s[2:3], v[152:153] op_sel_hi:[1,0,1]
	v_pk_fma_f32 v[150:151], v[30:31], s[2:3], v[150:151] op_sel_hi:[1,0,1]
	v_readlane_b32 s2, v211, 54
	s_waitcnt vmcnt(18)
	v_cvt_scalef32_pk32_f32_fp6 v[0:31], v[38:43], 1.0
	v_pk_fma_f32 v[38:39], v[0:1], s[2:3], v[50:51] op_sel_hi:[1,0,1]
	v_pk_fma_f32 v[40:41], v[2:3], s[2:3], v[52:53] op_sel_hi:[1,0,1]
	v_pk_fma_f32 v[42:43], v[4:5], s[2:3], v[54:55] op_sel_hi:[1,0,1]
	v_pk_fma_f32 v[50:51], v[6:7], s[2:3], v[62:63] op_sel_hi:[1,0,1]
	v_pk_fma_f32 v[52:53], v[8:9], s[2:3], v[64:65] op_sel_hi:[1,0,1]
	v_pk_fma_f32 v[54:55], v[10:11], s[2:3], v[66:67] op_sel_hi:[1,0,1]
	v_pk_fma_f32 v[62:63], v[12:13], s[2:3], v[164:165] op_sel_hi:[1,0,1]
	v_pk_fma_f32 v[64:65], v[14:15], s[2:3], v[166:167] op_sel_hi:[1,0,1]
	v_pk_fma_f32 v[66:67], v[16:17], s[2:3], v[168:169] op_sel_hi:[1,0,1]
	v_pk_fma_f32 v[162:163], v[18:19], s[2:3], v[162:163] op_sel_hi:[1,0,1]
	v_pk_fma_f32 v[160:161], v[20:21], s[2:3], v[160:161] op_sel_hi:[1,0,1]
	v_pk_fma_f32 v[158:159], v[22:23], s[2:3], v[158:159] op_sel_hi:[1,0,1]
	v_pk_fma_f32 v[156:157], v[24:25], s[2:3], v[156:157] op_sel_hi:[1,0,1]
	v_pk_fma_f32 v[154:155], v[26:27], s[2:3], v[154:155] op_sel_hi:[1,0,1]
	v_pk_fma_f32 v[152:153], v[28:29], s[2:3], v[152:153] op_sel_hi:[1,0,1]
	v_pk_fma_f32 v[150:151], v[30:31], s[2:3], v[150:151] op_sel_hi:[1,0,1]
	v_readlane_b32 s2, v211, 55
	s_waitcnt vmcnt(16)
	v_cvt_scalef32_pk32_f32_fp6 v[0:31], v[32:37], 1.0
	v_pk_fma_f32 v[164:165], v[0:1], s[2:3], v[38:39] op_sel_hi:[1,0,1]
	v_pk_fma_f32 v[166:167], v[2:3], s[2:3], v[40:41] op_sel_hi:[1,0,1]
	v_pk_fma_f32 v[168:169], v[4:5], s[2:3], v[42:43] op_sel_hi:[1,0,1]
	v_pk_fma_f32 v[170:171], v[6:7], s[2:3], v[50:51] op_sel_hi:[1,0,1]
	v_pk_fma_f32 v[172:173], v[8:9], s[2:3], v[52:53] op_sel_hi:[1,0,1]
	v_pk_fma_f32 v[174:175], v[10:11], s[2:3], v[54:55] op_sel_hi:[1,0,1]
	v_pk_fma_f32 v[176:177], v[12:13], s[2:3], v[62:63] op_sel_hi:[1,0,1]
	v_pk_fma_f32 v[178:179], v[14:15], s[2:3], v[64:65] op_sel_hi:[1,0,1]
	v_pk_fma_f32 v[180:181], v[16:17], s[2:3], v[66:67] op_sel_hi:[1,0,1]
	v_pk_fma_f32 v[162:163], v[18:19], s[2:3], v[162:163] op_sel_hi:[1,0,1]
	v_pk_fma_f32 v[160:161], v[20:21], s[2:3], v[160:161] op_sel_hi:[1,0,1]
	v_pk_fma_f32 v[158:159], v[22:23], s[2:3], v[158:159] op_sel_hi:[1,0,1]
	v_pk_fma_f32 v[156:157], v[24:25], s[2:3], v[156:157] op_sel_hi:[1,0,1]
	v_pk_fma_f32 v[154:155], v[26:27], s[2:3], v[154:155] op_sel_hi:[1,0,1]
	v_pk_fma_f32 v[152:153], v[28:29], s[2:3], v[152:153] op_sel_hi:[1,0,1]
	v_pk_fma_f32 v[150:151], v[30:31], s[2:3], v[150:151] op_sel_hi:[1,0,1]
	v_readlane_b32 s2, v241, 0
	v_readlane_b32 s3, v241, 1
	v_readlane_b32 s100, v241, 2
	v_readlane_b32 s101, v241, 3
	s_nop 1
	buffer_load_dwordx4 v[62:65], v129, s[44:47], s2 offen
	buffer_load_dwordx2 v[66:67], v210, s[44:47], s2 offen
	buffer_load_dwordx4 v[50:53], v129, s[44:47], s3 offen
	buffer_load_dwordx2 v[54:55], v210, s[44:47], s3 offen
	buffer_load_dwordx4 v[38:41], v129, s[44:47], s100 offen
	buffer_load_dwordx2 v[42:43], v210, s[44:47], s100 offen
	buffer_load_dwordx4 v[32:35], v129, s[44:47], s101 offen
	buffer_load_dwordx2 v[36:37], v210, s[44:47], s101 offen
	v_readlane_b32 s2, v211, 56
	s_waitcnt vmcnt(22)
	v_cvt_scalef32_pk32_f32_fp6 v[0:31], v[98:103], 1.0
	v_pk_fma_f32 v[98:99], v[0:1], s[2:3], v[164:165] op_sel_hi:[1,0,1]
	v_pk_fma_f32 v[100:101], v[2:3], s[2:3], v[166:167] op_sel_hi:[1,0,1]
	v_pk_fma_f32 v[102:103], v[4:5], s[2:3], v[168:169] op_sel_hi:[1,0,1]
	v_pk_fma_f32 v[164:165], v[6:7], s[2:3], v[170:171] op_sel_hi:[1,0,1]
	v_pk_fma_f32 v[166:167], v[8:9], s[2:3], v[172:173] op_sel_hi:[1,0,1]
	v_pk_fma_f32 v[168:169], v[10:11], s[2:3], v[174:175] op_sel_hi:[1,0,1]
	v_pk_fma_f32 v[170:171], v[12:13], s[2:3], v[176:177] op_sel_hi:[1,0,1]
	v_pk_fma_f32 v[172:173], v[14:15], s[2:3], v[178:179] op_sel_hi:[1,0,1]
	v_pk_fma_f32 v[174:175], v[16:17], s[2:3], v[180:181] op_sel_hi:[1,0,1]
	v_pk_fma_f32 v[162:163], v[18:19], s[2:3], v[162:163] op_sel_hi:[1,0,1]
	v_pk_fma_f32 v[160:161], v[20:21], s[2:3], v[160:161] op_sel_hi:[1,0,1]
	v_pk_fma_f32 v[158:159], v[22:23], s[2:3], v[158:159] op_sel_hi:[1,0,1]
	v_pk_fma_f32 v[156:157], v[24:25], s[2:3], v[156:157] op_sel_hi:[1,0,1]
	v_pk_fma_f32 v[154:155], v[26:27], s[2:3], v[154:155] op_sel_hi:[1,0,1]
	v_pk_fma_f32 v[152:153], v[28:29], s[2:3], v[152:153] op_sel_hi:[1,0,1]
	v_pk_fma_f32 v[150:151], v[30:31], s[2:3], v[150:151] op_sel_hi:[1,0,1]
	v_readlane_b32 s2, v211, 57
	s_waitcnt vmcnt(20)
	v_cvt_scalef32_pk32_f32_fp6 v[0:31], v[92:97], 1.0
	v_pk_fma_f32 v[92:93], v[0:1], s[2:3], v[98:99] op_sel_hi:[1,0,1]
	v_pk_fma_f32 v[94:95], v[2:3], s[2:3], v[100:101] op_sel_hi:[1,0,1]
	v_pk_fma_f32 v[96:97], v[4:5], s[2:3], v[102:103] op_sel_hi:[1,0,1]
	v_pk_fma_f32 v[98:99], v[6:7], s[2:3], v[164:165] op_sel_hi:[1,0,1]
	v_pk_fma_f32 v[100:101], v[8:9], s[2:3], v[166:167] op_sel_hi:[1,0,1]
	v_pk_fma_f32 v[102:103], v[10:11], s[2:3], v[168:169] op_sel_hi:[1,0,1]
	v_pk_fma_f32 v[164:165], v[12:13], s[2:3], v[170:171] op_sel_hi:[1,0,1]
	v_pk_fma_f32 v[166:167], v[14:15], s[2:3], v[172:173] op_sel_hi:[1,0,1]
	v_pk_fma_f32 v[168:169], v[16:17], s[2:3], v[174:175] op_sel_hi:[1,0,1]
	v_pk_fma_f32 v[162:163], v[18:19], s[2:3], v[162:163] op_sel_hi:[1,0,1]
	v_pk_fma_f32 v[160:161], v[20:21], s[2:3], v[160:161] op_sel_hi:[1,0,1]
	v_pk_fma_f32 v[158:159], v[22:23], s[2:3], v[158:159] op_sel_hi:[1,0,1]
	v_pk_fma_f32 v[156:157], v[24:25], s[2:3], v[156:157] op_sel_hi:[1,0,1]
	v_pk_fma_f32 v[154:155], v[26:27], s[2:3], v[154:155] op_sel_hi:[1,0,1]
	v_pk_fma_f32 v[152:153], v[28:29], s[2:3], v[152:153] op_sel_hi:[1,0,1]
	v_pk_fma_f32 v[150:151], v[30:31], s[2:3], v[150:151] op_sel_hi:[1,0,1]
	v_readlane_b32 s2, v211, 58
	s_waitcnt vmcnt(18)
	v_cvt_scalef32_pk32_f32_fp6 v[0:31], v[86:91], 1.0
	v_pk_fma_f32 v[86:87], v[0:1], s[2:3], v[92:93] op_sel_hi:[1,0,1]
	v_pk_fma_f32 v[88:89], v[2:3], s[2:3], v[94:95] op_sel_hi:[1,0,1]
	v_pk_fma_f32 v[90:91], v[4:5], s[2:3], v[96:97] op_sel_hi:[1,0,1]
	v_pk_fma_f32 v[92:93], v[6:7], s[2:3], v[98:99] op_sel_hi:[1,0,1]
	v_pk_fma_f32 v[94:95], v[8:9], s[2:3], v[100:101] op_sel_hi:[1,0,1]
	v_pk_fma_f32 v[96:97], v[10:11], s[2:3], v[102:103] op_sel_hi:[1,0,1]
	v_pk_fma_f32 v[98:99], v[12:13], s[2:3], v[164:165] op_sel_hi:[1,0,1]
	v_pk_fma_f32 v[100:101], v[14:15], s[2:3], v[166:167] op_sel_hi:[1,0,1]
	v_pk_fma_f32 v[102:103], v[16:17], s[2:3], v[168:169] op_sel_hi:[1,0,1]
	v_pk_fma_f32 v[162:163], v[18:19], s[2:3], v[162:163] op_sel_hi:[1,0,1]
	v_pk_fma_f32 v[160:161], v[20:21], s[2:3], v[160:161] op_sel_hi:[1,0,1]
	v_pk_fma_f32 v[158:159], v[22:23], s[2:3], v[158:159] op_sel_hi:[1,0,1]
	v_pk_fma_f32 v[156:157], v[24:25], s[2:3], v[156:157] op_sel_hi:[1,0,1]
	v_pk_fma_f32 v[154:155], v[26:27], s[2:3], v[154:155] op_sel_hi:[1,0,1]
	v_pk_fma_f32 v[152:153], v[28:29], s[2:3], v[152:153] op_sel_hi:[1,0,1]
	v_pk_fma_f32 v[150:151], v[30:31], s[2:3], v[150:151] op_sel_hi:[1,0,1]
	v_readlane_b32 s2, v211, 59
	s_waitcnt vmcnt(16)
	v_cvt_scalef32_pk32_f32_fp6 v[0:31], v[80:85], 1.0
	v_pk_fma_f32 v[180:181], v[0:1], s[2:3], v[86:87] op_sel_hi:[1,0,1]
	v_pk_fma_f32 v[178:179], v[2:3], s[2:3], v[88:89] op_sel_hi:[1,0,1]
	v_pk_fma_f32 v[176:177], v[4:5], s[2:3], v[90:91] op_sel_hi:[1,0,1]
	v_pk_fma_f32 v[174:175], v[6:7], s[2:3], v[92:93] op_sel_hi:[1,0,1]
	v_pk_fma_f32 v[172:173], v[8:9], s[2:3], v[94:95] op_sel_hi:[1,0,1]
	v_pk_fma_f32 v[170:171], v[10:11], s[2:3], v[96:97] op_sel_hi:[1,0,1]
	v_pk_fma_f32 v[168:169], v[12:13], s[2:3], v[98:99] op_sel_hi:[1,0,1]
	v_pk_fma_f32 v[166:167], v[14:15], s[2:3], v[100:101] op_sel_hi:[1,0,1]
	v_pk_fma_f32 v[164:165], v[16:17], s[2:3], v[102:103] op_sel_hi:[1,0,1]
	v_pk_fma_f32 v[162:163], v[18:19], s[2:3], v[162:163] op_sel_hi:[1,0,1]
	v_pk_fma_f32 v[160:161], v[20:21], s[2:3], v[160:161] op_sel_hi:[1,0,1]
	v_pk_fma_f32 v[158:159], v[22:23], s[2:3], v[158:159] op_sel_hi:[1,0,1]
	v_pk_fma_f32 v[156:157], v[24:25], s[2:3], v[156:157] op_sel_hi:[1,0,1]
	v_pk_fma_f32 v[154:155], v[26:27], s[2:3], v[154:155] op_sel_hi:[1,0,1]
	v_pk_fma_f32 v[152:153], v[28:29], s[2:3], v[152:153] op_sel_hi:[1,0,1]
	v_pk_fma_f32 v[150:151], v[30:31], s[2:3], v[150:151] op_sel_hi:[1,0,1]
	v_readlane_b32 s2, v241, 4
	v_readlane_b32 s3, v241, 5
	v_readlane_b32 s100, v241, 6
	v_readlane_b32 s101, v241, 7
	s_nop 1
	buffer_load_dwordx4 v[98:101], v129, s[44:47], s2 offen
	buffer_load_dwordx2 v[102:103], v210, s[44:47], s2 offen
	buffer_load_dwordx4 v[92:95], v129, s[44:47], s3 offen
	buffer_load_dwordx2 v[96:97], v210, s[44:47], s3 offen
	buffer_load_dwordx4 v[86:89], v129, s[44:47], s100 offen
	buffer_load_dwordx2 v[90:91], v210, s[44:47], s100 offen
	buffer_load_dwordx4 v[80:83], v129, s[44:47], s101 offen
	buffer_load_dwordx2 v[84:85], v210, s[44:47], s101 offen
	v_readlane_b32 s2, v211, 60
	s_waitcnt vmcnt(22)
	v_cvt_scalef32_pk32_f32_fp6 v[0:31], v[74:79], 1.0
	v_pk_fma_f32 v[74:75], v[0:1], s[2:3], v[180:181] op_sel_hi:[1,0,1]
	v_pk_fma_f32 v[76:77], v[2:3], s[2:3], v[178:179] op_sel_hi:[1,0,1]
	v_pk_fma_f32 v[78:79], v[4:5], s[2:3], v[176:177] op_sel_hi:[1,0,1]
	v_pk_fma_f32 v[174:175], v[6:7], s[2:3], v[174:175] op_sel_hi:[1,0,1]
	v_pk_fma_f32 v[172:173], v[8:9], s[2:3], v[172:173] op_sel_hi:[1,0,1]
	v_pk_fma_f32 v[170:171], v[10:11], s[2:3], v[170:171] op_sel_hi:[1,0,1]
	v_pk_fma_f32 v[168:169], v[12:13], s[2:3], v[168:169] op_sel_hi:[1,0,1]
	v_pk_fma_f32 v[166:167], v[14:15], s[2:3], v[166:167] op_sel_hi:[1,0,1]
	v_pk_fma_f32 v[164:165], v[16:17], s[2:3], v[164:165] op_sel_hi:[1,0,1]
	v_pk_fma_f32 v[162:163], v[18:19], s[2:3], v[162:163] op_sel_hi:[1,0,1]
	v_pk_fma_f32 v[160:161], v[20:21], s[2:3], v[160:161] op_sel_hi:[1,0,1]
	v_pk_fma_f32 v[158:159], v[22:23], s[2:3], v[158:159] op_sel_hi:[1,0,1]
	v_pk_fma_f32 v[156:157], v[24:25], s[2:3], v[156:157] op_sel_hi:[1,0,1]
	v_pk_fma_f32 v[154:155], v[26:27], s[2:3], v[154:155] op_sel_hi:[1,0,1]
	v_pk_fma_f32 v[152:153], v[28:29], s[2:3], v[152:153] op_sel_hi:[1,0,1]
	v_pk_fma_f32 v[150:151], v[30:31], s[2:3], v[150:151] op_sel_hi:[1,0,1]
	v_readlane_b32 s2, v211, 61
	s_waitcnt vmcnt(20)
	v_cvt_scalef32_pk32_f32_fp6 v[0:31], v[68:73], 1.0
	v_pk_fma_f32 v[68:69], v[0:1], s[2:3], v[74:75] op_sel_hi:[1,0,1]
	v_pk_fma_f32 v[70:71], v[2:3], s[2:3], v[76:77] op_sel_hi:[1,0,1]
	v_pk_fma_f32 v[72:73], v[4:5], s[2:3], v[78:79] op_sel_hi:[1,0,1]
	v_pk_fma_f32 v[74:75], v[6:7], s[2:3], v[174:175] op_sel_hi:[1,0,1]
	v_pk_fma_f32 v[76:77], v[8:9], s[2:3], v[172:173] op_sel_hi:[1,0,1]
	v_pk_fma_f32 v[78:79], v[10:11], s[2:3], v[170:171] op_sel_hi:[1,0,1]
	v_pk_fma_f32 v[168:169], v[12:13], s[2:3], v[168:169] op_sel_hi:[1,0,1]
	v_pk_fma_f32 v[166:167], v[14:15], s[2:3], v[166:167] op_sel_hi:[1,0,1]
	v_pk_fma_f32 v[164:165], v[16:17], s[2:3], v[164:165] op_sel_hi:[1,0,1]
	v_pk_fma_f32 v[162:163], v[18:19], s[2:3], v[162:163] op_sel_hi:[1,0,1]
	v_pk_fma_f32 v[160:161], v[20:21], s[2:3], v[160:161] op_sel_hi:[1,0,1]
	v_pk_fma_f32 v[158:159], v[22:23], s[2:3], v[158:159] op_sel_hi:[1,0,1]
	v_pk_fma_f32 v[156:157], v[24:25], s[2:3], v[156:157] op_sel_hi:[1,0,1]
	v_pk_fma_f32 v[154:155], v[26:27], s[2:3], v[154:155] op_sel_hi:[1,0,1]
	v_pk_fma_f32 v[152:153], v[28:29], s[2:3], v[152:153] op_sel_hi:[1,0,1]
	v_pk_fma_f32 v[150:151], v[30:31], s[2:3], v[150:151] op_sel_hi:[1,0,1]
	v_readlane_b32 s2, v211, 62
	s_waitcnt vmcnt(18)
	v_cvt_scalef32_pk32_f32_fp6 v[0:31], v[56:61], 1.0
	v_pk_fma_f32 v[56:57], v[0:1], s[2:3], v[68:69] op_sel_hi:[1,0,1]
	v_pk_fma_f32 v[58:59], v[2:3], s[2:3], v[70:71] op_sel_hi:[1,0,1]
	v_pk_fma_f32 v[60:61], v[4:5], s[2:3], v[72:73] op_sel_hi:[1,0,1]
	v_pk_fma_f32 v[68:69], v[6:7], s[2:3], v[74:75] op_sel_hi:[1,0,1]
	v_pk_fma_f32 v[70:71], v[8:9], s[2:3], v[76:77] op_sel_hi:[1,0,1]
	v_pk_fma_f32 v[72:73], v[10:11], s[2:3], v[78:79] op_sel_hi:[1,0,1]
	v_pk_fma_f32 v[74:75], v[12:13], s[2:3], v[168:169] op_sel_hi:[1,0,1]
	v_pk_fma_f32 v[76:77], v[14:15], s[2:3], v[166:167] op_sel_hi:[1,0,1]
	v_pk_fma_f32 v[78:79], v[16:17], s[2:3], v[164:165] op_sel_hi:[1,0,1]
	v_pk_fma_f32 v[162:163], v[18:19], s[2:3], v[162:163] op_sel_hi:[1,0,1]
	v_pk_fma_f32 v[160:161], v[20:21], s[2:3], v[160:161] op_sel_hi:[1,0,1]
	v_pk_fma_f32 v[158:159], v[22:23], s[2:3], v[158:159] op_sel_hi:[1,0,1]
	v_pk_fma_f32 v[156:157], v[24:25], s[2:3], v[156:157] op_sel_hi:[1,0,1]
	v_pk_fma_f32 v[154:155], v[26:27], s[2:3], v[154:155] op_sel_hi:[1,0,1]
	v_pk_fma_f32 v[152:153], v[28:29], s[2:3], v[152:153] op_sel_hi:[1,0,1]
	v_pk_fma_f32 v[150:151], v[30:31], s[2:3], v[150:151] op_sel_hi:[1,0,1]
	v_readlane_b32 s2, v211, 63
	s_waitcnt vmcnt(16)
	v_cvt_scalef32_pk32_f32_fp6 v[0:31], v[44:49], 1.0
	v_pk_fma_f32 v[164:165], v[0:1], s[2:3], v[56:57] op_sel_hi:[1,0,1]
	v_pk_fma_f32 v[166:167], v[2:3], s[2:3], v[58:59] op_sel_hi:[1,0,1]
	v_pk_fma_f32 v[168:169], v[4:5], s[2:3], v[60:61] op_sel_hi:[1,0,1]
	v_pk_fma_f32 v[170:171], v[6:7], s[2:3], v[68:69] op_sel_hi:[1,0,1]
	v_pk_fma_f32 v[172:173], v[8:9], s[2:3], v[70:71] op_sel_hi:[1,0,1]
	v_pk_fma_f32 v[174:175], v[10:11], s[2:3], v[72:73] op_sel_hi:[1,0,1]
	v_pk_fma_f32 v[176:177], v[12:13], s[2:3], v[74:75] op_sel_hi:[1,0,1]
	v_pk_fma_f32 v[178:179], v[14:15], s[2:3], v[76:77] op_sel_hi:[1,0,1]
	v_pk_fma_f32 v[180:181], v[16:17], s[2:3], v[78:79] op_sel_hi:[1,0,1]
	v_pk_fma_f32 v[162:163], v[18:19], s[2:3], v[162:163] op_sel_hi:[1,0,1]
	v_pk_fma_f32 v[160:161], v[20:21], s[2:3], v[160:161] op_sel_hi:[1,0,1]
	v_pk_fma_f32 v[158:159], v[22:23], s[2:3], v[158:159] op_sel_hi:[1,0,1]
	v_pk_fma_f32 v[156:157], v[24:25], s[2:3], v[156:157] op_sel_hi:[1,0,1]
	v_pk_fma_f32 v[154:155], v[26:27], s[2:3], v[154:155] op_sel_hi:[1,0,1]
	v_pk_fma_f32 v[152:153], v[28:29], s[2:3], v[152:153] op_sel_hi:[1,0,1]
	v_pk_fma_f32 v[150:151], v[30:31], s[2:3], v[150:151] op_sel_hi:[1,0,1]
	v_readlane_b32 s2, v241, 8
	v_readlane_b32 s3, v241, 9
	v_readlane_b32 s100, v241, 10
	v_readlane_b32 s101, v241, 11
	s_nop 1
	buffer_load_dwordx4 v[74:77], v129, s[44:47], s2 offen
	buffer_load_dwordx2 v[78:79], v210, s[44:47], s2 offen
	buffer_load_dwordx4 v[68:71], v129, s[44:47], s3 offen
	buffer_load_dwordx2 v[72:73], v210, s[44:47], s3 offen
	buffer_load_dwordx4 v[56:59], v129, s[44:47], s100 offen
	buffer_load_dwordx2 v[60:61], v210, s[44:47], s100 offen
	buffer_load_dwordx4 v[44:47], v129, s[44:47], s101 offen
	buffer_load_dwordx2 v[48:49], v210, s[44:47], s101 offen
	v_readlane_b32 s2, v131, 0
	s_waitcnt vmcnt(22)
	v_cvt_scalef32_pk32_f32_fp6 v[0:31], v[62:67], 1.0
	v_pk_fma_f32 v[62:63], v[0:1], s[2:3], v[164:165] op_sel_hi:[1,0,1]
	v_pk_fma_f32 v[64:65], v[2:3], s[2:3], v[166:167] op_sel_hi:[1,0,1]
	v_pk_fma_f32 v[66:67], v[4:5], s[2:3], v[168:169] op_sel_hi:[1,0,1]
	v_pk_fma_f32 v[164:165], v[6:7], s[2:3], v[170:171] op_sel_hi:[1,0,1]
	v_pk_fma_f32 v[166:167], v[8:9], s[2:3], v[172:173] op_sel_hi:[1,0,1]
	v_pk_fma_f32 v[168:169], v[10:11], s[2:3], v[174:175] op_sel_hi:[1,0,1]
	v_pk_fma_f32 v[170:171], v[12:13], s[2:3], v[176:177] op_sel_hi:[1,0,1]
	v_pk_fma_f32 v[172:173], v[14:15], s[2:3], v[178:179] op_sel_hi:[1,0,1]
	v_pk_fma_f32 v[174:175], v[16:17], s[2:3], v[180:181] op_sel_hi:[1,0,1]
	v_pk_fma_f32 v[162:163], v[18:19], s[2:3], v[162:163] op_sel_hi:[1,0,1]
	v_pk_fma_f32 v[160:161], v[20:21], s[2:3], v[160:161] op_sel_hi:[1,0,1]
	v_pk_fma_f32 v[158:159], v[22:23], s[2:3], v[158:159] op_sel_hi:[1,0,1]
	v_pk_fma_f32 v[156:157], v[24:25], s[2:3], v[156:157] op_sel_hi:[1,0,1]
	v_pk_fma_f32 v[154:155], v[26:27], s[2:3], v[154:155] op_sel_hi:[1,0,1]
	v_pk_fma_f32 v[152:153], v[28:29], s[2:3], v[152:153] op_sel_hi:[1,0,1]
	v_pk_fma_f32 v[150:151], v[30:31], s[2:3], v[150:151] op_sel_hi:[1,0,1]
	v_readlane_b32 s2, v131, 1
	s_waitcnt vmcnt(20)
	v_cvt_scalef32_pk32_f32_fp6 v[0:31], v[50:55], 1.0
	v_pk_fma_f32 v[50:51], v[0:1], s[2:3], v[62:63] op_sel_hi:[1,0,1]
	v_pk_fma_f32 v[52:53], v[2:3], s[2:3], v[64:65] op_sel_hi:[1,0,1]
	v_pk_fma_f32 v[54:55], v[4:5], s[2:3], v[66:67] op_sel_hi:[1,0,1]
	v_pk_fma_f32 v[62:63], v[6:7], s[2:3], v[164:165] op_sel_hi:[1,0,1]
	v_pk_fma_f32 v[64:65], v[8:9], s[2:3], v[166:167] op_sel_hi:[1,0,1]
	v_pk_fma_f32 v[66:67], v[10:11], s[2:3], v[168:169] op_sel_hi:[1,0,1]
	v_pk_fma_f32 v[164:165], v[12:13], s[2:3], v[170:171] op_sel_hi:[1,0,1]
	v_pk_fma_f32 v[166:167], v[14:15], s[2:3], v[172:173] op_sel_hi:[1,0,1]
	v_pk_fma_f32 v[168:169], v[16:17], s[2:3], v[174:175] op_sel_hi:[1,0,1]
	v_pk_fma_f32 v[162:163], v[18:19], s[2:3], v[162:163] op_sel_hi:[1,0,1]
	v_pk_fma_f32 v[160:161], v[20:21], s[2:3], v[160:161] op_sel_hi:[1,0,1]
	v_pk_fma_f32 v[158:159], v[22:23], s[2:3], v[158:159] op_sel_hi:[1,0,1]
	v_pk_fma_f32 v[156:157], v[24:25], s[2:3], v[156:157] op_sel_hi:[1,0,1]
	v_pk_fma_f32 v[154:155], v[26:27], s[2:3], v[154:155] op_sel_hi:[1,0,1]
	v_pk_fma_f32 v[152:153], v[28:29], s[2:3], v[152:153] op_sel_hi:[1,0,1]
	v_pk_fma_f32 v[150:151], v[30:31], s[2:3], v[150:151] op_sel_hi:[1,0,1]
	v_readlane_b32 s2, v131, 2
	s_waitcnt vmcnt(18)
	v_cvt_scalef32_pk32_f32_fp6 v[0:31], v[38:43], 1.0
	v_pk_fma_f32 v[38:39], v[0:1], s[2:3], v[50:51] op_sel_hi:[1,0,1]
	v_pk_fma_f32 v[40:41], v[2:3], s[2:3], v[52:53] op_sel_hi:[1,0,1]
	v_pk_fma_f32 v[42:43], v[4:5], s[2:3], v[54:55] op_sel_hi:[1,0,1]
	v_pk_fma_f32 v[50:51], v[6:7], s[2:3], v[62:63] op_sel_hi:[1,0,1]
	v_pk_fma_f32 v[52:53], v[8:9], s[2:3], v[64:65] op_sel_hi:[1,0,1]
	v_pk_fma_f32 v[54:55], v[10:11], s[2:3], v[66:67] op_sel_hi:[1,0,1]
	v_pk_fma_f32 v[62:63], v[12:13], s[2:3], v[164:165] op_sel_hi:[1,0,1]
	v_pk_fma_f32 v[64:65], v[14:15], s[2:3], v[166:167] op_sel_hi:[1,0,1]
	v_pk_fma_f32 v[66:67], v[16:17], s[2:3], v[168:169] op_sel_hi:[1,0,1]
	v_pk_fma_f32 v[162:163], v[18:19], s[2:3], v[162:163] op_sel_hi:[1,0,1]
	v_pk_fma_f32 v[160:161], v[20:21], s[2:3], v[160:161] op_sel_hi:[1,0,1]
	v_pk_fma_f32 v[158:159], v[22:23], s[2:3], v[158:159] op_sel_hi:[1,0,1]
	v_pk_fma_f32 v[156:157], v[24:25], s[2:3], v[156:157] op_sel_hi:[1,0,1]
	v_pk_fma_f32 v[154:155], v[26:27], s[2:3], v[154:155] op_sel_hi:[1,0,1]
	v_pk_fma_f32 v[152:153], v[28:29], s[2:3], v[152:153] op_sel_hi:[1,0,1]
	v_pk_fma_f32 v[150:151], v[30:31], s[2:3], v[150:151] op_sel_hi:[1,0,1]
	v_readlane_b32 s2, v131, 3
	s_waitcnt vmcnt(16)
	v_cvt_scalef32_pk32_f32_fp6 v[0:31], v[32:37], 1.0
	v_pk_fma_f32 v[164:165], v[0:1], s[2:3], v[38:39] op_sel_hi:[1,0,1]
	v_pk_fma_f32 v[166:167], v[2:3], s[2:3], v[40:41] op_sel_hi:[1,0,1]
	v_pk_fma_f32 v[168:169], v[4:5], s[2:3], v[42:43] op_sel_hi:[1,0,1]
	v_pk_fma_f32 v[170:171], v[6:7], s[2:3], v[50:51] op_sel_hi:[1,0,1]
	v_pk_fma_f32 v[172:173], v[8:9], s[2:3], v[52:53] op_sel_hi:[1,0,1]
	v_pk_fma_f32 v[174:175], v[10:11], s[2:3], v[54:55] op_sel_hi:[1,0,1]
	v_pk_fma_f32 v[176:177], v[12:13], s[2:3], v[62:63] op_sel_hi:[1,0,1]
	v_pk_fma_f32 v[178:179], v[14:15], s[2:3], v[64:65] op_sel_hi:[1,0,1]
	v_pk_fma_f32 v[180:181], v[16:17], s[2:3], v[66:67] op_sel_hi:[1,0,1]
	v_pk_fma_f32 v[162:163], v[18:19], s[2:3], v[162:163] op_sel_hi:[1,0,1]
	v_pk_fma_f32 v[160:161], v[20:21], s[2:3], v[160:161] op_sel_hi:[1,0,1]
	v_pk_fma_f32 v[158:159], v[22:23], s[2:3], v[158:159] op_sel_hi:[1,0,1]
	v_pk_fma_f32 v[156:157], v[24:25], s[2:3], v[156:157] op_sel_hi:[1,0,1]
	v_pk_fma_f32 v[154:155], v[26:27], s[2:3], v[154:155] op_sel_hi:[1,0,1]
	v_pk_fma_f32 v[152:153], v[28:29], s[2:3], v[152:153] op_sel_hi:[1,0,1]
	v_pk_fma_f32 v[150:151], v[30:31], s[2:3], v[150:151] op_sel_hi:[1,0,1]
	v_readlane_b32 s2, v241, 12
	v_readlane_b32 s3, v241, 13
	v_readlane_b32 s100, v241, 14
	v_readlane_b32 s101, v241, 15
	s_nop 1
	buffer_load_dwordx4 v[62:65], v129, s[44:47], s2 offen
	buffer_load_dwordx2 v[66:67], v210, s[44:47], s2 offen
	buffer_load_dwordx4 v[50:53], v129, s[44:47], s3 offen
	buffer_load_dwordx2 v[54:55], v210, s[44:47], s3 offen
	buffer_load_dwordx4 v[38:41], v129, s[44:47], s100 offen
	buffer_load_dwordx2 v[42:43], v210, s[44:47], s100 offen
	buffer_load_dwordx4 v[32:35], v129, s[44:47], s101 offen
	buffer_load_dwordx2 v[36:37], v210, s[44:47], s101 offen
	v_readlane_b32 s2, v131, 4
	s_waitcnt vmcnt(22)
	v_cvt_scalef32_pk32_f32_fp6 v[0:31], v[98:103], 1.0
	v_pk_fma_f32 v[98:99], v[0:1], s[2:3], v[164:165] op_sel_hi:[1,0,1]
	v_pk_fma_f32 v[100:101], v[2:3], s[2:3], v[166:167] op_sel_hi:[1,0,1]
	v_pk_fma_f32 v[102:103], v[4:5], s[2:3], v[168:169] op_sel_hi:[1,0,1]
	v_pk_fma_f32 v[164:165], v[6:7], s[2:3], v[170:171] op_sel_hi:[1,0,1]
	v_pk_fma_f32 v[166:167], v[8:9], s[2:3], v[172:173] op_sel_hi:[1,0,1]
	v_pk_fma_f32 v[168:169], v[10:11], s[2:3], v[174:175] op_sel_hi:[1,0,1]
	v_pk_fma_f32 v[170:171], v[12:13], s[2:3], v[176:177] op_sel_hi:[1,0,1]
	v_pk_fma_f32 v[172:173], v[14:15], s[2:3], v[178:179] op_sel_hi:[1,0,1]
	v_pk_fma_f32 v[174:175], v[16:17], s[2:3], v[180:181] op_sel_hi:[1,0,1]
	v_pk_fma_f32 v[162:163], v[18:19], s[2:3], v[162:163] op_sel_hi:[1,0,1]
	v_pk_fma_f32 v[160:161], v[20:21], s[2:3], v[160:161] op_sel_hi:[1,0,1]
	v_pk_fma_f32 v[158:159], v[22:23], s[2:3], v[158:159] op_sel_hi:[1,0,1]
	v_pk_fma_f32 v[156:157], v[24:25], s[2:3], v[156:157] op_sel_hi:[1,0,1]
	v_pk_fma_f32 v[154:155], v[26:27], s[2:3], v[154:155] op_sel_hi:[1,0,1]
	v_pk_fma_f32 v[152:153], v[28:29], s[2:3], v[152:153] op_sel_hi:[1,0,1]
	v_pk_fma_f32 v[150:151], v[30:31], s[2:3], v[150:151] op_sel_hi:[1,0,1]
	v_readlane_b32 s2, v131, 5
	s_waitcnt vmcnt(20)
	v_cvt_scalef32_pk32_f32_fp6 v[0:31], v[92:97], 1.0
	v_pk_fma_f32 v[92:93], v[0:1], s[2:3], v[98:99] op_sel_hi:[1,0,1]
	v_pk_fma_f32 v[94:95], v[2:3], s[2:3], v[100:101] op_sel_hi:[1,0,1]
	v_pk_fma_f32 v[96:97], v[4:5], s[2:3], v[102:103] op_sel_hi:[1,0,1]
	v_pk_fma_f32 v[98:99], v[6:7], s[2:3], v[164:165] op_sel_hi:[1,0,1]
	v_pk_fma_f32 v[100:101], v[8:9], s[2:3], v[166:167] op_sel_hi:[1,0,1]
	v_pk_fma_f32 v[102:103], v[10:11], s[2:3], v[168:169] op_sel_hi:[1,0,1]
	v_pk_fma_f32 v[164:165], v[12:13], s[2:3], v[170:171] op_sel_hi:[1,0,1]
	v_pk_fma_f32 v[166:167], v[14:15], s[2:3], v[172:173] op_sel_hi:[1,0,1]
	v_pk_fma_f32 v[168:169], v[16:17], s[2:3], v[174:175] op_sel_hi:[1,0,1]
	v_pk_fma_f32 v[162:163], v[18:19], s[2:3], v[162:163] op_sel_hi:[1,0,1]
	v_pk_fma_f32 v[160:161], v[20:21], s[2:3], v[160:161] op_sel_hi:[1,0,1]
	v_pk_fma_f32 v[158:159], v[22:23], s[2:3], v[158:159] op_sel_hi:[1,0,1]
	v_pk_fma_f32 v[156:157], v[24:25], s[2:3], v[156:157] op_sel_hi:[1,0,1]
	v_pk_fma_f32 v[154:155], v[26:27], s[2:3], v[154:155] op_sel_hi:[1,0,1]
	v_pk_fma_f32 v[152:153], v[28:29], s[2:3], v[152:153] op_sel_hi:[1,0,1]
	v_pk_fma_f32 v[150:151], v[30:31], s[2:3], v[150:151] op_sel_hi:[1,0,1]
	v_readlane_b32 s2, v131, 6
	s_waitcnt vmcnt(18)
	v_cvt_scalef32_pk32_f32_fp6 v[0:31], v[86:91], 1.0
	v_pk_fma_f32 v[86:87], v[0:1], s[2:3], v[92:93] op_sel_hi:[1,0,1]
	v_pk_fma_f32 v[88:89], v[2:3], s[2:3], v[94:95] op_sel_hi:[1,0,1]
	v_pk_fma_f32 v[90:91], v[4:5], s[2:3], v[96:97] op_sel_hi:[1,0,1]
	v_pk_fma_f32 v[92:93], v[6:7], s[2:3], v[98:99] op_sel_hi:[1,0,1]
	v_pk_fma_f32 v[94:95], v[8:9], s[2:3], v[100:101] op_sel_hi:[1,0,1]
	v_pk_fma_f32 v[96:97], v[10:11], s[2:3], v[102:103] op_sel_hi:[1,0,1]
	v_pk_fma_f32 v[98:99], v[12:13], s[2:3], v[164:165] op_sel_hi:[1,0,1]
	v_pk_fma_f32 v[100:101], v[14:15], s[2:3], v[166:167] op_sel_hi:[1,0,1]
	v_pk_fma_f32 v[102:103], v[16:17], s[2:3], v[168:169] op_sel_hi:[1,0,1]
	v_pk_fma_f32 v[162:163], v[18:19], s[2:3], v[162:163] op_sel_hi:[1,0,1]
	v_pk_fma_f32 v[160:161], v[20:21], s[2:3], v[160:161] op_sel_hi:[1,0,1]
	v_pk_fma_f32 v[158:159], v[22:23], s[2:3], v[158:159] op_sel_hi:[1,0,1]
	v_pk_fma_f32 v[156:157], v[24:25], s[2:3], v[156:157] op_sel_hi:[1,0,1]
	v_pk_fma_f32 v[154:155], v[26:27], s[2:3], v[154:155] op_sel_hi:[1,0,1]
	v_pk_fma_f32 v[152:153], v[28:29], s[2:3], v[152:153] op_sel_hi:[1,0,1]
	v_pk_fma_f32 v[150:151], v[30:31], s[2:3], v[150:151] op_sel_hi:[1,0,1]
	v_readlane_b32 s2, v131, 7
	s_waitcnt vmcnt(16)
	v_cvt_scalef32_pk32_f32_fp6 v[0:31], v[80:85], 1.0
	v_pk_fma_f32 v[180:181], v[0:1], s[2:3], v[86:87] op_sel_hi:[1,0,1]
	v_pk_fma_f32 v[178:179], v[2:3], s[2:3], v[88:89] op_sel_hi:[1,0,1]
	v_pk_fma_f32 v[176:177], v[4:5], s[2:3], v[90:91] op_sel_hi:[1,0,1]
	v_pk_fma_f32 v[174:175], v[6:7], s[2:3], v[92:93] op_sel_hi:[1,0,1]
	v_pk_fma_f32 v[172:173], v[8:9], s[2:3], v[94:95] op_sel_hi:[1,0,1]
	v_pk_fma_f32 v[170:171], v[10:11], s[2:3], v[96:97] op_sel_hi:[1,0,1]
	v_pk_fma_f32 v[168:169], v[12:13], s[2:3], v[98:99] op_sel_hi:[1,0,1]
	v_pk_fma_f32 v[166:167], v[14:15], s[2:3], v[100:101] op_sel_hi:[1,0,1]
	v_pk_fma_f32 v[164:165], v[16:17], s[2:3], v[102:103] op_sel_hi:[1,0,1]
	v_pk_fma_f32 v[162:163], v[18:19], s[2:3], v[162:163] op_sel_hi:[1,0,1]
	v_pk_fma_f32 v[160:161], v[20:21], s[2:3], v[160:161] op_sel_hi:[1,0,1]
	v_pk_fma_f32 v[158:159], v[22:23], s[2:3], v[158:159] op_sel_hi:[1,0,1]
	v_pk_fma_f32 v[156:157], v[24:25], s[2:3], v[156:157] op_sel_hi:[1,0,1]
	v_pk_fma_f32 v[154:155], v[26:27], s[2:3], v[154:155] op_sel_hi:[1,0,1]
	v_pk_fma_f32 v[152:153], v[28:29], s[2:3], v[152:153] op_sel_hi:[1,0,1]
	v_pk_fma_f32 v[150:151], v[30:31], s[2:3], v[150:151] op_sel_hi:[1,0,1]
	v_readlane_b32 s2, v241, 16
	v_readlane_b32 s3, v241, 17
	v_readlane_b32 s100, v241, 18
	v_readlane_b32 s101, v241, 19
	s_nop 1
	buffer_load_dwordx4 v[98:101], v129, s[44:47], s2 offen
	buffer_load_dwordx2 v[102:103], v210, s[44:47], s2 offen
	buffer_load_dwordx4 v[92:95], v129, s[44:47], s3 offen
	buffer_load_dwordx2 v[96:97], v210, s[44:47], s3 offen
	buffer_load_dwordx4 v[86:89], v129, s[44:47], s100 offen
	buffer_load_dwordx2 v[90:91], v210, s[44:47], s100 offen
	buffer_load_dwordx4 v[80:83], v129, s[44:47], s101 offen
	buffer_load_dwordx2 v[84:85], v210, s[44:47], s101 offen
	v_readlane_b32 s2, v131, 8
	s_waitcnt vmcnt(22)
	v_cvt_scalef32_pk32_f32_fp6 v[0:31], v[74:79], 1.0
	v_pk_fma_f32 v[74:75], v[0:1], s[2:3], v[180:181] op_sel_hi:[1,0,1]
	v_pk_fma_f32 v[76:77], v[2:3], s[2:3], v[178:179] op_sel_hi:[1,0,1]
	v_pk_fma_f32 v[78:79], v[4:5], s[2:3], v[176:177] op_sel_hi:[1,0,1]
	v_pk_fma_f32 v[174:175], v[6:7], s[2:3], v[174:175] op_sel_hi:[1,0,1]
	v_pk_fma_f32 v[172:173], v[8:9], s[2:3], v[172:173] op_sel_hi:[1,0,1]
	v_pk_fma_f32 v[170:171], v[10:11], s[2:3], v[170:171] op_sel_hi:[1,0,1]
	v_pk_fma_f32 v[168:169], v[12:13], s[2:3], v[168:169] op_sel_hi:[1,0,1]
	v_pk_fma_f32 v[166:167], v[14:15], s[2:3], v[166:167] op_sel_hi:[1,0,1]
	v_pk_fma_f32 v[164:165], v[16:17], s[2:3], v[164:165] op_sel_hi:[1,0,1]
	v_pk_fma_f32 v[162:163], v[18:19], s[2:3], v[162:163] op_sel_hi:[1,0,1]
	v_pk_fma_f32 v[160:161], v[20:21], s[2:3], v[160:161] op_sel_hi:[1,0,1]
	v_pk_fma_f32 v[158:159], v[22:23], s[2:3], v[158:159] op_sel_hi:[1,0,1]
	v_pk_fma_f32 v[156:157], v[24:25], s[2:3], v[156:157] op_sel_hi:[1,0,1]
	v_pk_fma_f32 v[154:155], v[26:27], s[2:3], v[154:155] op_sel_hi:[1,0,1]
	v_pk_fma_f32 v[152:153], v[28:29], s[2:3], v[152:153] op_sel_hi:[1,0,1]
	v_pk_fma_f32 v[150:151], v[30:31], s[2:3], v[150:151] op_sel_hi:[1,0,1]
	v_readlane_b32 s2, v131, 9
	s_waitcnt vmcnt(20)
	v_cvt_scalef32_pk32_f32_fp6 v[0:31], v[68:73], 1.0
	v_pk_fma_f32 v[68:69], v[0:1], s[2:3], v[74:75] op_sel_hi:[1,0,1]
	v_pk_fma_f32 v[70:71], v[2:3], s[2:3], v[76:77] op_sel_hi:[1,0,1]
	v_pk_fma_f32 v[72:73], v[4:5], s[2:3], v[78:79] op_sel_hi:[1,0,1]
	v_pk_fma_f32 v[74:75], v[6:7], s[2:3], v[174:175] op_sel_hi:[1,0,1]
	v_pk_fma_f32 v[76:77], v[8:9], s[2:3], v[172:173] op_sel_hi:[1,0,1]
	v_pk_fma_f32 v[78:79], v[10:11], s[2:3], v[170:171] op_sel_hi:[1,0,1]
	v_pk_fma_f32 v[168:169], v[12:13], s[2:3], v[168:169] op_sel_hi:[1,0,1]
	v_pk_fma_f32 v[166:167], v[14:15], s[2:3], v[166:167] op_sel_hi:[1,0,1]
	v_pk_fma_f32 v[164:165], v[16:17], s[2:3], v[164:165] op_sel_hi:[1,0,1]
	v_pk_fma_f32 v[162:163], v[18:19], s[2:3], v[162:163] op_sel_hi:[1,0,1]
	v_pk_fma_f32 v[160:161], v[20:21], s[2:3], v[160:161] op_sel_hi:[1,0,1]
	v_pk_fma_f32 v[158:159], v[22:23], s[2:3], v[158:159] op_sel_hi:[1,0,1]
	v_pk_fma_f32 v[156:157], v[24:25], s[2:3], v[156:157] op_sel_hi:[1,0,1]
	v_pk_fma_f32 v[154:155], v[26:27], s[2:3], v[154:155] op_sel_hi:[1,0,1]
	v_pk_fma_f32 v[152:153], v[28:29], s[2:3], v[152:153] op_sel_hi:[1,0,1]
	v_pk_fma_f32 v[150:151], v[30:31], s[2:3], v[150:151] op_sel_hi:[1,0,1]
	v_readlane_b32 s2, v131, 10
	s_waitcnt vmcnt(18)
	v_cvt_scalef32_pk32_f32_fp6 v[0:31], v[56:61], 1.0
	v_pk_fma_f32 v[56:57], v[0:1], s[2:3], v[68:69] op_sel_hi:[1,0,1]
	v_pk_fma_f32 v[58:59], v[2:3], s[2:3], v[70:71] op_sel_hi:[1,0,1]
	v_pk_fma_f32 v[60:61], v[4:5], s[2:3], v[72:73] op_sel_hi:[1,0,1]
	v_pk_fma_f32 v[68:69], v[6:7], s[2:3], v[74:75] op_sel_hi:[1,0,1]
	v_pk_fma_f32 v[70:71], v[8:9], s[2:3], v[76:77] op_sel_hi:[1,0,1]
	v_pk_fma_f32 v[72:73], v[10:11], s[2:3], v[78:79] op_sel_hi:[1,0,1]
	v_pk_fma_f32 v[74:75], v[12:13], s[2:3], v[168:169] op_sel_hi:[1,0,1]
	v_pk_fma_f32 v[76:77], v[14:15], s[2:3], v[166:167] op_sel_hi:[1,0,1]
	v_pk_fma_f32 v[78:79], v[16:17], s[2:3], v[164:165] op_sel_hi:[1,0,1]
	v_pk_fma_f32 v[162:163], v[18:19], s[2:3], v[162:163] op_sel_hi:[1,0,1]
	v_pk_fma_f32 v[160:161], v[20:21], s[2:3], v[160:161] op_sel_hi:[1,0,1]
	v_pk_fma_f32 v[158:159], v[22:23], s[2:3], v[158:159] op_sel_hi:[1,0,1]
	v_pk_fma_f32 v[156:157], v[24:25], s[2:3], v[156:157] op_sel_hi:[1,0,1]
	v_pk_fma_f32 v[154:155], v[26:27], s[2:3], v[154:155] op_sel_hi:[1,0,1]
	v_pk_fma_f32 v[152:153], v[28:29], s[2:3], v[152:153] op_sel_hi:[1,0,1]
	v_pk_fma_f32 v[150:151], v[30:31], s[2:3], v[150:151] op_sel_hi:[1,0,1]
	v_readlane_b32 s2, v131, 11
	s_waitcnt vmcnt(16)
	v_cvt_scalef32_pk32_f32_fp6 v[0:31], v[44:49], 1.0
	v_pk_fma_f32 v[164:165], v[0:1], s[2:3], v[56:57] op_sel_hi:[1,0,1]
	v_pk_fma_f32 v[166:167], v[2:3], s[2:3], v[58:59] op_sel_hi:[1,0,1]
	v_pk_fma_f32 v[168:169], v[4:5], s[2:3], v[60:61] op_sel_hi:[1,0,1]
	v_pk_fma_f32 v[170:171], v[6:7], s[2:3], v[68:69] op_sel_hi:[1,0,1]
	v_pk_fma_f32 v[172:173], v[8:9], s[2:3], v[70:71] op_sel_hi:[1,0,1]
	v_pk_fma_f32 v[174:175], v[10:11], s[2:3], v[72:73] op_sel_hi:[1,0,1]
	v_pk_fma_f32 v[176:177], v[12:13], s[2:3], v[74:75] op_sel_hi:[1,0,1]
	v_pk_fma_f32 v[178:179], v[14:15], s[2:3], v[76:77] op_sel_hi:[1,0,1]
	v_pk_fma_f32 v[180:181], v[16:17], s[2:3], v[78:79] op_sel_hi:[1,0,1]
	v_pk_fma_f32 v[162:163], v[18:19], s[2:3], v[162:163] op_sel_hi:[1,0,1]
	v_pk_fma_f32 v[160:161], v[20:21], s[2:3], v[160:161] op_sel_hi:[1,0,1]
	v_pk_fma_f32 v[158:159], v[22:23], s[2:3], v[158:159] op_sel_hi:[1,0,1]
	v_pk_fma_f32 v[156:157], v[24:25], s[2:3], v[156:157] op_sel_hi:[1,0,1]
	v_pk_fma_f32 v[154:155], v[26:27], s[2:3], v[154:155] op_sel_hi:[1,0,1]
	v_pk_fma_f32 v[152:153], v[28:29], s[2:3], v[152:153] op_sel_hi:[1,0,1]
	v_pk_fma_f32 v[150:151], v[30:31], s[2:3], v[150:151] op_sel_hi:[1,0,1]
	v_readlane_b32 s2, v241, 20
	v_readlane_b32 s3, v241, 21
	v_readlane_b32 s100, v241, 22
	v_readlane_b32 s101, v241, 23
	s_nop 1
	buffer_load_dwordx4 v[74:77], v129, s[44:47], s2 offen
	buffer_load_dwordx2 v[78:79], v210, s[44:47], s2 offen
	buffer_load_dwordx4 v[68:71], v129, s[44:47], s3 offen
	buffer_load_dwordx2 v[72:73], v210, s[44:47], s3 offen
	buffer_load_dwordx4 v[56:59], v129, s[44:47], s100 offen
	buffer_load_dwordx2 v[60:61], v210, s[44:47], s100 offen
	buffer_load_dwordx4 v[44:47], v129, s[44:47], s101 offen
	buffer_load_dwordx2 v[48:49], v210, s[44:47], s101 offen
	v_readlane_b32 s2, v131, 12
	s_waitcnt vmcnt(22)
	v_cvt_scalef32_pk32_f32_fp6 v[0:31], v[62:67], 1.0
	v_pk_fma_f32 v[62:63], v[0:1], s[2:3], v[164:165] op_sel_hi:[1,0,1]
	v_pk_fma_f32 v[64:65], v[2:3], s[2:3], v[166:167] op_sel_hi:[1,0,1]
	v_pk_fma_f32 v[66:67], v[4:5], s[2:3], v[168:169] op_sel_hi:[1,0,1]
	v_pk_fma_f32 v[164:165], v[6:7], s[2:3], v[170:171] op_sel_hi:[1,0,1]
	v_pk_fma_f32 v[166:167], v[8:9], s[2:3], v[172:173] op_sel_hi:[1,0,1]
	v_pk_fma_f32 v[168:169], v[10:11], s[2:3], v[174:175] op_sel_hi:[1,0,1]
	v_pk_fma_f32 v[170:171], v[12:13], s[2:3], v[176:177] op_sel_hi:[1,0,1]
	v_pk_fma_f32 v[172:173], v[14:15], s[2:3], v[178:179] op_sel_hi:[1,0,1]
	v_pk_fma_f32 v[174:175], v[16:17], s[2:3], v[180:181] op_sel_hi:[1,0,1]
	v_pk_fma_f32 v[162:163], v[18:19], s[2:3], v[162:163] op_sel_hi:[1,0,1]
	v_pk_fma_f32 v[160:161], v[20:21], s[2:3], v[160:161] op_sel_hi:[1,0,1]
	v_pk_fma_f32 v[158:159], v[22:23], s[2:3], v[158:159] op_sel_hi:[1,0,1]
	v_pk_fma_f32 v[156:157], v[24:25], s[2:3], v[156:157] op_sel_hi:[1,0,1]
	v_pk_fma_f32 v[154:155], v[26:27], s[2:3], v[154:155] op_sel_hi:[1,0,1]
	v_pk_fma_f32 v[152:153], v[28:29], s[2:3], v[152:153] op_sel_hi:[1,0,1]
	v_pk_fma_f32 v[150:151], v[30:31], s[2:3], v[150:151] op_sel_hi:[1,0,1]
	v_readlane_b32 s2, v131, 13
	s_waitcnt vmcnt(20)
	v_cvt_scalef32_pk32_f32_fp6 v[0:31], v[50:55], 1.0
	v_pk_fma_f32 v[50:51], v[0:1], s[2:3], v[62:63] op_sel_hi:[1,0,1]
	v_pk_fma_f32 v[52:53], v[2:3], s[2:3], v[64:65] op_sel_hi:[1,0,1]
	v_pk_fma_f32 v[54:55], v[4:5], s[2:3], v[66:67] op_sel_hi:[1,0,1]
	v_pk_fma_f32 v[62:63], v[6:7], s[2:3], v[164:165] op_sel_hi:[1,0,1]
	v_pk_fma_f32 v[64:65], v[8:9], s[2:3], v[166:167] op_sel_hi:[1,0,1]
	v_pk_fma_f32 v[66:67], v[10:11], s[2:3], v[168:169] op_sel_hi:[1,0,1]
	v_pk_fma_f32 v[164:165], v[12:13], s[2:3], v[170:171] op_sel_hi:[1,0,1]
	v_pk_fma_f32 v[166:167], v[14:15], s[2:3], v[172:173] op_sel_hi:[1,0,1]
	v_pk_fma_f32 v[168:169], v[16:17], s[2:3], v[174:175] op_sel_hi:[1,0,1]
	v_pk_fma_f32 v[162:163], v[18:19], s[2:3], v[162:163] op_sel_hi:[1,0,1]
	v_pk_fma_f32 v[160:161], v[20:21], s[2:3], v[160:161] op_sel_hi:[1,0,1]
	v_pk_fma_f32 v[158:159], v[22:23], s[2:3], v[158:159] op_sel_hi:[1,0,1]
	v_pk_fma_f32 v[156:157], v[24:25], s[2:3], v[156:157] op_sel_hi:[1,0,1]
	v_pk_fma_f32 v[154:155], v[26:27], s[2:3], v[154:155] op_sel_hi:[1,0,1]
	v_pk_fma_f32 v[152:153], v[28:29], s[2:3], v[152:153] op_sel_hi:[1,0,1]
	v_pk_fma_f32 v[150:151], v[30:31], s[2:3], v[150:151] op_sel_hi:[1,0,1]
	v_readlane_b32 s2, v131, 14
	s_waitcnt vmcnt(18)
	v_cvt_scalef32_pk32_f32_fp6 v[0:31], v[38:43], 1.0
	v_pk_fma_f32 v[38:39], v[0:1], s[2:3], v[50:51] op_sel_hi:[1,0,1]
	v_pk_fma_f32 v[40:41], v[2:3], s[2:3], v[52:53] op_sel_hi:[1,0,1]
	v_pk_fma_f32 v[42:43], v[4:5], s[2:3], v[54:55] op_sel_hi:[1,0,1]
	v_pk_fma_f32 v[50:51], v[6:7], s[2:3], v[62:63] op_sel_hi:[1,0,1]
	v_pk_fma_f32 v[52:53], v[8:9], s[2:3], v[64:65] op_sel_hi:[1,0,1]
	v_pk_fma_f32 v[54:55], v[10:11], s[2:3], v[66:67] op_sel_hi:[1,0,1]
	v_pk_fma_f32 v[62:63], v[12:13], s[2:3], v[164:165] op_sel_hi:[1,0,1]
	v_pk_fma_f32 v[64:65], v[14:15], s[2:3], v[166:167] op_sel_hi:[1,0,1]
	v_pk_fma_f32 v[66:67], v[16:17], s[2:3], v[168:169] op_sel_hi:[1,0,1]
	v_pk_fma_f32 v[162:163], v[18:19], s[2:3], v[162:163] op_sel_hi:[1,0,1]
	v_pk_fma_f32 v[160:161], v[20:21], s[2:3], v[160:161] op_sel_hi:[1,0,1]
	v_pk_fma_f32 v[158:159], v[22:23], s[2:3], v[158:159] op_sel_hi:[1,0,1]
	v_pk_fma_f32 v[156:157], v[24:25], s[2:3], v[156:157] op_sel_hi:[1,0,1]
	v_pk_fma_f32 v[154:155], v[26:27], s[2:3], v[154:155] op_sel_hi:[1,0,1]
	v_pk_fma_f32 v[152:153], v[28:29], s[2:3], v[152:153] op_sel_hi:[1,0,1]
	v_pk_fma_f32 v[150:151], v[30:31], s[2:3], v[150:151] op_sel_hi:[1,0,1]
	v_readlane_b32 s2, v131, 15
	s_waitcnt vmcnt(16)
	v_cvt_scalef32_pk32_f32_fp6 v[0:31], v[32:37], 1.0
	v_pk_fma_f32 v[164:165], v[0:1], s[2:3], v[38:39] op_sel_hi:[1,0,1]
	v_pk_fma_f32 v[166:167], v[2:3], s[2:3], v[40:41] op_sel_hi:[1,0,1]
	v_pk_fma_f32 v[168:169], v[4:5], s[2:3], v[42:43] op_sel_hi:[1,0,1]
	v_pk_fma_f32 v[170:171], v[6:7], s[2:3], v[50:51] op_sel_hi:[1,0,1]
	v_pk_fma_f32 v[172:173], v[8:9], s[2:3], v[52:53] op_sel_hi:[1,0,1]
	v_pk_fma_f32 v[174:175], v[10:11], s[2:3], v[54:55] op_sel_hi:[1,0,1]
	v_pk_fma_f32 v[176:177], v[12:13], s[2:3], v[62:63] op_sel_hi:[1,0,1]
	v_pk_fma_f32 v[178:179], v[14:15], s[2:3], v[64:65] op_sel_hi:[1,0,1]
	v_pk_fma_f32 v[180:181], v[16:17], s[2:3], v[66:67] op_sel_hi:[1,0,1]
	v_pk_fma_f32 v[162:163], v[18:19], s[2:3], v[162:163] op_sel_hi:[1,0,1]
	v_pk_fma_f32 v[160:161], v[20:21], s[2:3], v[160:161] op_sel_hi:[1,0,1]
	v_pk_fma_f32 v[158:159], v[22:23], s[2:3], v[158:159] op_sel_hi:[1,0,1]
	v_pk_fma_f32 v[156:157], v[24:25], s[2:3], v[156:157] op_sel_hi:[1,0,1]
	v_pk_fma_f32 v[154:155], v[26:27], s[2:3], v[154:155] op_sel_hi:[1,0,1]
	v_pk_fma_f32 v[152:153], v[28:29], s[2:3], v[152:153] op_sel_hi:[1,0,1]
	v_pk_fma_f32 v[150:151], v[30:31], s[2:3], v[150:151] op_sel_hi:[1,0,1]
	v_readlane_b32 s2, v241, 24
	v_readlane_b32 s3, v241, 25
	v_readlane_b32 s100, v241, 26
	v_readlane_b32 s101, v241, 27
	s_nop 1
	buffer_load_dwordx4 v[62:65], v129, s[44:47], s2 offen
	buffer_load_dwordx2 v[66:67], v210, s[44:47], s2 offen
	buffer_load_dwordx4 v[50:53], v129, s[44:47], s3 offen
	buffer_load_dwordx2 v[54:55], v210, s[44:47], s3 offen
	buffer_load_dwordx4 v[38:41], v129, s[44:47], s100 offen
	buffer_load_dwordx2 v[42:43], v210, s[44:47], s100 offen
	buffer_load_dwordx4 v[32:35], v129, s[44:47], s101 offen
	buffer_load_dwordx2 v[36:37], v210, s[44:47], s101 offen
	v_readlane_b32 s2, v131, 16
	s_waitcnt vmcnt(22)
	v_cvt_scalef32_pk32_f32_fp6 v[0:31], v[98:103], 1.0
	v_pk_fma_f32 v[98:99], v[0:1], s[2:3], v[164:165] op_sel_hi:[1,0,1]
	v_pk_fma_f32 v[100:101], v[2:3], s[2:3], v[166:167] op_sel_hi:[1,0,1]
	v_pk_fma_f32 v[102:103], v[4:5], s[2:3], v[168:169] op_sel_hi:[1,0,1]
	v_pk_fma_f32 v[164:165], v[6:7], s[2:3], v[170:171] op_sel_hi:[1,0,1]
	v_pk_fma_f32 v[166:167], v[8:9], s[2:3], v[172:173] op_sel_hi:[1,0,1]
	v_pk_fma_f32 v[168:169], v[10:11], s[2:3], v[174:175] op_sel_hi:[1,0,1]
	v_pk_fma_f32 v[170:171], v[12:13], s[2:3], v[176:177] op_sel_hi:[1,0,1]
	v_pk_fma_f32 v[172:173], v[14:15], s[2:3], v[178:179] op_sel_hi:[1,0,1]
	v_pk_fma_f32 v[174:175], v[16:17], s[2:3], v[180:181] op_sel_hi:[1,0,1]
	v_pk_fma_f32 v[162:163], v[18:19], s[2:3], v[162:163] op_sel_hi:[1,0,1]
	v_pk_fma_f32 v[160:161], v[20:21], s[2:3], v[160:161] op_sel_hi:[1,0,1]
	v_pk_fma_f32 v[158:159], v[22:23], s[2:3], v[158:159] op_sel_hi:[1,0,1]
	v_pk_fma_f32 v[156:157], v[24:25], s[2:3], v[156:157] op_sel_hi:[1,0,1]
	v_pk_fma_f32 v[154:155], v[26:27], s[2:3], v[154:155] op_sel_hi:[1,0,1]
	v_pk_fma_f32 v[152:153], v[28:29], s[2:3], v[152:153] op_sel_hi:[1,0,1]
	v_pk_fma_f32 v[150:151], v[30:31], s[2:3], v[150:151] op_sel_hi:[1,0,1]
	v_readlane_b32 s2, v131, 17
	s_waitcnt vmcnt(20)
	v_cvt_scalef32_pk32_f32_fp6 v[0:31], v[92:97], 1.0
	v_pk_fma_f32 v[92:93], v[0:1], s[2:3], v[98:99] op_sel_hi:[1,0,1]
	v_pk_fma_f32 v[94:95], v[2:3], s[2:3], v[100:101] op_sel_hi:[1,0,1]
	v_pk_fma_f32 v[96:97], v[4:5], s[2:3], v[102:103] op_sel_hi:[1,0,1]
	v_pk_fma_f32 v[98:99], v[6:7], s[2:3], v[164:165] op_sel_hi:[1,0,1]
	v_pk_fma_f32 v[100:101], v[8:9], s[2:3], v[166:167] op_sel_hi:[1,0,1]
	v_pk_fma_f32 v[102:103], v[10:11], s[2:3], v[168:169] op_sel_hi:[1,0,1]
	v_pk_fma_f32 v[164:165], v[12:13], s[2:3], v[170:171] op_sel_hi:[1,0,1]
	v_pk_fma_f32 v[166:167], v[14:15], s[2:3], v[172:173] op_sel_hi:[1,0,1]
	v_pk_fma_f32 v[168:169], v[16:17], s[2:3], v[174:175] op_sel_hi:[1,0,1]
	v_pk_fma_f32 v[162:163], v[18:19], s[2:3], v[162:163] op_sel_hi:[1,0,1]
	v_pk_fma_f32 v[160:161], v[20:21], s[2:3], v[160:161] op_sel_hi:[1,0,1]
	v_pk_fma_f32 v[158:159], v[22:23], s[2:3], v[158:159] op_sel_hi:[1,0,1]
	v_pk_fma_f32 v[156:157], v[24:25], s[2:3], v[156:157] op_sel_hi:[1,0,1]
	v_pk_fma_f32 v[154:155], v[26:27], s[2:3], v[154:155] op_sel_hi:[1,0,1]
	v_pk_fma_f32 v[152:153], v[28:29], s[2:3], v[152:153] op_sel_hi:[1,0,1]
	v_pk_fma_f32 v[150:151], v[30:31], s[2:3], v[150:151] op_sel_hi:[1,0,1]
	v_readlane_b32 s2, v131, 18
	s_waitcnt vmcnt(18)
	v_cvt_scalef32_pk32_f32_fp6 v[0:31], v[86:91], 1.0
	v_pk_fma_f32 v[86:87], v[0:1], s[2:3], v[92:93] op_sel_hi:[1,0,1]
	v_pk_fma_f32 v[88:89], v[2:3], s[2:3], v[94:95] op_sel_hi:[1,0,1]
	v_pk_fma_f32 v[90:91], v[4:5], s[2:3], v[96:97] op_sel_hi:[1,0,1]
	v_pk_fma_f32 v[92:93], v[6:7], s[2:3], v[98:99] op_sel_hi:[1,0,1]
	v_pk_fma_f32 v[94:95], v[8:9], s[2:3], v[100:101] op_sel_hi:[1,0,1]
	v_pk_fma_f32 v[96:97], v[10:11], s[2:3], v[102:103] op_sel_hi:[1,0,1]
	v_pk_fma_f32 v[98:99], v[12:13], s[2:3], v[164:165] op_sel_hi:[1,0,1]
	v_pk_fma_f32 v[100:101], v[14:15], s[2:3], v[166:167] op_sel_hi:[1,0,1]
	v_pk_fma_f32 v[102:103], v[16:17], s[2:3], v[168:169] op_sel_hi:[1,0,1]
	v_pk_fma_f32 v[162:163], v[18:19], s[2:3], v[162:163] op_sel_hi:[1,0,1]
	v_pk_fma_f32 v[160:161], v[20:21], s[2:3], v[160:161] op_sel_hi:[1,0,1]
	v_pk_fma_f32 v[158:159], v[22:23], s[2:3], v[158:159] op_sel_hi:[1,0,1]
	v_pk_fma_f32 v[156:157], v[24:25], s[2:3], v[156:157] op_sel_hi:[1,0,1]
	v_pk_fma_f32 v[154:155], v[26:27], s[2:3], v[154:155] op_sel_hi:[1,0,1]
	v_pk_fma_f32 v[152:153], v[28:29], s[2:3], v[152:153] op_sel_hi:[1,0,1]
	v_pk_fma_f32 v[150:151], v[30:31], s[2:3], v[150:151] op_sel_hi:[1,0,1]
	v_readlane_b32 s2, v131, 19
	s_waitcnt vmcnt(16)
	v_cvt_scalef32_pk32_f32_fp6 v[0:31], v[80:85], 1.0
	v_pk_fma_f32 v[180:181], v[0:1], s[2:3], v[86:87] op_sel_hi:[1,0,1]
	v_pk_fma_f32 v[178:179], v[2:3], s[2:3], v[88:89] op_sel_hi:[1,0,1]
	v_pk_fma_f32 v[176:177], v[4:5], s[2:3], v[90:91] op_sel_hi:[1,0,1]
	v_pk_fma_f32 v[174:175], v[6:7], s[2:3], v[92:93] op_sel_hi:[1,0,1]
	v_pk_fma_f32 v[172:173], v[8:9], s[2:3], v[94:95] op_sel_hi:[1,0,1]
	v_pk_fma_f32 v[170:171], v[10:11], s[2:3], v[96:97] op_sel_hi:[1,0,1]
	v_pk_fma_f32 v[168:169], v[12:13], s[2:3], v[98:99] op_sel_hi:[1,0,1]
	v_pk_fma_f32 v[166:167], v[14:15], s[2:3], v[100:101] op_sel_hi:[1,0,1]
	v_pk_fma_f32 v[164:165], v[16:17], s[2:3], v[102:103] op_sel_hi:[1,0,1]
	v_pk_fma_f32 v[162:163], v[18:19], s[2:3], v[162:163] op_sel_hi:[1,0,1]
	v_pk_fma_f32 v[160:161], v[20:21], s[2:3], v[160:161] op_sel_hi:[1,0,1]
	v_pk_fma_f32 v[158:159], v[22:23], s[2:3], v[158:159] op_sel_hi:[1,0,1]
	v_pk_fma_f32 v[156:157], v[24:25], s[2:3], v[156:157] op_sel_hi:[1,0,1]
	v_pk_fma_f32 v[154:155], v[26:27], s[2:3], v[154:155] op_sel_hi:[1,0,1]
	v_pk_fma_f32 v[152:153], v[28:29], s[2:3], v[152:153] op_sel_hi:[1,0,1]
	v_pk_fma_f32 v[150:151], v[30:31], s[2:3], v[150:151] op_sel_hi:[1,0,1]
	v_readlane_b32 s2, v241, 28
	v_readlane_b32 s3, v241, 29
	v_readlane_b32 s100, v241, 30
	v_readlane_b32 s101, v241, 31
	s_nop 1
	buffer_load_dwordx4 v[98:101], v129, s[44:47], s2 offen
	buffer_load_dwordx2 v[102:103], v210, s[44:47], s2 offen
	buffer_load_dwordx4 v[92:95], v129, s[44:47], s3 offen
	buffer_load_dwordx2 v[96:97], v210, s[44:47], s3 offen
	buffer_load_dwordx4 v[86:89], v129, s[44:47], s100 offen
	buffer_load_dwordx2 v[90:91], v210, s[44:47], s100 offen
	buffer_load_dwordx4 v[80:83], v129, s[44:47], s101 offen
	buffer_load_dwordx2 v[84:85], v210, s[44:47], s101 offen
	v_readlane_b32 s2, v131, 20
	s_waitcnt vmcnt(22)
	v_cvt_scalef32_pk32_f32_fp6 v[0:31], v[74:79], 1.0
	v_pk_fma_f32 v[74:75], v[0:1], s[2:3], v[180:181] op_sel_hi:[1,0,1]
	v_pk_fma_f32 v[76:77], v[2:3], s[2:3], v[178:179] op_sel_hi:[1,0,1]
	v_pk_fma_f32 v[78:79], v[4:5], s[2:3], v[176:177] op_sel_hi:[1,0,1]
	v_pk_fma_f32 v[174:175], v[6:7], s[2:3], v[174:175] op_sel_hi:[1,0,1]
	v_pk_fma_f32 v[172:173], v[8:9], s[2:3], v[172:173] op_sel_hi:[1,0,1]
	v_pk_fma_f32 v[170:171], v[10:11], s[2:3], v[170:171] op_sel_hi:[1,0,1]
	v_pk_fma_f32 v[168:169], v[12:13], s[2:3], v[168:169] op_sel_hi:[1,0,1]
	v_pk_fma_f32 v[166:167], v[14:15], s[2:3], v[166:167] op_sel_hi:[1,0,1]
	v_pk_fma_f32 v[164:165], v[16:17], s[2:3], v[164:165] op_sel_hi:[1,0,1]
	v_pk_fma_f32 v[162:163], v[18:19], s[2:3], v[162:163] op_sel_hi:[1,0,1]
	v_pk_fma_f32 v[160:161], v[20:21], s[2:3], v[160:161] op_sel_hi:[1,0,1]
	v_pk_fma_f32 v[158:159], v[22:23], s[2:3], v[158:159] op_sel_hi:[1,0,1]
	v_pk_fma_f32 v[156:157], v[24:25], s[2:3], v[156:157] op_sel_hi:[1,0,1]
	v_pk_fma_f32 v[154:155], v[26:27], s[2:3], v[154:155] op_sel_hi:[1,0,1]
	v_pk_fma_f32 v[152:153], v[28:29], s[2:3], v[152:153] op_sel_hi:[1,0,1]
	v_pk_fma_f32 v[150:151], v[30:31], s[2:3], v[150:151] op_sel_hi:[1,0,1]
	v_readlane_b32 s2, v131, 21
	s_waitcnt vmcnt(20)
	v_cvt_scalef32_pk32_f32_fp6 v[0:31], v[68:73], 1.0
	v_pk_fma_f32 v[68:69], v[0:1], s[2:3], v[74:75] op_sel_hi:[1,0,1]
	v_pk_fma_f32 v[70:71], v[2:3], s[2:3], v[76:77] op_sel_hi:[1,0,1]
	v_pk_fma_f32 v[72:73], v[4:5], s[2:3], v[78:79] op_sel_hi:[1,0,1]
	v_pk_fma_f32 v[74:75], v[6:7], s[2:3], v[174:175] op_sel_hi:[1,0,1]
	v_pk_fma_f32 v[76:77], v[8:9], s[2:3], v[172:173] op_sel_hi:[1,0,1]
	v_pk_fma_f32 v[78:79], v[10:11], s[2:3], v[170:171] op_sel_hi:[1,0,1]
	v_pk_fma_f32 v[168:169], v[12:13], s[2:3], v[168:169] op_sel_hi:[1,0,1]
	v_pk_fma_f32 v[166:167], v[14:15], s[2:3], v[166:167] op_sel_hi:[1,0,1]
	v_pk_fma_f32 v[164:165], v[16:17], s[2:3], v[164:165] op_sel_hi:[1,0,1]
	v_pk_fma_f32 v[162:163], v[18:19], s[2:3], v[162:163] op_sel_hi:[1,0,1]
	v_pk_fma_f32 v[160:161], v[20:21], s[2:3], v[160:161] op_sel_hi:[1,0,1]
	v_pk_fma_f32 v[158:159], v[22:23], s[2:3], v[158:159] op_sel_hi:[1,0,1]
	v_pk_fma_f32 v[156:157], v[24:25], s[2:3], v[156:157] op_sel_hi:[1,0,1]
	v_pk_fma_f32 v[154:155], v[26:27], s[2:3], v[154:155] op_sel_hi:[1,0,1]
	v_pk_fma_f32 v[152:153], v[28:29], s[2:3], v[152:153] op_sel_hi:[1,0,1]
	v_pk_fma_f32 v[150:151], v[30:31], s[2:3], v[150:151] op_sel_hi:[1,0,1]
	v_readlane_b32 s2, v131, 22
	s_waitcnt vmcnt(18)
	v_cvt_scalef32_pk32_f32_fp6 v[0:31], v[56:61], 1.0
	v_pk_fma_f32 v[56:57], v[0:1], s[2:3], v[68:69] op_sel_hi:[1,0,1]
	v_pk_fma_f32 v[58:59], v[2:3], s[2:3], v[70:71] op_sel_hi:[1,0,1]
	v_pk_fma_f32 v[60:61], v[4:5], s[2:3], v[72:73] op_sel_hi:[1,0,1]
	v_pk_fma_f32 v[68:69], v[6:7], s[2:3], v[74:75] op_sel_hi:[1,0,1]
	v_pk_fma_f32 v[70:71], v[8:9], s[2:3], v[76:77] op_sel_hi:[1,0,1]
	v_pk_fma_f32 v[72:73], v[10:11], s[2:3], v[78:79] op_sel_hi:[1,0,1]
	v_pk_fma_f32 v[74:75], v[12:13], s[2:3], v[168:169] op_sel_hi:[1,0,1]
	v_pk_fma_f32 v[76:77], v[14:15], s[2:3], v[166:167] op_sel_hi:[1,0,1]
	v_pk_fma_f32 v[78:79], v[16:17], s[2:3], v[164:165] op_sel_hi:[1,0,1]
	v_pk_fma_f32 v[162:163], v[18:19], s[2:3], v[162:163] op_sel_hi:[1,0,1]
	v_pk_fma_f32 v[160:161], v[20:21], s[2:3], v[160:161] op_sel_hi:[1,0,1]
	v_pk_fma_f32 v[158:159], v[22:23], s[2:3], v[158:159] op_sel_hi:[1,0,1]
	v_pk_fma_f32 v[156:157], v[24:25], s[2:3], v[156:157] op_sel_hi:[1,0,1]
	v_pk_fma_f32 v[154:155], v[26:27], s[2:3], v[154:155] op_sel_hi:[1,0,1]
	v_pk_fma_f32 v[152:153], v[28:29], s[2:3], v[152:153] op_sel_hi:[1,0,1]
	v_pk_fma_f32 v[150:151], v[30:31], s[2:3], v[150:151] op_sel_hi:[1,0,1]
	v_readlane_b32 s2, v131, 23
	s_waitcnt vmcnt(16)
	v_cvt_scalef32_pk32_f32_fp6 v[0:31], v[44:49], 1.0
	v_pk_fma_f32 v[164:165], v[0:1], s[2:3], v[56:57] op_sel_hi:[1,0,1]
	v_pk_fma_f32 v[166:167], v[2:3], s[2:3], v[58:59] op_sel_hi:[1,0,1]
	v_pk_fma_f32 v[168:169], v[4:5], s[2:3], v[60:61] op_sel_hi:[1,0,1]
	v_pk_fma_f32 v[170:171], v[6:7], s[2:3], v[68:69] op_sel_hi:[1,0,1]
	v_pk_fma_f32 v[172:173], v[8:9], s[2:3], v[70:71] op_sel_hi:[1,0,1]
	v_pk_fma_f32 v[174:175], v[10:11], s[2:3], v[72:73] op_sel_hi:[1,0,1]
	v_pk_fma_f32 v[176:177], v[12:13], s[2:3], v[74:75] op_sel_hi:[1,0,1]
	v_pk_fma_f32 v[178:179], v[14:15], s[2:3], v[76:77] op_sel_hi:[1,0,1]
	v_pk_fma_f32 v[180:181], v[16:17], s[2:3], v[78:79] op_sel_hi:[1,0,1]
	v_pk_fma_f32 v[162:163], v[18:19], s[2:3], v[162:163] op_sel_hi:[1,0,1]
	v_pk_fma_f32 v[160:161], v[20:21], s[2:3], v[160:161] op_sel_hi:[1,0,1]
	v_pk_fma_f32 v[158:159], v[22:23], s[2:3], v[158:159] op_sel_hi:[1,0,1]
	v_pk_fma_f32 v[156:157], v[24:25], s[2:3], v[156:157] op_sel_hi:[1,0,1]
	v_pk_fma_f32 v[154:155], v[26:27], s[2:3], v[154:155] op_sel_hi:[1,0,1]
	v_pk_fma_f32 v[152:153], v[28:29], s[2:3], v[152:153] op_sel_hi:[1,0,1]
	v_pk_fma_f32 v[150:151], v[30:31], s[2:3], v[150:151] op_sel_hi:[1,0,1]
	v_readlane_b32 s2, v241, 32
	v_readlane_b32 s3, v241, 33
	v_readlane_b32 s100, v241, 34
	v_readlane_b32 s101, v241, 35
	s_nop 1
	buffer_load_dwordx4 v[74:77], v129, s[44:47], s2 offen
	buffer_load_dwordx2 v[78:79], v210, s[44:47], s2 offen
	buffer_load_dwordx4 v[68:71], v129, s[44:47], s3 offen
	buffer_load_dwordx2 v[72:73], v210, s[44:47], s3 offen
	buffer_load_dwordx4 v[56:59], v129, s[44:47], s100 offen
	buffer_load_dwordx2 v[60:61], v210, s[44:47], s100 offen
	buffer_load_dwordx4 v[44:47], v129, s[44:47], s101 offen
	buffer_load_dwordx2 v[48:49], v210, s[44:47], s101 offen
	v_readlane_b32 s2, v131, 24
	s_waitcnt vmcnt(22)
	v_cvt_scalef32_pk32_f32_fp6 v[0:31], v[62:67], 1.0
	v_pk_fma_f32 v[62:63], v[0:1], s[2:3], v[164:165] op_sel_hi:[1,0,1]
	v_pk_fma_f32 v[64:65], v[2:3], s[2:3], v[166:167] op_sel_hi:[1,0,1]
	v_pk_fma_f32 v[66:67], v[4:5], s[2:3], v[168:169] op_sel_hi:[1,0,1]
	v_pk_fma_f32 v[164:165], v[6:7], s[2:3], v[170:171] op_sel_hi:[1,0,1]
	v_pk_fma_f32 v[166:167], v[8:9], s[2:3], v[172:173] op_sel_hi:[1,0,1]
	v_pk_fma_f32 v[168:169], v[10:11], s[2:3], v[174:175] op_sel_hi:[1,0,1]
	v_pk_fma_f32 v[170:171], v[12:13], s[2:3], v[176:177] op_sel_hi:[1,0,1]
	v_pk_fma_f32 v[172:173], v[14:15], s[2:3], v[178:179] op_sel_hi:[1,0,1]
	v_pk_fma_f32 v[174:175], v[16:17], s[2:3], v[180:181] op_sel_hi:[1,0,1]
	v_pk_fma_f32 v[162:163], v[18:19], s[2:3], v[162:163] op_sel_hi:[1,0,1]
	v_pk_fma_f32 v[160:161], v[20:21], s[2:3], v[160:161] op_sel_hi:[1,0,1]
	v_pk_fma_f32 v[158:159], v[22:23], s[2:3], v[158:159] op_sel_hi:[1,0,1]
	v_pk_fma_f32 v[156:157], v[24:25], s[2:3], v[156:157] op_sel_hi:[1,0,1]
	v_pk_fma_f32 v[154:155], v[26:27], s[2:3], v[154:155] op_sel_hi:[1,0,1]
	v_pk_fma_f32 v[152:153], v[28:29], s[2:3], v[152:153] op_sel_hi:[1,0,1]
	v_pk_fma_f32 v[150:151], v[30:31], s[2:3], v[150:151] op_sel_hi:[1,0,1]
	v_readlane_b32 s2, v131, 25
	s_waitcnt vmcnt(20)
	v_cvt_scalef32_pk32_f32_fp6 v[0:31], v[50:55], 1.0
	v_pk_fma_f32 v[50:51], v[0:1], s[2:3], v[62:63] op_sel_hi:[1,0,1]
	v_pk_fma_f32 v[52:53], v[2:3], s[2:3], v[64:65] op_sel_hi:[1,0,1]
	v_pk_fma_f32 v[54:55], v[4:5], s[2:3], v[66:67] op_sel_hi:[1,0,1]
	v_pk_fma_f32 v[62:63], v[6:7], s[2:3], v[164:165] op_sel_hi:[1,0,1]
	v_pk_fma_f32 v[64:65], v[8:9], s[2:3], v[166:167] op_sel_hi:[1,0,1]
	v_pk_fma_f32 v[66:67], v[10:11], s[2:3], v[168:169] op_sel_hi:[1,0,1]
	v_pk_fma_f32 v[164:165], v[12:13], s[2:3], v[170:171] op_sel_hi:[1,0,1]
	v_pk_fma_f32 v[166:167], v[14:15], s[2:3], v[172:173] op_sel_hi:[1,0,1]
	v_pk_fma_f32 v[168:169], v[16:17], s[2:3], v[174:175] op_sel_hi:[1,0,1]
	v_pk_fma_f32 v[162:163], v[18:19], s[2:3], v[162:163] op_sel_hi:[1,0,1]
	v_pk_fma_f32 v[160:161], v[20:21], s[2:3], v[160:161] op_sel_hi:[1,0,1]
	v_pk_fma_f32 v[158:159], v[22:23], s[2:3], v[158:159] op_sel_hi:[1,0,1]
	v_pk_fma_f32 v[156:157], v[24:25], s[2:3], v[156:157] op_sel_hi:[1,0,1]
	v_pk_fma_f32 v[154:155], v[26:27], s[2:3], v[154:155] op_sel_hi:[1,0,1]
	v_pk_fma_f32 v[152:153], v[28:29], s[2:3], v[152:153] op_sel_hi:[1,0,1]
	v_pk_fma_f32 v[150:151], v[30:31], s[2:3], v[150:151] op_sel_hi:[1,0,1]
	v_readlane_b32 s2, v131, 26
	s_waitcnt vmcnt(18)
	v_cvt_scalef32_pk32_f32_fp6 v[0:31], v[38:43], 1.0
	v_pk_fma_f32 v[38:39], v[0:1], s[2:3], v[50:51] op_sel_hi:[1,0,1]
	v_pk_fma_f32 v[40:41], v[2:3], s[2:3], v[52:53] op_sel_hi:[1,0,1]
	v_pk_fma_f32 v[42:43], v[4:5], s[2:3], v[54:55] op_sel_hi:[1,0,1]
	v_pk_fma_f32 v[50:51], v[6:7], s[2:3], v[62:63] op_sel_hi:[1,0,1]
	v_pk_fma_f32 v[52:53], v[8:9], s[2:3], v[64:65] op_sel_hi:[1,0,1]
	v_pk_fma_f32 v[54:55], v[10:11], s[2:3], v[66:67] op_sel_hi:[1,0,1]
	v_pk_fma_f32 v[62:63], v[12:13], s[2:3], v[164:165] op_sel_hi:[1,0,1]
	v_pk_fma_f32 v[64:65], v[14:15], s[2:3], v[166:167] op_sel_hi:[1,0,1]
	v_pk_fma_f32 v[66:67], v[16:17], s[2:3], v[168:169] op_sel_hi:[1,0,1]
	v_pk_fma_f32 v[162:163], v[18:19], s[2:3], v[162:163] op_sel_hi:[1,0,1]
	v_pk_fma_f32 v[160:161], v[20:21], s[2:3], v[160:161] op_sel_hi:[1,0,1]
	v_pk_fma_f32 v[158:159], v[22:23], s[2:3], v[158:159] op_sel_hi:[1,0,1]
	v_pk_fma_f32 v[156:157], v[24:25], s[2:3], v[156:157] op_sel_hi:[1,0,1]
	v_pk_fma_f32 v[154:155], v[26:27], s[2:3], v[154:155] op_sel_hi:[1,0,1]
	v_pk_fma_f32 v[152:153], v[28:29], s[2:3], v[152:153] op_sel_hi:[1,0,1]
	v_pk_fma_f32 v[150:151], v[30:31], s[2:3], v[150:151] op_sel_hi:[1,0,1]
	v_readlane_b32 s2, v131, 27
	s_waitcnt vmcnt(16)
	v_cvt_scalef32_pk32_f32_fp6 v[0:31], v[32:37], 1.0
	v_pk_fma_f32 v[164:165], v[0:1], s[2:3], v[38:39] op_sel_hi:[1,0,1]
	v_pk_fma_f32 v[166:167], v[2:3], s[2:3], v[40:41] op_sel_hi:[1,0,1]
	v_pk_fma_f32 v[168:169], v[4:5], s[2:3], v[42:43] op_sel_hi:[1,0,1]
	v_pk_fma_f32 v[170:171], v[6:7], s[2:3], v[50:51] op_sel_hi:[1,0,1]
	v_pk_fma_f32 v[172:173], v[8:9], s[2:3], v[52:53] op_sel_hi:[1,0,1]
	v_pk_fma_f32 v[174:175], v[10:11], s[2:3], v[54:55] op_sel_hi:[1,0,1]
	v_pk_fma_f32 v[176:177], v[12:13], s[2:3], v[62:63] op_sel_hi:[1,0,1]
	v_pk_fma_f32 v[178:179], v[14:15], s[2:3], v[64:65] op_sel_hi:[1,0,1]
	v_pk_fma_f32 v[180:181], v[16:17], s[2:3], v[66:67] op_sel_hi:[1,0,1]
	v_pk_fma_f32 v[162:163], v[18:19], s[2:3], v[162:163] op_sel_hi:[1,0,1]
	v_pk_fma_f32 v[160:161], v[20:21], s[2:3], v[160:161] op_sel_hi:[1,0,1]
	v_pk_fma_f32 v[158:159], v[22:23], s[2:3], v[158:159] op_sel_hi:[1,0,1]
	v_pk_fma_f32 v[156:157], v[24:25], s[2:3], v[156:157] op_sel_hi:[1,0,1]
	v_pk_fma_f32 v[154:155], v[26:27], s[2:3], v[154:155] op_sel_hi:[1,0,1]
	v_pk_fma_f32 v[152:153], v[28:29], s[2:3], v[152:153] op_sel_hi:[1,0,1]
	v_pk_fma_f32 v[150:151], v[30:31], s[2:3], v[150:151] op_sel_hi:[1,0,1]
	v_readlane_b32 s2, v241, 36
	v_readlane_b32 s3, v241, 37
	v_readlane_b32 s100, v241, 38
	v_readlane_b32 s101, v241, 39
	s_nop 1
	buffer_load_dwordx4 v[62:65], v129, s[44:47], s2 offen
	buffer_load_dwordx2 v[66:67], v210, s[44:47], s2 offen
	buffer_load_dwordx4 v[50:53], v129, s[44:47], s3 offen
	buffer_load_dwordx2 v[54:55], v210, s[44:47], s3 offen
	buffer_load_dwordx4 v[38:41], v129, s[44:47], s100 offen
	buffer_load_dwordx2 v[42:43], v210, s[44:47], s100 offen
	buffer_load_dwordx4 v[32:35], v129, s[44:47], s101 offen
	buffer_load_dwordx2 v[36:37], v210, s[44:47], s101 offen
	v_readlane_b32 s2, v131, 28
	s_waitcnt vmcnt(22)
	v_cvt_scalef32_pk32_f32_fp6 v[0:31], v[98:103], 1.0
	v_pk_fma_f32 v[98:99], v[0:1], s[2:3], v[164:165] op_sel_hi:[1,0,1]
	v_pk_fma_f32 v[100:101], v[2:3], s[2:3], v[166:167] op_sel_hi:[1,0,1]
	v_pk_fma_f32 v[102:103], v[4:5], s[2:3], v[168:169] op_sel_hi:[1,0,1]
	v_pk_fma_f32 v[164:165], v[6:7], s[2:3], v[170:171] op_sel_hi:[1,0,1]
	v_pk_fma_f32 v[166:167], v[8:9], s[2:3], v[172:173] op_sel_hi:[1,0,1]
	v_pk_fma_f32 v[168:169], v[10:11], s[2:3], v[174:175] op_sel_hi:[1,0,1]
	v_pk_fma_f32 v[170:171], v[12:13], s[2:3], v[176:177] op_sel_hi:[1,0,1]
	v_pk_fma_f32 v[172:173], v[14:15], s[2:3], v[178:179] op_sel_hi:[1,0,1]
	v_pk_fma_f32 v[174:175], v[16:17], s[2:3], v[180:181] op_sel_hi:[1,0,1]
	v_pk_fma_f32 v[162:163], v[18:19], s[2:3], v[162:163] op_sel_hi:[1,0,1]
	v_pk_fma_f32 v[160:161], v[20:21], s[2:3], v[160:161] op_sel_hi:[1,0,1]
	v_pk_fma_f32 v[158:159], v[22:23], s[2:3], v[158:159] op_sel_hi:[1,0,1]
	v_pk_fma_f32 v[156:157], v[24:25], s[2:3], v[156:157] op_sel_hi:[1,0,1]
	v_pk_fma_f32 v[154:155], v[26:27], s[2:3], v[154:155] op_sel_hi:[1,0,1]
	v_pk_fma_f32 v[152:153], v[28:29], s[2:3], v[152:153] op_sel_hi:[1,0,1]
	v_pk_fma_f32 v[150:151], v[30:31], s[2:3], v[150:151] op_sel_hi:[1,0,1]
	v_readlane_b32 s2, v131, 29
	s_waitcnt vmcnt(20)
	v_cvt_scalef32_pk32_f32_fp6 v[0:31], v[92:97], 1.0
	v_pk_fma_f32 v[92:93], v[0:1], s[2:3], v[98:99] op_sel_hi:[1,0,1]
	v_pk_fma_f32 v[94:95], v[2:3], s[2:3], v[100:101] op_sel_hi:[1,0,1]
	v_pk_fma_f32 v[96:97], v[4:5], s[2:3], v[102:103] op_sel_hi:[1,0,1]
	v_pk_fma_f32 v[98:99], v[6:7], s[2:3], v[164:165] op_sel_hi:[1,0,1]
	v_pk_fma_f32 v[100:101], v[8:9], s[2:3], v[166:167] op_sel_hi:[1,0,1]
	v_pk_fma_f32 v[102:103], v[10:11], s[2:3], v[168:169] op_sel_hi:[1,0,1]
	v_pk_fma_f32 v[164:165], v[12:13], s[2:3], v[170:171] op_sel_hi:[1,0,1]
	v_pk_fma_f32 v[166:167], v[14:15], s[2:3], v[172:173] op_sel_hi:[1,0,1]
	v_pk_fma_f32 v[168:169], v[16:17], s[2:3], v[174:175] op_sel_hi:[1,0,1]
	v_pk_fma_f32 v[162:163], v[18:19], s[2:3], v[162:163] op_sel_hi:[1,0,1]
	v_pk_fma_f32 v[160:161], v[20:21], s[2:3], v[160:161] op_sel_hi:[1,0,1]
	v_pk_fma_f32 v[158:159], v[22:23], s[2:3], v[158:159] op_sel_hi:[1,0,1]
	v_pk_fma_f32 v[156:157], v[24:25], s[2:3], v[156:157] op_sel_hi:[1,0,1]
	v_pk_fma_f32 v[154:155], v[26:27], s[2:3], v[154:155] op_sel_hi:[1,0,1]
	v_pk_fma_f32 v[152:153], v[28:29], s[2:3], v[152:153] op_sel_hi:[1,0,1]
	v_pk_fma_f32 v[150:151], v[30:31], s[2:3], v[150:151] op_sel_hi:[1,0,1]
	v_readlane_b32 s2, v131, 30
	s_waitcnt vmcnt(18)
	v_cvt_scalef32_pk32_f32_fp6 v[0:31], v[86:91], 1.0
	v_pk_fma_f32 v[86:87], v[0:1], s[2:3], v[92:93] op_sel_hi:[1,0,1]
	v_pk_fma_f32 v[88:89], v[2:3], s[2:3], v[94:95] op_sel_hi:[1,0,1]
	v_pk_fma_f32 v[90:91], v[4:5], s[2:3], v[96:97] op_sel_hi:[1,0,1]
	v_pk_fma_f32 v[92:93], v[6:7], s[2:3], v[98:99] op_sel_hi:[1,0,1]
	v_pk_fma_f32 v[94:95], v[8:9], s[2:3], v[100:101] op_sel_hi:[1,0,1]
	v_pk_fma_f32 v[96:97], v[10:11], s[2:3], v[102:103] op_sel_hi:[1,0,1]
	v_pk_fma_f32 v[98:99], v[12:13], s[2:3], v[164:165] op_sel_hi:[1,0,1]
	v_pk_fma_f32 v[100:101], v[14:15], s[2:3], v[166:167] op_sel_hi:[1,0,1]
	v_pk_fma_f32 v[102:103], v[16:17], s[2:3], v[168:169] op_sel_hi:[1,0,1]
	v_pk_fma_f32 v[162:163], v[18:19], s[2:3], v[162:163] op_sel_hi:[1,0,1]
	v_pk_fma_f32 v[160:161], v[20:21], s[2:3], v[160:161] op_sel_hi:[1,0,1]
	v_pk_fma_f32 v[158:159], v[22:23], s[2:3], v[158:159] op_sel_hi:[1,0,1]
	v_pk_fma_f32 v[156:157], v[24:25], s[2:3], v[156:157] op_sel_hi:[1,0,1]
	v_pk_fma_f32 v[154:155], v[26:27], s[2:3], v[154:155] op_sel_hi:[1,0,1]
	v_pk_fma_f32 v[152:153], v[28:29], s[2:3], v[152:153] op_sel_hi:[1,0,1]
	v_pk_fma_f32 v[150:151], v[30:31], s[2:3], v[150:151] op_sel_hi:[1,0,1]
	v_readlane_b32 s2, v131, 31
	s_waitcnt vmcnt(16)
	v_cvt_scalef32_pk32_f32_fp6 v[0:31], v[80:85], 1.0
	v_pk_fma_f32 v[180:181], v[0:1], s[2:3], v[86:87] op_sel_hi:[1,0,1]
	v_pk_fma_f32 v[178:179], v[2:3], s[2:3], v[88:89] op_sel_hi:[1,0,1]
	v_pk_fma_f32 v[176:177], v[4:5], s[2:3], v[90:91] op_sel_hi:[1,0,1]
	v_pk_fma_f32 v[174:175], v[6:7], s[2:3], v[92:93] op_sel_hi:[1,0,1]
	v_pk_fma_f32 v[172:173], v[8:9], s[2:3], v[94:95] op_sel_hi:[1,0,1]
	v_pk_fma_f32 v[170:171], v[10:11], s[2:3], v[96:97] op_sel_hi:[1,0,1]
	v_pk_fma_f32 v[168:169], v[12:13], s[2:3], v[98:99] op_sel_hi:[1,0,1]
	v_pk_fma_f32 v[166:167], v[14:15], s[2:3], v[100:101] op_sel_hi:[1,0,1]
	v_pk_fma_f32 v[164:165], v[16:17], s[2:3], v[102:103] op_sel_hi:[1,0,1]
	v_pk_fma_f32 v[162:163], v[18:19], s[2:3], v[162:163] op_sel_hi:[1,0,1]
	v_pk_fma_f32 v[160:161], v[20:21], s[2:3], v[160:161] op_sel_hi:[1,0,1]
	v_pk_fma_f32 v[158:159], v[22:23], s[2:3], v[158:159] op_sel_hi:[1,0,1]
	v_pk_fma_f32 v[156:157], v[24:25], s[2:3], v[156:157] op_sel_hi:[1,0,1]
	v_pk_fma_f32 v[154:155], v[26:27], s[2:3], v[154:155] op_sel_hi:[1,0,1]
	v_pk_fma_f32 v[152:153], v[28:29], s[2:3], v[152:153] op_sel_hi:[1,0,1]
	v_pk_fma_f32 v[150:151], v[30:31], s[2:3], v[150:151] op_sel_hi:[1,0,1]
	v_readlane_b32 s2, v241, 40
	v_readlane_b32 s3, v241, 41
	v_readlane_b32 s100, v241, 42
	v_readlane_b32 s101, v241, 43
	s_nop 1
	buffer_load_dwordx4 v[98:101], v129, s[44:47], s2 offen
	buffer_load_dwordx2 v[102:103], v210, s[44:47], s2 offen
	buffer_load_dwordx4 v[92:95], v129, s[44:47], s3 offen
	buffer_load_dwordx2 v[96:97], v210, s[44:47], s3 offen
	buffer_load_dwordx4 v[86:89], v129, s[44:47], s100 offen
	buffer_load_dwordx2 v[90:91], v210, s[44:47], s100 offen
	buffer_load_dwordx4 v[80:83], v129, s[44:47], s101 offen
	buffer_load_dwordx2 v[84:85], v210, s[44:47], s101 offen
	v_readlane_b32 s2, v131, 32
	s_waitcnt vmcnt(22)
	v_cvt_scalef32_pk32_f32_fp6 v[0:31], v[74:79], 1.0
	v_pk_fma_f32 v[74:75], v[0:1], s[2:3], v[180:181] op_sel_hi:[1,0,1]
	v_pk_fma_f32 v[76:77], v[2:3], s[2:3], v[178:179] op_sel_hi:[1,0,1]
	v_pk_fma_f32 v[78:79], v[4:5], s[2:3], v[176:177] op_sel_hi:[1,0,1]
	v_pk_fma_f32 v[174:175], v[6:7], s[2:3], v[174:175] op_sel_hi:[1,0,1]
	v_pk_fma_f32 v[172:173], v[8:9], s[2:3], v[172:173] op_sel_hi:[1,0,1]
	v_pk_fma_f32 v[170:171], v[10:11], s[2:3], v[170:171] op_sel_hi:[1,0,1]
	v_pk_fma_f32 v[168:169], v[12:13], s[2:3], v[168:169] op_sel_hi:[1,0,1]
	v_pk_fma_f32 v[166:167], v[14:15], s[2:3], v[166:167] op_sel_hi:[1,0,1]
	v_pk_fma_f32 v[164:165], v[16:17], s[2:3], v[164:165] op_sel_hi:[1,0,1]
	v_pk_fma_f32 v[162:163], v[18:19], s[2:3], v[162:163] op_sel_hi:[1,0,1]
	v_pk_fma_f32 v[160:161], v[20:21], s[2:3], v[160:161] op_sel_hi:[1,0,1]
	v_pk_fma_f32 v[158:159], v[22:23], s[2:3], v[158:159] op_sel_hi:[1,0,1]
	v_pk_fma_f32 v[156:157], v[24:25], s[2:3], v[156:157] op_sel_hi:[1,0,1]
	v_pk_fma_f32 v[154:155], v[26:27], s[2:3], v[154:155] op_sel_hi:[1,0,1]
	v_pk_fma_f32 v[152:153], v[28:29], s[2:3], v[152:153] op_sel_hi:[1,0,1]
	v_pk_fma_f32 v[150:151], v[30:31], s[2:3], v[150:151] op_sel_hi:[1,0,1]
	v_readlane_b32 s2, v131, 33
	s_waitcnt vmcnt(20)
	v_cvt_scalef32_pk32_f32_fp6 v[0:31], v[68:73], 1.0
	v_pk_fma_f32 v[68:69], v[0:1], s[2:3], v[74:75] op_sel_hi:[1,0,1]
	v_pk_fma_f32 v[70:71], v[2:3], s[2:3], v[76:77] op_sel_hi:[1,0,1]
	v_pk_fma_f32 v[72:73], v[4:5], s[2:3], v[78:79] op_sel_hi:[1,0,1]
	v_pk_fma_f32 v[74:75], v[6:7], s[2:3], v[174:175] op_sel_hi:[1,0,1]
	v_pk_fma_f32 v[76:77], v[8:9], s[2:3], v[172:173] op_sel_hi:[1,0,1]
	v_pk_fma_f32 v[78:79], v[10:11], s[2:3], v[170:171] op_sel_hi:[1,0,1]
	v_pk_fma_f32 v[168:169], v[12:13], s[2:3], v[168:169] op_sel_hi:[1,0,1]
	v_pk_fma_f32 v[166:167], v[14:15], s[2:3], v[166:167] op_sel_hi:[1,0,1]
	v_pk_fma_f32 v[164:165], v[16:17], s[2:3], v[164:165] op_sel_hi:[1,0,1]
	v_pk_fma_f32 v[162:163], v[18:19], s[2:3], v[162:163] op_sel_hi:[1,0,1]
	v_pk_fma_f32 v[160:161], v[20:21], s[2:3], v[160:161] op_sel_hi:[1,0,1]
	v_pk_fma_f32 v[158:159], v[22:23], s[2:3], v[158:159] op_sel_hi:[1,0,1]
	v_pk_fma_f32 v[156:157], v[24:25], s[2:3], v[156:157] op_sel_hi:[1,0,1]
	v_pk_fma_f32 v[154:155], v[26:27], s[2:3], v[154:155] op_sel_hi:[1,0,1]
	v_pk_fma_f32 v[152:153], v[28:29], s[2:3], v[152:153] op_sel_hi:[1,0,1]
	v_pk_fma_f32 v[150:151], v[30:31], s[2:3], v[150:151] op_sel_hi:[1,0,1]
	v_readlane_b32 s2, v131, 34
	s_waitcnt vmcnt(18)
	v_cvt_scalef32_pk32_f32_fp6 v[0:31], v[56:61], 1.0
	v_pk_fma_f32 v[56:57], v[0:1], s[2:3], v[68:69] op_sel_hi:[1,0,1]
	v_pk_fma_f32 v[58:59], v[2:3], s[2:3], v[70:71] op_sel_hi:[1,0,1]
	v_pk_fma_f32 v[60:61], v[4:5], s[2:3], v[72:73] op_sel_hi:[1,0,1]
	v_pk_fma_f32 v[68:69], v[6:7], s[2:3], v[74:75] op_sel_hi:[1,0,1]
	v_pk_fma_f32 v[70:71], v[8:9], s[2:3], v[76:77] op_sel_hi:[1,0,1]
	v_pk_fma_f32 v[72:73], v[10:11], s[2:3], v[78:79] op_sel_hi:[1,0,1]
	v_pk_fma_f32 v[74:75], v[12:13], s[2:3], v[168:169] op_sel_hi:[1,0,1]
	v_pk_fma_f32 v[76:77], v[14:15], s[2:3], v[166:167] op_sel_hi:[1,0,1]
	v_pk_fma_f32 v[78:79], v[16:17], s[2:3], v[164:165] op_sel_hi:[1,0,1]
	v_pk_fma_f32 v[162:163], v[18:19], s[2:3], v[162:163] op_sel_hi:[1,0,1]
	v_pk_fma_f32 v[160:161], v[20:21], s[2:3], v[160:161] op_sel_hi:[1,0,1]
	v_pk_fma_f32 v[158:159], v[22:23], s[2:3], v[158:159] op_sel_hi:[1,0,1]
	v_pk_fma_f32 v[156:157], v[24:25], s[2:3], v[156:157] op_sel_hi:[1,0,1]
	v_pk_fma_f32 v[154:155], v[26:27], s[2:3], v[154:155] op_sel_hi:[1,0,1]
	v_pk_fma_f32 v[152:153], v[28:29], s[2:3], v[152:153] op_sel_hi:[1,0,1]
	v_pk_fma_f32 v[150:151], v[30:31], s[2:3], v[150:151] op_sel_hi:[1,0,1]
	v_readlane_b32 s2, v131, 35
	s_waitcnt vmcnt(16)
	v_cvt_scalef32_pk32_f32_fp6 v[0:31], v[44:49], 1.0
	v_pk_fma_f32 v[164:165], v[0:1], s[2:3], v[56:57] op_sel_hi:[1,0,1]
	v_pk_fma_f32 v[166:167], v[2:3], s[2:3], v[58:59] op_sel_hi:[1,0,1]
	v_pk_fma_f32 v[168:169], v[4:5], s[2:3], v[60:61] op_sel_hi:[1,0,1]
	v_pk_fma_f32 v[170:171], v[6:7], s[2:3], v[68:69] op_sel_hi:[1,0,1]
	v_pk_fma_f32 v[172:173], v[8:9], s[2:3], v[70:71] op_sel_hi:[1,0,1]
	v_pk_fma_f32 v[174:175], v[10:11], s[2:3], v[72:73] op_sel_hi:[1,0,1]
	v_pk_fma_f32 v[176:177], v[12:13], s[2:3], v[74:75] op_sel_hi:[1,0,1]
	v_pk_fma_f32 v[178:179], v[14:15], s[2:3], v[76:77] op_sel_hi:[1,0,1]
	v_pk_fma_f32 v[180:181], v[16:17], s[2:3], v[78:79] op_sel_hi:[1,0,1]
	v_pk_fma_f32 v[162:163], v[18:19], s[2:3], v[162:163] op_sel_hi:[1,0,1]
	v_pk_fma_f32 v[160:161], v[20:21], s[2:3], v[160:161] op_sel_hi:[1,0,1]
	v_pk_fma_f32 v[158:159], v[22:23], s[2:3], v[158:159] op_sel_hi:[1,0,1]
	v_pk_fma_f32 v[156:157], v[24:25], s[2:3], v[156:157] op_sel_hi:[1,0,1]
	v_pk_fma_f32 v[154:155], v[26:27], s[2:3], v[154:155] op_sel_hi:[1,0,1]
	v_pk_fma_f32 v[152:153], v[28:29], s[2:3], v[152:153] op_sel_hi:[1,0,1]
	v_pk_fma_f32 v[150:151], v[30:31], s[2:3], v[150:151] op_sel_hi:[1,0,1]
	v_readlane_b32 s2, v241, 44
	v_readlane_b32 s3, v241, 45
	v_readlane_b32 s100, v241, 46
	v_readlane_b32 s101, v241, 47
	s_nop 1
	buffer_load_dwordx4 v[74:77], v129, s[44:47], s2 offen
	buffer_load_dwordx2 v[78:79], v210, s[44:47], s2 offen
	buffer_load_dwordx4 v[68:71], v129, s[44:47], s3 offen
	buffer_load_dwordx2 v[72:73], v210, s[44:47], s3 offen
	buffer_load_dwordx4 v[56:59], v129, s[44:47], s100 offen
	buffer_load_dwordx2 v[60:61], v210, s[44:47], s100 offen
	buffer_load_dwordx4 v[44:47], v129, s[44:47], s101 offen
	buffer_load_dwordx2 v[48:49], v210, s[44:47], s101 offen
	v_readlane_b32 s2, v131, 36
	s_waitcnt vmcnt(22)
	v_cvt_scalef32_pk32_f32_fp6 v[0:31], v[62:67], 1.0
	v_pk_fma_f32 v[62:63], v[0:1], s[2:3], v[164:165] op_sel_hi:[1,0,1]
	v_pk_fma_f32 v[64:65], v[2:3], s[2:3], v[166:167] op_sel_hi:[1,0,1]
	v_pk_fma_f32 v[66:67], v[4:5], s[2:3], v[168:169] op_sel_hi:[1,0,1]
	v_pk_fma_f32 v[164:165], v[6:7], s[2:3], v[170:171] op_sel_hi:[1,0,1]
	v_pk_fma_f32 v[166:167], v[8:9], s[2:3], v[172:173] op_sel_hi:[1,0,1]
	v_pk_fma_f32 v[168:169], v[10:11], s[2:3], v[174:175] op_sel_hi:[1,0,1]
	v_pk_fma_f32 v[170:171], v[12:13], s[2:3], v[176:177] op_sel_hi:[1,0,1]
	v_pk_fma_f32 v[172:173], v[14:15], s[2:3], v[178:179] op_sel_hi:[1,0,1]
	v_pk_fma_f32 v[174:175], v[16:17], s[2:3], v[180:181] op_sel_hi:[1,0,1]
	v_pk_fma_f32 v[162:163], v[18:19], s[2:3], v[162:163] op_sel_hi:[1,0,1]
	v_pk_fma_f32 v[160:161], v[20:21], s[2:3], v[160:161] op_sel_hi:[1,0,1]
	v_pk_fma_f32 v[158:159], v[22:23], s[2:3], v[158:159] op_sel_hi:[1,0,1]
	v_pk_fma_f32 v[156:157], v[24:25], s[2:3], v[156:157] op_sel_hi:[1,0,1]
	v_pk_fma_f32 v[154:155], v[26:27], s[2:3], v[154:155] op_sel_hi:[1,0,1]
	v_pk_fma_f32 v[152:153], v[28:29], s[2:3], v[152:153] op_sel_hi:[1,0,1]
	v_pk_fma_f32 v[150:151], v[30:31], s[2:3], v[150:151] op_sel_hi:[1,0,1]
	v_readlane_b32 s2, v131, 37
	s_waitcnt vmcnt(20)
	v_cvt_scalef32_pk32_f32_fp6 v[0:31], v[50:55], 1.0
	v_pk_fma_f32 v[50:51], v[0:1], s[2:3], v[62:63] op_sel_hi:[1,0,1]
	v_pk_fma_f32 v[52:53], v[2:3], s[2:3], v[64:65] op_sel_hi:[1,0,1]
	v_pk_fma_f32 v[54:55], v[4:5], s[2:3], v[66:67] op_sel_hi:[1,0,1]
	v_pk_fma_f32 v[62:63], v[6:7], s[2:3], v[164:165] op_sel_hi:[1,0,1]
	v_pk_fma_f32 v[64:65], v[8:9], s[2:3], v[166:167] op_sel_hi:[1,0,1]
	v_pk_fma_f32 v[66:67], v[10:11], s[2:3], v[168:169] op_sel_hi:[1,0,1]
	v_pk_fma_f32 v[164:165], v[12:13], s[2:3], v[170:171] op_sel_hi:[1,0,1]
	v_pk_fma_f32 v[166:167], v[14:15], s[2:3], v[172:173] op_sel_hi:[1,0,1]
	v_pk_fma_f32 v[168:169], v[16:17], s[2:3], v[174:175] op_sel_hi:[1,0,1]
	v_pk_fma_f32 v[162:163], v[18:19], s[2:3], v[162:163] op_sel_hi:[1,0,1]
	v_pk_fma_f32 v[160:161], v[20:21], s[2:3], v[160:161] op_sel_hi:[1,0,1]
	v_pk_fma_f32 v[158:159], v[22:23], s[2:3], v[158:159] op_sel_hi:[1,0,1]
	v_pk_fma_f32 v[156:157], v[24:25], s[2:3], v[156:157] op_sel_hi:[1,0,1]
	v_pk_fma_f32 v[154:155], v[26:27], s[2:3], v[154:155] op_sel_hi:[1,0,1]
	v_pk_fma_f32 v[152:153], v[28:29], s[2:3], v[152:153] op_sel_hi:[1,0,1]
	v_pk_fma_f32 v[150:151], v[30:31], s[2:3], v[150:151] op_sel_hi:[1,0,1]
	v_readlane_b32 s2, v131, 38
	s_waitcnt vmcnt(18)
	v_cvt_scalef32_pk32_f32_fp6 v[0:31], v[38:43], 1.0
	v_pk_fma_f32 v[38:39], v[0:1], s[2:3], v[50:51] op_sel_hi:[1,0,1]
	v_pk_fma_f32 v[40:41], v[2:3], s[2:3], v[52:53] op_sel_hi:[1,0,1]
	v_pk_fma_f32 v[42:43], v[4:5], s[2:3], v[54:55] op_sel_hi:[1,0,1]
	v_pk_fma_f32 v[50:51], v[6:7], s[2:3], v[62:63] op_sel_hi:[1,0,1]
	v_pk_fma_f32 v[52:53], v[8:9], s[2:3], v[64:65] op_sel_hi:[1,0,1]
	v_pk_fma_f32 v[54:55], v[10:11], s[2:3], v[66:67] op_sel_hi:[1,0,1]
	v_pk_fma_f32 v[62:63], v[12:13], s[2:3], v[164:165] op_sel_hi:[1,0,1]
	v_pk_fma_f32 v[64:65], v[14:15], s[2:3], v[166:167] op_sel_hi:[1,0,1]
	v_pk_fma_f32 v[66:67], v[16:17], s[2:3], v[168:169] op_sel_hi:[1,0,1]
	v_pk_fma_f32 v[162:163], v[18:19], s[2:3], v[162:163] op_sel_hi:[1,0,1]
	v_pk_fma_f32 v[160:161], v[20:21], s[2:3], v[160:161] op_sel_hi:[1,0,1]
	v_pk_fma_f32 v[158:159], v[22:23], s[2:3], v[158:159] op_sel_hi:[1,0,1]
	v_pk_fma_f32 v[156:157], v[24:25], s[2:3], v[156:157] op_sel_hi:[1,0,1]
	v_pk_fma_f32 v[154:155], v[26:27], s[2:3], v[154:155] op_sel_hi:[1,0,1]
	v_pk_fma_f32 v[152:153], v[28:29], s[2:3], v[152:153] op_sel_hi:[1,0,1]
	v_pk_fma_f32 v[150:151], v[30:31], s[2:3], v[150:151] op_sel_hi:[1,0,1]
	v_readlane_b32 s2, v131, 39
	s_waitcnt vmcnt(16)
	v_cvt_scalef32_pk32_f32_fp6 v[0:31], v[32:37], 1.0
	v_pk_fma_f32 v[164:165], v[0:1], s[2:3], v[38:39] op_sel_hi:[1,0,1]
	v_pk_fma_f32 v[166:167], v[2:3], s[2:3], v[40:41] op_sel_hi:[1,0,1]
	v_pk_fma_f32 v[168:169], v[4:5], s[2:3], v[42:43] op_sel_hi:[1,0,1]
	v_pk_fma_f32 v[170:171], v[6:7], s[2:3], v[50:51] op_sel_hi:[1,0,1]
	v_pk_fma_f32 v[172:173], v[8:9], s[2:3], v[52:53] op_sel_hi:[1,0,1]
	v_pk_fma_f32 v[174:175], v[10:11], s[2:3], v[54:55] op_sel_hi:[1,0,1]
	v_pk_fma_f32 v[176:177], v[12:13], s[2:3], v[62:63] op_sel_hi:[1,0,1]
	v_pk_fma_f32 v[178:179], v[14:15], s[2:3], v[64:65] op_sel_hi:[1,0,1]
	v_pk_fma_f32 v[180:181], v[16:17], s[2:3], v[66:67] op_sel_hi:[1,0,1]
	v_pk_fma_f32 v[162:163], v[18:19], s[2:3], v[162:163] op_sel_hi:[1,0,1]
	v_pk_fma_f32 v[160:161], v[20:21], s[2:3], v[160:161] op_sel_hi:[1,0,1]
	v_pk_fma_f32 v[158:159], v[22:23], s[2:3], v[158:159] op_sel_hi:[1,0,1]
	v_pk_fma_f32 v[156:157], v[24:25], s[2:3], v[156:157] op_sel_hi:[1,0,1]
	v_pk_fma_f32 v[154:155], v[26:27], s[2:3], v[154:155] op_sel_hi:[1,0,1]
	v_pk_fma_f32 v[152:153], v[28:29], s[2:3], v[152:153] op_sel_hi:[1,0,1]
	v_pk_fma_f32 v[150:151], v[30:31], s[2:3], v[150:151] op_sel_hi:[1,0,1]
	v_readlane_b32 s2, v241, 48
	v_readlane_b32 s3, v241, 49
	v_readlane_b32 s100, v241, 50
	v_readlane_b32 s101, v241, 51
	s_nop 1
	buffer_load_dwordx4 v[62:65], v129, s[44:47], s2 offen
	buffer_load_dwordx2 v[66:67], v210, s[44:47], s2 offen
	buffer_load_dwordx4 v[50:53], v129, s[44:47], s3 offen
	buffer_load_dwordx2 v[54:55], v210, s[44:47], s3 offen
	buffer_load_dwordx4 v[38:41], v129, s[44:47], s100 offen
	buffer_load_dwordx2 v[42:43], v210, s[44:47], s100 offen
	buffer_load_dwordx4 v[32:35], v129, s[44:47], s101 offen
	buffer_load_dwordx2 v[36:37], v210, s[44:47], s101 offen
	v_readlane_b32 s2, v131, 40
	s_waitcnt vmcnt(22)
	v_cvt_scalef32_pk32_f32_fp6 v[0:31], v[98:103], 1.0
	v_pk_fma_f32 v[98:99], v[0:1], s[2:3], v[164:165] op_sel_hi:[1,0,1]
	v_pk_fma_f32 v[100:101], v[2:3], s[2:3], v[166:167] op_sel_hi:[1,0,1]
	v_pk_fma_f32 v[102:103], v[4:5], s[2:3], v[168:169] op_sel_hi:[1,0,1]
	v_pk_fma_f32 v[164:165], v[6:7], s[2:3], v[170:171] op_sel_hi:[1,0,1]
	v_pk_fma_f32 v[166:167], v[8:9], s[2:3], v[172:173] op_sel_hi:[1,0,1]
	v_pk_fma_f32 v[168:169], v[10:11], s[2:3], v[174:175] op_sel_hi:[1,0,1]
	v_pk_fma_f32 v[170:171], v[12:13], s[2:3], v[176:177] op_sel_hi:[1,0,1]
	v_pk_fma_f32 v[172:173], v[14:15], s[2:3], v[178:179] op_sel_hi:[1,0,1]
	v_pk_fma_f32 v[174:175], v[16:17], s[2:3], v[180:181] op_sel_hi:[1,0,1]
	v_pk_fma_f32 v[162:163], v[18:19], s[2:3], v[162:163] op_sel_hi:[1,0,1]
	v_pk_fma_f32 v[160:161], v[20:21], s[2:3], v[160:161] op_sel_hi:[1,0,1]
	v_pk_fma_f32 v[158:159], v[22:23], s[2:3], v[158:159] op_sel_hi:[1,0,1]
	v_pk_fma_f32 v[156:157], v[24:25], s[2:3], v[156:157] op_sel_hi:[1,0,1]
	v_pk_fma_f32 v[154:155], v[26:27], s[2:3], v[154:155] op_sel_hi:[1,0,1]
	v_pk_fma_f32 v[152:153], v[28:29], s[2:3], v[152:153] op_sel_hi:[1,0,1]
	v_pk_fma_f32 v[150:151], v[30:31], s[2:3], v[150:151] op_sel_hi:[1,0,1]
	v_readlane_b32 s2, v131, 41
	s_waitcnt vmcnt(20)
	v_cvt_scalef32_pk32_f32_fp6 v[0:31], v[92:97], 1.0
	v_pk_fma_f32 v[92:93], v[0:1], s[2:3], v[98:99] op_sel_hi:[1,0,1]
	v_pk_fma_f32 v[94:95], v[2:3], s[2:3], v[100:101] op_sel_hi:[1,0,1]
	v_pk_fma_f32 v[96:97], v[4:5], s[2:3], v[102:103] op_sel_hi:[1,0,1]
	v_pk_fma_f32 v[98:99], v[6:7], s[2:3], v[164:165] op_sel_hi:[1,0,1]
	v_pk_fma_f32 v[100:101], v[8:9], s[2:3], v[166:167] op_sel_hi:[1,0,1]
	v_pk_fma_f32 v[102:103], v[10:11], s[2:3], v[168:169] op_sel_hi:[1,0,1]
	v_pk_fma_f32 v[164:165], v[12:13], s[2:3], v[170:171] op_sel_hi:[1,0,1]
	v_pk_fma_f32 v[166:167], v[14:15], s[2:3], v[172:173] op_sel_hi:[1,0,1]
	v_pk_fma_f32 v[168:169], v[16:17], s[2:3], v[174:175] op_sel_hi:[1,0,1]
	v_pk_fma_f32 v[162:163], v[18:19], s[2:3], v[162:163] op_sel_hi:[1,0,1]
	v_pk_fma_f32 v[160:161], v[20:21], s[2:3], v[160:161] op_sel_hi:[1,0,1]
	v_pk_fma_f32 v[158:159], v[22:23], s[2:3], v[158:159] op_sel_hi:[1,0,1]
	v_pk_fma_f32 v[156:157], v[24:25], s[2:3], v[156:157] op_sel_hi:[1,0,1]
	v_pk_fma_f32 v[154:155], v[26:27], s[2:3], v[154:155] op_sel_hi:[1,0,1]
	v_pk_fma_f32 v[152:153], v[28:29], s[2:3], v[152:153] op_sel_hi:[1,0,1]
	v_pk_fma_f32 v[150:151], v[30:31], s[2:3], v[150:151] op_sel_hi:[1,0,1]
	v_readlane_b32 s2, v131, 42
	s_waitcnt vmcnt(18)
	v_cvt_scalef32_pk32_f32_fp6 v[0:31], v[86:91], 1.0
	v_pk_fma_f32 v[86:87], v[0:1], s[2:3], v[92:93] op_sel_hi:[1,0,1]
	v_pk_fma_f32 v[88:89], v[2:3], s[2:3], v[94:95] op_sel_hi:[1,0,1]
	v_pk_fma_f32 v[90:91], v[4:5], s[2:3], v[96:97] op_sel_hi:[1,0,1]
	v_pk_fma_f32 v[92:93], v[6:7], s[2:3], v[98:99] op_sel_hi:[1,0,1]
	v_pk_fma_f32 v[94:95], v[8:9], s[2:3], v[100:101] op_sel_hi:[1,0,1]
	v_pk_fma_f32 v[96:97], v[10:11], s[2:3], v[102:103] op_sel_hi:[1,0,1]
	v_pk_fma_f32 v[98:99], v[12:13], s[2:3], v[164:165] op_sel_hi:[1,0,1]
	v_pk_fma_f32 v[100:101], v[14:15], s[2:3], v[166:167] op_sel_hi:[1,0,1]
	v_pk_fma_f32 v[102:103], v[16:17], s[2:3], v[168:169] op_sel_hi:[1,0,1]
	v_pk_fma_f32 v[162:163], v[18:19], s[2:3], v[162:163] op_sel_hi:[1,0,1]
	v_pk_fma_f32 v[160:161], v[20:21], s[2:3], v[160:161] op_sel_hi:[1,0,1]
	v_pk_fma_f32 v[158:159], v[22:23], s[2:3], v[158:159] op_sel_hi:[1,0,1]
	v_pk_fma_f32 v[156:157], v[24:25], s[2:3], v[156:157] op_sel_hi:[1,0,1]
	v_pk_fma_f32 v[154:155], v[26:27], s[2:3], v[154:155] op_sel_hi:[1,0,1]
	v_pk_fma_f32 v[152:153], v[28:29], s[2:3], v[152:153] op_sel_hi:[1,0,1]
	v_pk_fma_f32 v[150:151], v[30:31], s[2:3], v[150:151] op_sel_hi:[1,0,1]
	v_readlane_b32 s2, v131, 43
	s_waitcnt vmcnt(16)
	v_cvt_scalef32_pk32_f32_fp6 v[0:31], v[80:85], 1.0
	v_pk_fma_f32 v[180:181], v[0:1], s[2:3], v[86:87] op_sel_hi:[1,0,1]
	v_pk_fma_f32 v[178:179], v[2:3], s[2:3], v[88:89] op_sel_hi:[1,0,1]
	v_pk_fma_f32 v[176:177], v[4:5], s[2:3], v[90:91] op_sel_hi:[1,0,1]
	v_pk_fma_f32 v[174:175], v[6:7], s[2:3], v[92:93] op_sel_hi:[1,0,1]
	v_pk_fma_f32 v[172:173], v[8:9], s[2:3], v[94:95] op_sel_hi:[1,0,1]
	v_pk_fma_f32 v[170:171], v[10:11], s[2:3], v[96:97] op_sel_hi:[1,0,1]
	v_pk_fma_f32 v[168:169], v[12:13], s[2:3], v[98:99] op_sel_hi:[1,0,1]
	v_pk_fma_f32 v[166:167], v[14:15], s[2:3], v[100:101] op_sel_hi:[1,0,1]
	v_pk_fma_f32 v[164:165], v[16:17], s[2:3], v[102:103] op_sel_hi:[1,0,1]
	v_pk_fma_f32 v[162:163], v[18:19], s[2:3], v[162:163] op_sel_hi:[1,0,1]
	v_pk_fma_f32 v[160:161], v[20:21], s[2:3], v[160:161] op_sel_hi:[1,0,1]
	v_pk_fma_f32 v[158:159], v[22:23], s[2:3], v[158:159] op_sel_hi:[1,0,1]
	v_pk_fma_f32 v[156:157], v[24:25], s[2:3], v[156:157] op_sel_hi:[1,0,1]
	v_pk_fma_f32 v[154:155], v[26:27], s[2:3], v[154:155] op_sel_hi:[1,0,1]
	v_pk_fma_f32 v[152:153], v[28:29], s[2:3], v[152:153] op_sel_hi:[1,0,1]
	v_pk_fma_f32 v[150:151], v[30:31], s[2:3], v[150:151] op_sel_hi:[1,0,1]
	v_readlane_b32 s2, v241, 52
	v_readlane_b32 s3, v241, 53
	v_readlane_b32 s100, v241, 54
	v_readlane_b32 s101, v241, 55
	s_nop 1
	buffer_load_dwordx4 v[98:101], v129, s[44:47], s2 offen
	buffer_load_dwordx2 v[102:103], v210, s[44:47], s2 offen
	buffer_load_dwordx4 v[92:95], v129, s[44:47], s3 offen
	buffer_load_dwordx2 v[96:97], v210, s[44:47], s3 offen
	buffer_load_dwordx4 v[86:89], v129, s[44:47], s100 offen
	buffer_load_dwordx2 v[90:91], v210, s[44:47], s100 offen
	buffer_load_dwordx4 v[80:83], v129, s[44:47], s101 offen
	buffer_load_dwordx2 v[84:85], v210, s[44:47], s101 offen
	v_readlane_b32 s2, v131, 44
	s_waitcnt vmcnt(22)
	v_cvt_scalef32_pk32_f32_fp6 v[0:31], v[74:79], 1.0
	v_pk_fma_f32 v[74:75], v[0:1], s[2:3], v[180:181] op_sel_hi:[1,0,1]
	v_pk_fma_f32 v[76:77], v[2:3], s[2:3], v[178:179] op_sel_hi:[1,0,1]
	v_pk_fma_f32 v[78:79], v[4:5], s[2:3], v[176:177] op_sel_hi:[1,0,1]
	v_pk_fma_f32 v[174:175], v[6:7], s[2:3], v[174:175] op_sel_hi:[1,0,1]
	v_pk_fma_f32 v[172:173], v[8:9], s[2:3], v[172:173] op_sel_hi:[1,0,1]
	v_pk_fma_f32 v[170:171], v[10:11], s[2:3], v[170:171] op_sel_hi:[1,0,1]
	v_pk_fma_f32 v[168:169], v[12:13], s[2:3], v[168:169] op_sel_hi:[1,0,1]
	v_pk_fma_f32 v[166:167], v[14:15], s[2:3], v[166:167] op_sel_hi:[1,0,1]
	v_pk_fma_f32 v[164:165], v[16:17], s[2:3], v[164:165] op_sel_hi:[1,0,1]
	v_pk_fma_f32 v[162:163], v[18:19], s[2:3], v[162:163] op_sel_hi:[1,0,1]
	v_pk_fma_f32 v[160:161], v[20:21], s[2:3], v[160:161] op_sel_hi:[1,0,1]
	v_pk_fma_f32 v[158:159], v[22:23], s[2:3], v[158:159] op_sel_hi:[1,0,1]
	v_pk_fma_f32 v[156:157], v[24:25], s[2:3], v[156:157] op_sel_hi:[1,0,1]
	v_pk_fma_f32 v[154:155], v[26:27], s[2:3], v[154:155] op_sel_hi:[1,0,1]
	v_pk_fma_f32 v[152:153], v[28:29], s[2:3], v[152:153] op_sel_hi:[1,0,1]
	v_pk_fma_f32 v[150:151], v[30:31], s[2:3], v[150:151] op_sel_hi:[1,0,1]
	v_readlane_b32 s2, v131, 45
	s_waitcnt vmcnt(20)
	v_cvt_scalef32_pk32_f32_fp6 v[0:31], v[68:73], 1.0
	v_pk_fma_f32 v[68:69], v[0:1], s[2:3], v[74:75] op_sel_hi:[1,0,1]
	v_pk_fma_f32 v[70:71], v[2:3], s[2:3], v[76:77] op_sel_hi:[1,0,1]
	v_pk_fma_f32 v[72:73], v[4:5], s[2:3], v[78:79] op_sel_hi:[1,0,1]
	v_pk_fma_f32 v[74:75], v[6:7], s[2:3], v[174:175] op_sel_hi:[1,0,1]
	v_pk_fma_f32 v[76:77], v[8:9], s[2:3], v[172:173] op_sel_hi:[1,0,1]
	v_pk_fma_f32 v[78:79], v[10:11], s[2:3], v[170:171] op_sel_hi:[1,0,1]
	v_pk_fma_f32 v[168:169], v[12:13], s[2:3], v[168:169] op_sel_hi:[1,0,1]
	v_pk_fma_f32 v[166:167], v[14:15], s[2:3], v[166:167] op_sel_hi:[1,0,1]
	v_pk_fma_f32 v[164:165], v[16:17], s[2:3], v[164:165] op_sel_hi:[1,0,1]
	v_pk_fma_f32 v[162:163], v[18:19], s[2:3], v[162:163] op_sel_hi:[1,0,1]
	v_pk_fma_f32 v[160:161], v[20:21], s[2:3], v[160:161] op_sel_hi:[1,0,1]
	v_pk_fma_f32 v[158:159], v[22:23], s[2:3], v[158:159] op_sel_hi:[1,0,1]
	v_pk_fma_f32 v[156:157], v[24:25], s[2:3], v[156:157] op_sel_hi:[1,0,1]
	v_pk_fma_f32 v[154:155], v[26:27], s[2:3], v[154:155] op_sel_hi:[1,0,1]
	v_pk_fma_f32 v[152:153], v[28:29], s[2:3], v[152:153] op_sel_hi:[1,0,1]
	v_pk_fma_f32 v[150:151], v[30:31], s[2:3], v[150:151] op_sel_hi:[1,0,1]
	v_readlane_b32 s2, v131, 46
	s_waitcnt vmcnt(18)
	v_cvt_scalef32_pk32_f32_fp6 v[0:31], v[56:61], 1.0
	v_pk_fma_f32 v[56:57], v[0:1], s[2:3], v[68:69] op_sel_hi:[1,0,1]
	v_pk_fma_f32 v[58:59], v[2:3], s[2:3], v[70:71] op_sel_hi:[1,0,1]
	v_pk_fma_f32 v[60:61], v[4:5], s[2:3], v[72:73] op_sel_hi:[1,0,1]
	v_pk_fma_f32 v[68:69], v[6:7], s[2:3], v[74:75] op_sel_hi:[1,0,1]
	v_pk_fma_f32 v[70:71], v[8:9], s[2:3], v[76:77] op_sel_hi:[1,0,1]
	v_pk_fma_f32 v[72:73], v[10:11], s[2:3], v[78:79] op_sel_hi:[1,0,1]
	v_pk_fma_f32 v[74:75], v[12:13], s[2:3], v[168:169] op_sel_hi:[1,0,1]
	v_pk_fma_f32 v[76:77], v[14:15], s[2:3], v[166:167] op_sel_hi:[1,0,1]
	v_pk_fma_f32 v[78:79], v[16:17], s[2:3], v[164:165] op_sel_hi:[1,0,1]
	v_pk_fma_f32 v[162:163], v[18:19], s[2:3], v[162:163] op_sel_hi:[1,0,1]
	v_pk_fma_f32 v[160:161], v[20:21], s[2:3], v[160:161] op_sel_hi:[1,0,1]
	v_pk_fma_f32 v[158:159], v[22:23], s[2:3], v[158:159] op_sel_hi:[1,0,1]
	v_pk_fma_f32 v[156:157], v[24:25], s[2:3], v[156:157] op_sel_hi:[1,0,1]
	v_pk_fma_f32 v[154:155], v[26:27], s[2:3], v[154:155] op_sel_hi:[1,0,1]
	v_pk_fma_f32 v[152:153], v[28:29], s[2:3], v[152:153] op_sel_hi:[1,0,1]
	v_pk_fma_f32 v[150:151], v[30:31], s[2:3], v[150:151] op_sel_hi:[1,0,1]
	v_readlane_b32 s2, v131, 47
	s_waitcnt vmcnt(16)
	v_cvt_scalef32_pk32_f32_fp6 v[0:31], v[44:49], 1.0
	v_pk_fma_f32 v[164:165], v[0:1], s[2:3], v[56:57] op_sel_hi:[1,0,1]
	v_pk_fma_f32 v[166:167], v[2:3], s[2:3], v[58:59] op_sel_hi:[1,0,1]
	v_pk_fma_f32 v[168:169], v[4:5], s[2:3], v[60:61] op_sel_hi:[1,0,1]
	v_pk_fma_f32 v[170:171], v[6:7], s[2:3], v[68:69] op_sel_hi:[1,0,1]
	v_pk_fma_f32 v[172:173], v[8:9], s[2:3], v[70:71] op_sel_hi:[1,0,1]
	v_pk_fma_f32 v[174:175], v[10:11], s[2:3], v[72:73] op_sel_hi:[1,0,1]
	v_pk_fma_f32 v[176:177], v[12:13], s[2:3], v[74:75] op_sel_hi:[1,0,1]
	v_pk_fma_f32 v[178:179], v[14:15], s[2:3], v[76:77] op_sel_hi:[1,0,1]
	v_pk_fma_f32 v[180:181], v[16:17], s[2:3], v[78:79] op_sel_hi:[1,0,1]
	v_pk_fma_f32 v[162:163], v[18:19], s[2:3], v[162:163] op_sel_hi:[1,0,1]
	v_pk_fma_f32 v[160:161], v[20:21], s[2:3], v[160:161] op_sel_hi:[1,0,1]
	v_pk_fma_f32 v[158:159], v[22:23], s[2:3], v[158:159] op_sel_hi:[1,0,1]
	v_pk_fma_f32 v[156:157], v[24:25], s[2:3], v[156:157] op_sel_hi:[1,0,1]
	v_pk_fma_f32 v[154:155], v[26:27], s[2:3], v[154:155] op_sel_hi:[1,0,1]
	v_pk_fma_f32 v[152:153], v[28:29], s[2:3], v[152:153] op_sel_hi:[1,0,1]
	v_pk_fma_f32 v[150:151], v[30:31], s[2:3], v[150:151] op_sel_hi:[1,0,1]
	v_readlane_b32 s2, v241, 56
	v_readlane_b32 s3, v241, 57
	v_readlane_b32 s100, v241, 58
	v_readlane_b32 s101, v241, 59
	s_nop 1
	buffer_load_dwordx4 v[74:77], v129, s[44:47], s2 offen
	buffer_load_dwordx2 v[78:79], v210, s[44:47], s2 offen
	buffer_load_dwordx4 v[68:71], v129, s[44:47], s3 offen
	buffer_load_dwordx2 v[72:73], v210, s[44:47], s3 offen
	buffer_load_dwordx4 v[56:59], v129, s[44:47], s100 offen
	buffer_load_dwordx2 v[60:61], v210, s[44:47], s100 offen
	buffer_load_dwordx4 v[44:47], v129, s[44:47], s101 offen
	buffer_load_dwordx2 v[48:49], v210, s[44:47], s101 offen
	v_readlane_b32 s2, v131, 48
	s_waitcnt vmcnt(22)
	v_cvt_scalef32_pk32_f32_fp6 v[0:31], v[62:67], 1.0
	v_pk_fma_f32 v[62:63], v[0:1], s[2:3], v[164:165] op_sel_hi:[1,0,1]
	v_pk_fma_f32 v[64:65], v[2:3], s[2:3], v[166:167] op_sel_hi:[1,0,1]
	v_pk_fma_f32 v[66:67], v[4:5], s[2:3], v[168:169] op_sel_hi:[1,0,1]
	v_pk_fma_f32 v[164:165], v[6:7], s[2:3], v[170:171] op_sel_hi:[1,0,1]
	v_pk_fma_f32 v[166:167], v[8:9], s[2:3], v[172:173] op_sel_hi:[1,0,1]
	v_pk_fma_f32 v[168:169], v[10:11], s[2:3], v[174:175] op_sel_hi:[1,0,1]
	v_pk_fma_f32 v[170:171], v[12:13], s[2:3], v[176:177] op_sel_hi:[1,0,1]
	v_pk_fma_f32 v[172:173], v[14:15], s[2:3], v[178:179] op_sel_hi:[1,0,1]
	v_pk_fma_f32 v[174:175], v[16:17], s[2:3], v[180:181] op_sel_hi:[1,0,1]
	v_pk_fma_f32 v[162:163], v[18:19], s[2:3], v[162:163] op_sel_hi:[1,0,1]
	v_pk_fma_f32 v[160:161], v[20:21], s[2:3], v[160:161] op_sel_hi:[1,0,1]
	v_pk_fma_f32 v[158:159], v[22:23], s[2:3], v[158:159] op_sel_hi:[1,0,1]
	v_pk_fma_f32 v[156:157], v[24:25], s[2:3], v[156:157] op_sel_hi:[1,0,1]
	v_pk_fma_f32 v[154:155], v[26:27], s[2:3], v[154:155] op_sel_hi:[1,0,1]
	v_pk_fma_f32 v[152:153], v[28:29], s[2:3], v[152:153] op_sel_hi:[1,0,1]
	v_pk_fma_f32 v[150:151], v[30:31], s[2:3], v[150:151] op_sel_hi:[1,0,1]
	v_readlane_b32 s2, v131, 49
	s_waitcnt vmcnt(20)
	v_cvt_scalef32_pk32_f32_fp6 v[0:31], v[50:55], 1.0
	v_pk_fma_f32 v[50:51], v[0:1], s[2:3], v[62:63] op_sel_hi:[1,0,1]
	v_pk_fma_f32 v[52:53], v[2:3], s[2:3], v[64:65] op_sel_hi:[1,0,1]
	v_pk_fma_f32 v[54:55], v[4:5], s[2:3], v[66:67] op_sel_hi:[1,0,1]
	v_pk_fma_f32 v[62:63], v[6:7], s[2:3], v[164:165] op_sel_hi:[1,0,1]
	v_pk_fma_f32 v[64:65], v[8:9], s[2:3], v[166:167] op_sel_hi:[1,0,1]
	v_pk_fma_f32 v[66:67], v[10:11], s[2:3], v[168:169] op_sel_hi:[1,0,1]
	v_pk_fma_f32 v[164:165], v[12:13], s[2:3], v[170:171] op_sel_hi:[1,0,1]
	v_pk_fma_f32 v[166:167], v[14:15], s[2:3], v[172:173] op_sel_hi:[1,0,1]
	v_pk_fma_f32 v[168:169], v[16:17], s[2:3], v[174:175] op_sel_hi:[1,0,1]
	v_pk_fma_f32 v[162:163], v[18:19], s[2:3], v[162:163] op_sel_hi:[1,0,1]
	v_pk_fma_f32 v[160:161], v[20:21], s[2:3], v[160:161] op_sel_hi:[1,0,1]
	v_pk_fma_f32 v[158:159], v[22:23], s[2:3], v[158:159] op_sel_hi:[1,0,1]
	v_pk_fma_f32 v[156:157], v[24:25], s[2:3], v[156:157] op_sel_hi:[1,0,1]
	v_pk_fma_f32 v[154:155], v[26:27], s[2:3], v[154:155] op_sel_hi:[1,0,1]
	v_pk_fma_f32 v[152:153], v[28:29], s[2:3], v[152:153] op_sel_hi:[1,0,1]
	v_pk_fma_f32 v[150:151], v[30:31], s[2:3], v[150:151] op_sel_hi:[1,0,1]
	v_readlane_b32 s2, v131, 50
	s_waitcnt vmcnt(18)
	v_cvt_scalef32_pk32_f32_fp6 v[0:31], v[38:43], 1.0
	v_pk_fma_f32 v[38:39], v[0:1], s[2:3], v[50:51] op_sel_hi:[1,0,1]
	v_pk_fma_f32 v[40:41], v[2:3], s[2:3], v[52:53] op_sel_hi:[1,0,1]
	v_pk_fma_f32 v[42:43], v[4:5], s[2:3], v[54:55] op_sel_hi:[1,0,1]
	v_pk_fma_f32 v[50:51], v[6:7], s[2:3], v[62:63] op_sel_hi:[1,0,1]
	v_pk_fma_f32 v[52:53], v[8:9], s[2:3], v[64:65] op_sel_hi:[1,0,1]
	v_pk_fma_f32 v[54:55], v[10:11], s[2:3], v[66:67] op_sel_hi:[1,0,1]
	v_pk_fma_f32 v[62:63], v[12:13], s[2:3], v[164:165] op_sel_hi:[1,0,1]
	v_pk_fma_f32 v[64:65], v[14:15], s[2:3], v[166:167] op_sel_hi:[1,0,1]
	v_pk_fma_f32 v[66:67], v[16:17], s[2:3], v[168:169] op_sel_hi:[1,0,1]
	v_pk_fma_f32 v[162:163], v[18:19], s[2:3], v[162:163] op_sel_hi:[1,0,1]
	v_pk_fma_f32 v[160:161], v[20:21], s[2:3], v[160:161] op_sel_hi:[1,0,1]
	v_pk_fma_f32 v[158:159], v[22:23], s[2:3], v[158:159] op_sel_hi:[1,0,1]
	v_pk_fma_f32 v[156:157], v[24:25], s[2:3], v[156:157] op_sel_hi:[1,0,1]
	v_pk_fma_f32 v[154:155], v[26:27], s[2:3], v[154:155] op_sel_hi:[1,0,1]
	v_pk_fma_f32 v[152:153], v[28:29], s[2:3], v[152:153] op_sel_hi:[1,0,1]
	v_pk_fma_f32 v[150:151], v[30:31], s[2:3], v[150:151] op_sel_hi:[1,0,1]
	v_readlane_b32 s2, v131, 51
	s_waitcnt vmcnt(16)
	v_cvt_scalef32_pk32_f32_fp6 v[0:31], v[32:37], 1.0
	v_pk_fma_f32 v[164:165], v[0:1], s[2:3], v[38:39] op_sel_hi:[1,0,1]
	v_pk_fma_f32 v[166:167], v[2:3], s[2:3], v[40:41] op_sel_hi:[1,0,1]
	v_pk_fma_f32 v[168:169], v[4:5], s[2:3], v[42:43] op_sel_hi:[1,0,1]
	v_pk_fma_f32 v[170:171], v[6:7], s[2:3], v[50:51] op_sel_hi:[1,0,1]
	v_pk_fma_f32 v[172:173], v[8:9], s[2:3], v[52:53] op_sel_hi:[1,0,1]
	v_pk_fma_f32 v[174:175], v[10:11], s[2:3], v[54:55] op_sel_hi:[1,0,1]
	v_pk_fma_f32 v[176:177], v[12:13], s[2:3], v[62:63] op_sel_hi:[1,0,1]
	v_pk_fma_f32 v[178:179], v[14:15], s[2:3], v[64:65] op_sel_hi:[1,0,1]
	v_pk_fma_f32 v[180:181], v[16:17], s[2:3], v[66:67] op_sel_hi:[1,0,1]
	v_pk_fma_f32 v[162:163], v[18:19], s[2:3], v[162:163] op_sel_hi:[1,0,1]
	v_pk_fma_f32 v[160:161], v[20:21], s[2:3], v[160:161] op_sel_hi:[1,0,1]
	v_pk_fma_f32 v[158:159], v[22:23], s[2:3], v[158:159] op_sel_hi:[1,0,1]
	v_pk_fma_f32 v[156:157], v[24:25], s[2:3], v[156:157] op_sel_hi:[1,0,1]
	v_pk_fma_f32 v[154:155], v[26:27], s[2:3], v[154:155] op_sel_hi:[1,0,1]
	v_pk_fma_f32 v[152:153], v[28:29], s[2:3], v[152:153] op_sel_hi:[1,0,1]
	v_pk_fma_f32 v[150:151], v[30:31], s[2:3], v[150:151] op_sel_hi:[1,0,1]
	v_readlane_b32 s2, v241, 60
	v_readlane_b32 s3, v241, 61
	v_readlane_b32 s100, v241, 62
	v_readlane_b32 s101, v241, 63
	s_nop 1
	buffer_load_dwordx4 v[62:65], v129, s[44:47], s2 offen
	buffer_load_dwordx2 v[66:67], v210, s[44:47], s2 offen
	buffer_load_dwordx4 v[50:53], v129, s[44:47], s3 offen
	buffer_load_dwordx2 v[54:55], v210, s[44:47], s3 offen
	buffer_load_dwordx4 v[38:41], v129, s[44:47], s100 offen
	buffer_load_dwordx2 v[42:43], v210, s[44:47], s100 offen
	buffer_load_dwordx4 v[32:35], v129, s[44:47], s101 offen
	buffer_load_dwordx2 v[36:37], v210, s[44:47], s101 offen
	v_readlane_b32 s2, v131, 52
	s_waitcnt vmcnt(22)
	v_cvt_scalef32_pk32_f32_fp6 v[0:31], v[98:103], 1.0
	v_pk_fma_f32 v[98:99], v[0:1], s[2:3], v[164:165] op_sel_hi:[1,0,1]
	v_pk_fma_f32 v[100:101], v[2:3], s[2:3], v[166:167] op_sel_hi:[1,0,1]
	v_pk_fma_f32 v[102:103], v[4:5], s[2:3], v[168:169] op_sel_hi:[1,0,1]
	v_pk_fma_f32 v[164:165], v[6:7], s[2:3], v[170:171] op_sel_hi:[1,0,1]
	v_pk_fma_f32 v[166:167], v[8:9], s[2:3], v[172:173] op_sel_hi:[1,0,1]
	v_pk_fma_f32 v[168:169], v[10:11], s[2:3], v[174:175] op_sel_hi:[1,0,1]
	v_pk_fma_f32 v[170:171], v[12:13], s[2:3], v[176:177] op_sel_hi:[1,0,1]
	v_pk_fma_f32 v[172:173], v[14:15], s[2:3], v[178:179] op_sel_hi:[1,0,1]
	v_pk_fma_f32 v[174:175], v[16:17], s[2:3], v[180:181] op_sel_hi:[1,0,1]
	v_pk_fma_f32 v[162:163], v[18:19], s[2:3], v[162:163] op_sel_hi:[1,0,1]
	v_pk_fma_f32 v[160:161], v[20:21], s[2:3], v[160:161] op_sel_hi:[1,0,1]
	v_pk_fma_f32 v[158:159], v[22:23], s[2:3], v[158:159] op_sel_hi:[1,0,1]
	v_pk_fma_f32 v[156:157], v[24:25], s[2:3], v[156:157] op_sel_hi:[1,0,1]
	v_pk_fma_f32 v[154:155], v[26:27], s[2:3], v[154:155] op_sel_hi:[1,0,1]
	v_pk_fma_f32 v[152:153], v[28:29], s[2:3], v[152:153] op_sel_hi:[1,0,1]
	v_pk_fma_f32 v[150:151], v[30:31], s[2:3], v[150:151] op_sel_hi:[1,0,1]
	v_readlane_b32 s2, v131, 53
	s_waitcnt vmcnt(20)
	v_cvt_scalef32_pk32_f32_fp6 v[0:31], v[92:97], 1.0
	v_pk_fma_f32 v[92:93], v[0:1], s[2:3], v[98:99] op_sel_hi:[1,0,1]
	v_pk_fma_f32 v[94:95], v[2:3], s[2:3], v[100:101] op_sel_hi:[1,0,1]
	v_pk_fma_f32 v[96:97], v[4:5], s[2:3], v[102:103] op_sel_hi:[1,0,1]
	v_pk_fma_f32 v[98:99], v[6:7], s[2:3], v[164:165] op_sel_hi:[1,0,1]
	v_pk_fma_f32 v[100:101], v[8:9], s[2:3], v[166:167] op_sel_hi:[1,0,1]
	v_pk_fma_f32 v[102:103], v[10:11], s[2:3], v[168:169] op_sel_hi:[1,0,1]
	v_pk_fma_f32 v[164:165], v[12:13], s[2:3], v[170:171] op_sel_hi:[1,0,1]
	v_pk_fma_f32 v[166:167], v[14:15], s[2:3], v[172:173] op_sel_hi:[1,0,1]
	v_pk_fma_f32 v[168:169], v[16:17], s[2:3], v[174:175] op_sel_hi:[1,0,1]
	v_pk_fma_f32 v[162:163], v[18:19], s[2:3], v[162:163] op_sel_hi:[1,0,1]
	v_pk_fma_f32 v[160:161], v[20:21], s[2:3], v[160:161] op_sel_hi:[1,0,1]
	v_pk_fma_f32 v[158:159], v[22:23], s[2:3], v[158:159] op_sel_hi:[1,0,1]
	v_pk_fma_f32 v[156:157], v[24:25], s[2:3], v[156:157] op_sel_hi:[1,0,1]
	v_pk_fma_f32 v[154:155], v[26:27], s[2:3], v[154:155] op_sel_hi:[1,0,1]
	v_pk_fma_f32 v[152:153], v[28:29], s[2:3], v[152:153] op_sel_hi:[1,0,1]
	v_pk_fma_f32 v[150:151], v[30:31], s[2:3], v[150:151] op_sel_hi:[1,0,1]
	v_readlane_b32 s2, v131, 54
	s_waitcnt vmcnt(18)
	v_cvt_scalef32_pk32_f32_fp6 v[0:31], v[86:91], 1.0
	v_pk_fma_f32 v[86:87], v[0:1], s[2:3], v[92:93] op_sel_hi:[1,0,1]
	v_pk_fma_f32 v[88:89], v[2:3], s[2:3], v[94:95] op_sel_hi:[1,0,1]
	v_pk_fma_f32 v[90:91], v[4:5], s[2:3], v[96:97] op_sel_hi:[1,0,1]
	v_pk_fma_f32 v[92:93], v[6:7], s[2:3], v[98:99] op_sel_hi:[1,0,1]
	v_pk_fma_f32 v[94:95], v[8:9], s[2:3], v[100:101] op_sel_hi:[1,0,1]
	v_pk_fma_f32 v[96:97], v[10:11], s[2:3], v[102:103] op_sel_hi:[1,0,1]
	v_pk_fma_f32 v[98:99], v[12:13], s[2:3], v[164:165] op_sel_hi:[1,0,1]
	v_pk_fma_f32 v[100:101], v[14:15], s[2:3], v[166:167] op_sel_hi:[1,0,1]
	v_pk_fma_f32 v[102:103], v[16:17], s[2:3], v[168:169] op_sel_hi:[1,0,1]
	v_pk_fma_f32 v[162:163], v[18:19], s[2:3], v[162:163] op_sel_hi:[1,0,1]
	v_pk_fma_f32 v[160:161], v[20:21], s[2:3], v[160:161] op_sel_hi:[1,0,1]
	v_pk_fma_f32 v[158:159], v[22:23], s[2:3], v[158:159] op_sel_hi:[1,0,1]
	v_pk_fma_f32 v[156:157], v[24:25], s[2:3], v[156:157] op_sel_hi:[1,0,1]
	v_pk_fma_f32 v[154:155], v[26:27], s[2:3], v[154:155] op_sel_hi:[1,0,1]
	v_pk_fma_f32 v[152:153], v[28:29], s[2:3], v[152:153] op_sel_hi:[1,0,1]
	v_pk_fma_f32 v[150:151], v[30:31], s[2:3], v[150:151] op_sel_hi:[1,0,1]
	v_readlane_b32 s2, v131, 55
	s_waitcnt vmcnt(16)
	v_cvt_scalef32_pk32_f32_fp6 v[0:31], v[80:85], 1.0
	v_pk_fma_f32 v[180:181], v[0:1], s[2:3], v[86:87] op_sel_hi:[1,0,1]
	v_pk_fma_f32 v[178:179], v[2:3], s[2:3], v[88:89] op_sel_hi:[1,0,1]
	v_pk_fma_f32 v[176:177], v[4:5], s[2:3], v[90:91] op_sel_hi:[1,0,1]
	v_pk_fma_f32 v[174:175], v[6:7], s[2:3], v[92:93] op_sel_hi:[1,0,1]
	v_pk_fma_f32 v[172:173], v[8:9], s[2:3], v[94:95] op_sel_hi:[1,0,1]
	v_pk_fma_f32 v[170:171], v[10:11], s[2:3], v[96:97] op_sel_hi:[1,0,1]
	v_pk_fma_f32 v[168:169], v[12:13], s[2:3], v[98:99] op_sel_hi:[1,0,1]
	v_pk_fma_f32 v[166:167], v[14:15], s[2:3], v[100:101] op_sel_hi:[1,0,1]
	v_pk_fma_f32 v[164:165], v[16:17], s[2:3], v[102:103] op_sel_hi:[1,0,1]
	v_pk_fma_f32 v[162:163], v[18:19], s[2:3], v[162:163] op_sel_hi:[1,0,1]
	v_pk_fma_f32 v[160:161], v[20:21], s[2:3], v[160:161] op_sel_hi:[1,0,1]
	v_pk_fma_f32 v[158:159], v[22:23], s[2:3], v[158:159] op_sel_hi:[1,0,1]
	v_pk_fma_f32 v[156:157], v[24:25], s[2:3], v[156:157] op_sel_hi:[1,0,1]
	v_pk_fma_f32 v[154:155], v[26:27], s[2:3], v[154:155] op_sel_hi:[1,0,1]
	v_pk_fma_f32 v[152:153], v[28:29], s[2:3], v[152:153] op_sel_hi:[1,0,1]
	v_pk_fma_f32 v[150:151], v[30:31], s[2:3], v[150:151] op_sel_hi:[1,0,1]
	v_readlane_b32 s0, v131, 56
	s_waitcnt vmcnt(14)
	v_cvt_scalef32_pk32_f32_fp6 v[0:31], v[74:79], 1.0
	v_pk_fma_f32 v[74:75], v[0:1], s[0:1], v[180:181] op_sel_hi:[1,0,1]
	v_pk_fma_f32 v[76:77], v[2:3], s[0:1], v[178:179] op_sel_hi:[1,0,1]
	v_pk_fma_f32 v[78:79], v[4:5], s[0:1], v[176:177] op_sel_hi:[1,0,1]
	v_pk_fma_f32 v[80:81], v[6:7], s[0:1], v[174:175] op_sel_hi:[1,0,1]
	v_pk_fma_f32 v[82:83], v[8:9], s[0:1], v[172:173] op_sel_hi:[1,0,1]
	v_pk_fma_f32 v[84:85], v[10:11], s[0:1], v[170:171] op_sel_hi:[1,0,1]
	v_pk_fma_f32 v[86:87], v[12:13], s[0:1], v[168:169] op_sel_hi:[1,0,1]
	v_pk_fma_f32 v[88:89], v[14:15], s[0:1], v[166:167] op_sel_hi:[1,0,1]
	v_pk_fma_f32 v[90:91], v[16:17], s[0:1], v[164:165] op_sel_hi:[1,0,1]
	v_pk_fma_f32 v[92:93], v[18:19], s[0:1], v[162:163] op_sel_hi:[1,0,1]
	v_pk_fma_f32 v[94:95], v[20:21], s[0:1], v[160:161] op_sel_hi:[1,0,1]
	v_pk_fma_f32 v[96:97], v[22:23], s[0:1], v[158:159] op_sel_hi:[1,0,1]
	v_pk_fma_f32 v[98:99], v[24:25], s[0:1], v[156:157] op_sel_hi:[1,0,1]
	v_pk_fma_f32 v[100:101], v[26:27], s[0:1], v[154:155] op_sel_hi:[1,0,1]
	v_pk_fma_f32 v[102:103], v[28:29], s[0:1], v[152:153] op_sel_hi:[1,0,1]
	v_pk_fma_f32 v[150:151], v[30:31], s[0:1], v[150:151] op_sel_hi:[1,0,1]
	v_readlane_b32 s0, v131, 57
	s_waitcnt vmcnt(12)
	v_cvt_scalef32_pk32_f32_fp6 v[0:31], v[68:73], 1.0
	v_pk_fma_f32 v[68:69], v[0:1], s[0:1], v[74:75] op_sel_hi:[1,0,1]
	v_pk_fma_f32 v[70:71], v[2:3], s[0:1], v[76:77] op_sel_hi:[1,0,1]
	v_pk_fma_f32 v[72:73], v[4:5], s[0:1], v[78:79] op_sel_hi:[1,0,1]
	v_pk_fma_f32 v[74:75], v[6:7], s[0:1], v[80:81] op_sel_hi:[1,0,1]
	v_pk_fma_f32 v[76:77], v[8:9], s[0:1], v[82:83] op_sel_hi:[1,0,1]
	v_pk_fma_f32 v[78:79], v[10:11], s[0:1], v[84:85] op_sel_hi:[1,0,1]
	v_pk_fma_f32 v[80:81], v[12:13], s[0:1], v[86:87] op_sel_hi:[1,0,1]
	v_pk_fma_f32 v[82:83], v[14:15], s[0:1], v[88:89] op_sel_hi:[1,0,1]
	v_pk_fma_f32 v[84:85], v[16:17], s[0:1], v[90:91] op_sel_hi:[1,0,1]
	v_pk_fma_f32 v[86:87], v[18:19], s[0:1], v[92:93] op_sel_hi:[1,0,1]
	v_pk_fma_f32 v[88:89], v[20:21], s[0:1], v[94:95] op_sel_hi:[1,0,1]
	v_pk_fma_f32 v[90:91], v[22:23], s[0:1], v[96:97] op_sel_hi:[1,0,1]
	v_pk_fma_f32 v[92:93], v[24:25], s[0:1], v[98:99] op_sel_hi:[1,0,1]
	v_pk_fma_f32 v[94:95], v[26:27], s[0:1], v[100:101] op_sel_hi:[1,0,1]
	v_pk_fma_f32 v[96:97], v[28:29], s[0:1], v[102:103] op_sel_hi:[1,0,1]
	v_pk_fma_f32 v[98:99], v[30:31], s[0:1], v[150:151] op_sel_hi:[1,0,1]
	v_readlane_b32 s0, v131, 58
	s_waitcnt vmcnt(10)
	v_cvt_scalef32_pk32_f32_fp6 v[0:31], v[56:61], 1.0
	v_pk_fma_f32 v[56:57], v[0:1], s[0:1], v[68:69] op_sel_hi:[1,0,1]
	v_pk_fma_f32 v[58:59], v[2:3], s[0:1], v[70:71] op_sel_hi:[1,0,1]
	v_pk_fma_f32 v[60:61], v[4:5], s[0:1], v[72:73] op_sel_hi:[1,0,1]
	v_pk_fma_f32 v[68:69], v[6:7], s[0:1], v[74:75] op_sel_hi:[1,0,1]
	v_pk_fma_f32 v[70:71], v[8:9], s[0:1], v[76:77] op_sel_hi:[1,0,1]
	v_pk_fma_f32 v[72:73], v[10:11], s[0:1], v[78:79] op_sel_hi:[1,0,1]
	v_pk_fma_f32 v[74:75], v[12:13], s[0:1], v[80:81] op_sel_hi:[1,0,1]
	v_pk_fma_f32 v[76:77], v[14:15], s[0:1], v[82:83] op_sel_hi:[1,0,1]
	v_pk_fma_f32 v[78:79], v[16:17], s[0:1], v[84:85] op_sel_hi:[1,0,1]
	v_pk_fma_f32 v[80:81], v[18:19], s[0:1], v[86:87] op_sel_hi:[1,0,1]
	v_pk_fma_f32 v[82:83], v[20:21], s[0:1], v[88:89] op_sel_hi:[1,0,1]
	v_pk_fma_f32 v[84:85], v[22:23], s[0:1], v[90:91] op_sel_hi:[1,0,1]
	v_pk_fma_f32 v[86:87], v[24:25], s[0:1], v[92:93] op_sel_hi:[1,0,1]
	v_pk_fma_f32 v[88:89], v[26:27], s[0:1], v[94:95] op_sel_hi:[1,0,1]
	v_pk_fma_f32 v[90:91], v[28:29], s[0:1], v[96:97] op_sel_hi:[1,0,1]
	v_pk_fma_f32 v[92:93], v[30:31], s[0:1], v[98:99] op_sel_hi:[1,0,1]
	v_readlane_b32 s0, v131, 59
	s_waitcnt vmcnt(8)
	v_cvt_scalef32_pk32_f32_fp6 v[0:31], v[44:49], 1.0
	v_pk_fma_f32 v[46:47], v[2:3], s[0:1], v[58:59] op_sel_hi:[1,0,1]
	v_pk_fma_f32 v[44:45], v[0:1], s[0:1], v[56:57] op_sel_hi:[1,0,1]
	v_pk_fma_f32 v[48:49], v[4:5], s[0:1], v[60:61] op_sel_hi:[1,0,1]
	v_pk_fma_f32 v[56:57], v[6:7], s[0:1], v[68:69] op_sel_hi:[1,0,1]
	v_pk_fma_f32 v[58:59], v[8:9], s[0:1], v[70:71] op_sel_hi:[1,0,1]
	v_pk_fma_f32 v[60:61], v[10:11], s[0:1], v[72:73] op_sel_hi:[1,0,1]
	v_pk_fma_f32 v[68:69], v[12:13], s[0:1], v[74:75] op_sel_hi:[1,0,1]
	v_pk_fma_f32 v[70:71], v[14:15], s[0:1], v[76:77] op_sel_hi:[1,0,1]
	v_pk_fma_f32 v[72:73], v[16:17], s[0:1], v[78:79] op_sel_hi:[1,0,1]
	v_pk_fma_f32 v[74:75], v[18:19], s[0:1], v[80:81] op_sel_hi:[1,0,1]
	v_pk_fma_f32 v[76:77], v[20:21], s[0:1], v[82:83] op_sel_hi:[1,0,1]
	v_pk_fma_f32 v[78:79], v[22:23], s[0:1], v[84:85] op_sel_hi:[1,0,1]
	v_pk_fma_f32 v[80:81], v[24:25], s[0:1], v[86:87] op_sel_hi:[1,0,1]
	v_pk_fma_f32 v[82:83], v[26:27], s[0:1], v[88:89] op_sel_hi:[1,0,1]
	v_pk_fma_f32 v[84:85], v[28:29], s[0:1], v[90:91] op_sel_hi:[1,0,1]
	v_pk_fma_f32 v[86:87], v[30:31], s[0:1], v[92:93] op_sel_hi:[1,0,1]
	v_readlane_b32 s0, v131, 60
	s_waitcnt vmcnt(6)
	v_cvt_scalef32_pk32_f32_fp6 v[0:31], v[62:67], 1.0
	v_pk_fma_f32 v[44:45], v[0:1], s[0:1], v[44:45] op_sel_hi:[1,0,1]
	v_pk_fma_f32 v[46:47], v[2:3], s[0:1], v[46:47] op_sel_hi:[1,0,1]
	v_pk_fma_f32 v[48:49], v[4:5], s[0:1], v[48:49] op_sel_hi:[1,0,1]
	v_pk_fma_f32 v[56:57], v[6:7], s[0:1], v[56:57] op_sel_hi:[1,0,1]
	v_pk_fma_f32 v[58:59], v[8:9], s[0:1], v[58:59] op_sel_hi:[1,0,1]
	v_pk_fma_f32 v[60:61], v[10:11], s[0:1], v[60:61] op_sel_hi:[1,0,1]
	v_pk_fma_f32 v[62:63], v[12:13], s[0:1], v[68:69] op_sel_hi:[1,0,1]
	v_pk_fma_f32 v[64:65], v[14:15], s[0:1], v[70:71] op_sel_hi:[1,0,1]
	v_pk_fma_f32 v[66:67], v[16:17], s[0:1], v[72:73] op_sel_hi:[1,0,1]
	v_pk_fma_f32 v[68:69], v[18:19], s[0:1], v[74:75] op_sel_hi:[1,0,1]
	v_pk_fma_f32 v[70:71], v[20:21], s[0:1], v[76:77] op_sel_hi:[1,0,1]
	v_pk_fma_f32 v[72:73], v[22:23], s[0:1], v[78:79] op_sel_hi:[1,0,1]
	v_pk_fma_f32 v[74:75], v[24:25], s[0:1], v[80:81] op_sel_hi:[1,0,1]
	v_pk_fma_f32 v[76:77], v[26:27], s[0:1], v[82:83] op_sel_hi:[1,0,1]
	v_pk_fma_f32 v[78:79], v[28:29], s[0:1], v[84:85] op_sel_hi:[1,0,1]
	v_pk_fma_f32 v[80:81], v[30:31], s[0:1], v[86:87] op_sel_hi:[1,0,1]
	v_readlane_b32 s0, v131, 61
	s_waitcnt vmcnt(4)
	v_cvt_scalef32_pk32_f32_fp6 v[0:31], v[50:55], 1.0
	v_pk_fma_f32 v[44:45], v[0:1], s[0:1], v[44:45] op_sel_hi:[1,0,1]
	v_pk_fma_f32 v[46:47], v[2:3], s[0:1], v[46:47] op_sel_hi:[1,0,1]
	v_pk_fma_f32 v[48:49], v[4:5], s[0:1], v[48:49] op_sel_hi:[1,0,1]
	v_pk_fma_f32 v[50:51], v[6:7], s[0:1], v[56:57] op_sel_hi:[1,0,1]
	v_pk_fma_f32 v[52:53], v[8:9], s[0:1], v[58:59] op_sel_hi:[1,0,1]
	v_pk_fma_f32 v[54:55], v[10:11], s[0:1], v[60:61] op_sel_hi:[1,0,1]
	v_pk_fma_f32 v[56:57], v[12:13], s[0:1], v[62:63] op_sel_hi:[1,0,1]
	v_pk_fma_f32 v[58:59], v[14:15], s[0:1], v[64:65] op_sel_hi:[1,0,1]
	v_pk_fma_f32 v[60:61], v[16:17], s[0:1], v[66:67] op_sel_hi:[1,0,1]
	v_pk_fma_f32 v[62:63], v[18:19], s[0:1], v[68:69] op_sel_hi:[1,0,1]
	v_pk_fma_f32 v[64:65], v[20:21], s[0:1], v[70:71] op_sel_hi:[1,0,1]
	v_pk_fma_f32 v[66:67], v[22:23], s[0:1], v[72:73] op_sel_hi:[1,0,1]
	v_pk_fma_f32 v[68:69], v[24:25], s[0:1], v[74:75] op_sel_hi:[1,0,1]
	v_pk_fma_f32 v[70:71], v[26:27], s[0:1], v[76:77] op_sel_hi:[1,0,1]
	v_pk_fma_f32 v[72:73], v[28:29], s[0:1], v[78:79] op_sel_hi:[1,0,1]
	v_pk_fma_f32 v[74:75], v[30:31], s[0:1], v[80:81] op_sel_hi:[1,0,1]
	v_readlane_b32 s0, v131, 62
	s_waitcnt vmcnt(2)
	v_cvt_scalef32_pk32_f32_fp6 v[0:31], v[38:43], 1.0
	v_pk_fma_f32 v[38:39], v[0:1], s[0:1], v[44:45] op_sel_hi:[1,0,1]
	v_pk_fma_f32 v[40:41], v[2:3], s[0:1], v[46:47] op_sel_hi:[1,0,1]
	v_pk_fma_f32 v[42:43], v[4:5], s[0:1], v[48:49] op_sel_hi:[1,0,1]
	v_pk_fma_f32 v[44:45], v[6:7], s[0:1], v[50:51] op_sel_hi:[1,0,1]
	v_pk_fma_f32 v[46:47], v[8:9], s[0:1], v[52:53] op_sel_hi:[1,0,1]
	v_pk_fma_f32 v[48:49], v[10:11], s[0:1], v[54:55] op_sel_hi:[1,0,1]
	v_pk_fma_f32 v[50:51], v[12:13], s[0:1], v[56:57] op_sel_hi:[1,0,1]
	v_pk_fma_f32 v[52:53], v[14:15], s[0:1], v[58:59] op_sel_hi:[1,0,1]
	v_pk_fma_f32 v[54:55], v[16:17], s[0:1], v[60:61] op_sel_hi:[1,0,1]
	v_pk_fma_f32 v[56:57], v[18:19], s[0:1], v[62:63] op_sel_hi:[1,0,1]
	v_pk_fma_f32 v[58:59], v[20:21], s[0:1], v[64:65] op_sel_hi:[1,0,1]
	v_pk_fma_f32 v[62:63], v[22:23], s[0:1], v[66:67] op_sel_hi:[1,0,1]
	v_pk_fma_f32 v[64:65], v[24:25], s[0:1], v[68:69] op_sel_hi:[1,0,1]
	v_pk_fma_f32 v[66:67], v[26:27], s[0:1], v[70:71] op_sel_hi:[1,0,1]
	v_pk_fma_f32 v[68:69], v[28:29], s[0:1], v[72:73] op_sel_hi:[1,0,1]
	v_pk_fma_f32 v[70:71], v[30:31], s[0:1], v[74:75] op_sel_hi:[1,0,1]
	v_readlane_b32 s0, v131, 63
	s_waitcnt vmcnt(0)
	v_cvt_scalef32_pk32_f32_fp6 v[0:31], v[32:37], 1.0
	v_pk_fma_f32 v[34:35], v[0:1], s[0:1], v[38:39] op_sel_hi:[1,0,1]
	v_pk_fma_f32 v[32:33], v[2:3], s[0:1], v[40:41] op_sel_hi:[1,0,1]
	v_pk_fma_f32 v[38:39], v[4:5], s[0:1], v[42:43] op_sel_hi:[1,0,1]
	v_pk_fma_f32 v[36:37], v[6:7], s[0:1], v[44:45] op_sel_hi:[1,0,1]
	v_pk_fma_f32 v[42:43], v[8:9], s[0:1], v[46:47] op_sel_hi:[1,0,1]
	v_pk_fma_f32 v[40:41], v[10:11], s[0:1], v[48:49] op_sel_hi:[1,0,1]
	v_pk_fma_f32 v[48:49], v[12:13], s[0:1], v[50:51] op_sel_hi:[1,0,1]
	v_pk_fma_f32 v[46:47], v[14:15], s[0:1], v[52:53] op_sel_hi:[1,0,1]
	v_pk_fma_f32 v[50:51], v[18:19], s[0:1], v[56:57] op_sel_hi:[1,0,1]
	v_pk_fma_f32 v[54:55], v[16:17], s[0:1], v[54:55] op_sel_hi:[1,0,1]
	v_pk_fma_f32 v[60:61], v[20:21], s[0:1], v[58:59] op_sel_hi:[1,0,1]
	v_pk_fma_f32 v[56:57], v[22:23], s[0:1], v[62:63] op_sel_hi:[1,0,1]
	v_pk_fma_f32 v[44:45], v[24:25], s[0:1], v[64:65] op_sel_hi:[1,0,1]
	v_pk_fma_f32 v[64:65], v[26:27], s[0:1], v[66:67] op_sel_hi:[1,0,1]
	v_pk_fma_f32 v[18:19], v[28:29], s[0:1], v[68:69] op_sel_hi:[1,0,1]
	v_pk_fma_f32 v[24:25], v[30:31], s[0:1], v[70:71] op_sel_hi:[1,0,1]
	s_lshr_b32 s0, s58, 12
	s_ashr_i32 s59, s58, 31
	s_mul_i32 s4, s0, 0x3000
	s_lshl_b64 s[0:1], s[58:59], 12
	s_add_u32 s2, s71, s0
	v_lshlrev_b32_e32 v12, 2, v148
	s_addc_u32 s3, s74, s1
	v_ashrrev_i32_e32 v13, 31, v12
	v_lshlrev_b32_e32 v63, 3, v148
	v_lshl_add_u64 v[14:15], v[12:13], 1, s[2:3]
	v_add3_u32 v62, v201, s4, v63
	global_load_dwordx2 v[16:17], v[14:15], off
	ds_read2st64_b64 v[0:3], v62 offset1:1
	global_load_dwordx2 v[20:21], v[14:15], off offset:512
	global_load_dwordx2 v[22:23], v[14:15], off offset:1024
	ds_read2st64_b64 v[4:7], v62 offset0:2 offset1:3
	global_load_dwordx2 v[52:53], v[14:15], off offset:1536
	global_load_dwordx2 v[58:59], v[14:15], off offset:2048
	ds_read2st64_b64 v[8:11], v62 offset0:4 offset1:5
	global_load_dwordx2 v[66:67], v[14:15], off offset:2560
	global_load_dwordx2 v[68:69], v[14:15], off offset:3072
	global_load_dwordx2 v[26:27], v[14:15], off offset:3584
	ds_read2st64_b64 v[28:31], v62 offset0:6 offset1:7
	s_lshl_b64 s[2:3], s[58:59], 13
	s_add_u32 s4, s16, s2
	s_addc_u32 s5, s17, s3
	s_and_b64 vcc, exec, s[54:55]
	s_waitcnt lgkmcnt(0)
	v_lshlrev_b32_e32 v72, 16, v30
	v_and_b32_e32 v73, 0xffff0000, v30
	v_lshlrev_b32_e32 v30, 16, v31
	v_and_b32_e32 v31, 0xffff0000, v31
	v_pk_mul_f32 v[24:25], v[24:25], v[30:31]
	v_lshlrev_b32_e32 v30, 16, v28
	v_and_b32_e32 v31, 0xffff0000, v28
	v_pk_mul_f32 v[30:31], v[44:45], v[30:31]
	v_lshlrev_b32_e32 v28, 16, v29
	v_and_b32_e32 v29, 0xffff0000, v29
	v_pk_mul_f32 v[28:29], v[64:65], v[28:29]
	v_pk_mul_f32 v[18:19], v[18:19], v[72:73]
	s_waitcnt vmcnt(0)
	v_lshlrev_b32_e32 v70, 16, v26
	v_and_b32_e32 v71, 0xffff0000, v26
	v_lshlrev_b32_e32 v26, 16, v27
	v_and_b32_e32 v27, 0xffff0000, v27
	v_pk_fma_f32 v[24:25], v[26:27], s[38:39], v[24:25] op_sel_hi:[1,0,1]
	v_lshlrev_b32_e32 v26, 16, v68
	v_and_b32_e32 v27, 0xffff0000, v68
	v_pk_fma_f32 v[26:27], v[26:27], s[38:39], v[30:31] op_sel_hi:[1,0,1]
	v_lshlrev_b32_e32 v30, 16, v69
	v_and_b32_e32 v31, 0xffff0000, v69
	v_pk_fma_f32 v[44:45], v[30:31], s[38:39], v[28:29] op_sel_hi:[1,0,1]
	v_lshlrev_b32_e32 v30, 16, v10
	v_and_b32_e32 v31, 0xffff0000, v10
	v_lshlrev_b32_e32 v28, 16, v66
	v_and_b32_e32 v29, 0xffff0000, v66
	v_pk_mul_f32 v[30:31], v[60:61], v[30:31]
	v_lshlrev_b32_e32 v10, 16, v11
	v_and_b32_e32 v11, 0xffff0000, v11
	v_pk_fma_f32 v[28:29], v[28:29], s[38:39], v[30:31] op_sel_hi:[1,0,1]
	v_lshlrev_b32_e32 v30, 16, v67
	v_and_b32_e32 v31, 0xffff0000, v67
	v_pk_mul_f32 v[10:11], v[56:57], v[10:11]
	v_lshlrev_b32_e32 v56, 16, v8
	v_and_b32_e32 v57, 0xffff0000, v8
	v_pk_fma_f32 v[10:11], v[30:31], s[38:39], v[10:11] op_sel_hi:[1,0,1]
	v_lshlrev_b32_e32 v30, 16, v58
	v_and_b32_e32 v31, 0xffff0000, v58
	v_pk_mul_f32 v[54:55], v[54:55], v[56:57]
	v_lshlrev_b32_e32 v8, 16, v9
	v_and_b32_e32 v9, 0xffff0000, v9
	v_pk_fma_f32 v[30:31], v[30:31], s[38:39], v[54:55] op_sel_hi:[1,0,1]
	v_lshlrev_b32_e32 v54, 16, v59
	v_and_b32_e32 v55, 0xffff0000, v59
	v_pk_mul_f32 v[8:9], v[50:51], v[8:9]
	v_lshlrev_b32_e32 v50, 16, v52
	v_pk_fma_f32 v[8:9], v[54:55], s[38:39], v[8:9] op_sel_hi:[1,0,1]
	v_lshlrev_b32_e32 v54, 16, v6
	v_and_b32_e32 v55, 0xffff0000, v6
	v_and_b32_e32 v51, 0xffff0000, v52
	v_pk_mul_f32 v[48:49], v[48:49], v[54:55]
	v_lshlrev_b32_e32 v6, 16, v7
	v_and_b32_e32 v7, 0xffff0000, v7
	v_pk_fma_f32 v[48:49], v[50:51], s[38:39], v[48:49] op_sel_hi:[1,0,1]
	v_lshlrev_b32_e32 v50, 16, v53
	v_and_b32_e32 v51, 0xffff0000, v53
	v_pk_mul_f32 v[6:7], v[46:47], v[6:7]
	v_lshlrev_b32_e32 v46, 16, v22
	v_pk_fma_f32 v[6:7], v[50:51], s[38:39], v[6:7] op_sel_hi:[1,0,1]
	v_lshlrev_b32_e32 v50, 16, v4
	v_and_b32_e32 v51, 0xffff0000, v4
	v_lshlrev_b32_e32 v4, 16, v5
	v_and_b32_e32 v5, 0xffff0000, v5
	v_and_b32_e32 v47, 0xffff0000, v22
	v_lshlrev_b32_e32 v22, 16, v23
	v_and_b32_e32 v23, 0xffff0000, v23
	v_pk_mul_f32 v[4:5], v[40:41], v[4:5]
	v_lshlrev_b32_e32 v40, 16, v2
	v_and_b32_e32 v41, 0xffff0000, v2
	v_pk_fma_f32 v[4:5], v[22:23], s[38:39], v[4:5] op_sel_hi:[1,0,1]
	v_lshlrev_b32_e32 v22, 16, v20
	v_and_b32_e32 v23, 0xffff0000, v20
	v_pk_mul_f32 v[38:39], v[38:39], v[40:41]
	v_lshlrev_b32_e32 v40, 16, v0
	v_and_b32_e32 v41, 0xffff0000, v0
	v_pk_fma_f32 v[22:23], v[22:23], s[38:39], v[38:39] op_sel_hi:[1,0,1]
	v_lshlrev_b32_e32 v38, 16, v16
	v_and_b32_e32 v39, 0xffff0000, v16
	v_pk_mul_f32 v[34:35], v[34:35], v[40:41]
	v_lshlrev_b32_e32 v16, 16, v17
	v_pk_fma_f32 v[34:35], v[38:39], s[38:39], v[34:35] op_sel_hi:[1,0,1]
	v_and_b32_e32 v17, 0xffff0000, v17
	v_add_f32_e32 v0, 0, v34
	v_add_f32_e32 v38, v35, v0
	v_lshlrev_b32_e32 v0, 16, v1
	v_and_b32_e32 v1, 0xffff0000, v1
	v_pk_mul_f32 v[0:1], v[32:33], v[0:1]
	v_lshlrev_b32_e32 v2, 16, v3
	v_pk_fma_f32 v[0:1], v[16:17], s[38:39], v[0:1] op_sel_hi:[1,0,1]
	v_and_b32_e32 v3, 0xffff0000, v3
	v_add_f32_e32 v16, v0, v38
	v_add_f32_e32 v16, v1, v16
	v_lshlrev_b32_e32 v20, 16, v21
	v_and_b32_e32 v21, 0xffff0000, v21
	v_pk_mul_f32 v[2:3], v[36:37], v[2:3]
	v_add_f32_e32 v16, v22, v16
	v_pk_fma_f32 v[2:3], v[20:21], s[38:39], v[2:3] op_sel_hi:[1,0,1]
	v_add_f32_e32 v16, v23, v16
	v_pk_mul_f32 v[42:43], v[42:43], v[50:51]
	v_add_f32_e32 v16, v2, v16
	v_pk_fma_f32 v[52:53], v[46:47], s[38:39], v[42:43] op_sel_hi:[1,0,1]
	v_add_f32_e32 v16, v3, v16
	v_add_f32_e32 v16, v52, v16
	v_add_f32_e32 v16, v53, v16
	v_add_f32_e32 v16, v4, v16
	v_add_f32_e32 v16, v5, v16
	v_add_f32_e32 v16, v48, v16
	v_add_f32_e32 v16, v49, v16
	v_add_f32_e32 v16, v6, v16
	v_add_f32_e32 v16, v7, v16
	v_add_f32_e32 v16, v30, v16
	v_add_f32_e32 v16, v31, v16
	v_add_f32_e32 v16, v8, v16
	v_add_f32_e32 v16, v9, v16
	v_add_f32_e32 v16, v28, v16
	v_add_f32_e32 v16, v29, v16
	v_add_f32_e32 v16, v10, v16
	v_add_f32_e32 v16, v11, v16
	v_add_f32_e32 v16, v26, v16
	v_add_f32_e32 v16, v27, v16
	v_add_f32_e32 v16, v44, v16
	v_pk_fma_f32 v[18:19], v[70:71], s[38:39], v[18:19] op_sel_hi:[1,0,1]
	v_add_f32_e32 v16, v45, v16
	v_add_f32_e32 v16, v18, v16
	v_add_f32_e32 v16, v19, v16
	v_add_f32_e32 v16, v24, v16
	v_add_f32_e32 v16, v25, v16
	v_mov_b32_e32 v17, v105
	v_add_u32_e32 v50, v202, v63
	v_add_f32_dpp v16, v16, v16 quad_perm:[1,0,3,2] row_mask:0xf bank_mask:0xf bound_ctrl:1
	v_add_u32_e32 v51, v203, v63
	ds_read_b64 v[20:21], v50
	ds_read_b64 v[36:37], v51
	v_add_f32_dpp v16, v16, v16 quad_perm:[2,3,0,1] row_mask:0xf bank_mask:0xf bound_ctrl:1
	s_waitcnt lgkmcnt(1)
	v_lshlrev_b32_e32 v54, 16, v20
	v_add_f32_dpp v16, v16, v16 row_half_mirror row_mask:0xf bank_mask:0xf bound_ctrl:1
	s_waitcnt lgkmcnt(0)
	v_lshlrev_b32_e32 v56, 16, v36
	v_and_b32_e32 v57, 0xffff0000, v36
	v_add_f32_dpp v16, v16, v16 row_mirror row_mask:0xf bank_mask:0xf bound_ctrl:1
	v_lshlrev_b32_e32 v60, 16, v37
	v_and_b32_e32 v61, 0xffff0000, v37
	v_mov_b32_dpp v17, v16 row_bcast:15 row_mask:0xa bank_mask:0xf
	v_add_f32_e32 v16, v16, v17
	v_mov_b32_e32 v17, v105
	v_and_b32_e32 v55, 0xffff0000, v20
	v_lshlrev_b32_e32 v58, 16, v21
	v_mov_b32_dpp v17, v16 row_bcast:31 row_mask:0xc bank_mask:0xf
	v_add_f32_e32 v16, v16, v17
	v_and_b32_e32 v59, 0xffff0000, v21
	v_readlane_b32 s2, v16, 63
	s_nop 1
	v_mul_f32_e32 v64, s2, v187
	v_pk_add_f32 v[66:67], v[34:35], v[64:65] op_sel_hi:[1,0] neg_lo:[0,1] neg_hi:[0,1]
	v_pk_add_f32 v[70:71], v[0:1], v[64:65] op_sel_hi:[1,0] neg_lo:[0,1] neg_hi:[0,1]
	v_pk_mul_f32 v[68:69], v[66:67], v[66:67]
	v_pk_mul_f32 v[0:1], v[70:71], v[70:71]
	v_add_f32_e32 v63, v68, v69
	v_pk_add_f32 v[46:47], v[22:23], v[64:65] op_sel_hi:[1,0] neg_lo:[0,1] neg_hi:[0,1]
	v_add_f32_e32 v0, v0, v63
	v_pk_mul_f32 v[72:73], v[46:47], v[46:47]
	v_add_f32_e32 v0, v1, v0
	v_pk_add_f32 v[42:43], v[2:3], v[64:65] op_sel_hi:[1,0] neg_lo:[0,1] neg_hi:[0,1]
	v_add_f32_e32 v0, v72, v0
	v_pk_mul_f32 v[2:3], v[42:43], v[42:43]
	v_add_f32_e32 v0, v73, v0
	v_pk_add_f32 v[40:41], v[52:53], v[64:65] op_sel_hi:[1,0] neg_lo:[0,1] neg_hi:[0,1]
	v_add_f32_e32 v0, v2, v0
	v_pk_mul_f32 v[52:53], v[40:41], v[40:41]
	v_add_f32_e32 v0, v3, v0
	v_pk_add_f32 v[22:23], v[4:5], v[64:65] op_sel_hi:[1,0] neg_lo:[0,1] neg_hi:[0,1]
	v_add_f32_e32 v0, v52, v0
	v_pk_mul_f32 v[4:5], v[22:23], v[22:23]
	v_add_f32_e32 v0, v53, v0
	v_pk_add_f32 v[38:39], v[48:49], v[64:65] op_sel_hi:[1,0] neg_lo:[0,1] neg_hi:[0,1]
	v_add_f32_e32 v0, v4, v0
	v_pk_mul_f32 v[48:49], v[38:39], v[38:39]
	v_add_f32_e32 v0, v5, v0
	v_pk_add_f32 v[36:37], v[6:7], v[64:65] op_sel_hi:[1,0] neg_lo:[0,1] neg_hi:[0,1]
	v_add_f32_e32 v0, v48, v0
	v_pk_mul_f32 v[74:75], v[36:37], v[36:37]
	v_add_f32_e32 v0, v49, v0
	v_pk_add_f32 v[34:35], v[30:31], v[64:65] op_sel_hi:[1,0] neg_lo:[0,1] neg_hi:[0,1]
	v_add_f32_e32 v0, v74, v0
	v_pk_mul_f32 v[76:77], v[34:35], v[34:35]
	v_add_f32_e32 v0, v75, v0
	v_pk_add_f32 v[32:33], v[8:9], v[64:65] op_sel_hi:[1,0] neg_lo:[0,1] neg_hi:[0,1]
	v_add_f32_e32 v0, v76, v0
	v_pk_mul_f32 v[78:79], v[32:33], v[32:33]
	v_add_f32_e32 v0, v77, v0
	v_pk_add_f32 v[30:31], v[28:29], v[64:65] op_sel_hi:[1,0] neg_lo:[0,1] neg_hi:[0,1]
	v_add_f32_e32 v0, v78, v0
	v_pk_mul_f32 v[80:81], v[30:31], v[30:31]
	v_add_f32_e32 v0, v79, v0
	v_pk_add_f32 v[28:29], v[10:11], v[64:65] op_sel_hi:[1,0] neg_lo:[0,1] neg_hi:[0,1]
	v_add_f32_e32 v0, v80, v0
	v_pk_mul_f32 v[10:11], v[28:29], v[28:29]
	v_add_f32_e32 v0, v81, v0
	v_pk_add_f32 v[20:21], v[26:27], v[64:65] op_sel_hi:[1,0] neg_lo:[0,1] neg_hi:[0,1]
	v_add_f32_e32 v0, v10, v0
	v_pk_mul_f32 v[26:27], v[20:21], v[20:21]
	v_add_f32_e32 v0, v11, v0
	v_pk_add_f32 v[16:17], v[44:45], v[64:65] op_sel_hi:[1,0] neg_lo:[0,1] neg_hi:[0,1]
	v_add_f32_e32 v0, v26, v0
	v_pk_mul_f32 v[44:45], v[16:17], v[16:17]
	v_add_f32_e32 v0, v27, v0
	v_pk_add_f32 v[8:9], v[18:19], v[64:65] op_sel_hi:[1,0] neg_lo:[0,1] neg_hi:[0,1]
	v_add_f32_e32 v0, v44, v0
	v_pk_mul_f32 v[18:19], v[8:9], v[8:9]
	v_add_f32_e32 v0, v45, v0
	v_pk_add_f32 v[6:7], v[24:25], v[64:65] op_sel_hi:[1,0] neg_lo:[0,1] neg_hi:[0,1]
	v_add_f32_e32 v0, v18, v0
	v_pk_mul_f32 v[24:25], v[6:7], v[6:7]
	v_add_f32_e32 v0, v19, v0
	v_add_f32_e32 v0, v24, v0
	v_add_f32_e32 v0, v25, v0
	v_mov_b32_e32 v1, v105
	s_nop 0
	v_add_f32_dpp v0, v0, v0 quad_perm:[1,0,3,2] row_mask:0xf bank_mask:0xf bound_ctrl:1
	s_nop 1
	v_add_f32_dpp v0, v0, v0 quad_perm:[2,3,0,1] row_mask:0xf bank_mask:0xf bound_ctrl:1
	s_nop 1
	v_add_f32_dpp v0, v0, v0 row_half_mirror row_mask:0xf bank_mask:0xf bound_ctrl:1
	s_nop 1
	v_add_f32_dpp v0, v0, v0 row_mirror row_mask:0xf bank_mask:0xf bound_ctrl:1
	s_nop 1
	v_mov_b32_dpp v1, v0 row_bcast:15 row_mask:0xa bank_mask:0xf
	v_add_f32_e32 v0, v0, v1
	v_mov_b32_e32 v1, v105
	s_nop 1
	v_mov_b32_dpp v1, v0 row_bcast:31 row_mask:0xc bank_mask:0xf
	v_add_f32_e32 v0, v0, v1
	s_nop 0
	v_readlane_b32 s2, v0, 63
	s_nop 1
	v_fma_f32 v0, s2, v187, v183
	v_rsq_f32_e32 v10, v0
	s_mov_b64 s[2:3], -1
	v_pk_mul_f32 v[0:1], v[66:67], v[10:11] op_sel_hi:[1,0]
	v_pk_mul_f32 v[2:3], v[70:71], v[10:11] op_sel_hi:[1,0]
	v_pk_fma_f32 v[0:1], v[0:1], v[54:55], v[56:57]
	v_pk_fma_f32 v[2:3], v[2:3], v[58:59], v[60:61]
	s_cbranch_vccz .LBB0_1142
	ds_read2st64_b64 v[24:27], v62 offset0:8 offset1:16
	v_cvt_pk_bf16_f32 v4, v0, v1
	v_cvt_pk_bf16_f32 v5, v2, v3
	global_store_dwordx2 v[14:15], v[4:5], off
	s_mov_b64 s[2:3], 0
	s_waitcnt lgkmcnt(0)
	v_lshlrev_b32_e32 v18, 16, v26
	v_and_b32_e32 v19, 0xffff0000, v26
	v_lshlrev_b32_e32 v4, 16, v24
	v_and_b32_e32 v5, 0xffff0000, v24
	v_pk_add_f32 v[18:19], v[18:19], 1.0 op_sel_hi:[1,0]
	v_lshlrev_b32_e32 v24, 16, v27
	v_pk_fma_f32 v[4:5], v[0:1], v[18:19], v[4:5]
	v_lshlrev_b32_e32 v18, 16, v25
	v_and_b32_e32 v19, 0xffff0000, v25
	v_and_b32_e32 v25, 0xffff0000, v27
	v_pk_add_f32 v[24:25], v[24:25], 1.0 op_sel_hi:[1,0]
	v_cvt_pk_bf16_f32 v4, v4, v5
	v_pk_fma_f32 v[18:19], v[2:3], v[24:25], v[18:19]
	s_nop 0
	v_cvt_pk_bf16_f32 v5, v18, v19
